# v038 + sc1 (write-through) on all plain global_store_dwordx4 to cheapen grid-barrier release
# baseline (speedup 1.0000x reference)
; __device__ __forceinline__ u32x4 pack8(const f32x4 a, const f32x4 b) { u32x4 w; w.x = cvt_pk_bf16(a[0], a[1]); w.y = cvt_pk_bf16(a[2], a[3]); w.z = cvt_pk_bf16(b[0], b[1]); w.w = cvt_pk_bf16(b[2], b[3]); return w; }
;     __device__ __forceinline__ void operator()(const f32x4 (&acc)[2][2][4][2], const Unit& u, int wr, int wc, int fr, int fq) const {
;     ...
;             bf16_t* O = u.pn < 2 ? QN : KN; const int cb = (u.pn & 1) * BM + wc * 32 + 8 * fq;
; #pragma unroll
;             for (int ai = 0; ai < 2; ++ai)
; #pragma unroll
;                 for (int m = 0; m < 4; ++m) { const int tok = row0 + ai * HALF + m * 16;
; #pragma unroll
;                     for (int bj = 0; bj < 2; ++bj) { const int c = cb + bj * HALF, head = c >> 6, d0 = c & 63;
;                         *(u32x4*)(O + ((((size_t)(tok >> 5) * 8 + head) * 4 + (d0 >> 4)) * 64 + 32 * ((d0 >> 3) & 1) + (tok & 31)) * 8) = pack8(acc[ai][bj][m][0], acc[ai][bj][m][1]); } }
.LBB0_195:
	s_lshl_b32 s17, s26, 8
	s_add_i32 s17, s17, s49
	s_cmp_lt_i32 s24, 6
	s_mov_b64 s[4:5], -1
	s_cbranch_scc0 .LBB0_198
	s_cmp_lt_i32 s24, 2
	s_mov_b32 s4, 0x6313600
	s_cselect_b32 s4, s4, 0x7393600
	s_add_u32 s4, s90, s4
	s_addc_u32 s5, s91, 0
	s_lshl_b32 s19, s24, 8
	s_ashr_i32 s28, s17, 5
	s_or_b32 s19, s19, s50
	s_ashr_i32 s29, s28, 31
	s_lshl_b64 s[30:31], s[28:29], 5
	s_lshr_b32 s19, s19, 4
	v_or_b32_e32 v142, s30, v144
	s_and_b32 s19, s19, 20
	v_mov_b32_e32 v163, s31
	v_or_b32_e32 v162, s19, v142
	s_or_b32 s26, s19, 8
	v_lshlrev_b64 v[180:181], 10, v[162:163]
	v_or_b32_e32 v162, s26, v142
	v_lshl_add_u64 v[180:181], s[4:5], 0, v[180:181]
	v_lshlrev_b64 v[162:163], 10, v[162:163]
	v_cvt_pk_bf16_f32 v158, v126, v127
	v_cvt_pk_bf16_f32 v159, v128, v129
	v_cvt_pk_bf16_f32 v160, v122, v123
	v_cvt_pk_bf16_f32 v161, v124, v125
	v_lshl_add_u64 v[182:183], v[180:181], 0, v[146:147]
	v_lshl_add_u64 v[162:163], s[4:5], 0, v[162:163]
	s_or_b32 s28, s28, 1
	global_store_dwordx4 v[182:183], v[158:161], off sc1
	v_lshl_add_u64 v[182:183], v[162:163], 0, v[146:147]
	s_ashr_i32 s29, s28, 31
	v_cvt_pk_bf16_f32 v158, v118, v119
	v_cvt_pk_bf16_f32 v159, v120, v121
	v_cvt_pk_bf16_f32 v160, v114, v115
	v_cvt_pk_bf16_f32 v161, v116, v117
	global_store_dwordx4 v[182:183], v[158:161], off sc1
	v_lshl_add_u64 v[180:181], v[180:181], 0, v[148:149]
	s_lshl_b64 s[28:29], s[28:29], 5
	v_cvt_pk_bf16_f32 v158, v110, v111
	v_cvt_pk_bf16_f32 v159, v112, v113
	v_cvt_pk_bf16_f32 v160, v106, v107
	v_cvt_pk_bf16_f32 v161, v108, v109
	global_store_dwordx4 v[180:181], v[158:161], off sc1
	v_lshl_add_u64 v[162:163], v[162:163], 0, v[148:149]
	v_or_b32_e32 v142, s28, v144
	v_cvt_pk_bf16_f32 v158, v102, v103
	v_cvt_pk_bf16_f32 v159, v104, v105
	v_cvt_pk_bf16_f32 v160, v98, v99
	v_cvt_pk_bf16_f32 v161, v100, v101
	global_store_dwordx4 v[162:163], v[158:161], off sc1
	v_mov_b32_e32 v163, s29
	v_or_b32_e32 v162, s19, v142
	v_lshlrev_b64 v[180:181], 10, v[162:163]
	v_or_b32_e32 v162, s26, v142
	v_lshl_add_u64 v[180:181], s[4:5], 0, v[180:181]
	v_lshlrev_b64 v[162:163], 10, v[162:163]
	s_add_i32 s28, s17, 0x80
	v_cvt_pk_bf16_f32 v158, v94, v95
	v_cvt_pk_bf16_f32 v159, v96, v97
	v_cvt_pk_bf16_f32 v160, v90, v91
	v_cvt_pk_bf16_f32 v161, v92, v93
	v_lshl_add_u64 v[182:183], v[180:181], 0, v[146:147]
	v_lshl_add_u64 v[162:163], s[4:5], 0, v[162:163]
	s_ashr_i32 s28, s28, 5
	global_store_dwordx4 v[182:183], v[158:161], off sc1
	v_lshl_add_u64 v[182:183], v[162:163], 0, v[146:147]
	s_ashr_i32 s29, s28, 31
	v_cvt_pk_bf16_f32 v158, v86, v87
	v_cvt_pk_bf16_f32 v159, v88, v89
	v_cvt_pk_bf16_f32 v160, v82, v83
	v_cvt_pk_bf16_f32 v161, v84, v85
	global_store_dwordx4 v[182:183], v[158:161], off sc1
	v_lshl_add_u64 v[180:181], v[180:181], 0, v[148:149]
	s_lshl_b64 s[28:29], s[28:29], 5
	v_cvt_pk_bf16_f32 v158, v78, v79
	v_cvt_pk_bf16_f32 v159, v80, v81
	v_cvt_pk_bf16_f32 v160, v74, v75
	v_cvt_pk_bf16_f32 v161, v76, v77
	global_store_dwordx4 v[180:181], v[158:161], off sc1
	v_lshl_add_u64 v[162:163], v[162:163], 0, v[148:149]
	v_or_b32_e32 v142, s28, v144
	v_cvt_pk_bf16_f32 v158, v70, v71
	v_cvt_pk_bf16_f32 v159, v72, v73
	v_cvt_pk_bf16_f32 v160, v66, v67
	v_cvt_pk_bf16_f32 v161, v68, v69
	global_store_dwordx4 v[162:163], v[158:161], off sc1
	v_mov_b32_e32 v163, s29
	v_or_b32_e32 v162, s19, v142
	s_add_i32 s28, s17, 0x90
	v_lshlrev_b64 v[180:181], 10, v[162:163]
	v_or_b32_e32 v162, s26, v142
	s_ashr_i32 s28, s28, 5
	v_lshl_add_u64 v[180:181], s[4:5], 0, v[180:181]
	v_lshlrev_b64 v[162:163], 10, v[162:163]
	s_ashr_i32 s29, s28, 31
	v_cvt_pk_bf16_f32 v158, v62, v63
	v_cvt_pk_bf16_f32 v159, v64, v65
	v_cvt_pk_bf16_f32 v160, v58, v59
	v_cvt_pk_bf16_f32 v161, v60, v61
	v_lshl_add_u64 v[180:181], v[180:181], 0, v[146:147]
	v_lshl_add_u64 v[162:163], s[4:5], 0, v[162:163]
	s_lshl_b64 s[28:29], s[28:29], 5
	global_store_dwordx4 v[180:181], v[158:161], off sc1
	v_lshl_add_u64 v[162:163], v[162:163], 0, v[146:147]
	v_or_b32_e32 v142, s28, v144
	v_cvt_pk_bf16_f32 v158, v54, v55
	v_cvt_pk_bf16_f32 v159, v56, v57
	v_cvt_pk_bf16_f32 v160, v50, v51
	v_cvt_pk_bf16_f32 v161, v52, v53
	global_store_dwordx4 v[162:163], v[158:161], off sc1
	v_mov_b32_e32 v163, s29
	v_or_b32_e32 v162, s19, v142
	s_add_i32 s28, s17, 0xa0
	v_lshlrev_b64 v[180:181], 10, v[162:163]
	v_or_b32_e32 v162, s26, v142
	s_ashr_i32 s28, s28, 5
	v_lshl_add_u64 v[180:181], s[4:5], 0, v[180:181]
	v_lshlrev_b64 v[162:163], 10, v[162:163]
	s_ashr_i32 s29, s28, 31
	v_cvt_pk_bf16_f32 v158, v46, v47
	v_cvt_pk_bf16_f32 v159, v48, v49
	v_cvt_pk_bf16_f32 v160, v42, v43
	v_cvt_pk_bf16_f32 v161, v44, v45
	v_lshl_add_u64 v[180:181], v[180:181], 0, v[148:149]
	v_lshl_add_u64 v[162:163], s[4:5], 0, v[162:163]
	s_lshl_b64 s[28:29], s[28:29], 5
	global_store_dwordx4 v[180:181], v[158:161], off sc1
	v_lshl_add_u64 v[162:163], v[162:163], 0, v[148:149]
	v_or_b32_e32 v142, s28, v144
	v_cvt_pk_bf16_f32 v158, v38, v39
	v_cvt_pk_bf16_f32 v159, v40, v41
	v_cvt_pk_bf16_f32 v160, v34, v35
	v_cvt_pk_bf16_f32 v161, v36, v37
	global_store_dwordx4 v[162:163], v[158:161], off sc1
	v_mov_b32_e32 v163, s29
	v_or_b32_e32 v162, s19, v142
	s_add_i32 s28, s17, 0xb0
	v_lshlrev_b64 v[180:181], 10, v[162:163]
	v_or_b32_e32 v162, s26, v142
	s_ashr_i32 s28, s28, 5
	v_lshl_add_u64 v[180:181], s[4:5], 0, v[180:181]
	v_lshlrev_b64 v[162:163], 10, v[162:163]
	s_ashr_i32 s29, s28, 31
	v_cvt_pk_bf16_f32 v158, v30, v31
	v_cvt_pk_bf16_f32 v159, v32, v33
	v_cvt_pk_bf16_f32 v160, v26, v27
	v_cvt_pk_bf16_f32 v161, v28, v29
	v_lshl_add_u64 v[180:181], v[180:181], 0, v[146:147]
	v_lshl_add_u64 v[162:163], s[4:5], 0, v[162:163]
	s_lshl_b64 s[28:29], s[28:29], 5
	global_store_dwordx4 v[180:181], v[158:161], off sc1
	v_lshl_add_u64 v[162:163], v[162:163], 0, v[146:147]
	v_or_b32_e32 v142, s28, v144
	v_cvt_pk_bf16_f32 v158, v22, v23
	v_cvt_pk_bf16_f32 v159, v24, v25
	v_cvt_pk_bf16_f32 v160, v18, v19
	v_cvt_pk_bf16_f32 v161, v20, v21
	global_store_dwordx4 v[162:163], v[158:161], off sc1
	v_mov_b32_e32 v163, s29
	v_or_b32_e32 v162, s19, v142
	v_lshlrev_b64 v[180:181], 10, v[162:163]
	v_or_b32_e32 v162, s26, v142
	v_lshl_add_u64 v[180:181], s[4:5], 0, v[180:181]
	v_lshlrev_b64 v[162:163], 10, v[162:163]
	v_cvt_pk_bf16_f32 v158, v14, v15
	v_cvt_pk_bf16_f32 v159, v16, v17
	v_cvt_pk_bf16_f32 v160, v10, v11
	v_cvt_pk_bf16_f32 v161, v12, v13
	v_lshl_add_u64 v[180:181], v[180:181], 0, v[148:149]
	v_lshl_add_u64 v[162:163], s[4:5], 0, v[162:163]
	global_store_dwordx4 v[180:181], v[158:161], off sc1
	v_lshl_add_u64 v[162:163], v[162:163], 0, v[148:149]
	s_nop 0
	v_cvt_pk_bf16_f32 v158, v6, v7
	v_cvt_pk_bf16_f32 v159, v8, v9
	v_cvt_pk_bf16_f32 v160, v2, v3
	v_cvt_pk_bf16_f32 v161, v4, v5
	global_store_dwordx4 v[162:163], v[158:161], off sc1
	s_cbranch_execz .LBB0_199

; __device__ __forceinline__ float gelu_fast(float x) { const float u = 0.7978845608028654f * (x + 0.044715f * x * x * x); return x * __builtin_amdgcn_rcpf(1.f + __builtin_amdgcn_exp2f(-2.8853900817779268f * u)); }
; __device__ __forceinline__ u32x4 pack8(const f32x4 a, const f32x4 b) { u32x4 w; w.x = cvt_pk_bf16(a[0], a[1]); w.y = cvt_pk_bf16(a[2], a[3]); w.z = cvt_pk_bf16(b[0], b[1]); w.w = cvt_pk_bf16(b[2], b[3]); return w; }
;     __device__ __forceinline__ void operator()(const f32x4 (&acc)[2][2][4][2], const Unit& u, int wr, int wc, int fr, int fq) const {
;     ...
;         if (u.pn >= 6) {
;             const int col0 = (u.pn - 6) * BM + wc * 32 + 8 * fq;
; #pragma unroll
;             for (int ai = 0; ai < 2; ++ai)
; #pragma unroll
;                 for (int m = 0; m < 4; ++m) { bf16_t* rowp = U + (size_t)(row0 + ai * HALF + m * 16) * 512 + col0;
; #pragma unroll
;                     for (int bj = 0; bj < 2; ++bj) { f32x4 v0 = acc[ai][bj][m][0], v1 = acc[ai][bj][m][1];
; #pragma unroll
;                         for (int j = 0; j < 4; ++j) { v0[j] = gelu_fast(v0[j]); v1[j] = gelu_fast(v1[j]); }
;                         *(u32x4*)(rowp + bj * HALF) = pack8(v0, v1); } }
.LBB0_199:
	v_or_b32_e32 v162, s17, v1
	v_lshl_add_u32 v142, s24, 8, v164
	v_ashrrev_i32_e32 v163, 31, v162
	v_lshlrev_b64 v[160:161], 1, v[142:143]
	v_mul_f32_e32 v142, 0x3d372713, v126
	v_lshlrev_b64 v[158:159], 10, v[162:163]
	v_mul_f32_e32 v142, v126, v142
	v_mul_f32_e32 v163, 0x3d372713, v122
	v_fma_f32 v142, v126, v142, v126
	v_mul_f32_e32 v163, v122, v163
	v_mul_f32_e32 v142, 0x3f4c422a, v142
	v_fma_f32 v163, v122, v163, v122
	v_mul_f32_e32 v142, 0xc038aa3b, v142
	v_mul_f32_e32 v163, 0x3f4c422a, v163
	v_exp_f32_e32 v142, v142
	v_mul_f32_e32 v163, 0xc038aa3b, v163
	v_exp_f32_e32 v163, v163
	v_mul_f32_e32 v181, 0x3d372713, v123
	v_add_f32_e32 v142, 1.0, v142
	v_rcp_f32_e32 v180, v142
	v_add_f32_e32 v142, 1.0, v163
	v_mul_f32_e32 v163, 0x3d372713, v127
	v_mul_f32_e32 v163, v127, v163
	v_fma_f32 v163, v127, v163, v127
	v_mul_f32_e32 v181, v123, v181
	v_mul_f32_e32 v163, 0x3f4c422a, v163
	v_fma_f32 v181, v123, v181, v123
	v_mul_f32_e32 v163, 0xc038aa3b, v163
	v_mul_f32_e32 v181, 0x3f4c422a, v181
	v_exp_f32_e32 v163, v163
	v_mul_f32_e32 v181, 0xc038aa3b, v181
	v_exp_f32_e32 v183, v181
	v_rcp_f32_e32 v182, v142
	v_add_f32_e32 v142, 1.0, v163
	v_mul_f32_e32 v163, 0x3d372713, v128
	v_rcp_f32_e32 v181, v142
	v_add_f32_e32 v142, 1.0, v183
	v_mul_f32_e32 v163, v128, v163
	v_mul_f32_e32 v183, 0x3d372713, v124
	v_fma_f32 v163, v128, v163, v128
	v_mul_f32_e32 v183, v124, v183
	v_mul_f32_e32 v163, 0x3f4c422a, v163
	v_fma_f32 v183, v124, v183, v124
	v_mul_f32_e32 v163, 0xc038aa3b, v163
	v_mul_f32_e32 v183, 0x3f4c422a, v183
	v_exp_f32_e32 v163, v163
	v_mul_f32_e32 v183, 0xc038aa3b, v183
	v_exp_f32_e32 v185, v183
	v_rcp_f32_e32 v183, v142
	v_add_f32_e32 v142, 1.0, v163
	v_mul_f32_e32 v163, 0x3d372713, v129
	v_rcp_f32_e32 v184, v142
	v_add_f32_e32 v142, 1.0, v185
	v_mul_f32_e32 v163, v129, v163
	v_mul_f32_e32 v185, 0x3d372713, v125
	v_fma_f32 v163, v129, v163, v129
	v_mul_f32_e32 v185, v125, v185
	v_mul_f32_e32 v163, 0x3f4c422a, v163
	v_fma_f32 v185, v125, v185, v125
	v_mul_f32_e32 v163, 0xc038aa3b, v163
	v_mul_f32_e32 v185, 0x3f4c422a, v185
	v_exp_f32_e32 v163, v163
	v_mul_f32_e32 v185, 0xc038aa3b, v185
	v_exp_f32_e32 v187, v185
	v_rcp_f32_e32 v186, v142
	v_add_f32_e32 v142, 1.0, v163
	v_rcp_f32_e32 v185, v142
	v_add_f32_e32 v142, 1.0, v187
	v_rcp_f32_e32 v187, v142
	v_lshl_add_u64 v[158:159], s[2:3], 0, v[158:159]
	v_pk_mul_f32 v[126:127], v[126:127], v[180:181]
	v_pk_mul_f32 v[180:181], v[122:123], v[182:183]
	v_pk_mul_f32 v[128:129], v[128:129], v[184:185]
	v_pk_mul_f32 v[182:183], v[124:125], v[186:187]
	v_lshl_add_u64 v[158:159], v[158:159], 0, v[160:161]
	v_cvt_pk_bf16_f32 v122, v126, v127
	v_cvt_pk_bf16_f32 v123, v128, v129
	v_cvt_pk_bf16_f32 v124, v180, v181
	v_cvt_pk_bf16_f32 v125, v182, v183
	global_store_dwordx4 v[158:159], v[122:125], off sc1
	v_mul_f32_e32 v126, 0x3d372713, v118
	v_mul_f32_e32 v126, v118, v126
	v_mul_f32_e32 v124, 0x3d372713, v119
	v_mul_f32_e32 v124, v119, v124
	v_fma_f32 v124, v119, v124, v119
	v_fma_f32 v126, v118, v126, v118
	v_mul_f32_e32 v124, 0x3f4c422a, v124
	v_mul_f32_e32 v126, 0x3f4c422a, v126
	v_mul_f32_e32 v127, 0x3d372713, v114
	v_mul_f32_e32 v124, 0xc038aa3b, v124
	v_mul_f32_e32 v126, 0xc038aa3b, v126
	v_mul_f32_e32 v127, v114, v127
	v_exp_f32_e32 v125, v124
	v_mul_f32_e32 v124, 0x3d372713, v115
	v_exp_f32_e32 v126, v126
	v_fma_f32 v127, v114, v127, v114
	v_mul_f32_e32 v124, v115, v124
	v_mul_f32_e32 v127, 0x3f4c422a, v127
	v_fma_f32 v124, v115, v124, v115
	v_mul_f32_e32 v127, 0xc038aa3b, v127
	v_mul_f32_e32 v124, 0x3f4c422a, v124
	v_exp_f32_e32 v127, v127
	v_mul_f32_e32 v124, 0xc038aa3b, v124
	v_mul_f32_e32 v128, 0x3d372713, v121
	v_add_f32_e32 v122, 1.0, v126
	v_exp_f32_e32 v126, v124
	v_mul_f32_e32 v128, v121, v128
	v_fma_f32 v128, v121, v128, v121
	v_mul_f32_e32 v128, 0x3f4c422a, v128
	v_add_f32_e32 v123, 1.0, v127
	v_mul_f32_e32 v127, 0x3d372713, v116
	v_mul_f32_e32 v128, 0xc038aa3b, v128
	v_rcp_f32_e32 v124, v123
	v_add_f32_e32 v123, 1.0, v125
	v_add_f32_e32 v125, 1.0, v126
	v_mul_f32_e32 v126, 0x3d372713, v120
	v_mul_f32_e32 v127, v116, v127
	v_exp_f32_e32 v129, v128
	v_mul_f32_e32 v128, 0x3d372713, v117
	v_mul_f32_e32 v126, v120, v126
	v_fma_f32 v127, v116, v127, v116
	v_mul_f32_e32 v128, v117, v128
	v_fma_f32 v126, v120, v126, v120
	v_mul_f32_e32 v127, 0x3f4c422a, v127
	v_fma_f32 v128, v117, v128, v117
	v_mul_f32_e32 v126, 0x3f4c422a, v126
	v_mul_f32_e32 v127, 0xc038aa3b, v127
	v_mul_f32_e32 v128, 0x3f4c422a, v128
	v_mul_f32_e32 v126, 0xc038aa3b, v126
	v_exp_f32_e32 v127, v127
	v_mul_f32_e32 v128, 0xc038aa3b, v128
	v_exp_f32_e32 v126, v126
	v_exp_f32_e32 v142, v128
	v_rcp_f32_e32 v122, v122
	v_rcp_f32_e32 v123, v123
	v_rcp_f32_e32 v125, v125
	v_add_f32_e32 v127, 1.0, v127
	v_add_f32_e32 v126, 1.0, v126
	v_rcp_f32_e32 v128, v127
	v_add_f32_e32 v127, 1.0, v129
	v_add_f32_e32 v129, 1.0, v142
	v_rcp_f32_e32 v126, v126
	v_rcp_f32_e32 v127, v127
	v_rcp_f32_e32 v129, v129
	v_pk_mul_f32 v[118:119], v[118:119], v[122:123]
	v_pk_mul_f32 v[122:123], v[114:115], v[124:125]
	v_cvt_pk_bf16_f32 v114, v118, v119
	v_mul_f32_e32 v118, 0x3d372713, v111
	v_mul_f32_e32 v118, v111, v118
	v_pk_mul_f32 v[120:121], v[120:121], v[126:127]
	v_pk_mul_f32 v[124:125], v[116:117], v[128:129]
	v_fma_f32 v118, v111, v118, v111
	v_cvt_pk_bf16_f32 v115, v120, v121
	v_cvt_pk_bf16_f32 v116, v122, v123
	v_cvt_pk_bf16_f32 v117, v124, v125
	v_mul_f32_e32 v118, 0x3f4c422a, v118
	global_store_dwordx4 v[158:159], v[114:117], off offset:256 sc1
	v_mul_f32_e32 v118, 0xc038aa3b, v118
	v_exp_f32_e32 v119, v118
	v_mul_f32_e32 v117, 0x3d372713, v106
	v_mul_f32_e32 v117, v106, v117
	v_mul_f32_e32 v118, 0x3d372713, v107
	v_fma_f32 v117, v106, v117, v106
; __device__ __forceinline__ float gelu_fast(float x) { const float u = 0.7978845608028654f * (x + 0.044715f * x * x * x); return x * __builtin_amdgcn_rcpf(1.f + __builtin_amdgcn_exp2f(-2.8853900817779268f * u)); }
; __device__ __forceinline__ u32x4 pack8(const f32x4 a, const f32x4 b) { u32x4 w; w.x = cvt_pk_bf16(a[0], a[1]); w.y = cvt_pk_bf16(a[2], a[3]); w.z = cvt_pk_bf16(b[0], b[1]); w.w = cvt_pk_bf16(b[2], b[3]); return w; }
;     __device__ __forceinline__ void operator()(const f32x4 (&acc)[2][2][4][2], const Unit& u, int wr, int wc, int fr, int fq) const {
;     ...
;         if (u.pn >= 6) {
;             const int col0 = (u.pn - 6) * BM + wc * 32 + 8 * fq;
; #pragma unroll
;             for (int ai = 0; ai < 2; ++ai)
; #pragma unroll
;                 for (int m = 0; m < 4; ++m) { bf16_t* rowp = U + (size_t)(row0 + ai * HALF + m * 16) * 512 + col0;
; #pragma unroll
;                     for (int bj = 0; bj < 2; ++bj) { f32x4 v0 = acc[ai][bj][m][0], v1 = acc[ai][bj][m][1];
; #pragma unroll
;                         for (int j = 0; j < 4; ++j) { v0[j] = gelu_fast(v0[j]); v1[j] = gelu_fast(v1[j]); }
;                         *(u32x4*)(rowp + bj * HALF) = pack8(v0, v1); } }
	v_mul_f32_e32 v118, v107, v118
	v_mul_f32_e32 v117, 0x3f4c422a, v117
	v_fma_f32 v118, v107, v118, v107
	v_mul_f32_e32 v117, 0xc038aa3b, v117
	v_mul_f32_e32 v118, 0x3f4c422a, v118
	v_exp_f32_e32 v117, v117
	v_mul_f32_e32 v118, 0xc038aa3b, v118
	v_mul_f32_e32 v122, 0x3d372713, v113
	v_exp_f32_e32 v120, v118
	v_mul_f32_e32 v122, v113, v122
	v_fma_f32 v122, v113, v122, v113
	v_mul_f32_e32 v122, 0x3f4c422a, v122
	v_add_f32_e32 v117, 1.0, v117
	v_mul_f32_e32 v121, 0x3d372713, v108
	v_mul_f32_e32 v122, 0xc038aa3b, v122
	v_mul_f32_e32 v116, 0x3d372713, v110
	v_rcp_f32_e32 v118, v117
	v_add_f32_e32 v117, 1.0, v119
	v_add_f32_e32 v119, 1.0, v120
	v_mul_f32_e32 v120, 0x3d372713, v112
	v_mul_f32_e32 v121, v108, v121
	v_exp_f32_e32 v123, v122
	v_mul_f32_e32 v122, 0x3d372713, v109
	v_mul_f32_e32 v116, v110, v116
	v_mul_f32_e32 v120, v112, v120
	v_fma_f32 v121, v108, v121, v108
	v_mul_f32_e32 v122, v109, v122
	v_fma_f32 v116, v110, v116, v110
	v_fma_f32 v120, v112, v120, v112
	v_mul_f32_e32 v121, 0x3f4c422a, v121
	v_fma_f32 v122, v109, v122, v109
	v_mul_f32_e32 v116, 0x3f4c422a, v116
	v_mul_f32_e32 v120, 0x3f4c422a, v120
	v_mul_f32_e32 v121, 0xc038aa3b, v121
	v_mul_f32_e32 v122, 0x3f4c422a, v122
	v_mul_f32_e32 v116, 0xc038aa3b, v116
	v_mul_f32_e32 v120, 0xc038aa3b, v120
	v_exp_f32_e32 v121, v121
	v_mul_f32_e32 v122, 0xc038aa3b, v122
	v_exp_f32_e32 v116, v116
	v_exp_f32_e32 v120, v120
	v_exp_f32_e32 v124, v122
	v_add_f32_e32 v121, 1.0, v121
	v_add_f32_e32 v116, 1.0, v116
	v_add_f32_e32 v120, 1.0, v120
	v_rcp_f32_e32 v122, v121
	v_add_f32_e32 v121, 1.0, v123
	v_add_f32_e32 v123, 1.0, v124
	v_rcp_f32_e32 v116, v116
	v_rcp_f32_e32 v117, v117
	v_rcp_f32_e32 v119, v119
	v_rcp_f32_e32 v120, v120
	v_rcp_f32_e32 v121, v121
	v_rcp_f32_e32 v123, v123
	v_or_b32_e32 v114, 16, v162
	v_ashrrev_i32_e32 v115, 31, v114
	v_lshlrev_b64 v[114:115], 10, v[114:115]
	v_lshl_add_u64 v[114:115], s[2:3], 0, v[114:115]
	v_pk_mul_f32 v[110:111], v[110:111], v[116:117]
	v_pk_mul_f32 v[116:117], v[106:107], v[118:119]
	v_pk_mul_f32 v[112:113], v[112:113], v[120:121]
	v_pk_mul_f32 v[118:119], v[108:109], v[122:123]
	v_lshl_add_u64 v[114:115], v[114:115], 0, v[160:161]
	v_cvt_pk_bf16_f32 v106, v110, v111
	v_cvt_pk_bf16_f32 v107, v112, v113
	v_cvt_pk_bf16_f32 v108, v116, v117
	v_cvt_pk_bf16_f32 v109, v118, v119
	global_store_dwordx4 v[114:115], v[106:109], off sc1
	v_mul_f32_e32 v110, 0x3d372713, v102
	v_mul_f32_e32 v110, v102, v110
	v_mul_f32_e32 v108, 0x3d372713, v103
	v_mul_f32_e32 v108, v103, v108
	v_fma_f32 v108, v103, v108, v103
	v_fma_f32 v110, v102, v110, v102
	v_mul_f32_e32 v108, 0x3f4c422a, v108
	v_mul_f32_e32 v110, 0x3f4c422a, v110
	v_mul_f32_e32 v111, 0x3d372713, v98
	v_mul_f32_e32 v108, 0xc038aa3b, v108
	v_mul_f32_e32 v110, 0xc038aa3b, v110
	v_mul_f32_e32 v111, v98, v111
	v_exp_f32_e32 v109, v108
	v_mul_f32_e32 v108, 0x3d372713, v99
	v_exp_f32_e32 v110, v110
	v_fma_f32 v111, v98, v111, v98
	v_mul_f32_e32 v108, v99, v108
	v_mul_f32_e32 v111, 0x3f4c422a, v111
	v_fma_f32 v108, v99, v108, v99
	v_mul_f32_e32 v111, 0xc038aa3b, v111
	v_mul_f32_e32 v108, 0x3f4c422a, v108
	v_exp_f32_e32 v111, v111
	v_mul_f32_e32 v108, 0xc038aa3b, v108
	v_mul_f32_e32 v112, 0x3d372713, v105
	v_add_f32_e32 v106, 1.0, v110
	v_exp_f32_e32 v110, v108
	v_mul_f32_e32 v112, v105, v112
	v_fma_f32 v112, v105, v112, v105
	v_mul_f32_e32 v112, 0x3f4c422a, v112
	v_add_f32_e32 v107, 1.0, v111
	v_mul_f32_e32 v111, 0x3d372713, v100
	v_mul_f32_e32 v112, 0xc038aa3b, v112
	v_rcp_f32_e32 v108, v107
	v_add_f32_e32 v107, 1.0, v109
	v_add_f32_e32 v109, 1.0, v110
	v_mul_f32_e32 v110, 0x3d372713, v104
	v_mul_f32_e32 v111, v100, v111
	v_exp_f32_e32 v113, v112
	v_mul_f32_e32 v112, 0x3d372713, v101
	v_mul_f32_e32 v110, v104, v110
	v_fma_f32 v111, v100, v111, v100
	v_mul_f32_e32 v112, v101, v112
	v_fma_f32 v110, v104, v110, v104
	v_mul_f32_e32 v111, 0x3f4c422a, v111
	v_fma_f32 v112, v101, v112, v101
	v_mul_f32_e32 v110, 0x3f4c422a, v110
	v_mul_f32_e32 v111, 0xc038aa3b, v111
	v_mul_f32_e32 v112, 0x3f4c422a, v112
	v_mul_f32_e32 v110, 0xc038aa3b, v110
	v_exp_f32_e32 v111, v111
	v_mul_f32_e32 v112, 0xc038aa3b, v112
	v_exp_f32_e32 v110, v110
	v_exp_f32_e32 v116, v112
	v_rcp_f32_e32 v106, v106
	v_rcp_f32_e32 v107, v107
	v_rcp_f32_e32 v109, v109
	v_add_f32_e32 v111, 1.0, v111
	v_add_f32_e32 v110, 1.0, v110
	v_rcp_f32_e32 v112, v111
	v_add_f32_e32 v111, 1.0, v113
	v_add_f32_e32 v113, 1.0, v116
	v_rcp_f32_e32 v110, v110
	v_rcp_f32_e32 v111, v111
	v_rcp_f32_e32 v113, v113
	v_pk_mul_f32 v[102:103], v[102:103], v[106:107]
	v_pk_mul_f32 v[106:107], v[98:99], v[108:109]
	v_cvt_pk_bf16_f32 v98, v102, v103
	v_mul_f32_e32 v102, 0x3d372713, v95
	v_mul_f32_e32 v102, v95, v102
	v_pk_mul_f32 v[104:105], v[104:105], v[110:111]
	v_pk_mul_f32 v[108:109], v[100:101], v[112:113]
	v_fma_f32 v102, v95, v102, v95
	v_cvt_pk_bf16_f32 v99, v104, v105
	v_cvt_pk_bf16_f32 v100, v106, v107
	v_cvt_pk_bf16_f32 v101, v108, v109
	v_mul_f32_e32 v102, 0x3f4c422a, v102
	global_store_dwordx4 v[114:115], v[98:101], off offset:256 sc1
	v_mul_f32_e32 v102, 0xc038aa3b, v102
	v_exp_f32_e32 v103, v102
	v_mul_f32_e32 v101, 0x3d372713, v90
	v_mul_f32_e32 v101, v90, v101
	v_mul_f32_e32 v102, 0x3d372713, v91
	v_fma_f32 v101, v90, v101, v90
	v_mul_f32_e32 v102, v91, v102
	v_mul_f32_e32 v101, 0x3f4c422a, v101
	v_fma_f32 v102, v91, v102, v91
	v_mul_f32_e32 v101, 0xc038aa3b, v101
	v_mul_f32_e32 v102, 0x3f4c422a, v102
	v_exp_f32_e32 v101, v101
	v_mul_f32_e32 v102, 0xc038aa3b, v102
	v_mul_f32_e32 v106, 0x3d372713, v97
	v_exp_f32_e32 v104, v102
	v_mul_f32_e32 v106, v97, v106
	v_fma_f32 v106, v97, v106, v97
	v_mul_f32_e32 v106, 0x3f4c422a, v106
	v_add_f32_e32 v101, 1.0, v101
; __device__ __forceinline__ float gelu_fast(float x) { const float u = 0.7978845608028654f * (x + 0.044715f * x * x * x); return x * __builtin_amdgcn_rcpf(1.f + __builtin_amdgcn_exp2f(-2.8853900817779268f * u)); }
; __device__ __forceinline__ u32x4 pack8(const f32x4 a, const f32x4 b) { u32x4 w; w.x = cvt_pk_bf16(a[0], a[1]); w.y = cvt_pk_bf16(a[2], a[3]); w.z = cvt_pk_bf16(b[0], b[1]); w.w = cvt_pk_bf16(b[2], b[3]); return w; }
;     __device__ __forceinline__ void operator()(const f32x4 (&acc)[2][2][4][2], const Unit& u, int wr, int wc, int fr, int fq) const {
;     ...
;         if (u.pn >= 6) {
;             const int col0 = (u.pn - 6) * BM + wc * 32 + 8 * fq;
; #pragma unroll
;             for (int ai = 0; ai < 2; ++ai)
; #pragma unroll
;                 for (int m = 0; m < 4; ++m) { bf16_t* rowp = U + (size_t)(row0 + ai * HALF + m * 16) * 512 + col0;
; #pragma unroll
;                     for (int bj = 0; bj < 2; ++bj) { f32x4 v0 = acc[ai][bj][m][0], v1 = acc[ai][bj][m][1];
; #pragma unroll
;                         for (int j = 0; j < 4; ++j) { v0[j] = gelu_fast(v0[j]); v1[j] = gelu_fast(v1[j]); }
;                         *(u32x4*)(rowp + bj * HALF) = pack8(v0, v1); } }
	v_mul_f32_e32 v105, 0x3d372713, v92
	v_mul_f32_e32 v106, 0xc038aa3b, v106
	v_mul_f32_e32 v100, 0x3d372713, v94
	v_rcp_f32_e32 v102, v101
	v_add_f32_e32 v101, 1.0, v103
	v_add_f32_e32 v103, 1.0, v104
	v_mul_f32_e32 v104, 0x3d372713, v96
	v_mul_f32_e32 v105, v92, v105
	v_exp_f32_e32 v107, v106
	v_mul_f32_e32 v106, 0x3d372713, v93
	v_mul_f32_e32 v100, v94, v100
	v_mul_f32_e32 v104, v96, v104
	v_fma_f32 v105, v92, v105, v92
	v_mul_f32_e32 v106, v93, v106
	v_fma_f32 v100, v94, v100, v94
	v_fma_f32 v104, v96, v104, v96
	v_mul_f32_e32 v105, 0x3f4c422a, v105
	v_fma_f32 v106, v93, v106, v93
	v_mul_f32_e32 v100, 0x3f4c422a, v100
	v_mul_f32_e32 v104, 0x3f4c422a, v104
	v_mul_f32_e32 v105, 0xc038aa3b, v105
	v_mul_f32_e32 v106, 0x3f4c422a, v106
	v_mul_f32_e32 v100, 0xc038aa3b, v100
	v_mul_f32_e32 v104, 0xc038aa3b, v104
	v_exp_f32_e32 v105, v105
	v_mul_f32_e32 v106, 0xc038aa3b, v106
	v_exp_f32_e32 v100, v100
	v_exp_f32_e32 v104, v104
	v_exp_f32_e32 v108, v106
	v_add_f32_e32 v105, 1.0, v105
	v_add_f32_e32 v100, 1.0, v100
	v_add_f32_e32 v104, 1.0, v104
	v_rcp_f32_e32 v106, v105
	v_add_f32_e32 v105, 1.0, v107
	v_add_f32_e32 v107, 1.0, v108
	v_rcp_f32_e32 v100, v100
	v_rcp_f32_e32 v101, v101
	v_rcp_f32_e32 v103, v103
	v_rcp_f32_e32 v104, v104
	v_rcp_f32_e32 v105, v105
	v_rcp_f32_e32 v107, v107
	v_or_b32_e32 v98, 32, v162
	v_ashrrev_i32_e32 v99, 31, v98
	v_lshlrev_b64 v[98:99], 10, v[98:99]
	v_lshl_add_u64 v[98:99], s[2:3], 0, v[98:99]
	v_pk_mul_f32 v[94:95], v[94:95], v[100:101]
	v_pk_mul_f32 v[100:101], v[90:91], v[102:103]
	v_pk_mul_f32 v[96:97], v[96:97], v[104:105]
	v_pk_mul_f32 v[102:103], v[92:93], v[106:107]
	v_lshl_add_u64 v[98:99], v[98:99], 0, v[160:161]
	v_cvt_pk_bf16_f32 v90, v94, v95
	v_cvt_pk_bf16_f32 v91, v96, v97
	v_cvt_pk_bf16_f32 v92, v100, v101
	v_cvt_pk_bf16_f32 v93, v102, v103
	global_store_dwordx4 v[98:99], v[90:93], off sc1
	v_mul_f32_e32 v94, 0x3d372713, v86
	v_mul_f32_e32 v94, v86, v94
	v_mul_f32_e32 v92, 0x3d372713, v87
	v_mul_f32_e32 v92, v87, v92
	v_fma_f32 v92, v87, v92, v87
	v_fma_f32 v94, v86, v94, v86
	v_mul_f32_e32 v92, 0x3f4c422a, v92
	v_mul_f32_e32 v94, 0x3f4c422a, v94
	v_mul_f32_e32 v95, 0x3d372713, v82
	v_mul_f32_e32 v92, 0xc038aa3b, v92
	v_mul_f32_e32 v94, 0xc038aa3b, v94
	v_mul_f32_e32 v95, v82, v95
	v_exp_f32_e32 v93, v92
	v_mul_f32_e32 v92, 0x3d372713, v83
	v_exp_f32_e32 v94, v94
	v_fma_f32 v95, v82, v95, v82
	v_mul_f32_e32 v92, v83, v92
	v_mul_f32_e32 v95, 0x3f4c422a, v95
	v_fma_f32 v92, v83, v92, v83
	v_mul_f32_e32 v95, 0xc038aa3b, v95
	v_mul_f32_e32 v92, 0x3f4c422a, v92
	v_exp_f32_e32 v95, v95
	v_mul_f32_e32 v92, 0xc038aa3b, v92
	v_mul_f32_e32 v96, 0x3d372713, v89
	v_add_f32_e32 v90, 1.0, v94
	v_exp_f32_e32 v94, v92
	v_mul_f32_e32 v96, v89, v96
	v_fma_f32 v96, v89, v96, v89
	v_mul_f32_e32 v96, 0x3f4c422a, v96
	v_add_f32_e32 v91, 1.0, v95
	v_mul_f32_e32 v95, 0x3d372713, v84
	v_mul_f32_e32 v96, 0xc038aa3b, v96
	v_rcp_f32_e32 v92, v91
	v_add_f32_e32 v91, 1.0, v93
	v_add_f32_e32 v93, 1.0, v94
	v_mul_f32_e32 v94, 0x3d372713, v88
	v_mul_f32_e32 v95, v84, v95
	v_exp_f32_e32 v97, v96
	v_mul_f32_e32 v96, 0x3d372713, v85
	v_mul_f32_e32 v94, v88, v94
	v_fma_f32 v95, v84, v95, v84
	v_mul_f32_e32 v96, v85, v96
	v_fma_f32 v94, v88, v94, v88
	v_mul_f32_e32 v95, 0x3f4c422a, v95
	v_fma_f32 v96, v85, v96, v85
	v_mul_f32_e32 v94, 0x3f4c422a, v94
	v_mul_f32_e32 v95, 0xc038aa3b, v95
	v_mul_f32_e32 v96, 0x3f4c422a, v96
	v_mul_f32_e32 v94, 0xc038aa3b, v94
	v_exp_f32_e32 v95, v95
	v_mul_f32_e32 v96, 0xc038aa3b, v96
	v_exp_f32_e32 v94, v94
	v_exp_f32_e32 v100, v96
	v_rcp_f32_e32 v90, v90
	v_rcp_f32_e32 v91, v91
	v_rcp_f32_e32 v93, v93
	v_add_f32_e32 v95, 1.0, v95
	v_add_f32_e32 v94, 1.0, v94
	v_rcp_f32_e32 v96, v95
	v_add_f32_e32 v95, 1.0, v97
	v_add_f32_e32 v97, 1.0, v100
	v_rcp_f32_e32 v94, v94
	v_rcp_f32_e32 v95, v95
	v_rcp_f32_e32 v97, v97
	v_pk_mul_f32 v[86:87], v[86:87], v[90:91]
	v_pk_mul_f32 v[90:91], v[82:83], v[92:93]
	v_cvt_pk_bf16_f32 v82, v86, v87
	v_mul_f32_e32 v86, 0x3d372713, v79
	v_mul_f32_e32 v86, v79, v86
	v_pk_mul_f32 v[88:89], v[88:89], v[94:95]
	v_pk_mul_f32 v[92:93], v[84:85], v[96:97]
	v_fma_f32 v86, v79, v86, v79
	v_cvt_pk_bf16_f32 v83, v88, v89
	v_cvt_pk_bf16_f32 v84, v90, v91
	v_cvt_pk_bf16_f32 v85, v92, v93
	v_mul_f32_e32 v86, 0x3f4c422a, v86
	global_store_dwordx4 v[98:99], v[82:85], off offset:256 sc1
	v_mul_f32_e32 v86, 0xc038aa3b, v86
	v_exp_f32_e32 v87, v86
	v_mul_f32_e32 v85, 0x3d372713, v74
	v_mul_f32_e32 v85, v74, v85
	v_mul_f32_e32 v86, 0x3d372713, v75
	v_fma_f32 v85, v74, v85, v74
	v_mul_f32_e32 v86, v75, v86
	v_mul_f32_e32 v85, 0x3f4c422a, v85
	v_fma_f32 v86, v75, v86, v75
	v_mul_f32_e32 v85, 0xc038aa3b, v85
	v_mul_f32_e32 v86, 0x3f4c422a, v86
	v_exp_f32_e32 v85, v85
	v_mul_f32_e32 v86, 0xc038aa3b, v86
	v_mul_f32_e32 v90, 0x3d372713, v81
	v_exp_f32_e32 v88, v86
	v_mul_f32_e32 v90, v81, v90
	v_fma_f32 v90, v81, v90, v81
	v_mul_f32_e32 v90, 0x3f4c422a, v90
	v_add_f32_e32 v85, 1.0, v85
	v_mul_f32_e32 v89, 0x3d372713, v76
	v_mul_f32_e32 v90, 0xc038aa3b, v90
	v_mul_f32_e32 v84, 0x3d372713, v78
	v_rcp_f32_e32 v86, v85
	v_add_f32_e32 v85, 1.0, v87
	v_add_f32_e32 v87, 1.0, v88
	v_mul_f32_e32 v88, 0x3d372713, v80
	v_mul_f32_e32 v89, v76, v89
	v_exp_f32_e32 v91, v90
	v_mul_f32_e32 v90, 0x3d372713, v77
	v_mul_f32_e32 v84, v78, v84
	v_mul_f32_e32 v88, v80, v88
	v_fma_f32 v89, v76, v89, v76
	v_mul_f32_e32 v90, v77, v90
	v_fma_f32 v84, v78, v84, v78
	v_fma_f32 v88, v80, v88, v80
	v_mul_f32_e32 v89, 0x3f4c422a, v89
	v_fma_f32 v90, v77, v90, v77
	v_mul_f32_e32 v84, 0x3f4c422a, v84
	v_mul_f32_e32 v88, 0x3f4c422a, v88
	v_mul_f32_e32 v89, 0xc038aa3b, v89
	v_mul_f32_e32 v90, 0x3f4c422a, v90
	v_mul_f32_e32 v84, 0xc038aa3b, v84
; __device__ __forceinline__ float gelu_fast(float x) { const float u = 0.7978845608028654f * (x + 0.044715f * x * x * x); return x * __builtin_amdgcn_rcpf(1.f + __builtin_amdgcn_exp2f(-2.8853900817779268f * u)); }
; __device__ __forceinline__ u32x4 pack8(const f32x4 a, const f32x4 b) { u32x4 w; w.x = cvt_pk_bf16(a[0], a[1]); w.y = cvt_pk_bf16(a[2], a[3]); w.z = cvt_pk_bf16(b[0], b[1]); w.w = cvt_pk_bf16(b[2], b[3]); return w; }
;     __device__ __forceinline__ void operator()(const f32x4 (&acc)[2][2][4][2], const Unit& u, int wr, int wc, int fr, int fq) const {
;     ...
;         if (u.pn >= 6) {
;             const int col0 = (u.pn - 6) * BM + wc * 32 + 8 * fq;
; #pragma unroll
;             for (int ai = 0; ai < 2; ++ai)
; #pragma unroll
;                 for (int m = 0; m < 4; ++m) { bf16_t* rowp = U + (size_t)(row0 + ai * HALF + m * 16) * 512 + col0;
; #pragma unroll
;                     for (int bj = 0; bj < 2; ++bj) { f32x4 v0 = acc[ai][bj][m][0], v1 = acc[ai][bj][m][1];
; #pragma unroll
;                         for (int j = 0; j < 4; ++j) { v0[j] = gelu_fast(v0[j]); v1[j] = gelu_fast(v1[j]); }
;                         *(u32x4*)(rowp + bj * HALF) = pack8(v0, v1); } }
	v_mul_f32_e32 v88, 0xc038aa3b, v88
	v_exp_f32_e32 v89, v89
	v_mul_f32_e32 v90, 0xc038aa3b, v90
	v_exp_f32_e32 v84, v84
	v_exp_f32_e32 v88, v88
	v_exp_f32_e32 v92, v90
	v_add_f32_e32 v89, 1.0, v89
	v_add_f32_e32 v84, 1.0, v84
	v_add_f32_e32 v88, 1.0, v88
	v_rcp_f32_e32 v90, v89
	v_add_f32_e32 v89, 1.0, v91
	v_add_f32_e32 v91, 1.0, v92
	v_rcp_f32_e32 v84, v84
	v_rcp_f32_e32 v85, v85
	v_rcp_f32_e32 v87, v87
	v_rcp_f32_e32 v88, v88
	v_rcp_f32_e32 v89, v89
	v_rcp_f32_e32 v91, v91
	v_or_b32_e32 v82, 48, v162
	v_ashrrev_i32_e32 v83, 31, v82
	v_lshlrev_b64 v[82:83], 10, v[82:83]
	v_lshl_add_u64 v[82:83], s[2:3], 0, v[82:83]
	v_pk_mul_f32 v[78:79], v[78:79], v[84:85]
	v_pk_mul_f32 v[84:85], v[74:75], v[86:87]
	v_pk_mul_f32 v[80:81], v[80:81], v[88:89]
	v_pk_mul_f32 v[86:87], v[76:77], v[90:91]
	v_lshl_add_u64 v[82:83], v[82:83], 0, v[160:161]
	v_cvt_pk_bf16_f32 v74, v78, v79
	v_cvt_pk_bf16_f32 v75, v80, v81
	v_cvt_pk_bf16_f32 v76, v84, v85
	v_cvt_pk_bf16_f32 v77, v86, v87
	global_store_dwordx4 v[82:83], v[74:77], off sc1
	v_mul_f32_e32 v78, 0x3d372713, v70
	v_mul_f32_e32 v78, v70, v78
	v_mul_f32_e32 v76, 0x3d372713, v71
	v_mul_f32_e32 v76, v71, v76
	v_fma_f32 v76, v71, v76, v71
	v_fma_f32 v78, v70, v78, v70
	v_mul_f32_e32 v76, 0x3f4c422a, v76
	v_mul_f32_e32 v78, 0x3f4c422a, v78
	v_mul_f32_e32 v79, 0x3d372713, v66
	v_mul_f32_e32 v76, 0xc038aa3b, v76
	v_mul_f32_e32 v78, 0xc038aa3b, v78
	v_mul_f32_e32 v79, v66, v79
	v_exp_f32_e32 v77, v76
	v_mul_f32_e32 v76, 0x3d372713, v67
	v_exp_f32_e32 v78, v78
	v_fma_f32 v79, v66, v79, v66
	v_mul_f32_e32 v76, v67, v76
	v_mul_f32_e32 v79, 0x3f4c422a, v79
	v_fma_f32 v76, v67, v76, v67
	v_mul_f32_e32 v79, 0xc038aa3b, v79
	v_mul_f32_e32 v76, 0x3f4c422a, v76
	v_exp_f32_e32 v79, v79
	v_mul_f32_e32 v76, 0xc038aa3b, v76
	v_mul_f32_e32 v80, 0x3d372713, v73
	v_add_f32_e32 v74, 1.0, v78
	v_exp_f32_e32 v78, v76
	v_mul_f32_e32 v80, v73, v80
	v_fma_f32 v80, v73, v80, v73
	v_mul_f32_e32 v80, 0x3f4c422a, v80
	v_add_f32_e32 v75, 1.0, v79
	v_mul_f32_e32 v79, 0x3d372713, v68
	v_mul_f32_e32 v80, 0xc038aa3b, v80
	v_rcp_f32_e32 v76, v75
	v_add_f32_e32 v75, 1.0, v77
	v_add_f32_e32 v77, 1.0, v78
	v_mul_f32_e32 v78, 0x3d372713, v72
	v_mul_f32_e32 v79, v68, v79
	v_exp_f32_e32 v81, v80
	v_mul_f32_e32 v80, 0x3d372713, v69
	v_mul_f32_e32 v78, v72, v78
	v_fma_f32 v79, v68, v79, v68
	v_mul_f32_e32 v80, v69, v80
	v_fma_f32 v78, v72, v78, v72
	v_mul_f32_e32 v79, 0x3f4c422a, v79
	v_fma_f32 v80, v69, v80, v69
	v_mul_f32_e32 v78, 0x3f4c422a, v78
	v_mul_f32_e32 v79, 0xc038aa3b, v79
	v_mul_f32_e32 v80, 0x3f4c422a, v80
	v_mul_f32_e32 v78, 0xc038aa3b, v78
	v_exp_f32_e32 v79, v79
	v_mul_f32_e32 v80, 0xc038aa3b, v80
	v_exp_f32_e32 v78, v78
	v_exp_f32_e32 v84, v80
	v_add_f32_e32 v79, 1.0, v79
	v_rcp_f32_e32 v80, v79
	v_add_f32_e32 v78, 1.0, v78
	v_add_f32_e32 v79, 1.0, v81
	v_add_f32_e32 v81, 1.0, v84
	v_rcp_f32_e32 v74, v74
	v_rcp_f32_e32 v75, v75
	v_rcp_f32_e32 v77, v77
	v_rcp_f32_e32 v78, v78
	v_rcp_f32_e32 v79, v79
	v_rcp_f32_e32 v81, v81
	v_pk_mul_f32 v[70:71], v[70:71], v[74:75]
	v_pk_mul_f32 v[74:75], v[66:67], v[76:77]
	v_pk_mul_f32 v[72:73], v[72:73], v[78:79]
	v_pk_mul_f32 v[76:77], v[68:69], v[80:81]
	v_cvt_pk_bf16_f32 v66, v70, v71
	v_cvt_pk_bf16_f32 v67, v72, v73
	v_cvt_pk_bf16_f32 v68, v74, v75
	v_cvt_pk_bf16_f32 v69, v76, v77
	global_store_dwordx4 v[82:83], v[66:69], off offset:256 sc1
	v_mul_f32_e32 v70, 0x3d372713, v63
	v_mul_f32_e32 v70, v63, v70
	v_mul_f32_e32 v66, 0x3d372713, v62
	v_mul_f32_e32 v66, v62, v66
	v_fma_f32 v66, v62, v66, v62
	v_mul_f32_e32 v66, 0x3f4c422a, v66
	v_fma_f32 v70, v63, v70, v63
	v_mul_f32_e32 v66, 0xc038aa3b, v66
	v_mul_f32_e32 v70, 0x3f4c422a, v70
	v_exp_f32_e32 v68, v66
	v_mul_f32_e32 v66, 0x3d372713, v58
	v_mul_f32_e32 v70, 0xc038aa3b, v70
	v_mul_f32_e32 v66, v58, v66
	v_exp_f32_e32 v71, v70
	v_mul_f32_e32 v70, 0x3d372713, v59
	v_fma_f32 v66, v58, v66, v58
	v_mul_f32_e32 v70, v59, v70
	v_mul_f32_e32 v66, 0x3f4c422a, v66
	v_fma_f32 v70, v59, v70, v59
	v_mul_f32_e32 v66, 0xc038aa3b, v66
	v_mul_f32_e32 v70, 0x3f4c422a, v70
	v_exp_f32_e32 v69, v66
	v_mul_f32_e32 v70, 0xc038aa3b, v70
	v_mul_f32_e32 v74, 0x3d372713, v65
	v_exp_f32_e32 v72, v70
	v_mul_f32_e32 v74, v65, v74
	v_fma_f32 v74, v65, v74, v65
	v_mul_f32_e32 v74, 0x3f4c422a, v74
	v_add_f32_e32 v69, 1.0, v69
	v_mul_f32_e32 v73, 0x3d372713, v60
	v_mul_f32_e32 v74, 0xc038aa3b, v74
	v_rcp_f32_e32 v70, v69
	v_add_f32_e32 v69, 1.0, v71
	v_add_f32_e32 v71, 1.0, v72
	v_mul_f32_e32 v72, 0x3d372713, v64
	v_mul_f32_e32 v73, v60, v73
	v_exp_f32_e32 v75, v74
	v_mul_f32_e32 v74, 0x3d372713, v61
	v_mul_f32_e32 v72, v64, v72
	v_fma_f32 v73, v60, v73, v60
	v_mul_f32_e32 v74, v61, v74
	v_fma_f32 v72, v64, v72, v64
	v_mul_f32_e32 v73, 0x3f4c422a, v73
	v_fma_f32 v74, v61, v74, v61
	v_mul_f32_e32 v72, 0x3f4c422a, v72
	v_mul_f32_e32 v73, 0xc038aa3b, v73
	v_mul_f32_e32 v74, 0x3f4c422a, v74
	v_mul_f32_e32 v72, 0xc038aa3b, v72
	v_exp_f32_e32 v73, v73
	v_mul_f32_e32 v74, 0xc038aa3b, v74
	v_exp_f32_e32 v72, v72
	v_exp_f32_e32 v76, v74
	v_add_f32_e32 v68, 1.0, v68
	v_add_f32_e32 v73, 1.0, v73
	v_rcp_f32_e32 v68, v68
	v_rcp_f32_e32 v69, v69
	v_add_f32_e32 v72, 1.0, v72
	v_rcp_f32_e32 v74, v73
	v_add_f32_e32 v73, 1.0, v75
	v_add_f32_e32 v75, 1.0, v76
	v_rcp_f32_e32 v71, v71
	v_rcp_f32_e32 v72, v72
	v_rcp_f32_e32 v73, v73
	v_rcp_f32_e32 v75, v75
	s_mov_b64 s[4:5], 0x20000
	v_lshl_add_u64 v[66:67], v[158:159], 0, s[4:5]
	v_pk_mul_f32 v[62:63], v[62:63], v[68:69]
	s_mov_b32 s4, 0x20000
	v_pk_mul_f32 v[68:69], v[58:59], v[70:71]
	v_pk_mul_f32 v[64:65], v[64:65], v[72:73]
	v_pk_mul_f32 v[70:71], v[60:61], v[74:75]
	v_cvt_pk_bf16_f32 v58, v62, v63
	v_add_co_u32_e32 v62, vcc, s4, v158
; __device__ __forceinline__ float gelu_fast(float x) { const float u = 0.7978845608028654f * (x + 0.044715f * x * x * x); return x * __builtin_amdgcn_rcpf(1.f + __builtin_amdgcn_exp2f(-2.8853900817779268f * u)); }
; __device__ __forceinline__ u32x4 pack8(const f32x4 a, const f32x4 b) { u32x4 w; w.x = cvt_pk_bf16(a[0], a[1]); w.y = cvt_pk_bf16(a[2], a[3]); w.z = cvt_pk_bf16(b[0], b[1]); w.w = cvt_pk_bf16(b[2], b[3]); return w; }
;     __device__ __forceinline__ void operator()(const f32x4 (&acc)[2][2][4][2], const Unit& u, int wr, int wc, int fr, int fq) const {
;     ...
;         if (u.pn >= 6) {
;             const int col0 = (u.pn - 6) * BM + wc * 32 + 8 * fq;
; #pragma unroll
;             for (int ai = 0; ai < 2; ++ai)
; #pragma unroll
;                 for (int m = 0; m < 4; ++m) { bf16_t* rowp = U + (size_t)(row0 + ai * HALF + m * 16) * 512 + col0;
; #pragma unroll
;                     for (int bj = 0; bj < 2; ++bj) { f32x4 v0 = acc[ai][bj][m][0], v1 = acc[ai][bj][m][1];
; #pragma unroll
;                         for (int j = 0; j < 4; ++j) { v0[j] = gelu_fast(v0[j]); v1[j] = gelu_fast(v1[j]); }
;                         *(u32x4*)(rowp + bj * HALF) = pack8(v0, v1); } }
	v_cvt_pk_bf16_f32 v59, v64, v65
	v_cvt_pk_bf16_f32 v60, v68, v69
	v_cvt_pk_bf16_f32 v61, v70, v71
	v_addc_co_u32_e32 v63, vcc, 0, v159, vcc
	v_mul_f32_e32 v64, 0x3d372713, v54
	global_store_dwordx4 v[62:63], v[58:61], off sc1
	v_mul_f32_e32 v64, v54, v64
	v_fma_f32 v64, v54, v64, v54
	v_mul_f32_e32 v60, 0x3d372713, v55
	v_mul_f32_e32 v60, v55, v60
	v_fma_f32 v60, v55, v60, v55
	v_mul_f32_e32 v64, 0x3f4c422a, v64
	v_mul_f32_e32 v60, 0x3f4c422a, v60
	v_mul_f32_e32 v64, 0xc038aa3b, v64
	v_mul_f32_e32 v65, 0x3d372713, v50
	v_mul_f32_e32 v60, 0xc038aa3b, v60
	v_exp_f32_e32 v64, v64
	v_mul_f32_e32 v65, v50, v65
	v_exp_f32_e32 v61, v60
	v_mul_f32_e32 v60, 0x3d372713, v51
	v_fma_f32 v65, v50, v65, v50
	v_mul_f32_e32 v60, v51, v60
	v_mul_f32_e32 v65, 0x3f4c422a, v65
	v_fma_f32 v60, v51, v60, v51
	v_mul_f32_e32 v65, 0xc038aa3b, v65
	v_mul_f32_e32 v60, 0x3f4c422a, v60
	v_exp_f32_e32 v65, v65
	v_add_f32_e32 v58, 1.0, v64
	v_mul_f32_e32 v60, 0xc038aa3b, v60
	v_mul_f32_e32 v64, 0x3d372713, v57
	v_exp_f32_e32 v62, v60
	v_mul_f32_e32 v64, v57, v64
	v_fma_f32 v64, v57, v64, v57
	v_mul_f32_e32 v64, 0x3f4c422a, v64
	v_add_f32_e32 v59, 1.0, v65
	v_mul_f32_e32 v63, 0x3d372713, v52
	v_mul_f32_e32 v64, 0xc038aa3b, v64
	v_rcp_f32_e32 v60, v59
	v_add_f32_e32 v59, 1.0, v61
	v_add_f32_e32 v61, 1.0, v62
	v_mul_f32_e32 v62, 0x3d372713, v56
	v_mul_f32_e32 v63, v52, v63
	v_exp_f32_e32 v65, v64
	v_mul_f32_e32 v64, 0x3d372713, v53
	v_mul_f32_e32 v62, v56, v62
	v_fma_f32 v63, v52, v63, v52
	v_mul_f32_e32 v64, v53, v64
	v_fma_f32 v62, v56, v62, v56
	v_mul_f32_e32 v63, 0x3f4c422a, v63
	v_fma_f32 v64, v53, v64, v53
	v_mul_f32_e32 v62, 0x3f4c422a, v62
	v_mul_f32_e32 v63, 0xc038aa3b, v63
	v_mul_f32_e32 v64, 0x3f4c422a, v64
	v_mul_f32_e32 v62, 0xc038aa3b, v62
	v_exp_f32_e32 v63, v63
	v_mul_f32_e32 v64, 0xc038aa3b, v64
	v_exp_f32_e32 v62, v62
	v_exp_f32_e32 v68, v64
	v_add_f32_e32 v63, 1.0, v63
	v_rcp_f32_e32 v64, v63
	v_add_f32_e32 v62, 1.0, v62
	v_add_f32_e32 v63, 1.0, v65
	v_add_f32_e32 v65, 1.0, v68
	v_rcp_f32_e32 v58, v58
	v_rcp_f32_e32 v59, v59
	v_rcp_f32_e32 v61, v61
	v_rcp_f32_e32 v62, v62
	v_rcp_f32_e32 v63, v63
	v_rcp_f32_e32 v65, v65
	v_pk_mul_f32 v[54:55], v[54:55], v[58:59]
	v_pk_mul_f32 v[58:59], v[50:51], v[60:61]
	v_pk_mul_f32 v[56:57], v[56:57], v[62:63]
	v_pk_mul_f32 v[60:61], v[52:53], v[64:65]
	v_cvt_pk_bf16_f32 v50, v54, v55
	v_cvt_pk_bf16_f32 v51, v56, v57
	v_cvt_pk_bf16_f32 v52, v58, v59
	v_cvt_pk_bf16_f32 v53, v60, v61
	global_store_dwordx4 v[66:67], v[50:53], off offset:256 sc1
	v_mul_f32_e32 v54, 0x3d372713, v47
	v_mul_f32_e32 v54, v47, v54
	v_mul_f32_e32 v50, 0x3d372713, v46
	v_mul_f32_e32 v50, v46, v50
	v_fma_f32 v50, v46, v50, v46
	v_mul_f32_e32 v50, 0x3f4c422a, v50
	v_fma_f32 v54, v47, v54, v47
	v_mul_f32_e32 v50, 0xc038aa3b, v50
	v_mul_f32_e32 v54, 0x3f4c422a, v54
	v_exp_f32_e32 v52, v50
	v_mul_f32_e32 v50, 0x3d372713, v42
	v_mul_f32_e32 v54, 0xc038aa3b, v54
	v_mul_f32_e32 v50, v42, v50
	v_exp_f32_e32 v55, v54
	v_mul_f32_e32 v54, 0x3d372713, v43
	v_fma_f32 v50, v42, v50, v42
	v_mul_f32_e32 v54, v43, v54
	v_mul_f32_e32 v50, 0x3f4c422a, v50
	v_fma_f32 v54, v43, v54, v43
	v_mul_f32_e32 v50, 0xc038aa3b, v50
	v_mul_f32_e32 v54, 0x3f4c422a, v54
	v_exp_f32_e32 v53, v50
	v_mul_f32_e32 v54, 0xc038aa3b, v54
	v_mul_f32_e32 v58, 0x3d372713, v49
	v_exp_f32_e32 v56, v54
	v_mul_f32_e32 v58, v49, v58
	v_fma_f32 v58, v49, v58, v49
	v_mul_f32_e32 v58, 0x3f4c422a, v58
	v_add_f32_e32 v53, 1.0, v53
	v_mul_f32_e32 v57, 0x3d372713, v44
	v_mul_f32_e32 v58, 0xc038aa3b, v58
	v_rcp_f32_e32 v54, v53
	v_add_f32_e32 v53, 1.0, v55
	v_add_f32_e32 v55, 1.0, v56
	v_mul_f32_e32 v56, 0x3d372713, v48
	v_mul_f32_e32 v57, v44, v57
	v_exp_f32_e32 v59, v58
	v_mul_f32_e32 v58, 0x3d372713, v45
	v_mul_f32_e32 v56, v48, v56
	v_fma_f32 v57, v44, v57, v44
	v_mul_f32_e32 v58, v45, v58
	v_fma_f32 v56, v48, v56, v48
	v_mul_f32_e32 v57, 0x3f4c422a, v57
	v_fma_f32 v58, v45, v58, v45
	v_mul_f32_e32 v56, 0x3f4c422a, v56
	v_mul_f32_e32 v57, 0xc038aa3b, v57
	v_mul_f32_e32 v58, 0x3f4c422a, v58
	v_mul_f32_e32 v56, 0xc038aa3b, v56
	v_exp_f32_e32 v57, v57
	v_mul_f32_e32 v58, 0xc038aa3b, v58
	v_exp_f32_e32 v56, v56
	v_exp_f32_e32 v60, v58
	v_add_f32_e32 v52, 1.0, v52
	v_add_f32_e32 v57, 1.0, v57
	v_rcp_f32_e32 v52, v52
	v_rcp_f32_e32 v53, v53
	v_add_f32_e32 v56, 1.0, v56
	v_rcp_f32_e32 v58, v57
	v_add_f32_e32 v57, 1.0, v59
	v_add_f32_e32 v59, 1.0, v60
	v_rcp_f32_e32 v55, v55
	v_rcp_f32_e32 v56, v56
	v_rcp_f32_e32 v57, v57
	v_rcp_f32_e32 v59, v59
	s_mov_b64 s[4:5], 0x24000
	v_lshl_add_u64 v[50:51], v[158:159], 0, s[4:5]
	v_pk_mul_f32 v[46:47], v[46:47], v[52:53]
	s_mov_b32 s4, 0x24000
	v_pk_mul_f32 v[52:53], v[42:43], v[54:55]
	v_pk_mul_f32 v[48:49], v[48:49], v[56:57]
	v_pk_mul_f32 v[54:55], v[44:45], v[58:59]
	v_cvt_pk_bf16_f32 v42, v46, v47
	v_add_co_u32_e32 v46, vcc, s4, v158
	v_cvt_pk_bf16_f32 v43, v48, v49
	v_cvt_pk_bf16_f32 v44, v52, v53
	v_cvt_pk_bf16_f32 v45, v54, v55
	v_addc_co_u32_e32 v47, vcc, 0, v159, vcc
	v_mul_f32_e32 v48, 0x3d372713, v38
	global_store_dwordx4 v[46:47], v[42:45], off sc1
	v_mul_f32_e32 v48, v38, v48
	v_fma_f32 v48, v38, v48, v38
	v_mul_f32_e32 v44, 0x3d372713, v39
	v_mul_f32_e32 v44, v39, v44
	v_fma_f32 v44, v39, v44, v39
	v_mul_f32_e32 v48, 0x3f4c422a, v48
	v_mul_f32_e32 v44, 0x3f4c422a, v44
	v_mul_f32_e32 v48, 0xc038aa3b, v48
	v_mul_f32_e32 v49, 0x3d372713, v34
	v_mul_f32_e32 v44, 0xc038aa3b, v44
	v_exp_f32_e32 v48, v48
	v_mul_f32_e32 v49, v34, v49
	v_exp_f32_e32 v45, v44
	v_mul_f32_e32 v44, 0x3d372713, v35
	v_fma_f32 v49, v34, v49, v34
	v_mul_f32_e32 v44, v35, v44
	v_mul_f32_e32 v49, 0x3f4c422a, v49
	v_fma_f32 v44, v35, v44, v35
	v_mul_f32_e32 v49, 0xc038aa3b, v49
; __device__ __forceinline__ float gelu_fast(float x) { const float u = 0.7978845608028654f * (x + 0.044715f * x * x * x); return x * __builtin_amdgcn_rcpf(1.f + __builtin_amdgcn_exp2f(-2.8853900817779268f * u)); }
; __device__ __forceinline__ u32x4 pack8(const f32x4 a, const f32x4 b) { u32x4 w; w.x = cvt_pk_bf16(a[0], a[1]); w.y = cvt_pk_bf16(a[2], a[3]); w.z = cvt_pk_bf16(b[0], b[1]); w.w = cvt_pk_bf16(b[2], b[3]); return w; }
;     __device__ __forceinline__ void operator()(const f32x4 (&acc)[2][2][4][2], const Unit& u, int wr, int wc, int fr, int fq) const {
;     ...
;         if (u.pn >= 6) {
;             const int col0 = (u.pn - 6) * BM + wc * 32 + 8 * fq;
; #pragma unroll
;             for (int ai = 0; ai < 2; ++ai)
; #pragma unroll
;                 for (int m = 0; m < 4; ++m) { bf16_t* rowp = U + (size_t)(row0 + ai * HALF + m * 16) * 512 + col0;
; #pragma unroll
;                     for (int bj = 0; bj < 2; ++bj) { f32x4 v0 = acc[ai][bj][m][0], v1 = acc[ai][bj][m][1];
; #pragma unroll
;                         for (int j = 0; j < 4; ++j) { v0[j] = gelu_fast(v0[j]); v1[j] = gelu_fast(v1[j]); }
;                         *(u32x4*)(rowp + bj * HALF) = pack8(v0, v1); } }
	v_mul_f32_e32 v44, 0x3f4c422a, v44
	v_exp_f32_e32 v49, v49
	v_add_f32_e32 v42, 1.0, v48
	v_mul_f32_e32 v44, 0xc038aa3b, v44
	v_mul_f32_e32 v48, 0x3d372713, v41
	v_exp_f32_e32 v46, v44
	v_mul_f32_e32 v48, v41, v48
	v_fma_f32 v48, v41, v48, v41
	v_mul_f32_e32 v48, 0x3f4c422a, v48
	v_add_f32_e32 v43, 1.0, v49
	v_mul_f32_e32 v47, 0x3d372713, v36
	v_mul_f32_e32 v48, 0xc038aa3b, v48
	v_rcp_f32_e32 v44, v43
	v_add_f32_e32 v43, 1.0, v45
	v_add_f32_e32 v45, 1.0, v46
	v_mul_f32_e32 v46, 0x3d372713, v40
	v_mul_f32_e32 v47, v36, v47
	v_exp_f32_e32 v49, v48
	v_mul_f32_e32 v48, 0x3d372713, v37
	v_mul_f32_e32 v46, v40, v46
	v_fma_f32 v47, v36, v47, v36
	v_mul_f32_e32 v48, v37, v48
	v_fma_f32 v46, v40, v46, v40
	v_mul_f32_e32 v47, 0x3f4c422a, v47
	v_fma_f32 v48, v37, v48, v37
	v_mul_f32_e32 v46, 0x3f4c422a, v46
	v_mul_f32_e32 v47, 0xc038aa3b, v47
	v_mul_f32_e32 v48, 0x3f4c422a, v48
	v_mul_f32_e32 v46, 0xc038aa3b, v46
	v_exp_f32_e32 v47, v47
	v_mul_f32_e32 v48, 0xc038aa3b, v48
	v_exp_f32_e32 v46, v46
	v_exp_f32_e32 v52, v48
	v_add_f32_e32 v47, 1.0, v47
	v_rcp_f32_e32 v48, v47
	v_add_f32_e32 v46, 1.0, v46
	v_add_f32_e32 v47, 1.0, v49
	v_add_f32_e32 v49, 1.0, v52
	v_rcp_f32_e32 v42, v42
	v_rcp_f32_e32 v43, v43
	v_rcp_f32_e32 v45, v45
	v_rcp_f32_e32 v46, v46
	v_rcp_f32_e32 v47, v47
	v_rcp_f32_e32 v49, v49
	v_pk_mul_f32 v[38:39], v[38:39], v[42:43]
	v_pk_mul_f32 v[42:43], v[34:35], v[44:45]
	v_pk_mul_f32 v[40:41], v[40:41], v[46:47]
	v_pk_mul_f32 v[44:45], v[36:37], v[48:49]
	v_cvt_pk_bf16_f32 v34, v38, v39
	v_cvt_pk_bf16_f32 v35, v40, v41
	v_cvt_pk_bf16_f32 v36, v42, v43
	v_cvt_pk_bf16_f32 v37, v44, v45
	global_store_dwordx4 v[50:51], v[34:37], off offset:256 sc1
	v_mul_f32_e32 v38, 0x3d372713, v31
	v_mul_f32_e32 v38, v31, v38
	v_mul_f32_e32 v34, 0x3d372713, v30
	v_mul_f32_e32 v34, v30, v34
	v_fma_f32 v34, v30, v34, v30
	v_mul_f32_e32 v34, 0x3f4c422a, v34
	v_fma_f32 v38, v31, v38, v31
	v_mul_f32_e32 v34, 0xc038aa3b, v34
	v_mul_f32_e32 v38, 0x3f4c422a, v38
	v_exp_f32_e32 v36, v34
	v_mul_f32_e32 v34, 0x3d372713, v26
	v_mul_f32_e32 v38, 0xc038aa3b, v38
	v_mul_f32_e32 v34, v26, v34
	v_exp_f32_e32 v39, v38
	v_mul_f32_e32 v38, 0x3d372713, v27
	v_fma_f32 v34, v26, v34, v26
	v_mul_f32_e32 v38, v27, v38
	v_mul_f32_e32 v34, 0x3f4c422a, v34
	v_fma_f32 v38, v27, v38, v27
	v_mul_f32_e32 v34, 0xc038aa3b, v34
	v_mul_f32_e32 v38, 0x3f4c422a, v38
	v_exp_f32_e32 v37, v34
	v_mul_f32_e32 v38, 0xc038aa3b, v38
	v_mul_f32_e32 v42, 0x3d372713, v33
	v_exp_f32_e32 v40, v38
	v_mul_f32_e32 v42, v33, v42
	v_fma_f32 v42, v33, v42, v33
	v_mul_f32_e32 v42, 0x3f4c422a, v42
	v_add_f32_e32 v37, 1.0, v37
	v_mul_f32_e32 v41, 0x3d372713, v28
	v_mul_f32_e32 v42, 0xc038aa3b, v42
	v_rcp_f32_e32 v38, v37
	v_add_f32_e32 v37, 1.0, v39
	v_add_f32_e32 v39, 1.0, v40
	v_mul_f32_e32 v40, 0x3d372713, v32
	v_mul_f32_e32 v41, v28, v41
	v_exp_f32_e32 v43, v42
	v_mul_f32_e32 v42, 0x3d372713, v29
	v_mul_f32_e32 v40, v32, v40
	v_fma_f32 v41, v28, v41, v28
	v_mul_f32_e32 v42, v29, v42
	v_fma_f32 v40, v32, v40, v32
	v_mul_f32_e32 v41, 0x3f4c422a, v41
	v_fma_f32 v42, v29, v42, v29
	v_mul_f32_e32 v40, 0x3f4c422a, v40
	v_mul_f32_e32 v41, 0xc038aa3b, v41
	v_mul_f32_e32 v42, 0x3f4c422a, v42
	v_mul_f32_e32 v40, 0xc038aa3b, v40
	v_exp_f32_e32 v41, v41
	v_mul_f32_e32 v42, 0xc038aa3b, v42
	v_exp_f32_e32 v40, v40
	v_exp_f32_e32 v44, v42
	v_add_f32_e32 v36, 1.0, v36
	v_add_f32_e32 v41, 1.0, v41
	v_rcp_f32_e32 v36, v36
	v_rcp_f32_e32 v37, v37
	v_add_f32_e32 v40, 1.0, v40
	v_rcp_f32_e32 v42, v41
	v_add_f32_e32 v41, 1.0, v43
	v_add_f32_e32 v43, 1.0, v44
	v_rcp_f32_e32 v39, v39
	v_rcp_f32_e32 v40, v40
	v_rcp_f32_e32 v41, v41
	v_rcp_f32_e32 v43, v43
	v_pk_mul_f32 v[30:31], v[30:31], v[36:37]
	v_pk_mul_f32 v[36:37], v[26:27], v[38:39]
	v_pk_mul_f32 v[32:33], v[32:33], v[40:41]
	v_pk_mul_f32 v[38:39], v[28:29], v[42:43]
	v_cvt_pk_bf16_f32 v26, v30, v31
	v_add_co_u32_e32 v30, vcc, s58, v158
	v_cvt_pk_bf16_f32 v27, v32, v33
	v_cvt_pk_bf16_f32 v28, v36, v37
	v_cvt_pk_bf16_f32 v29, v38, v39
	v_addc_co_u32_e32 v31, vcc, 0, v159, vcc
	v_mul_f32_e32 v32, 0x3d372713, v22
	global_store_dwordx4 v[30:31], v[26:29], off sc1
	v_mul_f32_e32 v32, v22, v32
	v_fma_f32 v32, v22, v32, v22
	v_mul_f32_e32 v28, 0x3d372713, v23
	v_mul_f32_e32 v28, v23, v28
	v_fma_f32 v28, v23, v28, v23
	v_mul_f32_e32 v32, 0x3f4c422a, v32
	v_mul_f32_e32 v28, 0x3f4c422a, v28
	v_mul_f32_e32 v32, 0xc038aa3b, v32
	v_mul_f32_e32 v33, 0x3d372713, v18
	v_mul_f32_e32 v28, 0xc038aa3b, v28
	v_exp_f32_e32 v32, v32
	v_mul_f32_e32 v33, v18, v33
	v_exp_f32_e32 v29, v28
	v_mul_f32_e32 v28, 0x3d372713, v19
	v_fma_f32 v33, v18, v33, v18
	v_mul_f32_e32 v28, v19, v28
	v_mul_f32_e32 v33, 0x3f4c422a, v33
	v_fma_f32 v28, v19, v28, v19
	v_mul_f32_e32 v33, 0xc038aa3b, v33
	v_mul_f32_e32 v28, 0x3f4c422a, v28
	v_exp_f32_e32 v33, v33
	v_add_f32_e32 v26, 1.0, v32
	v_mul_f32_e32 v28, 0xc038aa3b, v28
	v_mul_f32_e32 v32, 0x3d372713, v25
	v_exp_f32_e32 v30, v28
	v_mul_f32_e32 v32, v25, v32
	v_fma_f32 v32, v25, v32, v25
	v_mul_f32_e32 v32, 0x3f4c422a, v32
	v_add_f32_e32 v27, 1.0, v33
	v_mul_f32_e32 v31, 0x3d372713, v20
	v_mul_f32_e32 v32, 0xc038aa3b, v32
	v_rcp_f32_e32 v28, v27
	v_add_f32_e32 v27, 1.0, v29
	v_add_f32_e32 v29, 1.0, v30
	v_mul_f32_e32 v30, 0x3d372713, v24
	v_mul_f32_e32 v31, v20, v31
	v_exp_f32_e32 v33, v32
	v_mul_f32_e32 v32, 0x3d372713, v21
	v_mul_f32_e32 v30, v24, v30
	v_fma_f32 v31, v20, v31, v20
	v_mul_f32_e32 v32, v21, v32
	v_fma_f32 v30, v24, v30, v24
	v_mul_f32_e32 v31, 0x3f4c422a, v31
	v_fma_f32 v32, v21, v32, v21
	v_mul_f32_e32 v30, 0x3f4c422a, v30
	v_mul_f32_e32 v31, 0xc038aa3b, v31
	v_mul_f32_e32 v32, 0x3f4c422a, v32
	v_mul_f32_e32 v30, 0xc038aa3b, v30
; __device__ __forceinline__ float gelu_fast(float x) { const float u = 0.7978845608028654f * (x + 0.044715f * x * x * x); return x * __builtin_amdgcn_rcpf(1.f + __builtin_amdgcn_exp2f(-2.8853900817779268f * u)); }
; __device__ __forceinline__ u32x4 pack8(const f32x4 a, const f32x4 b) { u32x4 w; w.x = cvt_pk_bf16(a[0], a[1]); w.y = cvt_pk_bf16(a[2], a[3]); w.z = cvt_pk_bf16(b[0], b[1]); w.w = cvt_pk_bf16(b[2], b[3]); return w; }
;     __device__ __forceinline__ void operator()(const f32x4 (&acc)[2][2][4][2], const Unit& u, int wr, int wc, int fr, int fq) const {
;     ...
;         if (u.pn >= 6) {
;             const int col0 = (u.pn - 6) * BM + wc * 32 + 8 * fq;
; #pragma unroll
;             for (int ai = 0; ai < 2; ++ai)
; #pragma unroll
;                 for (int m = 0; m < 4; ++m) { bf16_t* rowp = U + (size_t)(row0 + ai * HALF + m * 16) * 512 + col0;
; #pragma unroll
;                     for (int bj = 0; bj < 2; ++bj) { f32x4 v0 = acc[ai][bj][m][0], v1 = acc[ai][bj][m][1];
; #pragma unroll
;                         for (int j = 0; j < 4; ++j) { v0[j] = gelu_fast(v0[j]); v1[j] = gelu_fast(v1[j]); }
;                         *(u32x4*)(rowp + bj * HALF) = pack8(v0, v1); } }
	v_exp_f32_e32 v31, v31
	v_mul_f32_e32 v32, 0xc038aa3b, v32
	v_exp_f32_e32 v30, v30
	v_exp_f32_e32 v36, v32
	v_add_f32_e32 v31, 1.0, v31
	v_rcp_f32_e32 v32, v31
	v_add_f32_e32 v30, 1.0, v30
	v_add_f32_e32 v31, 1.0, v33
	v_add_f32_e32 v33, 1.0, v36
	v_rcp_f32_e32 v26, v26
	v_rcp_f32_e32 v27, v27
	v_rcp_f32_e32 v29, v29
	v_rcp_f32_e32 v30, v30
	v_rcp_f32_e32 v31, v31
	v_rcp_f32_e32 v33, v33
	s_mov_b64 s[4:5], 0x28000
	v_pk_mul_f32 v[22:23], v[22:23], v[26:27]
	v_pk_mul_f32 v[26:27], v[18:19], v[28:29]
	v_pk_mul_f32 v[24:25], v[24:25], v[30:31]
	v_pk_mul_f32 v[28:29], v[20:21], v[32:33]
	v_lshl_add_u64 v[34:35], v[158:159], 0, s[4:5]
	v_cvt_pk_bf16_f32 v18, v22, v23
	v_cvt_pk_bf16_f32 v19, v24, v25
	v_cvt_pk_bf16_f32 v20, v26, v27
	v_cvt_pk_bf16_f32 v21, v28, v29
	global_store_dwordx4 v[34:35], v[18:21], off offset:256 sc1
	v_mul_f32_e32 v22, 0x3d372713, v15
	v_mul_f32_e32 v22, v15, v22
	v_mul_f32_e32 v18, 0x3d372713, v14
	v_mul_f32_e32 v18, v14, v18
	v_fma_f32 v18, v14, v18, v14
	v_mul_f32_e32 v18, 0x3f4c422a, v18
	v_fma_f32 v22, v15, v22, v15
	v_mul_f32_e32 v18, 0xc038aa3b, v18
	v_mul_f32_e32 v22, 0x3f4c422a, v22
	v_exp_f32_e32 v20, v18
	v_mul_f32_e32 v18, 0x3d372713, v10
	v_mul_f32_e32 v22, 0xc038aa3b, v22
	v_mul_f32_e32 v18, v10, v18
	v_exp_f32_e32 v23, v22
	v_mul_f32_e32 v22, 0x3d372713, v11
	v_fma_f32 v18, v10, v18, v10
	v_mul_f32_e32 v22, v11, v22
	v_mul_f32_e32 v18, 0x3f4c422a, v18
	v_fma_f32 v22, v11, v22, v11
	v_mul_f32_e32 v18, 0xc038aa3b, v18
	v_mul_f32_e32 v22, 0x3f4c422a, v22
	v_exp_f32_e32 v21, v18
	v_mul_f32_e32 v22, 0xc038aa3b, v22
	v_mul_f32_e32 v26, 0x3d372713, v17
	v_exp_f32_e32 v24, v22
	v_mul_f32_e32 v26, v17, v26
	v_fma_f32 v26, v17, v26, v17
	v_mul_f32_e32 v26, 0x3f4c422a, v26
	v_add_f32_e32 v21, 1.0, v21
	v_mul_f32_e32 v25, 0x3d372713, v12
	v_mul_f32_e32 v26, 0xc038aa3b, v26
	v_rcp_f32_e32 v22, v21
	v_add_f32_e32 v21, 1.0, v23
	v_add_f32_e32 v23, 1.0, v24
	v_mul_f32_e32 v24, 0x3d372713, v16
	v_mul_f32_e32 v25, v12, v25
	v_exp_f32_e32 v27, v26
	v_mul_f32_e32 v26, 0x3d372713, v13
	v_mul_f32_e32 v24, v16, v24
	v_fma_f32 v25, v12, v25, v12
	v_mul_f32_e32 v26, v13, v26
	v_fma_f32 v24, v16, v24, v16
	v_mul_f32_e32 v25, 0x3f4c422a, v25
	v_fma_f32 v26, v13, v26, v13
	v_mul_f32_e32 v24, 0x3f4c422a, v24
	v_mul_f32_e32 v25, 0xc038aa3b, v25
	v_mul_f32_e32 v26, 0x3f4c422a, v26
	v_mul_f32_e32 v24, 0xc038aa3b, v24
	v_exp_f32_e32 v25, v25
	v_mul_f32_e32 v26, 0xc038aa3b, v26
	v_exp_f32_e32 v24, v24
	v_exp_f32_e32 v28, v26
	v_add_f32_e32 v20, 1.0, v20
	v_add_f32_e32 v25, 1.0, v25
	v_rcp_f32_e32 v20, v20
	v_rcp_f32_e32 v21, v21
	v_add_f32_e32 v24, 1.0, v24
	v_rcp_f32_e32 v26, v25
	v_add_f32_e32 v25, 1.0, v27
	v_add_f32_e32 v27, 1.0, v28
	v_rcp_f32_e32 v23, v23
	v_rcp_f32_e32 v24, v24
	v_rcp_f32_e32 v25, v25
	v_rcp_f32_e32 v27, v27
	v_pk_mul_f32 v[14:15], v[14:15], v[20:21]
	v_pk_mul_f32 v[20:21], v[10:11], v[22:23]
	v_pk_mul_f32 v[16:17], v[16:17], v[24:25]
	v_pk_mul_f32 v[22:23], v[12:13], v[26:27]
	v_cvt_pk_bf16_f32 v10, v14, v15
	v_add_co_u32_e32 v14, vcc, s59, v158
	v_cvt_pk_bf16_f32 v11, v16, v17
	v_cvt_pk_bf16_f32 v12, v20, v21
	v_cvt_pk_bf16_f32 v13, v22, v23
	v_addc_co_u32_e32 v15, vcc, 0, v159, vcc
	v_mul_f32_e32 v16, 0x3d372713, v6
	global_store_dwordx4 v[14:15], v[10:13], off sc1
	v_mul_f32_e32 v16, v6, v16
	v_fma_f32 v16, v6, v16, v6
	v_mul_f32_e32 v12, 0x3d372713, v7
	v_mul_f32_e32 v12, v7, v12
	v_fma_f32 v12, v7, v12, v7
	v_mul_f32_e32 v16, 0x3f4c422a, v16
	v_mul_f32_e32 v12, 0x3f4c422a, v12
	v_mul_f32_e32 v16, 0xc038aa3b, v16
	v_mul_f32_e32 v17, 0x3d372713, v2
	v_mul_f32_e32 v12, 0xc038aa3b, v12
	v_exp_f32_e32 v16, v16
	v_mul_f32_e32 v17, v2, v17
	v_exp_f32_e32 v13, v12
	v_mul_f32_e32 v12, 0x3d372713, v3
	v_fma_f32 v17, v2, v17, v2
	v_mul_f32_e32 v12, v3, v12
	v_mul_f32_e32 v17, 0x3f4c422a, v17
	v_fma_f32 v12, v3, v12, v3
	v_mul_f32_e32 v17, 0xc038aa3b, v17
	v_mul_f32_e32 v12, 0x3f4c422a, v12
	v_exp_f32_e32 v17, v17
	v_add_f32_e32 v10, 1.0, v16
	v_mul_f32_e32 v12, 0xc038aa3b, v12
	v_mul_f32_e32 v16, 0x3d372713, v9
	v_exp_f32_e32 v14, v12
	v_mul_f32_e32 v16, v9, v16
	v_fma_f32 v16, v9, v16, v9
	v_mul_f32_e32 v16, 0x3f4c422a, v16
	v_add_f32_e32 v11, 1.0, v17
	v_mul_f32_e32 v15, 0x3d372713, v4
	v_mul_f32_e32 v16, 0xc038aa3b, v16
	v_rcp_f32_e32 v12, v11
	v_add_f32_e32 v11, 1.0, v13
	v_add_f32_e32 v13, 1.0, v14
	v_mul_f32_e32 v14, 0x3d372713, v8
	v_mul_f32_e32 v15, v4, v15
	v_exp_f32_e32 v17, v16
	v_mul_f32_e32 v16, 0x3d372713, v5
	v_mul_f32_e32 v14, v8, v14
	v_fma_f32 v15, v4, v15, v4
	v_mul_f32_e32 v16, v5, v16
	v_fma_f32 v14, v8, v14, v8
	v_mul_f32_e32 v15, 0x3f4c422a, v15
	v_fma_f32 v16, v5, v16, v5
	v_mul_f32_e32 v14, 0x3f4c422a, v14
	v_mul_f32_e32 v15, 0xc038aa3b, v15
	v_mul_f32_e32 v16, 0x3f4c422a, v16
	v_mul_f32_e32 v14, 0xc038aa3b, v14
	v_exp_f32_e32 v15, v15
	v_mul_f32_e32 v16, 0xc038aa3b, v16
	v_exp_f32_e32 v14, v14
	v_exp_f32_e32 v20, v16
	v_add_f32_e32 v15, 1.0, v15
	v_rcp_f32_e32 v16, v15
	v_add_f32_e32 v14, 1.0, v14
	v_add_f32_e32 v15, 1.0, v17
	v_add_f32_e32 v17, 1.0, v20
	v_rcp_f32_e32 v10, v10
	v_rcp_f32_e32 v11, v11
	v_rcp_f32_e32 v13, v13
	v_rcp_f32_e32 v14, v14
	v_rcp_f32_e32 v15, v15
	v_rcp_f32_e32 v17, v17
	v_pk_mul_f32 v[6:7], v[6:7], v[10:11]
	v_pk_mul_f32 v[10:11], v[2:3], v[12:13]
	v_pk_mul_f32 v[8:9], v[8:9], v[14:15]
	v_pk_mul_f32 v[12:13], v[4:5], v[16:17]
	v_lshl_add_u64 v[18:19], v[158:159], 0, s[14:15]
	v_cvt_pk_bf16_f32 v2, v6, v7
	v_cvt_pk_bf16_f32 v3, v8, v9
	v_cvt_pk_bf16_f32 v4, v10, v11
	v_cvt_pk_bf16_f32 v5, v12, v13
	global_store_dwordx4 v[18:19], v[2:5], off offset:256 sc1
	s_andn2_b64 vcc, exec, s[0:1]
	s_mov_b64 s[0:1], -1
	s_cbranch_vccnz .LBB0_184

; __device__ __forceinline__ float gelu_fast(float x) { const float u = 0.7978845608028654f * (x + 0.044715f * x * x * x); return x * __builtin_amdgcn_rcpf(1.f + __builtin_amdgcn_exp2f(-2.8853900817779268f * u)); }
; __device__ __forceinline__ u32x4 pack8(const f32x4 a, const f32x4 b) { u32x4 w; w.x = cvt_pk_bf16(a[0], a[1]); w.y = cvt_pk_bf16(a[2], a[3]); w.z = cvt_pk_bf16(b[0], b[1]); w.w = cvt_pk_bf16(b[2], b[3]); return w; }
;     __device__ __forceinline__ void operator()(const f32x4 (&acc)[2][2][4][2], const Unit& u, int wr, int wc, int fr, int fq) const {
;     ...
;             const int rb = (u.pm - 8) * BM + wr * 64 + fr;
; #pragma unroll
;             for (int ai = 0; ai < 2; ++ai)
; #pragma unroll
;                 for (int m = 0; m < 4; ++m)
; #pragma unroll
;                     for (int bj = 0; bj < 2; ++bj) { f32x4 v0 = acc[ai][bj][m][0], v1 = acc[ai][bj][m][1];
; #pragma unroll
;                         for (int j = 0; j < 4; ++j) { v0[j] = gelu_fast(v0[j]); v1[j] = gelu_fast(v1[j]); }
;                         *(u32x4*)(GVT + (size_t)(rb + ai * HALF + m * 16) * MT + col0 + bj * HALF) = pack8(v0, v1); }
.LBB0_219:
	v_mul_f32_e32 v169, 0x3d372713, v126
	v_mul_f32_e32 v169, v126, v169
	v_mul_f32_e32 v172, 0x3d372713, v127
	v_fma_f32 v169, v126, v169, v126
	v_mul_f32_e32 v172, v127, v172
	v_mul_f32_e32 v169, 0x3f4c422a, v169
	v_fma_f32 v172, v127, v172, v127
	v_mul_f32_e32 v169, 0xc038aa3b, v169
	v_mul_f32_e32 v172, 0x3f4c422a, v172
	v_exp_f32_e32 v170, v169
	v_mul_f32_e32 v169, 0x3d372713, v122
	v_mul_f32_e32 v172, 0xc038aa3b, v172
	v_mul_f32_e32 v169, v122, v169
	v_exp_f32_e32 v173, v172
	v_mul_f32_e32 v172, 0x3d372713, v123
	v_fma_f32 v169, v122, v169, v122
	v_mul_f32_e32 v172, v123, v172
	v_mul_f32_e32 v169, 0x3f4c422a, v169
	v_fma_f32 v172, v123, v172, v123
	v_mul_f32_e32 v169, 0xc038aa3b, v169
	v_mul_f32_e32 v172, 0x3f4c422a, v172
	v_exp_f32_e32 v171, v169
	v_mul_f32_e32 v172, 0xc038aa3b, v172
	v_exp_f32_e32 v174, v172
	v_mul_f32_e32 v176, 0x3d372713, v129
	v_mul_f32_e32 v176, v129, v176
	v_fma_f32 v176, v129, v176, v129
	v_add_f32_e32 v171, 1.0, v171
	v_mul_f32_e32 v175, 0x3d372713, v124
	v_mul_f32_e32 v176, 0x3f4c422a, v176
	v_rcp_f32_e32 v172, v171
	v_add_f32_e32 v171, 1.0, v173
	v_add_f32_e32 v173, 1.0, v174
	v_mul_f32_e32 v174, 0x3d372713, v128
	v_mul_f32_e32 v175, v124, v175
	v_mul_f32_e32 v176, 0xc038aa3b, v176
	v_mul_f32_e32 v174, v128, v174
	v_fma_f32 v175, v124, v175, v124
	v_exp_f32_e32 v177, v176
	v_mul_f32_e32 v176, 0x3d372713, v125
	v_fma_f32 v174, v128, v174, v128
	v_mul_f32_e32 v175, 0x3f4c422a, v175
	v_mul_f32_e32 v176, v125, v176
	v_mul_f32_e32 v174, 0x3f4c422a, v174
	v_mul_f32_e32 v175, 0xc038aa3b, v175
	v_fma_f32 v176, v125, v176, v125
	v_mul_f32_e32 v174, 0xc038aa3b, v174
	v_exp_f32_e32 v175, v175
	v_mul_f32_e32 v176, 0x3f4c422a, v176
	v_exp_f32_e32 v174, v174
	v_mul_f32_e32 v176, 0xc038aa3b, v176
	v_exp_f32_e32 v178, v176
	v_add_f32_e32 v175, 1.0, v175
	v_add_f32_e32 v170, 1.0, v170
	v_add_f32_e32 v174, 1.0, v174
	v_rcp_f32_e32 v176, v175
	v_add_f32_e32 v175, 1.0, v177
	v_rcp_f32_e32 v170, v170
	v_rcp_f32_e32 v171, v171
	v_rcp_f32_e32 v173, v173
	v_rcp_f32_e32 v174, v174
	v_rcp_f32_e32 v175, v175
	v_add_f32_e32 v177, 1.0, v178
	v_rcp_f32_e32 v177, v177
	v_or_b32_e32 v168, s17, v1
	v_pk_mul_f32 v[126:127], v[126:127], v[170:171]
	v_pk_mul_f32 v[122:123], v[122:123], v[172:173]
	v_pk_mul_f32 v[128:129], v[128:129], v[174:175]
	v_lshl_add_u32 v167, s26, 8, v147
	v_ashrrev_i32_e32 v169, 31, v168
	v_pk_mul_f32 v[124:125], v[124:125], v[176:177]
	v_cvt_pk_bf16_f32 v126, v126, v127
	v_cvt_pk_bf16_f32 v127, v128, v129
	v_cvt_pk_bf16_f32 v128, v122, v123
	v_mov_b64_e32 v[122:123], s[6:7]
	v_cvt_pk_bf16_f32 v129, v124, v125
	v_mad_i64_i32 v[170:171], s[4:5], v167, s60, v[122:123]
	v_lshlrev_b64 v[124:125], 1, v[168:169]
	v_lshl_add_u64 v[168:169], v[170:171], 0, v[124:125]
	global_store_dwordx4 v[168:169], v[126:129], off sc1
	v_mul_f32_e32 v170, 0x3d372713, v118
	v_mul_f32_e32 v170, v118, v170
	v_mul_f32_e32 v128, 0x3d372713, v119
	v_mul_f32_e32 v128, v119, v128
	v_fma_f32 v128, v119, v128, v119
	v_fma_f32 v170, v118, v170, v118
	v_mul_f32_e32 v128, 0x3f4c422a, v128
	v_mul_f32_e32 v170, 0x3f4c422a, v170
	v_mul_f32_e32 v171, 0x3d372713, v114
	v_mul_f32_e32 v128, 0xc038aa3b, v128
	v_mul_f32_e32 v170, 0xc038aa3b, v170
	v_mul_f32_e32 v171, v114, v171
	v_exp_f32_e32 v129, v128
	v_mul_f32_e32 v128, 0x3d372713, v115
	v_exp_f32_e32 v170, v170
	v_fma_f32 v171, v114, v171, v114
	v_mul_f32_e32 v128, v115, v128
	v_mul_f32_e32 v171, 0x3f4c422a, v171
	v_fma_f32 v128, v115, v128, v115
	v_mul_f32_e32 v171, 0xc038aa3b, v171
	v_mul_f32_e32 v128, 0x3f4c422a, v128
	v_exp_f32_e32 v171, v171
	v_mul_f32_e32 v128, 0xc038aa3b, v128
	v_mul_f32_e32 v172, 0x3d372713, v121
	v_add_f32_e32 v126, 1.0, v170
	v_exp_f32_e32 v170, v128
	v_mul_f32_e32 v172, v121, v172
	v_fma_f32 v172, v121, v172, v121
	v_mul_f32_e32 v172, 0x3f4c422a, v172
	v_add_f32_e32 v127, 1.0, v171
	v_mul_f32_e32 v171, 0x3d372713, v116
	v_mul_f32_e32 v172, 0xc038aa3b, v172
	v_rcp_f32_e32 v128, v127
	v_add_f32_e32 v127, 1.0, v129
	v_add_f32_e32 v129, 1.0, v170
	v_mul_f32_e32 v170, 0x3d372713, v120
	v_mul_f32_e32 v171, v116, v171
	v_exp_f32_e32 v173, v172
	v_mul_f32_e32 v172, 0x3d372713, v117
	v_mul_f32_e32 v170, v120, v170
	v_fma_f32 v171, v116, v171, v116
	v_mul_f32_e32 v172, v117, v172
	v_fma_f32 v170, v120, v170, v120
	v_mul_f32_e32 v171, 0x3f4c422a, v171
	v_fma_f32 v172, v117, v172, v117
	v_mul_f32_e32 v170, 0x3f4c422a, v170
	v_mul_f32_e32 v171, 0xc038aa3b, v171
	v_mul_f32_e32 v172, 0x3f4c422a, v172
	v_mul_f32_e32 v170, 0xc038aa3b, v170
	v_exp_f32_e32 v171, v171
	v_mul_f32_e32 v172, 0xc038aa3b, v172
	v_exp_f32_e32 v170, v170
	v_exp_f32_e32 v174, v172
	v_add_f32_e32 v171, 1.0, v171
	v_rcp_f32_e32 v172, v171
	v_add_f32_e32 v170, 1.0, v170
	v_add_f32_e32 v171, 1.0, v173
	v_add_f32_e32 v173, 1.0, v174
	v_rcp_f32_e32 v126, v126
	v_rcp_f32_e32 v127, v127
	v_rcp_f32_e32 v129, v129
	v_rcp_f32_e32 v170, v170
	v_rcp_f32_e32 v171, v171
	v_rcp_f32_e32 v173, v173
	v_pk_mul_f32 v[118:119], v[118:119], v[126:127]
	v_pk_mul_f32 v[126:127], v[114:115], v[128:129]
	v_pk_mul_f32 v[120:121], v[120:121], v[170:171]
	v_pk_mul_f32 v[128:129], v[116:117], v[172:173]
	v_cvt_pk_bf16_f32 v114, v118, v119
	v_cvt_pk_bf16_f32 v115, v120, v121
	v_cvt_pk_bf16_f32 v116, v126, v127
	v_cvt_pk_bf16_f32 v117, v128, v129
	global_store_dwordx4 v[168:169], v[114:117], off offset:256 sc1
	v_mul_f32_e32 v120, 0x3d372713, v113
	v_mul_f32_e32 v120, v113, v120
	v_mul_f32_e32 v116, 0x3d372713, v111
	v_mul_f32_e32 v116, v111, v116
	v_fma_f32 v116, v111, v116, v111
	v_mul_f32_e32 v116, 0x3f4c422a, v116
	v_mul_f32_e32 v115, 0x3d372713, v106
	v_mul_f32_e32 v116, 0xc038aa3b, v116
	v_mul_f32_e32 v115, v106, v115
	v_exp_f32_e32 v117, v116
; __device__ __forceinline__ float gelu_fast(float x) { const float u = 0.7978845608028654f * (x + 0.044715f * x * x * x); return x * __builtin_amdgcn_rcpf(1.f + __builtin_amdgcn_exp2f(-2.8853900817779268f * u)); }
; __device__ __forceinline__ u32x4 pack8(const f32x4 a, const f32x4 b) { u32x4 w; w.x = cvt_pk_bf16(a[0], a[1]); w.y = cvt_pk_bf16(a[2], a[3]); w.z = cvt_pk_bf16(b[0], b[1]); w.w = cvt_pk_bf16(b[2], b[3]); return w; }
;     __device__ __forceinline__ void operator()(const f32x4 (&acc)[2][2][4][2], const Unit& u, int wr, int wc, int fr, int fq) const {
;     ...
;             const int rb = (u.pm - 8) * BM + wr * 64 + fr;
; #pragma unroll
;             for (int ai = 0; ai < 2; ++ai)
; #pragma unroll
;                 for (int m = 0; m < 4; ++m)
; #pragma unroll
;                     for (int bj = 0; bj < 2; ++bj) { f32x4 v0 = acc[ai][bj][m][0], v1 = acc[ai][bj][m][1];
; #pragma unroll
;                         for (int j = 0; j < 4; ++j) { v0[j] = gelu_fast(v0[j]); v1[j] = gelu_fast(v1[j]); }
;                         *(u32x4*)(GVT + (size_t)(rb + ai * HALF + m * 16) * MT + col0 + bj * HALF) = pack8(v0, v1); }
	v_mul_f32_e32 v116, 0x3d372713, v107
	v_fma_f32 v115, v106, v115, v106
	v_mul_f32_e32 v116, v107, v116
	v_mul_f32_e32 v115, 0x3f4c422a, v115
	v_fma_f32 v116, v107, v116, v107
	v_mul_f32_e32 v115, 0xc038aa3b, v115
	v_mul_f32_e32 v116, 0x3f4c422a, v116
	v_exp_f32_e32 v115, v115
	v_mul_f32_e32 v116, 0xc038aa3b, v116
	v_exp_f32_e32 v118, v116
	v_fma_f32 v120, v113, v120, v113
	v_mul_f32_e32 v120, 0x3f4c422a, v120
	v_mul_f32_e32 v114, 0x3d372713, v110
	v_add_f32_e32 v115, 1.0, v115
	v_mul_f32_e32 v119, 0x3d372713, v108
	v_mul_f32_e32 v120, 0xc038aa3b, v120
	v_mul_f32_e32 v114, v110, v114
	v_rcp_f32_e32 v116, v115
	v_add_f32_e32 v115, 1.0, v117
	v_add_f32_e32 v117, 1.0, v118
	v_mul_f32_e32 v118, 0x3d372713, v112
	v_mul_f32_e32 v119, v108, v119
	v_exp_f32_e32 v121, v120
	v_mul_f32_e32 v120, 0x3d372713, v109
	v_fma_f32 v114, v110, v114, v110
	v_mul_f32_e32 v118, v112, v118
	v_fma_f32 v119, v108, v119, v108
	v_mul_f32_e32 v120, v109, v120
	v_mul_f32_e32 v114, 0x3f4c422a, v114
	v_fma_f32 v118, v112, v118, v112
	v_mul_f32_e32 v119, 0x3f4c422a, v119
	v_fma_f32 v120, v109, v120, v109
	v_mul_f32_e32 v114, 0xc038aa3b, v114
	v_mul_f32_e32 v118, 0x3f4c422a, v118
	v_mul_f32_e32 v119, 0xc038aa3b, v119
	v_mul_f32_e32 v120, 0x3f4c422a, v120
	v_exp_f32_e32 v114, v114
	v_mul_f32_e32 v118, 0xc038aa3b, v118
	v_exp_f32_e32 v119, v119
	v_mul_f32_e32 v120, 0xc038aa3b, v120
	v_exp_f32_e32 v118, v118
	v_exp_f32_e32 v127, v120
	v_add_f32_e32 v114, 1.0, v114
	v_add_f32_e32 v119, 1.0, v119
	v_rcp_f32_e32 v114, v114
	v_rcp_f32_e32 v115, v115
	v_add_f32_e32 v118, 1.0, v118
	v_rcp_f32_e32 v120, v119
	v_add_f32_e32 v119, 1.0, v121
	v_add_f32_e32 v121, 1.0, v127
	v_rcp_f32_e32 v117, v117
	v_rcp_f32_e32 v118, v118
	v_rcp_f32_e32 v119, v119
	v_rcp_f32_e32 v121, v121
	v_or_b32_e32 v126, 16, v167
	v_pk_mul_f32 v[110:111], v[110:111], v[114:115]
	v_pk_mul_f32 v[114:115], v[106:107], v[116:117]
	v_pk_mul_f32 v[112:113], v[112:113], v[118:119]
	v_pk_mul_f32 v[116:117], v[108:109], v[120:121]
	v_cvt_pk_bf16_f32 v106, v110, v111
	v_mad_i64_i32 v[110:111], s[4:5], v126, s60, v[122:123]
	v_cvt_pk_bf16_f32 v107, v112, v113
	v_cvt_pk_bf16_f32 v108, v114, v115
	v_cvt_pk_bf16_f32 v109, v116, v117
	v_lshl_add_u64 v[110:111], v[110:111], 0, v[124:125]
	global_store_dwordx4 v[110:111], v[106:109], off sc1
	v_mul_f32_e32 v112, 0x3d372713, v102
	v_mul_f32_e32 v112, v102, v112
	v_mul_f32_e32 v108, 0x3d372713, v103
	v_mul_f32_e32 v108, v103, v108
	v_fma_f32 v108, v103, v108, v103
	v_fma_f32 v112, v102, v112, v102
	v_mul_f32_e32 v108, 0x3f4c422a, v108
	v_mul_f32_e32 v112, 0x3f4c422a, v112
	v_mul_f32_e32 v113, 0x3d372713, v98
	v_mul_f32_e32 v108, 0xc038aa3b, v108
	v_mul_f32_e32 v112, 0xc038aa3b, v112
	v_mul_f32_e32 v113, v98, v113
	v_exp_f32_e32 v109, v108
	v_mul_f32_e32 v108, 0x3d372713, v99
	v_exp_f32_e32 v112, v112
	v_fma_f32 v113, v98, v113, v98
	v_mul_f32_e32 v108, v99, v108
	v_mul_f32_e32 v113, 0x3f4c422a, v113
	v_fma_f32 v108, v99, v108, v99
	v_mul_f32_e32 v113, 0xc038aa3b, v113
	v_mul_f32_e32 v108, 0x3f4c422a, v108
	v_exp_f32_e32 v113, v113
	v_mul_f32_e32 v108, 0xc038aa3b, v108
	v_mul_f32_e32 v114, 0x3d372713, v105
	v_add_f32_e32 v106, 1.0, v112
	v_exp_f32_e32 v112, v108
	v_mul_f32_e32 v114, v105, v114
	v_fma_f32 v114, v105, v114, v105
	v_mul_f32_e32 v114, 0x3f4c422a, v114
	v_add_f32_e32 v107, 1.0, v113
	v_mul_f32_e32 v113, 0x3d372713, v100
	v_mul_f32_e32 v114, 0xc038aa3b, v114
	v_rcp_f32_e32 v108, v107
	v_add_f32_e32 v107, 1.0, v109
	v_add_f32_e32 v109, 1.0, v112
	v_mul_f32_e32 v112, 0x3d372713, v104
	v_mul_f32_e32 v113, v100, v113
	v_exp_f32_e32 v115, v114
	v_mul_f32_e32 v114, 0x3d372713, v101
	v_mul_f32_e32 v112, v104, v112
	v_fma_f32 v113, v100, v113, v100
	v_mul_f32_e32 v114, v101, v114
	v_fma_f32 v112, v104, v112, v104
	v_mul_f32_e32 v113, 0x3f4c422a, v113
	v_fma_f32 v114, v101, v114, v101
	v_mul_f32_e32 v112, 0x3f4c422a, v112
	v_mul_f32_e32 v113, 0xc038aa3b, v113
	v_mul_f32_e32 v114, 0x3f4c422a, v114
	v_mul_f32_e32 v112, 0xc038aa3b, v112
	v_exp_f32_e32 v113, v113
	v_mul_f32_e32 v114, 0xc038aa3b, v114
	v_exp_f32_e32 v112, v112
	v_exp_f32_e32 v116, v114
	v_add_f32_e32 v113, 1.0, v113
	v_rcp_f32_e32 v114, v113
	v_add_f32_e32 v112, 1.0, v112
	v_add_f32_e32 v113, 1.0, v115
	v_add_f32_e32 v115, 1.0, v116
	v_rcp_f32_e32 v106, v106
	v_rcp_f32_e32 v107, v107
	v_rcp_f32_e32 v109, v109
	v_rcp_f32_e32 v112, v112
	v_rcp_f32_e32 v113, v113
	v_rcp_f32_e32 v115, v115
	v_pk_mul_f32 v[102:103], v[102:103], v[106:107]
	v_pk_mul_f32 v[106:107], v[98:99], v[108:109]
	v_pk_mul_f32 v[104:105], v[104:105], v[112:113]
	v_pk_mul_f32 v[108:109], v[100:101], v[114:115]
	v_cvt_pk_bf16_f32 v98, v102, v103
	v_cvt_pk_bf16_f32 v99, v104, v105
	v_cvt_pk_bf16_f32 v100, v106, v107
	v_cvt_pk_bf16_f32 v101, v108, v109
	global_store_dwordx4 v[110:111], v[98:101], off offset:256 sc1
	v_mul_f32_e32 v104, 0x3d372713, v97
	v_mul_f32_e32 v104, v97, v104
	v_mul_f32_e32 v100, 0x3d372713, v95
	v_mul_f32_e32 v100, v95, v100
	v_fma_f32 v100, v95, v100, v95
	v_mul_f32_e32 v100, 0x3f4c422a, v100
	v_mul_f32_e32 v99, 0x3d372713, v90
	v_mul_f32_e32 v100, 0xc038aa3b, v100
	v_mul_f32_e32 v99, v90, v99
	v_exp_f32_e32 v101, v100
	v_mul_f32_e32 v100, 0x3d372713, v91
	v_fma_f32 v99, v90, v99, v90
	v_mul_f32_e32 v100, v91, v100
	v_mul_f32_e32 v99, 0x3f4c422a, v99
	v_fma_f32 v100, v91, v100, v91
	v_mul_f32_e32 v99, 0xc038aa3b, v99
	v_mul_f32_e32 v100, 0x3f4c422a, v100
	v_exp_f32_e32 v99, v99
	v_mul_f32_e32 v100, 0xc038aa3b, v100
	v_exp_f32_e32 v102, v100
	v_fma_f32 v104, v97, v104, v97
	v_mul_f32_e32 v104, 0x3f4c422a, v104
	v_mul_f32_e32 v98, 0x3d372713, v94
	v_add_f32_e32 v99, 1.0, v99
	v_mul_f32_e32 v103, 0x3d372713, v92
; __device__ __forceinline__ float gelu_fast(float x) { const float u = 0.7978845608028654f * (x + 0.044715f * x * x * x); return x * __builtin_amdgcn_rcpf(1.f + __builtin_amdgcn_exp2f(-2.8853900817779268f * u)); }
; __device__ __forceinline__ u32x4 pack8(const f32x4 a, const f32x4 b) { u32x4 w; w.x = cvt_pk_bf16(a[0], a[1]); w.y = cvt_pk_bf16(a[2], a[3]); w.z = cvt_pk_bf16(b[0], b[1]); w.w = cvt_pk_bf16(b[2], b[3]); return w; }
;     __device__ __forceinline__ void operator()(const f32x4 (&acc)[2][2][4][2], const Unit& u, int wr, int wc, int fr, int fq) const {
;     ...
;             const int rb = (u.pm - 8) * BM + wr * 64 + fr;
; #pragma unroll
;             for (int ai = 0; ai < 2; ++ai)
; #pragma unroll
;                 for (int m = 0; m < 4; ++m)
; #pragma unroll
;                     for (int bj = 0; bj < 2; ++bj) { f32x4 v0 = acc[ai][bj][m][0], v1 = acc[ai][bj][m][1];
; #pragma unroll
;                         for (int j = 0; j < 4; ++j) { v0[j] = gelu_fast(v0[j]); v1[j] = gelu_fast(v1[j]); }
;                         *(u32x4*)(GVT + (size_t)(rb + ai * HALF + m * 16) * MT + col0 + bj * HALF) = pack8(v0, v1); }
	v_mul_f32_e32 v104, 0xc038aa3b, v104
	v_mul_f32_e32 v98, v94, v98
	v_rcp_f32_e32 v100, v99
	v_add_f32_e32 v99, 1.0, v101
	v_add_f32_e32 v101, 1.0, v102
	v_mul_f32_e32 v102, 0x3d372713, v96
	v_mul_f32_e32 v103, v92, v103
	v_exp_f32_e32 v105, v104
	v_mul_f32_e32 v104, 0x3d372713, v93
	v_fma_f32 v98, v94, v98, v94
	v_mul_f32_e32 v102, v96, v102
	v_fma_f32 v103, v92, v103, v92
	v_mul_f32_e32 v104, v93, v104
	v_mul_f32_e32 v98, 0x3f4c422a, v98
	v_fma_f32 v102, v96, v102, v96
	v_mul_f32_e32 v103, 0x3f4c422a, v103
	v_fma_f32 v104, v93, v104, v93
	v_mul_f32_e32 v98, 0xc038aa3b, v98
	v_mul_f32_e32 v102, 0x3f4c422a, v102
	v_mul_f32_e32 v103, 0xc038aa3b, v103
	v_mul_f32_e32 v104, 0x3f4c422a, v104
	v_exp_f32_e32 v98, v98
	v_mul_f32_e32 v102, 0xc038aa3b, v102
	v_exp_f32_e32 v103, v103
	v_mul_f32_e32 v104, 0xc038aa3b, v104
	v_exp_f32_e32 v102, v102
	v_exp_f32_e32 v107, v104
	v_add_f32_e32 v98, 1.0, v98
	v_add_f32_e32 v103, 1.0, v103
	v_rcp_f32_e32 v98, v98
	v_rcp_f32_e32 v99, v99
	v_add_f32_e32 v102, 1.0, v102
	v_rcp_f32_e32 v104, v103
	v_add_f32_e32 v103, 1.0, v105
	v_add_f32_e32 v105, 1.0, v107
	v_rcp_f32_e32 v101, v101
	v_rcp_f32_e32 v102, v102
	v_rcp_f32_e32 v103, v103
	v_rcp_f32_e32 v105, v105
	v_or_b32_e32 v106, 32, v167
	v_pk_mul_f32 v[94:95], v[94:95], v[98:99]
	v_pk_mul_f32 v[98:99], v[90:91], v[100:101]
	v_pk_mul_f32 v[96:97], v[96:97], v[102:103]
	v_pk_mul_f32 v[100:101], v[92:93], v[104:105]
	v_cvt_pk_bf16_f32 v90, v94, v95
	v_mad_i64_i32 v[94:95], s[4:5], v106, s60, v[122:123]
	v_cvt_pk_bf16_f32 v91, v96, v97
	v_cvt_pk_bf16_f32 v92, v98, v99
	v_cvt_pk_bf16_f32 v93, v100, v101
	v_lshl_add_u64 v[94:95], v[94:95], 0, v[124:125]
	global_store_dwordx4 v[94:95], v[90:93], off sc1
	v_mul_f32_e32 v96, 0x3d372713, v86
	v_mul_f32_e32 v96, v86, v96
	v_mul_f32_e32 v92, 0x3d372713, v87
	v_mul_f32_e32 v92, v87, v92
	v_fma_f32 v92, v87, v92, v87
	v_fma_f32 v96, v86, v96, v86
	v_mul_f32_e32 v92, 0x3f4c422a, v92
	v_mul_f32_e32 v96, 0x3f4c422a, v96
	v_mul_f32_e32 v97, 0x3d372713, v82
	v_mul_f32_e32 v92, 0xc038aa3b, v92
	v_mul_f32_e32 v96, 0xc038aa3b, v96
	v_mul_f32_e32 v97, v82, v97
	v_exp_f32_e32 v93, v92
	v_mul_f32_e32 v92, 0x3d372713, v83
	v_exp_f32_e32 v96, v96
	v_fma_f32 v97, v82, v97, v82
	v_mul_f32_e32 v92, v83, v92
	v_mul_f32_e32 v97, 0x3f4c422a, v97
	v_fma_f32 v92, v83, v92, v83
	v_mul_f32_e32 v97, 0xc038aa3b, v97
	v_mul_f32_e32 v92, 0x3f4c422a, v92
	v_exp_f32_e32 v97, v97
	v_mul_f32_e32 v92, 0xc038aa3b, v92
	v_mul_f32_e32 v98, 0x3d372713, v89
	v_add_f32_e32 v90, 1.0, v96
	v_exp_f32_e32 v96, v92
	v_mul_f32_e32 v98, v89, v98
	v_fma_f32 v98, v89, v98, v89
	v_mul_f32_e32 v98, 0x3f4c422a, v98
	v_add_f32_e32 v91, 1.0, v97
	v_mul_f32_e32 v97, 0x3d372713, v84
	v_mul_f32_e32 v98, 0xc038aa3b, v98
	v_rcp_f32_e32 v92, v91
	v_add_f32_e32 v91, 1.0, v93
	v_add_f32_e32 v93, 1.0, v96
	v_mul_f32_e32 v96, 0x3d372713, v88
	v_mul_f32_e32 v97, v84, v97
	v_exp_f32_e32 v99, v98
	v_mul_f32_e32 v98, 0x3d372713, v85
	v_mul_f32_e32 v96, v88, v96
	v_fma_f32 v97, v84, v97, v84
	v_mul_f32_e32 v98, v85, v98
	v_fma_f32 v96, v88, v96, v88
	v_mul_f32_e32 v97, 0x3f4c422a, v97
	v_fma_f32 v98, v85, v98, v85
	v_mul_f32_e32 v96, 0x3f4c422a, v96
	v_mul_f32_e32 v97, 0xc038aa3b, v97
	v_mul_f32_e32 v98, 0x3f4c422a, v98
	v_mul_f32_e32 v96, 0xc038aa3b, v96
	v_exp_f32_e32 v97, v97
	v_mul_f32_e32 v98, 0xc038aa3b, v98
	v_exp_f32_e32 v96, v96
	v_exp_f32_e32 v100, v98
	v_add_f32_e32 v97, 1.0, v97
	v_rcp_f32_e32 v98, v97
	v_add_f32_e32 v96, 1.0, v96
	v_add_f32_e32 v97, 1.0, v99
	v_add_f32_e32 v99, 1.0, v100
	v_rcp_f32_e32 v90, v90
	v_rcp_f32_e32 v91, v91
	v_rcp_f32_e32 v93, v93
	v_rcp_f32_e32 v96, v96
	v_rcp_f32_e32 v97, v97
	v_rcp_f32_e32 v99, v99
	v_pk_mul_f32 v[86:87], v[86:87], v[90:91]
	v_pk_mul_f32 v[90:91], v[82:83], v[92:93]
	v_pk_mul_f32 v[88:89], v[88:89], v[96:97]
	v_pk_mul_f32 v[92:93], v[84:85], v[98:99]
	v_cvt_pk_bf16_f32 v82, v86, v87
	v_cvt_pk_bf16_f32 v83, v88, v89
	v_cvt_pk_bf16_f32 v84, v90, v91
	v_cvt_pk_bf16_f32 v85, v92, v93
	global_store_dwordx4 v[94:95], v[82:85], off offset:256 sc1
	v_mul_f32_e32 v88, 0x3d372713, v81
	v_mul_f32_e32 v88, v81, v88
	v_mul_f32_e32 v84, 0x3d372713, v79
	v_mul_f32_e32 v84, v79, v84
	v_fma_f32 v84, v79, v84, v79
	v_mul_f32_e32 v84, 0x3f4c422a, v84
	v_mul_f32_e32 v83, 0x3d372713, v74
	v_mul_f32_e32 v84, 0xc038aa3b, v84
	v_mul_f32_e32 v83, v74, v83
	v_exp_f32_e32 v85, v84
	v_mul_f32_e32 v84, 0x3d372713, v75
	v_fma_f32 v83, v74, v83, v74
	v_mul_f32_e32 v84, v75, v84
	v_mul_f32_e32 v83, 0x3f4c422a, v83
	v_fma_f32 v84, v75, v84, v75
	v_mul_f32_e32 v83, 0xc038aa3b, v83
	v_mul_f32_e32 v84, 0x3f4c422a, v84
	v_exp_f32_e32 v83, v83
	v_mul_f32_e32 v84, 0xc038aa3b, v84
	v_exp_f32_e32 v86, v84
	v_fma_f32 v88, v81, v88, v81
	v_mul_f32_e32 v88, 0x3f4c422a, v88
	v_mul_f32_e32 v82, 0x3d372713, v78
	v_add_f32_e32 v83, 1.0, v83
	v_mul_f32_e32 v87, 0x3d372713, v76
	v_mul_f32_e32 v88, 0xc038aa3b, v88
	v_mul_f32_e32 v82, v78, v82
	v_rcp_f32_e32 v84, v83
	v_add_f32_e32 v83, 1.0, v85
	v_add_f32_e32 v85, 1.0, v86
	v_mul_f32_e32 v86, 0x3d372713, v80
	v_mul_f32_e32 v87, v76, v87
	v_exp_f32_e32 v89, v88
	v_mul_f32_e32 v88, 0x3d372713, v77
	v_fma_f32 v82, v78, v82, v78
	v_mul_f32_e32 v86, v80, v86
	v_fma_f32 v87, v76, v87, v76
	v_mul_f32_e32 v88, v77, v88
	v_mul_f32_e32 v82, 0x3f4c422a, v82
	v_fma_f32 v86, v80, v86, v80
	v_mul_f32_e32 v87, 0x3f4c422a, v87
	v_fma_f32 v88, v77, v88, v77
	v_mul_f32_e32 v82, 0xc038aa3b, v82
	v_mul_f32_e32 v86, 0x3f4c422a, v86
	v_mul_f32_e32 v87, 0xc038aa3b, v87
	v_mul_f32_e32 v88, 0x3f4c422a, v88
	v_exp_f32_e32 v82, v82
	v_mul_f32_e32 v86, 0xc038aa3b, v86
	v_exp_f32_e32 v87, v87
	v_mul_f32_e32 v88, 0xc038aa3b, v88
	v_exp_f32_e32 v86, v86
; __device__ __forceinline__ float gelu_fast(float x) { const float u = 0.7978845608028654f * (x + 0.044715f * x * x * x); return x * __builtin_amdgcn_rcpf(1.f + __builtin_amdgcn_exp2f(-2.8853900817779268f * u)); }
; __device__ __forceinline__ u32x4 pack8(const f32x4 a, const f32x4 b) { u32x4 w; w.x = cvt_pk_bf16(a[0], a[1]); w.y = cvt_pk_bf16(a[2], a[3]); w.z = cvt_pk_bf16(b[0], b[1]); w.w = cvt_pk_bf16(b[2], b[3]); return w; }
;     __device__ __forceinline__ void operator()(const f32x4 (&acc)[2][2][4][2], const Unit& u, int wr, int wc, int fr, int fq) const {
;     ...
;             const int rb = (u.pm - 8) * BM + wr * 64 + fr;
; #pragma unroll
;             for (int ai = 0; ai < 2; ++ai)
; #pragma unroll
;                 for (int m = 0; m < 4; ++m)
; #pragma unroll
;                     for (int bj = 0; bj < 2; ++bj) { f32x4 v0 = acc[ai][bj][m][0], v1 = acc[ai][bj][m][1];
; #pragma unroll
;                         for (int j = 0; j < 4; ++j) { v0[j] = gelu_fast(v0[j]); v1[j] = gelu_fast(v1[j]); }
;                         *(u32x4*)(GVT + (size_t)(rb + ai * HALF + m * 16) * MT + col0 + bj * HALF) = pack8(v0, v1); }
	v_exp_f32_e32 v91, v88
	v_add_f32_e32 v82, 1.0, v82
	v_add_f32_e32 v87, 1.0, v87
	v_rcp_f32_e32 v82, v82
	v_rcp_f32_e32 v83, v83
	v_add_f32_e32 v86, 1.0, v86
	v_rcp_f32_e32 v88, v87
	v_add_f32_e32 v87, 1.0, v89
	v_add_f32_e32 v89, 1.0, v91
	v_rcp_f32_e32 v85, v85
	v_rcp_f32_e32 v86, v86
	v_rcp_f32_e32 v87, v87
	v_rcp_f32_e32 v89, v89
	v_or_b32_e32 v90, 48, v167
	v_pk_mul_f32 v[78:79], v[78:79], v[82:83]
	v_pk_mul_f32 v[82:83], v[74:75], v[84:85]
	v_pk_mul_f32 v[80:81], v[80:81], v[86:87]
	v_pk_mul_f32 v[84:85], v[76:77], v[88:89]
	v_cvt_pk_bf16_f32 v74, v78, v79
	v_mad_i64_i32 v[78:79], s[4:5], v90, s60, v[122:123]
	v_cvt_pk_bf16_f32 v75, v80, v81
	v_cvt_pk_bf16_f32 v76, v82, v83
	v_cvt_pk_bf16_f32 v77, v84, v85
	v_lshl_add_u64 v[78:79], v[78:79], 0, v[124:125]
	global_store_dwordx4 v[78:79], v[74:77], off sc1
	v_mul_f32_e32 v80, 0x3d372713, v70
	v_mul_f32_e32 v80, v70, v80
	v_mul_f32_e32 v76, 0x3d372713, v71
	v_mul_f32_e32 v76, v71, v76
	v_fma_f32 v76, v71, v76, v71
	v_fma_f32 v80, v70, v80, v70
	v_mul_f32_e32 v76, 0x3f4c422a, v76
	v_mul_f32_e32 v80, 0x3f4c422a, v80
	v_mul_f32_e32 v81, 0x3d372713, v66
	v_mul_f32_e32 v76, 0xc038aa3b, v76
	v_mul_f32_e32 v80, 0xc038aa3b, v80
	v_mul_f32_e32 v81, v66, v81
	v_exp_f32_e32 v77, v76
	v_mul_f32_e32 v76, 0x3d372713, v67
	v_exp_f32_e32 v80, v80
	v_fma_f32 v81, v66, v81, v66
	v_mul_f32_e32 v76, v67, v76
	v_mul_f32_e32 v81, 0x3f4c422a, v81
	v_fma_f32 v76, v67, v76, v67
	v_mul_f32_e32 v81, 0xc038aa3b, v81
	v_mul_f32_e32 v76, 0x3f4c422a, v76
	v_exp_f32_e32 v81, v81
	v_mul_f32_e32 v76, 0xc038aa3b, v76
	v_mul_f32_e32 v82, 0x3d372713, v73
	v_add_f32_e32 v74, 1.0, v80
	v_exp_f32_e32 v80, v76
	v_mul_f32_e32 v82, v73, v82
	v_fma_f32 v82, v73, v82, v73
	v_mul_f32_e32 v82, 0x3f4c422a, v82
	v_add_f32_e32 v75, 1.0, v81
	v_mul_f32_e32 v81, 0x3d372713, v68
	v_mul_f32_e32 v82, 0xc038aa3b, v82
	v_rcp_f32_e32 v76, v75
	v_add_f32_e32 v75, 1.0, v77
	v_add_f32_e32 v77, 1.0, v80
	v_mul_f32_e32 v80, 0x3d372713, v72
	v_mul_f32_e32 v81, v68, v81
	v_exp_f32_e32 v83, v82
	v_mul_f32_e32 v82, 0x3d372713, v69
	v_mul_f32_e32 v80, v72, v80
	v_fma_f32 v81, v68, v81, v68
	v_mul_f32_e32 v82, v69, v82
	v_fma_f32 v80, v72, v80, v72
	v_mul_f32_e32 v81, 0x3f4c422a, v81
	v_fma_f32 v82, v69, v82, v69
	v_mul_f32_e32 v80, 0x3f4c422a, v80
	v_mul_f32_e32 v81, 0xc038aa3b, v81
	v_mul_f32_e32 v82, 0x3f4c422a, v82
	v_mul_f32_e32 v80, 0xc038aa3b, v80
	v_exp_f32_e32 v81, v81
	v_mul_f32_e32 v82, 0xc038aa3b, v82
	v_exp_f32_e32 v80, v80
	v_exp_f32_e32 v84, v82
	v_add_f32_e32 v81, 1.0, v81
	v_rcp_f32_e32 v82, v81
	v_add_f32_e32 v80, 1.0, v80
	v_add_f32_e32 v81, 1.0, v83
	v_add_f32_e32 v83, 1.0, v84
	v_rcp_f32_e32 v74, v74
	v_rcp_f32_e32 v75, v75
	v_rcp_f32_e32 v77, v77
	v_rcp_f32_e32 v80, v80
	v_rcp_f32_e32 v81, v81
	v_rcp_f32_e32 v83, v83
	v_pk_mul_f32 v[70:71], v[70:71], v[74:75]
	v_pk_mul_f32 v[74:75], v[66:67], v[76:77]
	v_pk_mul_f32 v[72:73], v[72:73], v[80:81]
	v_pk_mul_f32 v[76:77], v[68:69], v[82:83]
	v_cvt_pk_bf16_f32 v66, v70, v71
	v_cvt_pk_bf16_f32 v67, v72, v73
	v_cvt_pk_bf16_f32 v68, v74, v75
	v_cvt_pk_bf16_f32 v69, v76, v77
	global_store_dwordx4 v[78:79], v[66:69], off offset:256 sc1
	v_mul_f32_e32 v72, 0x3d372713, v65
	v_mul_f32_e32 v72, v65, v72
	v_mul_f32_e32 v68, 0x3d372713, v63
	v_mul_f32_e32 v68, v63, v68
	v_fma_f32 v68, v63, v68, v63
	v_mul_f32_e32 v68, 0x3f4c422a, v68
	v_mul_f32_e32 v67, 0x3d372713, v58
	v_mul_f32_e32 v68, 0xc038aa3b, v68
	v_mul_f32_e32 v67, v58, v67
	v_exp_f32_e32 v69, v68
	v_mul_f32_e32 v68, 0x3d372713, v59
	v_fma_f32 v67, v58, v67, v58
	v_mul_f32_e32 v68, v59, v68
	v_mul_f32_e32 v67, 0x3f4c422a, v67
	v_fma_f32 v68, v59, v68, v59
	v_mul_f32_e32 v67, 0xc038aa3b, v67
	v_mul_f32_e32 v68, 0x3f4c422a, v68
	v_exp_f32_e32 v67, v67
	v_mul_f32_e32 v68, 0xc038aa3b, v68
	v_exp_f32_e32 v70, v68
	v_fma_f32 v72, v65, v72, v65
	v_mul_f32_e32 v72, 0x3f4c422a, v72
	v_mul_f32_e32 v66, 0x3d372713, v62
	v_add_f32_e32 v67, 1.0, v67
	v_mul_f32_e32 v71, 0x3d372713, v60
	v_mul_f32_e32 v72, 0xc038aa3b, v72
	v_mul_f32_e32 v66, v62, v66
	v_rcp_f32_e32 v68, v67
	v_add_f32_e32 v67, 1.0, v69
	v_add_f32_e32 v69, 1.0, v70
	v_mul_f32_e32 v70, 0x3d372713, v64
	v_mul_f32_e32 v71, v60, v71
	v_exp_f32_e32 v73, v72
	v_mul_f32_e32 v72, 0x3d372713, v61
	v_fma_f32 v66, v62, v66, v62
	v_mul_f32_e32 v70, v64, v70
	v_fma_f32 v71, v60, v71, v60
	v_mul_f32_e32 v72, v61, v72
	v_mul_f32_e32 v66, 0x3f4c422a, v66
	v_fma_f32 v70, v64, v70, v64
	v_mul_f32_e32 v71, 0x3f4c422a, v71
	v_fma_f32 v72, v61, v72, v61
	v_mul_f32_e32 v66, 0xc038aa3b, v66
	v_mul_f32_e32 v70, 0x3f4c422a, v70
	v_mul_f32_e32 v71, 0xc038aa3b, v71
	v_mul_f32_e32 v72, 0x3f4c422a, v72
	v_exp_f32_e32 v66, v66
	v_mul_f32_e32 v70, 0xc038aa3b, v70
	v_exp_f32_e32 v71, v71
	v_mul_f32_e32 v72, 0xc038aa3b, v72
	v_exp_f32_e32 v70, v70
	v_exp_f32_e32 v75, v72
	v_add_f32_e32 v66, 1.0, v66
	v_add_f32_e32 v71, 1.0, v71
	v_rcp_f32_e32 v66, v66
	v_rcp_f32_e32 v67, v67
	v_add_f32_e32 v70, 1.0, v70
	v_rcp_f32_e32 v72, v71
	v_add_f32_e32 v71, 1.0, v73
	v_add_f32_e32 v73, 1.0, v75
	v_rcp_f32_e32 v69, v69
	v_rcp_f32_e32 v70, v70
	v_rcp_f32_e32 v71, v71
	v_rcp_f32_e32 v73, v73
	v_add_u32_e32 v74, 0x80, v167
	v_pk_mul_f32 v[62:63], v[62:63], v[66:67]
	v_pk_mul_f32 v[66:67], v[58:59], v[68:69]
	v_pk_mul_f32 v[64:65], v[64:65], v[70:71]
	v_pk_mul_f32 v[68:69], v[60:61], v[72:73]
	v_cvt_pk_bf16_f32 v58, v62, v63
	v_mad_i64_i32 v[62:63], s[4:5], v74, s60, v[122:123]
	v_cvt_pk_bf16_f32 v59, v64, v65
	v_cvt_pk_bf16_f32 v60, v66, v67
	v_cvt_pk_bf16_f32 v61, v68, v69
	v_lshl_add_u64 v[62:63], v[62:63], 0, v[124:125]
	global_store_dwordx4 v[62:63], v[58:61], off sc1
	v_mul_f32_e32 v64, 0x3d372713, v54
	v_mul_f32_e32 v64, v54, v64
; __device__ __forceinline__ float gelu_fast(float x) { const float u = 0.7978845608028654f * (x + 0.044715f * x * x * x); return x * __builtin_amdgcn_rcpf(1.f + __builtin_amdgcn_exp2f(-2.8853900817779268f * u)); }
; __device__ __forceinline__ u32x4 pack8(const f32x4 a, const f32x4 b) { u32x4 w; w.x = cvt_pk_bf16(a[0], a[1]); w.y = cvt_pk_bf16(a[2], a[3]); w.z = cvt_pk_bf16(b[0], b[1]); w.w = cvt_pk_bf16(b[2], b[3]); return w; }
;     __device__ __forceinline__ void operator()(const f32x4 (&acc)[2][2][4][2], const Unit& u, int wr, int wc, int fr, int fq) const {
;     ...
;             const int rb = (u.pm - 8) * BM + wr * 64 + fr;
; #pragma unroll
;             for (int ai = 0; ai < 2; ++ai)
; #pragma unroll
;                 for (int m = 0; m < 4; ++m)
; #pragma unroll
;                     for (int bj = 0; bj < 2; ++bj) { f32x4 v0 = acc[ai][bj][m][0], v1 = acc[ai][bj][m][1];
; #pragma unroll
;                         for (int j = 0; j < 4; ++j) { v0[j] = gelu_fast(v0[j]); v1[j] = gelu_fast(v1[j]); }
;                         *(u32x4*)(GVT + (size_t)(rb + ai * HALF + m * 16) * MT + col0 + bj * HALF) = pack8(v0, v1); }
	v_mul_f32_e32 v60, 0x3d372713, v55
	v_mul_f32_e32 v60, v55, v60
	v_fma_f32 v60, v55, v60, v55
	v_fma_f32 v64, v54, v64, v54
	v_mul_f32_e32 v60, 0x3f4c422a, v60
	v_mul_f32_e32 v64, 0x3f4c422a, v64
	v_mul_f32_e32 v65, 0x3d372713, v50
	v_mul_f32_e32 v60, 0xc038aa3b, v60
	v_mul_f32_e32 v64, 0xc038aa3b, v64
	v_mul_f32_e32 v65, v50, v65
	v_exp_f32_e32 v61, v60
	v_mul_f32_e32 v60, 0x3d372713, v51
	v_exp_f32_e32 v64, v64
	v_fma_f32 v65, v50, v65, v50
	v_mul_f32_e32 v60, v51, v60
	v_mul_f32_e32 v65, 0x3f4c422a, v65
	v_fma_f32 v60, v51, v60, v51
	v_mul_f32_e32 v65, 0xc038aa3b, v65
	v_mul_f32_e32 v60, 0x3f4c422a, v60
	v_exp_f32_e32 v65, v65
	v_mul_f32_e32 v60, 0xc038aa3b, v60
	v_mul_f32_e32 v66, 0x3d372713, v57
	v_add_f32_e32 v58, 1.0, v64
	v_exp_f32_e32 v64, v60
	v_mul_f32_e32 v66, v57, v66
	v_fma_f32 v66, v57, v66, v57
	v_mul_f32_e32 v66, 0x3f4c422a, v66
	v_add_f32_e32 v59, 1.0, v65
	v_mul_f32_e32 v65, 0x3d372713, v52
	v_mul_f32_e32 v66, 0xc038aa3b, v66
	v_rcp_f32_e32 v60, v59
	v_add_f32_e32 v59, 1.0, v61
	v_add_f32_e32 v61, 1.0, v64
	v_mul_f32_e32 v64, 0x3d372713, v56
	v_mul_f32_e32 v65, v52, v65
	v_exp_f32_e32 v67, v66
	v_mul_f32_e32 v66, 0x3d372713, v53
	v_mul_f32_e32 v64, v56, v64
	v_fma_f32 v65, v52, v65, v52
	v_mul_f32_e32 v66, v53, v66
	v_fma_f32 v64, v56, v64, v56
	v_mul_f32_e32 v65, 0x3f4c422a, v65
	v_fma_f32 v66, v53, v66, v53
	v_mul_f32_e32 v64, 0x3f4c422a, v64
	v_mul_f32_e32 v65, 0xc038aa3b, v65
	v_mul_f32_e32 v66, 0x3f4c422a, v66
	v_mul_f32_e32 v64, 0xc038aa3b, v64
	v_exp_f32_e32 v65, v65
	v_mul_f32_e32 v66, 0xc038aa3b, v66
	v_exp_f32_e32 v64, v64
	v_exp_f32_e32 v68, v66
	v_add_f32_e32 v65, 1.0, v65
	v_rcp_f32_e32 v66, v65
	v_add_f32_e32 v64, 1.0, v64
	v_add_f32_e32 v65, 1.0, v67
	v_add_f32_e32 v67, 1.0, v68
	v_rcp_f32_e32 v58, v58
	v_rcp_f32_e32 v59, v59
	v_rcp_f32_e32 v61, v61
	v_rcp_f32_e32 v64, v64
	v_rcp_f32_e32 v65, v65
	v_rcp_f32_e32 v67, v67
	v_pk_mul_f32 v[54:55], v[54:55], v[58:59]
	v_pk_mul_f32 v[58:59], v[50:51], v[60:61]
	v_pk_mul_f32 v[56:57], v[56:57], v[64:65]
	v_pk_mul_f32 v[60:61], v[52:53], v[66:67]
	v_cvt_pk_bf16_f32 v50, v54, v55
	v_cvt_pk_bf16_f32 v51, v56, v57
	v_cvt_pk_bf16_f32 v52, v58, v59
	v_cvt_pk_bf16_f32 v53, v60, v61
	global_store_dwordx4 v[62:63], v[50:53], off offset:256 sc1
	v_mul_f32_e32 v56, 0x3d372713, v49
	v_mul_f32_e32 v56, v49, v56
	v_mul_f32_e32 v52, 0x3d372713, v47
	v_mul_f32_e32 v52, v47, v52
	v_fma_f32 v52, v47, v52, v47
	v_mul_f32_e32 v52, 0x3f4c422a, v52
	v_mul_f32_e32 v51, 0x3d372713, v42
	v_mul_f32_e32 v52, 0xc038aa3b, v52
	v_mul_f32_e32 v51, v42, v51
	v_exp_f32_e32 v53, v52
	v_mul_f32_e32 v52, 0x3d372713, v43
	v_fma_f32 v51, v42, v51, v42
	v_mul_f32_e32 v52, v43, v52
	v_mul_f32_e32 v51, 0x3f4c422a, v51
	v_fma_f32 v52, v43, v52, v43
	v_mul_f32_e32 v51, 0xc038aa3b, v51
	v_mul_f32_e32 v52, 0x3f4c422a, v52
	v_exp_f32_e32 v51, v51
	v_mul_f32_e32 v52, 0xc038aa3b, v52
	v_exp_f32_e32 v54, v52
	v_fma_f32 v56, v49, v56, v49
	v_mul_f32_e32 v56, 0x3f4c422a, v56
	v_mul_f32_e32 v50, 0x3d372713, v46
	v_add_f32_e32 v51, 1.0, v51
	v_mul_f32_e32 v55, 0x3d372713, v44
	v_mul_f32_e32 v56, 0xc038aa3b, v56
	v_mul_f32_e32 v50, v46, v50
	v_rcp_f32_e32 v52, v51
	v_add_f32_e32 v51, 1.0, v53
	v_add_f32_e32 v53, 1.0, v54
	v_mul_f32_e32 v54, 0x3d372713, v48
	v_mul_f32_e32 v55, v44, v55
	v_exp_f32_e32 v57, v56
	v_mul_f32_e32 v56, 0x3d372713, v45
	v_fma_f32 v50, v46, v50, v46
	v_mul_f32_e32 v54, v48, v54
	v_fma_f32 v55, v44, v55, v44
	v_mul_f32_e32 v56, v45, v56
	v_mul_f32_e32 v50, 0x3f4c422a, v50
	v_fma_f32 v54, v48, v54, v48
	v_mul_f32_e32 v55, 0x3f4c422a, v55
	v_fma_f32 v56, v45, v56, v45
	v_mul_f32_e32 v50, 0xc038aa3b, v50
	v_mul_f32_e32 v54, 0x3f4c422a, v54
	v_mul_f32_e32 v55, 0xc038aa3b, v55
	v_mul_f32_e32 v56, 0x3f4c422a, v56
	v_exp_f32_e32 v50, v50
	v_mul_f32_e32 v54, 0xc038aa3b, v54
	v_exp_f32_e32 v55, v55
	v_mul_f32_e32 v56, 0xc038aa3b, v56
	v_exp_f32_e32 v54, v54
	v_exp_f32_e32 v59, v56
	v_add_f32_e32 v50, 1.0, v50
	v_add_f32_e32 v55, 1.0, v55
	v_rcp_f32_e32 v50, v50
	v_rcp_f32_e32 v51, v51
	v_add_f32_e32 v54, 1.0, v54
	v_rcp_f32_e32 v56, v55
	v_add_f32_e32 v55, 1.0, v57
	v_add_f32_e32 v57, 1.0, v59
	v_rcp_f32_e32 v53, v53
	v_rcp_f32_e32 v54, v54
	v_rcp_f32_e32 v55, v55
	v_rcp_f32_e32 v57, v57
	v_add_u32_e32 v58, 0x90, v167
	v_pk_mul_f32 v[46:47], v[46:47], v[50:51]
	v_pk_mul_f32 v[50:51], v[42:43], v[52:53]
	v_pk_mul_f32 v[48:49], v[48:49], v[54:55]
	v_pk_mul_f32 v[52:53], v[44:45], v[56:57]
	v_cvt_pk_bf16_f32 v42, v46, v47
	v_mad_i64_i32 v[46:47], s[4:5], v58, s60, v[122:123]
	v_cvt_pk_bf16_f32 v43, v48, v49
	v_cvt_pk_bf16_f32 v44, v50, v51
	v_cvt_pk_bf16_f32 v45, v52, v53
	v_lshl_add_u64 v[46:47], v[46:47], 0, v[124:125]
	global_store_dwordx4 v[46:47], v[42:45], off sc1
	v_mul_f32_e32 v48, 0x3d372713, v38
	v_mul_f32_e32 v48, v38, v48
	v_mul_f32_e32 v44, 0x3d372713, v39
	v_mul_f32_e32 v44, v39, v44
	v_fma_f32 v44, v39, v44, v39
	v_fma_f32 v48, v38, v48, v38
	v_mul_f32_e32 v44, 0x3f4c422a, v44
	v_mul_f32_e32 v48, 0x3f4c422a, v48
	v_mul_f32_e32 v49, 0x3d372713, v34
	v_mul_f32_e32 v44, 0xc038aa3b, v44
	v_mul_f32_e32 v48, 0xc038aa3b, v48
	v_mul_f32_e32 v49, v34, v49
	v_exp_f32_e32 v45, v44
	v_mul_f32_e32 v44, 0x3d372713, v35
	v_exp_f32_e32 v48, v48
	v_fma_f32 v49, v34, v49, v34
	v_mul_f32_e32 v44, v35, v44
	v_mul_f32_e32 v49, 0x3f4c422a, v49
	v_fma_f32 v44, v35, v44, v35
	v_mul_f32_e32 v49, 0xc038aa3b, v49
	v_mul_f32_e32 v44, 0x3f4c422a, v44
	v_exp_f32_e32 v49, v49
	v_mul_f32_e32 v44, 0xc038aa3b, v44
	v_mul_f32_e32 v50, 0x3d372713, v41
	v_add_f32_e32 v42, 1.0, v48
	v_exp_f32_e32 v48, v44
	v_mul_f32_e32 v50, v41, v50
	v_fma_f32 v50, v41, v50, v41
	v_mul_f32_e32 v50, 0x3f4c422a, v50
	v_add_f32_e32 v43, 1.0, v49
; __device__ __forceinline__ float gelu_fast(float x) { const float u = 0.7978845608028654f * (x + 0.044715f * x * x * x); return x * __builtin_amdgcn_rcpf(1.f + __builtin_amdgcn_exp2f(-2.8853900817779268f * u)); }
; __device__ __forceinline__ u32x4 pack8(const f32x4 a, const f32x4 b) { u32x4 w; w.x = cvt_pk_bf16(a[0], a[1]); w.y = cvt_pk_bf16(a[2], a[3]); w.z = cvt_pk_bf16(b[0], b[1]); w.w = cvt_pk_bf16(b[2], b[3]); return w; }
;     __device__ __forceinline__ void operator()(const f32x4 (&acc)[2][2][4][2], const Unit& u, int wr, int wc, int fr, int fq) const {
;     ...
;             const int rb = (u.pm - 8) * BM + wr * 64 + fr;
; #pragma unroll
;             for (int ai = 0; ai < 2; ++ai)
; #pragma unroll
;                 for (int m = 0; m < 4; ++m)
; #pragma unroll
;                     for (int bj = 0; bj < 2; ++bj) { f32x4 v0 = acc[ai][bj][m][0], v1 = acc[ai][bj][m][1];
; #pragma unroll
;                         for (int j = 0; j < 4; ++j) { v0[j] = gelu_fast(v0[j]); v1[j] = gelu_fast(v1[j]); }
;                         *(u32x4*)(GVT + (size_t)(rb + ai * HALF + m * 16) * MT + col0 + bj * HALF) = pack8(v0, v1); }
	v_mul_f32_e32 v49, 0x3d372713, v36
	v_mul_f32_e32 v50, 0xc038aa3b, v50
	v_rcp_f32_e32 v44, v43
	v_add_f32_e32 v43, 1.0, v45
	v_add_f32_e32 v45, 1.0, v48
	v_mul_f32_e32 v48, 0x3d372713, v40
	v_mul_f32_e32 v49, v36, v49
	v_exp_f32_e32 v51, v50
	v_mul_f32_e32 v50, 0x3d372713, v37
	v_mul_f32_e32 v48, v40, v48
	v_fma_f32 v49, v36, v49, v36
	v_mul_f32_e32 v50, v37, v50
	v_fma_f32 v48, v40, v48, v40
	v_mul_f32_e32 v49, 0x3f4c422a, v49
	v_fma_f32 v50, v37, v50, v37
	v_mul_f32_e32 v48, 0x3f4c422a, v48
	v_mul_f32_e32 v49, 0xc038aa3b, v49
	v_mul_f32_e32 v50, 0x3f4c422a, v50
	v_mul_f32_e32 v48, 0xc038aa3b, v48
	v_exp_f32_e32 v49, v49
	v_mul_f32_e32 v50, 0xc038aa3b, v50
	v_exp_f32_e32 v48, v48
	v_exp_f32_e32 v52, v50
	v_add_f32_e32 v49, 1.0, v49
	v_rcp_f32_e32 v50, v49
	v_add_f32_e32 v48, 1.0, v48
	v_add_f32_e32 v49, 1.0, v51
	v_add_f32_e32 v51, 1.0, v52
	v_rcp_f32_e32 v42, v42
	v_rcp_f32_e32 v43, v43
	v_rcp_f32_e32 v45, v45
	v_rcp_f32_e32 v48, v48
	v_rcp_f32_e32 v49, v49
	v_rcp_f32_e32 v51, v51
	v_pk_mul_f32 v[38:39], v[38:39], v[42:43]
	v_pk_mul_f32 v[42:43], v[34:35], v[44:45]
	v_pk_mul_f32 v[40:41], v[40:41], v[48:49]
	v_pk_mul_f32 v[44:45], v[36:37], v[50:51]
	v_cvt_pk_bf16_f32 v34, v38, v39
	v_cvt_pk_bf16_f32 v35, v40, v41
	v_cvt_pk_bf16_f32 v36, v42, v43
	v_cvt_pk_bf16_f32 v37, v44, v45
	global_store_dwordx4 v[46:47], v[34:37], off offset:256 sc1
	v_mul_f32_e32 v40, 0x3d372713, v33
	v_mul_f32_e32 v40, v33, v40
	v_mul_f32_e32 v36, 0x3d372713, v31
	v_mul_f32_e32 v36, v31, v36
	v_fma_f32 v36, v31, v36, v31
	v_mul_f32_e32 v36, 0x3f4c422a, v36
	v_mul_f32_e32 v35, 0x3d372713, v26
	v_mul_f32_e32 v36, 0xc038aa3b, v36
	v_mul_f32_e32 v35, v26, v35
	v_exp_f32_e32 v37, v36
	v_mul_f32_e32 v36, 0x3d372713, v27
	v_fma_f32 v35, v26, v35, v26
	v_mul_f32_e32 v36, v27, v36
	v_mul_f32_e32 v35, 0x3f4c422a, v35
	v_fma_f32 v36, v27, v36, v27
	v_mul_f32_e32 v35, 0xc038aa3b, v35
	v_mul_f32_e32 v36, 0x3f4c422a, v36
	v_exp_f32_e32 v35, v35
	v_mul_f32_e32 v36, 0xc038aa3b, v36
	v_exp_f32_e32 v38, v36
	v_fma_f32 v40, v33, v40, v33
	v_mul_f32_e32 v40, 0x3f4c422a, v40
	v_mul_f32_e32 v34, 0x3d372713, v30
	v_add_f32_e32 v35, 1.0, v35
	v_mul_f32_e32 v39, 0x3d372713, v28
	v_mul_f32_e32 v40, 0xc038aa3b, v40
	v_mul_f32_e32 v34, v30, v34
	v_rcp_f32_e32 v36, v35
	v_add_f32_e32 v35, 1.0, v37
	v_add_f32_e32 v37, 1.0, v38
	v_mul_f32_e32 v38, 0x3d372713, v32
	v_mul_f32_e32 v39, v28, v39
	v_exp_f32_e32 v41, v40
	v_mul_f32_e32 v40, 0x3d372713, v29
	v_fma_f32 v34, v30, v34, v30
	v_mul_f32_e32 v38, v32, v38
	v_fma_f32 v39, v28, v39, v28
	v_mul_f32_e32 v40, v29, v40
	v_mul_f32_e32 v34, 0x3f4c422a, v34
	v_fma_f32 v38, v32, v38, v32
	v_mul_f32_e32 v39, 0x3f4c422a, v39
	v_fma_f32 v40, v29, v40, v29
	v_mul_f32_e32 v34, 0xc038aa3b, v34
	v_mul_f32_e32 v38, 0x3f4c422a, v38
	v_mul_f32_e32 v39, 0xc038aa3b, v39
	v_mul_f32_e32 v40, 0x3f4c422a, v40
	v_exp_f32_e32 v34, v34
	v_mul_f32_e32 v38, 0xc038aa3b, v38
	v_exp_f32_e32 v39, v39
	v_mul_f32_e32 v40, 0xc038aa3b, v40
	v_exp_f32_e32 v38, v38
	v_exp_f32_e32 v43, v40
	v_add_f32_e32 v34, 1.0, v34
	v_add_f32_e32 v39, 1.0, v39
	v_rcp_f32_e32 v34, v34
	v_rcp_f32_e32 v35, v35
	v_add_f32_e32 v38, 1.0, v38
	v_rcp_f32_e32 v40, v39
	v_add_f32_e32 v39, 1.0, v41
	v_add_f32_e32 v41, 1.0, v43
	v_rcp_f32_e32 v37, v37
	v_rcp_f32_e32 v38, v38
	v_rcp_f32_e32 v39, v39
	v_rcp_f32_e32 v41, v41
	v_add_u32_e32 v42, 0xa0, v167
	v_pk_mul_f32 v[30:31], v[30:31], v[34:35]
	v_pk_mul_f32 v[34:35], v[26:27], v[36:37]
	v_pk_mul_f32 v[32:33], v[32:33], v[38:39]
	v_pk_mul_f32 v[36:37], v[28:29], v[40:41]
	v_cvt_pk_bf16_f32 v26, v30, v31
	v_mad_i64_i32 v[30:31], s[4:5], v42, s60, v[122:123]
	v_cvt_pk_bf16_f32 v27, v32, v33
	v_cvt_pk_bf16_f32 v28, v34, v35
	v_cvt_pk_bf16_f32 v29, v36, v37
	v_lshl_add_u64 v[30:31], v[30:31], 0, v[124:125]
	global_store_dwordx4 v[30:31], v[26:29], off sc1
	v_mul_f32_e32 v32, 0x3d372713, v22
	v_mul_f32_e32 v32, v22, v32
	v_mul_f32_e32 v28, 0x3d372713, v23
	v_mul_f32_e32 v28, v23, v28
	v_fma_f32 v28, v23, v28, v23
	v_fma_f32 v32, v22, v32, v22
	v_mul_f32_e32 v28, 0x3f4c422a, v28
	v_mul_f32_e32 v32, 0x3f4c422a, v32
	v_mul_f32_e32 v33, 0x3d372713, v18
	v_mul_f32_e32 v28, 0xc038aa3b, v28
	v_mul_f32_e32 v32, 0xc038aa3b, v32
	v_mul_f32_e32 v33, v18, v33
	v_exp_f32_e32 v29, v28
	v_mul_f32_e32 v28, 0x3d372713, v19
	v_exp_f32_e32 v32, v32
	v_fma_f32 v33, v18, v33, v18
	v_mul_f32_e32 v28, v19, v28
	v_mul_f32_e32 v33, 0x3f4c422a, v33
	v_fma_f32 v28, v19, v28, v19
	v_mul_f32_e32 v33, 0xc038aa3b, v33
	v_mul_f32_e32 v28, 0x3f4c422a, v28
	v_exp_f32_e32 v33, v33
	v_mul_f32_e32 v28, 0xc038aa3b, v28
	v_mul_f32_e32 v34, 0x3d372713, v25
	v_add_f32_e32 v26, 1.0, v32
	v_exp_f32_e32 v32, v28
	v_mul_f32_e32 v34, v25, v34
	v_fma_f32 v34, v25, v34, v25
	v_mul_f32_e32 v34, 0x3f4c422a, v34
	v_add_f32_e32 v27, 1.0, v33
	v_mul_f32_e32 v33, 0x3d372713, v20
	v_mul_f32_e32 v34, 0xc038aa3b, v34
	v_rcp_f32_e32 v28, v27
	v_add_f32_e32 v27, 1.0, v29
	v_add_f32_e32 v29, 1.0, v32
	v_mul_f32_e32 v32, 0x3d372713, v24
	v_mul_f32_e32 v33, v20, v33
	v_exp_f32_e32 v35, v34
	v_mul_f32_e32 v34, 0x3d372713, v21
	v_mul_f32_e32 v32, v24, v32
	v_fma_f32 v33, v20, v33, v20
	v_mul_f32_e32 v34, v21, v34
	v_fma_f32 v32, v24, v32, v24
	v_mul_f32_e32 v33, 0x3f4c422a, v33
	v_fma_f32 v34, v21, v34, v21
	v_mul_f32_e32 v32, 0x3f4c422a, v32
	v_mul_f32_e32 v33, 0xc038aa3b, v33
	v_mul_f32_e32 v34, 0x3f4c422a, v34
	v_mul_f32_e32 v32, 0xc038aa3b, v32
	v_exp_f32_e32 v33, v33
	v_mul_f32_e32 v34, 0xc038aa3b, v34
	v_exp_f32_e32 v32, v32
; __device__ __forceinline__ float gelu_fast(float x) { const float u = 0.7978845608028654f * (x + 0.044715f * x * x * x); return x * __builtin_amdgcn_rcpf(1.f + __builtin_amdgcn_exp2f(-2.8853900817779268f * u)); }
; __device__ __forceinline__ u32x4 pack8(const f32x4 a, const f32x4 b) { u32x4 w; w.x = cvt_pk_bf16(a[0], a[1]); w.y = cvt_pk_bf16(a[2], a[3]); w.z = cvt_pk_bf16(b[0], b[1]); w.w = cvt_pk_bf16(b[2], b[3]); return w; }
;     __device__ __forceinline__ void operator()(const f32x4 (&acc)[2][2][4][2], const Unit& u, int wr, int wc, int fr, int fq) const {
;     ...
;             const int rb = (u.pm - 8) * BM + wr * 64 + fr;
; #pragma unroll
;             for (int ai = 0; ai < 2; ++ai)
; #pragma unroll
;                 for (int m = 0; m < 4; ++m)
; #pragma unroll
;                     for (int bj = 0; bj < 2; ++bj) { f32x4 v0 = acc[ai][bj][m][0], v1 = acc[ai][bj][m][1];
; #pragma unroll
;                         for (int j = 0; j < 4; ++j) { v0[j] = gelu_fast(v0[j]); v1[j] = gelu_fast(v1[j]); }
;                         *(u32x4*)(GVT + (size_t)(rb + ai * HALF + m * 16) * MT + col0 + bj * HALF) = pack8(v0, v1); }
	v_exp_f32_e32 v36, v34
	v_add_f32_e32 v33, 1.0, v33
	v_rcp_f32_e32 v34, v33
	v_add_f32_e32 v32, 1.0, v32
	v_add_f32_e32 v33, 1.0, v35
	v_add_f32_e32 v35, 1.0, v36
	v_rcp_f32_e32 v26, v26
	v_rcp_f32_e32 v27, v27
	v_rcp_f32_e32 v29, v29
	v_rcp_f32_e32 v32, v32
	v_rcp_f32_e32 v33, v33
	v_rcp_f32_e32 v35, v35
	v_pk_mul_f32 v[22:23], v[22:23], v[26:27]
	v_pk_mul_f32 v[26:27], v[18:19], v[28:29]
	v_pk_mul_f32 v[24:25], v[24:25], v[32:33]
	v_pk_mul_f32 v[28:29], v[20:21], v[34:35]
	v_cvt_pk_bf16_f32 v18, v22, v23
	v_cvt_pk_bf16_f32 v19, v24, v25
	v_cvt_pk_bf16_f32 v20, v26, v27
	v_cvt_pk_bf16_f32 v21, v28, v29
	global_store_dwordx4 v[30:31], v[18:21], off offset:256 sc1
	v_mul_f32_e32 v24, 0x3d372713, v17
	v_mul_f32_e32 v24, v17, v24
	v_mul_f32_e32 v20, 0x3d372713, v15
	v_mul_f32_e32 v20, v15, v20
	v_fma_f32 v20, v15, v20, v15
	v_mul_f32_e32 v20, 0x3f4c422a, v20
	v_mul_f32_e32 v19, 0x3d372713, v10
	v_mul_f32_e32 v20, 0xc038aa3b, v20
	v_mul_f32_e32 v19, v10, v19
	v_exp_f32_e32 v21, v20
	v_mul_f32_e32 v20, 0x3d372713, v11
	v_fma_f32 v19, v10, v19, v10
	v_mul_f32_e32 v20, v11, v20
	v_mul_f32_e32 v19, 0x3f4c422a, v19
	v_fma_f32 v20, v11, v20, v11
	v_mul_f32_e32 v19, 0xc038aa3b, v19
	v_mul_f32_e32 v20, 0x3f4c422a, v20
	v_exp_f32_e32 v19, v19
	v_mul_f32_e32 v20, 0xc038aa3b, v20
	v_exp_f32_e32 v22, v20
	v_fma_f32 v24, v17, v24, v17
	v_mul_f32_e32 v24, 0x3f4c422a, v24
	v_mul_f32_e32 v18, 0x3d372713, v14
	v_add_f32_e32 v19, 1.0, v19
	v_mul_f32_e32 v23, 0x3d372713, v12
	v_mul_f32_e32 v24, 0xc038aa3b, v24
	v_mul_f32_e32 v18, v14, v18
	v_rcp_f32_e32 v20, v19
	v_add_f32_e32 v19, 1.0, v21
	v_add_f32_e32 v21, 1.0, v22
	v_mul_f32_e32 v22, 0x3d372713, v16
	v_mul_f32_e32 v23, v12, v23
	v_exp_f32_e32 v25, v24
	v_mul_f32_e32 v24, 0x3d372713, v13
	v_fma_f32 v18, v14, v18, v14
	v_mul_f32_e32 v22, v16, v22
	v_fma_f32 v23, v12, v23, v12
	v_mul_f32_e32 v24, v13, v24
	v_mul_f32_e32 v18, 0x3f4c422a, v18
	v_fma_f32 v22, v16, v22, v16
	v_mul_f32_e32 v23, 0x3f4c422a, v23
	v_fma_f32 v24, v13, v24, v13
	v_mul_f32_e32 v18, 0xc038aa3b, v18
	v_mul_f32_e32 v22, 0x3f4c422a, v22
	v_mul_f32_e32 v23, 0xc038aa3b, v23
	v_mul_f32_e32 v24, 0x3f4c422a, v24
	v_exp_f32_e32 v18, v18
	v_mul_f32_e32 v22, 0xc038aa3b, v22
	v_exp_f32_e32 v23, v23
	v_mul_f32_e32 v24, 0xc038aa3b, v24
	v_exp_f32_e32 v22, v22
	v_exp_f32_e32 v27, v24
	v_add_f32_e32 v18, 1.0, v18
	v_add_f32_e32 v23, 1.0, v23
	v_rcp_f32_e32 v18, v18
	v_rcp_f32_e32 v19, v19
	v_add_f32_e32 v22, 1.0, v22
	v_rcp_f32_e32 v24, v23
	v_add_f32_e32 v23, 1.0, v25
	v_add_f32_e32 v25, 1.0, v27
	v_rcp_f32_e32 v21, v21
	v_rcp_f32_e32 v22, v22
	v_rcp_f32_e32 v23, v23
	v_rcp_f32_e32 v25, v25
	v_add_u32_e32 v26, 0xb0, v167
	v_pk_mul_f32 v[14:15], v[14:15], v[18:19]
	v_pk_mul_f32 v[18:19], v[10:11], v[20:21]
	v_pk_mul_f32 v[16:17], v[16:17], v[22:23]
	v_pk_mul_f32 v[20:21], v[12:13], v[24:25]
	v_cvt_pk_bf16_f32 v10, v14, v15
	v_mad_i64_i32 v[14:15], s[4:5], v26, s60, v[122:123]
	v_cvt_pk_bf16_f32 v11, v16, v17
	v_cvt_pk_bf16_f32 v12, v18, v19
	v_cvt_pk_bf16_f32 v13, v20, v21
	v_lshl_add_u64 v[14:15], v[14:15], 0, v[124:125]
	global_store_dwordx4 v[14:15], v[10:13], off sc1
	v_mul_f32_e32 v16, 0x3d372713, v6
	v_mul_f32_e32 v16, v6, v16
	v_mul_f32_e32 v12, 0x3d372713, v7
	v_mul_f32_e32 v12, v7, v12
	v_fma_f32 v12, v7, v12, v7
	v_fma_f32 v16, v6, v16, v6
	v_mul_f32_e32 v12, 0x3f4c422a, v12
	v_mul_f32_e32 v16, 0x3f4c422a, v16
	v_mul_f32_e32 v17, 0x3d372713, v2
	v_mul_f32_e32 v12, 0xc038aa3b, v12
	v_mul_f32_e32 v16, 0xc038aa3b, v16
	v_mul_f32_e32 v17, v2, v17
	v_exp_f32_e32 v13, v12
	v_mul_f32_e32 v12, 0x3d372713, v3
	v_exp_f32_e32 v16, v16
	v_fma_f32 v17, v2, v17, v2
	v_mul_f32_e32 v12, v3, v12
	v_mul_f32_e32 v17, 0x3f4c422a, v17
	v_fma_f32 v12, v3, v12, v3
	v_mul_f32_e32 v17, 0xc038aa3b, v17
	v_mul_f32_e32 v12, 0x3f4c422a, v12
	v_exp_f32_e32 v17, v17
	v_mul_f32_e32 v12, 0xc038aa3b, v12
	v_mul_f32_e32 v18, 0x3d372713, v9
	v_add_f32_e32 v10, 1.0, v16
	v_exp_f32_e32 v16, v12
	v_mul_f32_e32 v18, v9, v18
	v_fma_f32 v18, v9, v18, v9
	v_mul_f32_e32 v18, 0x3f4c422a, v18
	v_add_f32_e32 v11, 1.0, v17
	v_mul_f32_e32 v17, 0x3d372713, v4
	v_mul_f32_e32 v18, 0xc038aa3b, v18
	v_rcp_f32_e32 v12, v11
	v_add_f32_e32 v11, 1.0, v13
	v_add_f32_e32 v13, 1.0, v16
	v_mul_f32_e32 v16, 0x3d372713, v8
	v_mul_f32_e32 v17, v4, v17
	v_exp_f32_e32 v19, v18
	v_mul_f32_e32 v18, 0x3d372713, v5
	v_mul_f32_e32 v16, v8, v16
	v_fma_f32 v17, v4, v17, v4
	v_mul_f32_e32 v18, v5, v18
	v_fma_f32 v16, v8, v16, v8
	v_mul_f32_e32 v17, 0x3f4c422a, v17
	v_fma_f32 v18, v5, v18, v5
	v_mul_f32_e32 v16, 0x3f4c422a, v16
	v_mul_f32_e32 v17, 0xc038aa3b, v17
	v_mul_f32_e32 v18, 0x3f4c422a, v18
	v_mul_f32_e32 v16, 0xc038aa3b, v16
	v_exp_f32_e32 v17, v17
	v_mul_f32_e32 v18, 0xc038aa3b, v18
	v_exp_f32_e32 v16, v16
	v_exp_f32_e32 v20, v18
	v_add_f32_e32 v17, 1.0, v17
	v_rcp_f32_e32 v18, v17
	v_add_f32_e32 v16, 1.0, v16
	v_add_f32_e32 v17, 1.0, v19
	v_add_f32_e32 v19, 1.0, v20
	v_rcp_f32_e32 v10, v10
	v_rcp_f32_e32 v11, v11
	v_rcp_f32_e32 v13, v13
	v_rcp_f32_e32 v16, v16
	v_rcp_f32_e32 v17, v17
	v_rcp_f32_e32 v19, v19
	v_pk_mul_f32 v[6:7], v[6:7], v[10:11]
	v_pk_mul_f32 v[10:11], v[2:3], v[12:13]
	v_pk_mul_f32 v[8:9], v[8:9], v[16:17]
	v_pk_mul_f32 v[12:13], v[4:5], v[18:19]
	v_cvt_pk_bf16_f32 v2, v6, v7
	v_cvt_pk_bf16_f32 v3, v8, v9
	v_cvt_pk_bf16_f32 v4, v10, v11
	v_cvt_pk_bf16_f32 v5, v12, v13
	global_store_dwordx4 v[14:15], v[2:5], off offset:256 sc1
	s_andn2_b64 vcc, exec, s[22:23]
	s_mov_b64 s[4:5], -1
	s_cbranch_vccnz .LBB0_208

; __device__ __forceinline__ u32x4 pack8(const f32x4 a, const f32x4 b) { u32x4 w; w.x = cvt_pk_bf16(a[0], a[1]); w.y = cvt_pk_bf16(a[2], a[3]); w.z = cvt_pk_bf16(b[0], b[1]); w.w = cvt_pk_bf16(b[2], b[3]); return w; }
;     __device__ __forceinline__ void fused(f32x4 (&acc)[2][2][4][2], const pg8::Unit& u_, int wr_, int wc_, int fr_, int fq_, LAS unsigned char* lds, int tid_) const {
;     ...
;         {   const float* gp = gate + bidx * MODW + col0; f32x4 gv[2][2];
; #pragma unroll
;             for (int bj = 0; bj < 2; ++bj)
; #pragma unroll
;                 for (int n = 0; n < 2; ++n) gv[bj][n] = *(const f32x4*)(gp + bj * HALF + 4 * n);
; #pragma unroll
;             for (int ai = 0; ai < 2; ++ai)
; #pragma unroll
;                 for (int m = 0; m < 4; ++m) { bf16_t* rowp = X + (size_t)(row0 + ai * HALF + m * 16) * D + col0;
; #pragma unroll
;                     for (int bj = 0; bj < 2; ++bj) { f32x4 s0, s1;
;                         if (LAYER == 0) { const float* sp = (isctx ? srcC + (size_t)(row0 - ML + ai * HALF + m * 16) * D : srcL + (size_t)(row0 + ai * HALF + m * 16) * D) + col0 + bj * HALF;
;                             s0 = __builtin_nontemporal_load((const f32x4*)sp); s1 = __builtin_nontemporal_load((const f32x4*)(sp + 4)); }
;                         else { const u32x4 xb = *(const u32x4*)(rowp + bj * HALF);
;                             s0 = (f32x4){__uint_as_float(xb.x << 16), __uint_as_float(xb.x & 0xffff0000u), __uint_as_float(xb.y << 16), __uint_as_float(xb.y & 0xffff0000u)};
;                             s1 = (f32x4){__uint_as_float(xb.z << 16), __uint_as_float(xb.z & 0xffff0000u), __uint_as_float(xb.w << 16), __uint_as_float(xb.w & 0xffff0000u)}; }
;                         const u32x4 w = pack8(s0 + gv[bj][0] * acc[ai][bj][m][0], s1 + gv[bj][1] * acc[ai][bj][m][1]);
;                         *(u32x4*)(rowp + bj * HALF) = w;
;                         acc[ai][bj][m][0] = (f32x4){__uint_as_float(w.x << 16), __uint_as_float(w.x & 0xffff0000u), __uint_as_float(w.y << 16), __uint_as_float(w.y & 0xffff0000u)};
;                         acc[ai][bj][m][1] = (f32x4){__uint_as_float(w.z << 16), __uint_as_float(w.z & 0xffff0000u), __uint_as_float(w.w << 16), __uint_as_float(w.w & 0xffff0000u)}; } }
;         }
;         asm volatile("s_waitcnt vmcnt(0)" ::: "memory"); __builtin_amdgcn_s_barrier(); asm volatile("" ::: "memory");
.LBB0_465:
	s_lshl_b32 s29, s80, 8
	v_lshlrev_b32_e64 v183, 5, s42
	v_lshlrev_b32_e32 v182, 3, v180
	s_lshl_b32 s27, s36, 8
	v_lshl_add_u32 v220, s4, 6, v181
	v_add3_u32 v168, v182, v183, s29
	s_lshl_b64 s[2:3], s[2:3], 2
	v_add_u32_e32 v174, s27, v220
	s_add_u32 s4, s59, s2
	v_ashrrev_i32_e32 v169, 31, v168
	s_addc_u32 s5, s60, s3
	v_lshlrev_b64 v[172:173], 2, v[168:169]
	v_ashrrev_i32_e32 v175, 31, v174
	v_readlane_b32 s8, v250, 10
	v_lshl_add_u64 v[134:135], s[4:5], 0, v[172:173]
	v_lshlrev_b64 v[130:131], 12, v[174:175]
	v_readlane_b32 s12, v250, 14
	v_readlane_b32 s13, v250, 15
	s_brev_b32 s4, 63
	v_readlane_b32 s9, v250, 11
	v_lshl_add_u64 v[178:179], s[12:13], 0, v[130:131]
	s_mov_b32 s5, -1
	v_lshl_add_u64 v[132:133], v[178:179], 0, s[4:5]
	v_lshl_add_u64 v[130:131], s[8:9], 0, v[130:131]
	v_cndmask_b32_e64 v131, v131, v133, s[6:7]
	v_cndmask_b32_e64 v130, v130, v132, s[6:7]
	v_lshl_add_u64 v[192:193], v[130:131], 0, v[172:173]
	global_load_dwordx4 v[184:187], v[192:193], off nt
	global_load_dwordx4 v[142:145], v[134:135], off
	global_load_dwordx4 v[138:141], v[134:135], off offset:16
	global_load_dwordx4 v[188:191], v[192:193], off offset:16 nt
	v_lshl_add_u64 v[176:177], v[168:169], 1, s[94:95]
	v_lshlrev_b64 v[170:171], 11, v[174:175]
	v_lshl_add_u64 v[194:195], v[176:177], 0, v[170:171]
	global_load_dwordx4 v[130:133], v[134:135], off offset:528
	s_nop 0
	global_load_dwordx4 v[134:137], v[134:135], off offset:512
	s_mov_b32 s4, 0xfc010000
	s_mov_b32 s5, -1
	s_add_u32 s38, s84, s2
	v_readlane_b32 s22, v250, 24
	v_readlane_b32 s23, v250, 25
	s_addc_u32 s39, s85, s3
	v_and_b32_e32 v158, 15, v221
	v_readlane_b32 s10, v250, 12
	v_readlane_b32 s11, v250, 13
	v_readlane_b32 s14, v250, 16
	v_readlane_b32 s15, v250, 17
	v_readlane_b32 s16, v250, 18
	v_readlane_b32 s17, v250, 19
	v_readlane_b32 s18, v250, 20
	v_readlane_b32 s19, v250, 21
	v_readlane_b32 s20, v250, 22
	v_readlane_b32 s21, v250, 23
	s_waitcnt vmcnt(0)
	v_pk_fma_f32 v[128:129], v[128:129], v[144:145], v[186:187]
	v_pk_fma_f32 v[126:127], v[126:127], v[142:143], v[184:185]
	v_pk_fma_f32 v[184:185], v[60:61], v[140:141], v[190:191]
	v_pk_fma_f32 v[60:61], v[58:59], v[138:139], v[188:189]
	v_cvt_pk_bf16_f32 v58, v126, v127
	v_cvt_pk_bf16_f32 v59, v128, v129
	v_cvt_pk_bf16_f32 v60, v60, v61
	v_cvt_pk_bf16_f32 v61, v184, v185
	global_store_dwordx4 v[194:195], v[58:61], off sc1
	global_load_dwordx4 v[126:129], v[192:193], off offset:512 nt
	global_load_dwordx4 v[184:187], v[192:193], off offset:528 nt
	v_add_u32_e32 v188, 16, v174
	v_ashrrev_i32_e32 v189, 31, v188
	v_lshlrev_b64 v[190:191], 12, v[188:189]
	v_lshl_add_u64 v[192:193], v[178:179], 0, s[4:5]
	v_lshl_add_u64 v[190:191], s[8:9], 0, v[190:191]
	v_cndmask_b32_e64 v191, v191, v193, s[6:7]
	v_cndmask_b32_e64 v190, v190, v192, s[6:7]
	v_lshl_add_u64 v[190:191], v[190:191], 0, v[172:173]
	s_mov_b32 s4, 0xfc020000
	s_mov_b32 s5, -1
	s_waitcnt vmcnt(1)
	v_pk_fma_f32 v[68:69], v[68:69], v[136:137], v[128:129]
	v_pk_fma_f32 v[66:67], v[66:67], v[134:135], v[126:127]
	s_waitcnt vmcnt(0)
	v_pk_fma_f32 v[52:53], v[52:53], v[132:133], v[186:187]
	v_pk_fma_f32 v[50:51], v[50:51], v[130:131], v[184:185]
	v_cvt_pk_bf16_f32 v66, v66, v67
	v_cvt_pk_bf16_f32 v67, v68, v69
	v_cvt_pk_bf16_f32 v68, v50, v51
	v_cvt_pk_bf16_f32 v69, v52, v53
	global_store_dwordx4 v[194:195], v[66:69], off offset:256 sc1
	global_load_dwordx4 v[50:53], v[190:191], off nt
	global_load_dwordx4 v[126:129], v[190:191], off offset:16 nt
	v_lshlrev_b64 v[184:185], 11, v[188:189]
	v_lshl_add_u64 v[184:185], v[176:177], 0, v[184:185]
	v_lshl_add_u64 v[186:187], v[178:179], 0, s[4:5]
	s_mov_b32 s4, 0xfc030000
	s_mov_b32 s5, -1
	s_waitcnt vmcnt(1)
	v_pk_fma_f32 v[52:53], v[124:125], v[144:145], v[52:53]
	v_pk_fma_f32 v[50:51], v[122:123], v[142:143], v[50:51]
	s_waitcnt vmcnt(0)
	v_pk_fma_f32 v[120:121], v[120:121], v[140:141], v[128:129]
	v_pk_fma_f32 v[118:119], v[118:119], v[138:139], v[126:127]
	v_cvt_pk_bf16_f32 v50, v50, v51
	v_cvt_pk_bf16_f32 v51, v52, v53
	v_cvt_pk_bf16_f32 v52, v118, v119
	v_cvt_pk_bf16_f32 v53, v120, v121
	global_store_dwordx4 v[184:185], v[50:53], off sc1
	global_load_dwordx4 v[118:121], v[190:191], off offset:512 nt
	global_load_dwordx4 v[122:125], v[190:191], off offset:528 nt
	v_add_u32_e32 v126, 32, v174
	v_ashrrev_i32_e32 v127, 31, v126
	v_lshlrev_b64 v[128:129], 12, v[126:127]
	v_lshl_add_u64 v[128:129], s[8:9], 0, v[128:129]
	v_cndmask_b32_e64 v129, v129, v187, s[6:7]
	v_cndmask_b32_e64 v128, v128, v186, s[6:7]
	v_lshl_add_u64 v[128:129], v[128:129], 0, v[172:173]
	s_waitcnt vmcnt(1)
	v_pk_fma_f32 v[56:57], v[56:57], v[136:137], v[120:121]
	v_pk_fma_f32 v[54:55], v[54:55], v[134:135], v[118:119]
	s_waitcnt vmcnt(0)
	v_pk_fma_f32 v[44:45], v[44:45], v[132:133], v[124:125]
	v_pk_fma_f32 v[42:43], v[42:43], v[130:131], v[122:123]
	v_cvt_pk_bf16_f32 v54, v54, v55
	v_cvt_pk_bf16_f32 v55, v56, v57
	v_cvt_pk_bf16_f32 v56, v42, v43
	v_cvt_pk_bf16_f32 v57, v44, v45
	global_store_dwordx4 v[184:185], v[54:57], off offset:256 sc1
	global_load_dwordx4 v[42:45], v[128:129], off nt
	global_load_dwordx4 v[118:121], v[128:129], off offset:16 nt
	v_lshlrev_b64 v[122:123], 11, v[126:127]
	v_lshl_add_u64 v[122:123], v[176:177], 0, v[122:123]
	v_lshl_add_u64 v[124:125], v[178:179], 0, s[4:5]
	s_mov_b32 s4, 0xfc080000
	s_mov_b32 s5, -1
	s_waitcnt vmcnt(1)
	v_pk_fma_f32 v[44:45], v[116:117], v[144:145], v[44:45]
	v_pk_fma_f32 v[42:43], v[114:115], v[142:143], v[42:43]
	s_waitcnt vmcnt(0)
; __device__ __forceinline__ u32x4 pack8(const f32x4 a, const f32x4 b) { u32x4 w; w.x = cvt_pk_bf16(a[0], a[1]); w.y = cvt_pk_bf16(a[2], a[3]); w.z = cvt_pk_bf16(b[0], b[1]); w.w = cvt_pk_bf16(b[2], b[3]); return w; }
;     __device__ __forceinline__ void fused(f32x4 (&acc)[2][2][4][2], const pg8::Unit& u_, int wr_, int wc_, int fr_, int fq_, LAS unsigned char* lds, int tid_) const {
;     ...
;             for (int ai = 0; ai < 2; ++ai)
; #pragma unroll
;                 for (int m = 0; m < 4; ++m) { bf16_t* rowp = X + (size_t)(row0 + ai * HALF + m * 16) * D + col0;
; #pragma unroll
;                     for (int bj = 0; bj < 2; ++bj) { f32x4 s0, s1;
;                         if (LAYER == 0) { const float* sp = (isctx ? srcC + (size_t)(row0 - ML + ai * HALF + m * 16) * D : srcL + (size_t)(row0 + ai * HALF + m * 16) * D) + col0 + bj * HALF;
;                             s0 = __builtin_nontemporal_load((const f32x4*)sp); s1 = __builtin_nontemporal_load((const f32x4*)(sp + 4)); }
;                         else { const u32x4 xb = *(const u32x4*)(rowp + bj * HALF);
;                             s0 = (f32x4){__uint_as_float(xb.x << 16), __uint_as_float(xb.x & 0xffff0000u), __uint_as_float(xb.y << 16), __uint_as_float(xb.y & 0xffff0000u)};
;                             s1 = (f32x4){__uint_as_float(xb.z << 16), __uint_as_float(xb.z & 0xffff0000u), __uint_as_float(xb.w << 16), __uint_as_float(xb.w & 0xffff0000u)}; }
;                         const u32x4 w = pack8(s0 + gv[bj][0] * acc[ai][bj][m][0], s1 + gv[bj][1] * acc[ai][bj][m][1]);
;                         *(u32x4*)(rowp + bj * HALF) = w;
;                         acc[ai][bj][m][0] = (f32x4){__uint_as_float(w.x << 16), __uint_as_float(w.x & 0xffff0000u), __uint_as_float(w.y << 16), __uint_as_float(w.y & 0xffff0000u)};
;                         acc[ai][bj][m][1] = (f32x4){__uint_as_float(w.z << 16), __uint_as_float(w.z & 0xffff0000u), __uint_as_float(w.w << 16), __uint_as_float(w.w & 0xffff0000u)}; } }
	v_pk_fma_f32 v[112:113], v[112:113], v[140:141], v[120:121]
	v_pk_fma_f32 v[110:111], v[110:111], v[138:139], v[118:119]
	v_cvt_pk_bf16_f32 v42, v42, v43
	v_cvt_pk_bf16_f32 v43, v44, v45
	v_cvt_pk_bf16_f32 v44, v110, v111
	v_cvt_pk_bf16_f32 v45, v112, v113
	global_store_dwordx4 v[122:123], v[42:45], off sc1
	global_load_dwordx4 v[110:113], v[128:129], off offset:512 nt
	global_load_dwordx4 v[114:117], v[128:129], off offset:528 nt
	v_add_u32_e32 v118, 48, v174
	v_ashrrev_i32_e32 v119, 31, v118
	v_lshlrev_b64 v[120:121], 12, v[118:119]
	v_lshl_add_u64 v[120:121], s[8:9], 0, v[120:121]
	v_cndmask_b32_e64 v121, v121, v125, s[6:7]
	v_cndmask_b32_e64 v120, v120, v124, s[6:7]
	v_lshl_add_u64 v[120:121], v[120:121], 0, v[172:173]
	s_waitcnt vmcnt(1)
	v_pk_fma_f32 v[48:49], v[48:49], v[136:137], v[112:113]
	v_pk_fma_f32 v[46:47], v[46:47], v[134:135], v[110:111]
	s_waitcnt vmcnt(0)
	v_pk_fma_f32 v[36:37], v[36:37], v[132:133], v[116:117]
	v_pk_fma_f32 v[34:35], v[34:35], v[130:131], v[114:115]
	v_cvt_pk_bf16_f32 v46, v46, v47
	v_cvt_pk_bf16_f32 v47, v48, v49
	v_cvt_pk_bf16_f32 v48, v34, v35
	v_cvt_pk_bf16_f32 v49, v36, v37
	global_store_dwordx4 v[122:123], v[46:49], off offset:256 sc1
	global_load_dwordx4 v[34:37], v[120:121], off nt
	global_load_dwordx4 v[110:113], v[120:121], off offset:16 nt
	v_lshlrev_b64 v[114:115], 11, v[118:119]
	v_lshl_add_u64 v[114:115], v[176:177], 0, v[114:115]
	v_lshl_add_u64 v[116:117], v[178:179], 0, s[4:5]
	s_mov_b32 s4, 0xfc090000
	s_mov_b32 s5, -1
	s_waitcnt vmcnt(1)
	v_pk_fma_f32 v[36:37], v[108:109], v[144:145], v[36:37]
	v_pk_fma_f32 v[34:35], v[106:107], v[142:143], v[34:35]
	s_waitcnt vmcnt(0)
	v_pk_fma_f32 v[104:105], v[104:105], v[140:141], v[112:113]
	v_pk_fma_f32 v[102:103], v[102:103], v[138:139], v[110:111]
	v_cvt_pk_bf16_f32 v34, v34, v35
	v_cvt_pk_bf16_f32 v35, v36, v37
	v_cvt_pk_bf16_f32 v36, v102, v103
	v_cvt_pk_bf16_f32 v37, v104, v105
	global_store_dwordx4 v[114:115], v[34:37], off sc1
	global_load_dwordx4 v[102:105], v[120:121], off offset:512 nt
	global_load_dwordx4 v[106:109], v[120:121], off offset:528 nt
	v_add_u32_e32 v110, 0x80, v174
	v_ashrrev_i32_e32 v111, 31, v110
	v_lshlrev_b64 v[112:113], 12, v[110:111]
	v_lshl_add_u64 v[112:113], s[8:9], 0, v[112:113]
	v_cndmask_b32_e64 v113, v113, v117, s[6:7]
	v_cndmask_b32_e64 v112, v112, v116, s[6:7]
	v_lshl_add_u64 v[112:113], v[112:113], 0, v[172:173]
	s_waitcnt vmcnt(1)
	v_pk_fma_f32 v[100:101], v[100:101], v[136:137], v[104:105]
	v_pk_fma_f32 v[98:99], v[98:99], v[134:135], v[102:103]
	s_waitcnt vmcnt(0)
	v_pk_fma_f32 v[102:103], v[40:41], v[132:133], v[108:109]
	v_pk_fma_f32 v[40:41], v[38:39], v[130:131], v[106:107]
	v_cvt_pk_bf16_f32 v38, v98, v99
	v_cvt_pk_bf16_f32 v39, v100, v101
	v_cvt_pk_bf16_f32 v40, v40, v41
	v_cvt_pk_bf16_f32 v41, v102, v103
	global_store_dwordx4 v[114:115], v[38:41], off offset:256 sc1
	global_load_dwordx4 v[98:101], v[112:113], off nt
	global_load_dwordx4 v[102:105], v[112:113], off offset:16 nt
	v_lshlrev_b64 v[106:107], 11, v[110:111]
	v_lshl_add_u64 v[106:107], v[176:177], 0, v[106:107]
	v_lshl_add_u64 v[108:109], v[178:179], 0, s[4:5]
	s_mov_b32 s4, 0xfc0a0000
	s_mov_b32 s5, -1
	s_waitcnt vmcnt(1)
	v_pk_fma_f32 v[96:97], v[96:97], v[144:145], v[100:101]
	v_pk_fma_f32 v[94:95], v[94:95], v[142:143], v[98:99]
	s_waitcnt vmcnt(0)
	v_pk_fma_f32 v[98:99], v[28:29], v[140:141], v[104:105]
	v_pk_fma_f32 v[28:29], v[26:27], v[138:139], v[102:103]
	v_cvt_pk_bf16_f32 v26, v94, v95
	v_cvt_pk_bf16_f32 v27, v96, v97
	v_cvt_pk_bf16_f32 v28, v28, v29
	v_cvt_pk_bf16_f32 v29, v98, v99
	global_store_dwordx4 v[106:107], v[26:29], off sc1
	global_load_dwordx4 v[94:97], v[112:113], off offset:512 nt
	global_load_dwordx4 v[98:101], v[112:113], off offset:528 nt
	v_add_u32_e32 v102, 0x90, v174
	v_ashrrev_i32_e32 v103, 31, v102
	v_lshlrev_b64 v[104:105], 12, v[102:103]
	v_lshl_add_u64 v[104:105], s[8:9], 0, v[104:105]
	v_cndmask_b32_e64 v105, v105, v109, s[6:7]
	v_cndmask_b32_e64 v104, v104, v108, s[6:7]
	v_lshl_add_u64 v[104:105], v[104:105], 0, v[172:173]
	s_waitcnt vmcnt(1)
	v_pk_fma_f32 v[32:33], v[32:33], v[136:137], v[96:97]
	v_pk_fma_f32 v[30:31], v[30:31], v[134:135], v[94:95]
	s_waitcnt vmcnt(0)
	v_pk_fma_f32 v[20:21], v[20:21], v[132:133], v[100:101]
	v_pk_fma_f32 v[18:19], v[18:19], v[130:131], v[98:99]
	v_cvt_pk_bf16_f32 v30, v30, v31
	v_cvt_pk_bf16_f32 v31, v32, v33
	v_cvt_pk_bf16_f32 v32, v18, v19
	v_cvt_pk_bf16_f32 v33, v20, v21
	global_store_dwordx4 v[106:107], v[30:33], off offset:256 sc1
	global_load_dwordx4 v[18:21], v[104:105], off nt
	global_load_dwordx4 v[94:97], v[104:105], off offset:16 nt
	v_lshlrev_b64 v[98:99], 11, v[102:103]
	v_lshl_add_u64 v[98:99], v[176:177], 0, v[98:99]
	v_lshl_add_u64 v[100:101], v[178:179], 0, s[4:5]
	s_mov_b32 s4, 0xfc0b0000
	s_mov_b32 s5, -1
	s_waitcnt vmcnt(1)
; __device__ __forceinline__ float bf2f(bf16_t v) { return __uint_as_float((unsigned)v << 16); }
;     __device__ __forceinline__ void fused(f32x4 (&acc)[2][2][4][2], const pg8::Unit& u_, int wr_, int wc_, int fr_, int fq_, LAS unsigned char* lds, int tid_) const {
;     ...
;             for (int ai = 0; ai < 2; ++ai)
; #pragma unroll
;                 for (int m = 0; m < 4; ++m) { bf16_t* rowp = X + (size_t)(row0 + ai * HALF + m * 16) * D + col0;
; #pragma unroll
;                     for (int bj = 0; bj < 2; ++bj) { f32x4 s0, s1;
;                         if (LAYER == 0) { const float* sp = (isctx ? srcC + (size_t)(row0 - ML + ai * HALF + m * 16) * D : srcL + (size_t)(row0 + ai * HALF + m * 16) * D) + col0 + bj * HALF;
;                             s0 = __builtin_nontemporal_load((const f32x4*)sp); s1 = __builtin_nontemporal_load((const f32x4*)(sp + 4)); }
;                         else { const u32x4 xb = *(const u32x4*)(rowp + bj * HALF);
;                             s0 = (f32x4){__uint_as_float(xb.x << 16), __uint_as_float(xb.x & 0xffff0000u), __uint_as_float(xb.y << 16), __uint_as_float(xb.y & 0xffff0000u)};
;                             s1 = (f32x4){__uint_as_float(xb.z << 16), __uint_as_float(xb.z & 0xffff0000u), __uint_as_float(xb.w << 16), __uint_as_float(xb.w & 0xffff0000u)}; }
;                         const u32x4 w = pack8(s0 + gv[bj][0] * acc[ai][bj][m][0], s1 + gv[bj][1] * acc[ai][bj][m][1]);
;                         *(u32x4*)(rowp + bj * HALF) = w;
;                         acc[ai][bj][m][0] = (f32x4){__uint_as_float(w.x << 16), __uint_as_float(w.x & 0xffff0000u), __uint_as_float(w.y << 16), __uint_as_float(w.y & 0xffff0000u)};
;                         acc[ai][bj][m][1] = (f32x4){__uint_as_float(w.z << 16), __uint_as_float(w.z & 0xffff0000u), __uint_as_float(w.w << 16), __uint_as_float(w.w & 0xffff0000u)}; } }
;         }
;         asm volatile("s_waitcnt vmcnt(0)" ::: "memory"); __builtin_amdgcn_s_barrier(); asm volatile("" ::: "memory");
;     ...
;         for (int idx = tid; idx < 4096; idx += NTHR) { const int e = idx & 15, c = idx >> 4, cg = u.pn * BM + c; const float wv = wrt[cg * 16 + e] * g2[cg] * (mrow[4 * D + cg] + 1.f);
;             const bf16_t hi = f2bf(wv); WLh[e * 264 + c] = hi; WLl[e * 264 + c] = f2bf(wv - bf2f(hi)); }
	v_pk_fma_f32 v[20:21], v[92:93], v[144:145], v[20:21]
	v_pk_fma_f32 v[18:19], v[90:91], v[142:143], v[18:19]
	s_waitcnt vmcnt(0)
	v_pk_fma_f32 v[88:89], v[88:89], v[140:141], v[96:97]
	v_pk_fma_f32 v[86:87], v[86:87], v[138:139], v[94:95]
	v_cvt_pk_bf16_f32 v18, v18, v19
	v_cvt_pk_bf16_f32 v19, v20, v21
	v_cvt_pk_bf16_f32 v20, v86, v87
	v_cvt_pk_bf16_f32 v21, v88, v89
	global_store_dwordx4 v[98:99], v[18:21], off sc1
	global_load_dwordx4 v[86:89], v[104:105], off offset:512 nt
	global_load_dwordx4 v[90:93], v[104:105], off offset:528 nt
	v_add_u32_e32 v94, 0xa0, v174
	v_ashrrev_i32_e32 v95, 31, v94
	v_lshlrev_b64 v[96:97], 12, v[94:95]
	v_lshl_add_u64 v[96:97], s[8:9], 0, v[96:97]
	v_cndmask_b32_e64 v97, v97, v101, s[6:7]
	v_cndmask_b32_e64 v96, v96, v100, s[6:7]
	v_lshl_add_u64 v[96:97], v[96:97], 0, v[172:173]
	s_waitcnt vmcnt(1)
	v_pk_fma_f32 v[24:25], v[24:25], v[136:137], v[88:89]
	v_pk_fma_f32 v[22:23], v[22:23], v[134:135], v[86:87]
	s_waitcnt vmcnt(0)
	v_pk_fma_f32 v[12:13], v[12:13], v[132:133], v[92:93]
	v_pk_fma_f32 v[10:11], v[10:11], v[130:131], v[90:91]
	v_cvt_pk_bf16_f32 v22, v22, v23
	v_cvt_pk_bf16_f32 v23, v24, v25
	v_cvt_pk_bf16_f32 v24, v10, v11
	v_cvt_pk_bf16_f32 v25, v12, v13
	global_store_dwordx4 v[98:99], v[22:25], off offset:256 sc1
	global_load_dwordx4 v[10:13], v[96:97], off nt
	global_load_dwordx4 v[86:89], v[96:97], off offset:16 nt
	v_lshlrev_b64 v[90:91], 11, v[94:95]
	v_lshl_add_u64 v[90:91], v[176:177], 0, v[90:91]
	v_lshl_add_u64 v[92:93], v[178:179], 0, s[4:5]
	s_movk_i32 s4, 0x1000
	v_cmp_gt_i32_e32 vcc, s4, v221
	s_waitcnt vmcnt(1)
	v_pk_fma_f32 v[12:13], v[84:85], v[144:145], v[12:13]
	v_pk_fma_f32 v[10:11], v[82:83], v[142:143], v[10:11]
	s_waitcnt vmcnt(0)
	v_pk_fma_f32 v[80:81], v[80:81], v[140:141], v[88:89]
	v_pk_fma_f32 v[78:79], v[78:79], v[138:139], v[86:87]
	v_cvt_pk_bf16_f32 v10, v10, v11
	v_cvt_pk_bf16_f32 v11, v12, v13
	v_cvt_pk_bf16_f32 v12, v78, v79
	v_cvt_pk_bf16_f32 v13, v80, v81
	global_store_dwordx4 v[90:91], v[10:13], off sc1
	global_load_dwordx4 v[78:81], v[96:97], off offset:512 nt
	global_load_dwordx4 v[82:85], v[96:97], off offset:528 nt
	v_add_u32_e32 v86, 0xb0, v174
	v_ashrrev_i32_e32 v87, 31, v86
	v_lshlrev_b64 v[88:89], 12, v[86:87]
	v_lshl_add_u64 v[88:89], s[8:9], 0, v[88:89]
	v_cndmask_b32_e64 v89, v89, v93, s[6:7]
	v_cndmask_b32_e64 v88, v88, v92, s[6:7]
	v_lshl_add_u64 v[88:89], v[88:89], 0, v[172:173]
	s_waitcnt vmcnt(1)
	v_pk_fma_f32 v[16:17], v[16:17], v[136:137], v[80:81]
	v_pk_fma_f32 v[14:15], v[14:15], v[134:135], v[78:79]
	s_waitcnt vmcnt(0)
	v_pk_fma_f32 v[4:5], v[4:5], v[132:133], v[84:85]
	v_pk_fma_f32 v[2:3], v[2:3], v[130:131], v[82:83]
	v_cvt_pk_bf16_f32 v14, v14, v15
	v_cvt_pk_bf16_f32 v15, v16, v17
	v_cvt_pk_bf16_f32 v16, v2, v3
	v_cvt_pk_bf16_f32 v17, v4, v5
	global_store_dwordx4 v[90:91], v[14:17], off offset:256 sc1
	global_load_dwordx4 v[2:5], v[88:89], off nt
	global_load_dwordx4 v[78:81], v[88:89], off offset:16 nt
	v_lshlrev_b64 v[82:83], 11, v[86:87]
	v_lshl_add_u64 v[82:83], v[176:177], 0, v[82:83]
	s_waitcnt vmcnt(1)
	v_pk_fma_f32 v[4:5], v[76:77], v[144:145], v[4:5]
	v_pk_fma_f32 v[2:3], v[74:75], v[142:143], v[2:3]
	s_waitcnt vmcnt(0)
	v_pk_fma_f32 v[72:73], v[72:73], v[140:141], v[80:81]
	v_pk_fma_f32 v[70:71], v[70:71], v[138:139], v[78:79]
	v_cvt_pk_bf16_f32 v2, v2, v3
	v_cvt_pk_bf16_f32 v3, v4, v5
	v_cvt_pk_bf16_f32 v4, v70, v71
	v_cvt_pk_bf16_f32 v5, v72, v73
	global_store_dwordx4 v[82:83], v[2:5], off sc1
	global_load_dwordx4 v[70:73], v[88:89], off offset:512 nt
	global_load_dwordx4 v[74:77], v[88:89], off offset:528 nt
	s_waitcnt vmcnt(1)
	v_pk_fma_f32 v[64:65], v[64:65], v[136:137], v[72:73]
	v_pk_fma_f32 v[62:63], v[62:63], v[134:135], v[70:71]
	s_waitcnt vmcnt(0)
	v_pk_fma_f32 v[70:71], v[8:9], v[132:133], v[76:77]
	v_pk_fma_f32 v[8:9], v[6:7], v[130:131], v[74:75]
	v_cvt_pk_bf16_f32 v6, v62, v63
	v_cvt_pk_bf16_f32 v7, v64, v65
	v_cvt_pk_bf16_f32 v8, v8, v9
	v_cvt_pk_bf16_f32 v9, v70, v71
	global_store_dwordx4 v[82:83], v[6:9], off offset:256 sc1
	s_waitcnt vmcnt(0)
	s_barrier
	s_and_saveexec_b64 s[4:5], vcc
	s_cbranch_execz .LBB0_468
	v_mul_u32_u24_e32 v62, 0x108, v158
	s_mov_b64 s[6:7], 0
	v_mov_b32_e32 v63, v221

; __device__ __forceinline__ u32x4 pack8(const f32x4 a, const f32x4 b) { u32x4 w; w.x = cvt_pk_bf16(a[0], a[1]); w.y = cvt_pk_bf16(a[2], a[3]); w.z = cvt_pk_bf16(b[0], b[1]); w.w = cvt_pk_bf16(b[2], b[3]); return w; }
;     __device__ __forceinline__ void fused(f32x4 (&acc)[2][2][4][2], const pg8::Unit& u_, int wr_, int wc_, int fr_, int fq_, LAS unsigned char* lds, int tid_) const {
;     ...
; #pragma unroll
;         for (int bj = 0; bj < 2; ++bj) { f32x4 G[2], SH[2];
; #pragma unroll
;             for (int n = 0; n < 2; ++n) { const int c = col0 + bj * HALF + 4 * n; const f32x4 gg = *(const f32x4*)(g2 + c), sc = *(const f32x4*)(mrow + 4 * D + c);
;                 G[n] = gg * (sc + 1.f); SH[n] = *(const f32x4*)(mrow + 3 * D + c); }
; #pragma unroll
;             for (int ai = 0; ai < 2; ++ai)
; #pragma unroll
;                 for (int m = 0; m < 4; ++m) { const int rl = ai * HALF + wr * 64 + m * 16 + fr; const float r = bad ? __builtin_nanf("") : Sr[rl];
;                     *(u32x4*)(HB + (size_t)(u.pm * BM + rl) * D + col0 + bj * HALF) = pack8(acc[ai][bj][m][0] * r * G[0] + SH[0], acc[ai][bj][m][1] * r * G[1] + SH[1]); }
;             asm volatile("" ::: "memory"); }
.LBB0_512:
	s_waitcnt vmcnt(3)
	v_pk_add_f32 v[24:25], v[24:25], 1.0 op_sel_hi:[1,0]
	v_pk_add_f32 v[22:23], v[22:23], 1.0 op_sel_hi:[1,0]
	s_waitcnt vmcnt(1)
	v_pk_add_f32 v[18:19], v[18:19], 1.0 op_sel_hi:[1,0]
	v_pk_add_f32 v[20:21], v[20:21], 1.0 op_sel_hi:[1,0]
	v_pk_mul_f32 v[16:17], v[16:17], v[24:25]
	v_pk_mul_f32 v[14:15], v[14:15], v[22:23]
	v_pk_mul_f32 v[12:13], v[12:13], v[20:21]
	v_pk_mul_f32 v[10:11], v[10:11], v[18:19]
	s_waitcnt lgkmcnt(0)
	v_pk_mul_f32 v[18:19], v[64:65], v[90:91] op_sel_hi:[0,1]
	v_pk_mul_f32 v[20:21], v[64:65], v[88:89] op_sel_hi:[0,1]
	v_pk_fma_f32 v[22:23], v[16:17], v[18:19], v[8:9]
	v_pk_fma_f32 v[18:19], v[14:15], v[20:21], v[6:7]
	v_pk_mul_f32 v[20:21], v[64:65], v[86:87] op_sel_hi:[0,1]
	v_pk_mul_f32 v[24:25], v[64:65], v[84:85] op_sel_hi:[0,1]
	v_lshl_add_u64 v[72:73], v[168:169], 1, s[82:83]
	s_waitcnt vmcnt(0)
	v_pk_fma_f32 v[64:65], v[12:13], v[20:21], v[4:5]
	v_pk_fma_f32 v[20:21], v[10:11], v[24:25], v[2:3]
	v_cvt_pk_bf16_f32 v18, v18, v19
	v_cvt_pk_bf16_f32 v19, v22, v23
	v_cvt_pk_bf16_f32 v20, v20, v21
	v_cvt_pk_bf16_f32 v21, v64, v65
	v_lshl_add_u64 v[64:65], v[72:73], 0, v[170:171]
	s_and_b64 vcc, exec, s[8:9]
	v_add_u32_e32 v90, 16, v220
	global_store_dwordx4 v[64:65], v[18:21], off sc1
	s_cbranch_vccnz .LBB0_514
	s_nop 0
	v_lshl_add_u32 v18, v90, 2, 0
	v_add_u32_e32 v18, 0x18300, v18
	ds_read_b32 v66, v18
.LBB0_514:
	s_waitcnt lgkmcnt(0)
	v_pk_mul_f32 v[18:19], v[66:67], v[102:103] op_sel_hi:[0,1]
	v_pk_mul_f32 v[20:21], v[66:67], v[98:99] op_sel_hi:[0,1]
	v_pk_fma_f32 v[22:23], v[16:17], v[18:19], v[8:9]
	v_pk_fma_f32 v[18:19], v[14:15], v[20:21], v[6:7]
	v_pk_mul_f32 v[20:21], v[66:67], v[94:95] op_sel_hi:[0,1]
	v_cvt_pk_bf16_f32 v18, v18, v19
	v_cvt_pk_bf16_f32 v19, v22, v23
	v_add_u32_e32 v22, s27, v90
	v_pk_mul_f32 v[24:25], v[66:67], v[92:93] op_sel_hi:[0,1]
	v_ashrrev_i32_e32 v23, 31, v22
	v_pk_fma_f32 v[66:67], v[12:13], v[20:21], v[4:5]
	v_pk_fma_f32 v[20:21], v[10:11], v[24:25], v[2:3]
	v_lshlrev_b64 v[22:23], 11, v[22:23]
	v_cvt_pk_bf16_f32 v20, v20, v21
	v_cvt_pk_bf16_f32 v21, v66, v67
	v_lshl_add_u64 v[66:67], v[72:73], 0, v[22:23]
	global_store_dwordx4 v[66:67], v[18:21], off sc1
	v_add_u32_e32 v91, 32, v220
	s_and_b64 vcc, exec, s[8:9]
	v_mov_b32_e32 v18, 0x7fc00000
	v_mov_b32_e32 v20, 0x7fc00000
	s_cbranch_vccnz .LBB0_516
	v_lshl_add_u32 v19, v91, 2, 0
	v_add_u32_e32 v19, 0x18300, v19
	ds_read_b32 v20, v19
.LBB0_516:
	s_waitcnt lgkmcnt(0)
	v_pk_mul_f32 v[24:25], v[20:21], v[110:111] op_sel_hi:[0,1]
	v_pk_mul_f32 v[22:23], v[20:21], v[112:113] op_sel_hi:[0,1]
	v_pk_fma_f32 v[24:25], v[14:15], v[24:25], v[6:7]
	v_pk_mul_f32 v[68:69], v[20:21], v[108:109] op_sel_hi:[0,1]
	v_pk_mul_f32 v[20:21], v[20:21], v[106:107] op_sel_hi:[0,1]
	v_pk_fma_f32 v[70:71], v[10:11], v[20:21], v[2:3]
	v_cvt_pk_bf16_f32 v20, v24, v25
	v_add_u32_e32 v24, s27, v91
	v_ashrrev_i32_e32 v25, 31, v24
	v_pk_fma_f32 v[22:23], v[16:17], v[22:23], v[8:9]
	v_pk_fma_f32 v[68:69], v[12:13], v[68:69], v[4:5]
	v_lshlrev_b64 v[24:25], 11, v[24:25]
	v_cvt_pk_bf16_f32 v21, v22, v23
	v_cvt_pk_bf16_f32 v22, v70, v71
	v_cvt_pk_bf16_f32 v23, v68, v69
	v_lshl_add_u64 v[68:69], v[72:73], 0, v[24:25]
	s_and_b64 vcc, exec, s[8:9]
	v_add_u32_e32 v92, 48, v220
	global_store_dwordx4 v[68:69], v[20:23], off sc1
	s_cbranch_vccnz .LBB0_518
	v_lshl_add_u32 v18, v92, 2, 0
	v_add_u32_e32 v18, 0x18300, v18
	ds_read_b32 v18, v18
.LBB0_518:
	s_waitcnt lgkmcnt(0)
	v_pk_mul_f32 v[22:23], v[18:19], v[126:127] op_sel_hi:[0,1]
	v_pk_mul_f32 v[20:21], v[18:19], v[128:129] op_sel_hi:[0,1]
	v_pk_fma_f32 v[22:23], v[14:15], v[22:23], v[6:7]
	v_pk_mul_f32 v[24:25], v[18:19], v[124:125] op_sel_hi:[0,1]
	v_pk_mul_f32 v[18:19], v[18:19], v[122:123] op_sel_hi:[0,1]
	v_pk_fma_f32 v[70:71], v[10:11], v[18:19], v[2:3]
	v_cvt_pk_bf16_f32 v18, v22, v23
	v_add_u32_e32 v22, s27, v92
	v_ashrrev_i32_e32 v23, 31, v22
	v_pk_fma_f32 v[20:21], v[16:17], v[20:21], v[8:9]
	v_pk_fma_f32 v[24:25], v[12:13], v[24:25], v[4:5]
	v_lshlrev_b64 v[22:23], 11, v[22:23]
	v_cvt_pk_bf16_f32 v19, v20, v21
	v_cvt_pk_bf16_f32 v20, v70, v71
	v_cvt_pk_bf16_f32 v21, v24, v25
	v_lshl_add_u64 v[70:71], v[72:73], 0, v[22:23]
	global_store_dwordx4 v[70:71], v[18:21], off sc1
	v_add_u32_e32 v93, 0x80, v220
	s_and_b64 vcc, exec, s[8:9]
	v_mov_b32_e32 v18, 0x7fc00000
	v_mov_b32_e32 v20, 0x7fc00000
	s_cbranch_vccnz .LBB0_520
	v_lshl_add_u32 v19, v93, 2, 0
	v_add_u32_e32 v19, 0x18300, v19
	ds_read_b32 v20, v19
.LBB0_520:
	s_waitcnt lgkmcnt(0)
	v_pk_mul_f32 v[24:25], v[20:21], v[142:143] op_sel_hi:[0,1]
	v_pk_mul_f32 v[22:23], v[20:21], v[144:145] op_sel_hi:[0,1]
	v_pk_fma_f32 v[24:25], v[14:15], v[24:25], v[6:7]
	v_pk_mul_f32 v[84:85], v[20:21], v[140:141] op_sel_hi:[0,1]
	v_pk_mul_f32 v[20:21], v[20:21], v[138:139] op_sel_hi:[0,1]
	v_pk_fma_f32 v[86:87], v[10:11], v[20:21], v[2:3]
	v_cvt_pk_bf16_f32 v20, v24, v25
	v_add_u32_e32 v24, s27, v93
	v_ashrrev_i32_e32 v25, 31, v24
	v_pk_fma_f32 v[22:23], v[16:17], v[22:23], v[8:9]
	v_pk_fma_f32 v[84:85], v[12:13], v[84:85], v[4:5]
	v_lshlrev_b64 v[24:25], 11, v[24:25]
	v_cvt_pk_bf16_f32 v21, v22, v23
	v_cvt_pk_bf16_f32 v22, v86, v87
	v_cvt_pk_bf16_f32 v23, v84, v85
	v_lshl_add_u64 v[84:85], v[72:73], 0, v[24:25]
	s_and_b64 vcc, exec, s[8:9]
	v_add_u32_e32 v94, 0x90, v220
	global_store_dwordx4 v[84:85], v[20:23], off sc1
	s_cbranch_vccnz .LBB0_522
	v_lshl_add_u32 v18, v94, 2, 0
	v_add_u32_e32 v18, 0x18300, v18
	ds_read_b32 v18, v18
; __device__ __forceinline__ u32x4 pack8(const f32x4 a, const f32x4 b) { u32x4 w; w.x = cvt_pk_bf16(a[0], a[1]); w.y = cvt_pk_bf16(a[2], a[3]); w.z = cvt_pk_bf16(b[0], b[1]); w.w = cvt_pk_bf16(b[2], b[3]); return w; }
;     __device__ __forceinline__ void fused(f32x4 (&acc)[2][2][4][2], const pg8::Unit& u_, int wr_, int wc_, int fr_, int fq_, LAS unsigned char* lds, int tid_) const {
;     ...
; #pragma unroll
;         for (int bj = 0; bj < 2; ++bj) { f32x4 G[2], SH[2];
; #pragma unroll
;             for (int n = 0; n < 2; ++n) { const int c = col0 + bj * HALF + 4 * n; const f32x4 gg = *(const f32x4*)(g2 + c), sc = *(const f32x4*)(mrow + 4 * D + c);
;                 G[n] = gg * (sc + 1.f); SH[n] = *(const f32x4*)(mrow + 3 * D + c); }
; #pragma unroll
;             for (int ai = 0; ai < 2; ++ai)
; #pragma unroll
;                 for (int m = 0; m < 4; ++m) { const int rl = ai * HALF + wr * 64 + m * 16 + fr; const float r = bad ? __builtin_nanf("") : Sr[rl];
;                     *(u32x4*)(HB + (size_t)(u.pm * BM + rl) * D + col0 + bj * HALF) = pack8(acc[ai][bj][m][0] * r * G[0] + SH[0], acc[ai][bj][m][1] * r * G[1] + SH[1]); }
;             asm volatile("" ::: "memory"); }
.LBB0_522:
	s_waitcnt lgkmcnt(0)
	v_pk_mul_f32 v[22:23], v[18:19], v[178:179] op_sel_hi:[0,1]
	v_pk_mul_f32 v[20:21], v[18:19], v[180:181] op_sel_hi:[0,1]
	v_pk_fma_f32 v[22:23], v[14:15], v[22:23], v[6:7]
	v_pk_mul_f32 v[24:25], v[18:19], v[176:177] op_sel_hi:[0,1]
	v_pk_mul_f32 v[18:19], v[18:19], v[174:175] op_sel_hi:[0,1]
	v_pk_fma_f32 v[86:87], v[10:11], v[18:19], v[2:3]
	v_cvt_pk_bf16_f32 v18, v22, v23
	v_add_u32_e32 v22, s27, v94
	v_ashrrev_i32_e32 v23, 31, v22
	v_pk_fma_f32 v[20:21], v[16:17], v[20:21], v[8:9]
	v_pk_fma_f32 v[24:25], v[12:13], v[24:25], v[4:5]
	v_lshlrev_b64 v[22:23], 11, v[22:23]
	v_cvt_pk_bf16_f32 v19, v20, v21
	v_cvt_pk_bf16_f32 v20, v86, v87
	v_cvt_pk_bf16_f32 v21, v24, v25
	v_lshl_add_u64 v[86:87], v[72:73], 0, v[22:23]
	global_store_dwordx4 v[86:87], v[18:21], off sc1
	v_add_u32_e32 v95, 0xa0, v220
	s_and_b64 vcc, exec, s[8:9]
	v_mov_b32_e32 v18, 0x7fc00000
	v_mov_b32_e32 v20, 0x7fc00000
	s_cbranch_vccnz .LBB0_524
	v_lshl_add_u32 v19, v95, 2, 0
	v_add_u32_e32 v19, 0x18300, v19
	ds_read_b32 v20, v19
.LBB0_524:
	s_waitcnt lgkmcnt(0)
	v_pk_mul_f32 v[24:25], v[20:21], v[186:187] op_sel_hi:[0,1]
	v_pk_mul_f32 v[22:23], v[20:21], v[188:189] op_sel_hi:[0,1]
	v_pk_fma_f32 v[24:25], v[14:15], v[24:25], v[6:7]
	v_pk_mul_f32 v[88:89], v[20:21], v[184:185] op_sel_hi:[0,1]
	v_pk_mul_f32 v[20:21], v[20:21], v[182:183] op_sel_hi:[0,1]
	v_pk_fma_f32 v[98:99], v[10:11], v[20:21], v[2:3]
	v_cvt_pk_bf16_f32 v20, v24, v25
	v_add_u32_e32 v24, s27, v95
	v_ashrrev_i32_e32 v25, 31, v24
	v_pk_fma_f32 v[22:23], v[16:17], v[22:23], v[8:9]
	v_pk_fma_f32 v[88:89], v[12:13], v[88:89], v[4:5]
	v_lshlrev_b64 v[24:25], 11, v[24:25]
	v_cvt_pk_bf16_f32 v21, v22, v23
	v_cvt_pk_bf16_f32 v22, v98, v99
	v_cvt_pk_bf16_f32 v23, v88, v89
	v_lshl_add_u64 v[88:89], v[72:73], 0, v[24:25]
	s_and_b64 vcc, exec, s[8:9]
	v_add_u32_e32 v98, 0xb0, v220
	global_store_dwordx4 v[88:89], v[20:23], off sc1
	s_cbranch_vccnz .LBB0_526
	v_lshl_add_u32 v18, v98, 2, 0
	v_add_u32_e32 v18, 0x18300, v18
	ds_read_b32 v18, v18
.LBB0_526:
	s_waitcnt lgkmcnt(0)
	v_pk_mul_f32 v[20:21], v[18:19], v[196:197] op_sel_hi:[0,1]
	v_pk_mul_f32 v[22:23], v[18:19], v[194:195] op_sel_hi:[0,1]
	v_pk_fma_f32 v[8:9], v[16:17], v[20:21], v[8:9]
	v_pk_fma_f32 v[6:7], v[14:15], v[22:23], v[6:7]
	v_pk_mul_f32 v[14:15], v[18:19], v[192:193] op_sel_hi:[0,1]
	v_pk_mul_f32 v[16:17], v[18:19], v[190:191] op_sel_hi:[0,1]
	v_pk_fma_f32 v[12:13], v[12:13], v[14:15], v[4:5]
	v_pk_fma_f32 v[4:5], v[10:11], v[16:17], v[2:3]
	v_cvt_pk_bf16_f32 v2, v6, v7
	v_add_u32_e32 v6, s27, v98
	v_ashrrev_i32_e32 v7, 31, v6
	v_lshlrev_b64 v[6:7], 11, v[6:7]
	v_cvt_pk_bf16_f32 v3, v8, v9
	v_cvt_pk_bf16_f32 v4, v4, v5
	v_cvt_pk_bf16_f32 v5, v12, v13
	v_lshl_add_u64 v[72:73], v[72:73], 0, v[6:7]
	global_store_dwordx4 v[72:73], v[2:5], off sc1
	global_load_dwordx4 v[10:13], v[58:59], off offset:528
	global_load_dwordx4 v[18:21], v[58:59], off offset:512
	global_load_dwordx4 v[14:17], v[60:61], off offset:528
	global_load_dwordx4 v[22:25], v[60:61], off offset:512
	global_load_dwordx4 v[2:5], v[62:63], off offset:528
	global_load_dwordx4 v[6:9], v[62:63], off offset:512
	v_mov_b32_e32 v58, 0x7fc00000
	s_and_b64 vcc, exec, s[8:9]
	v_mov_b32_e32 v60, 0x7fc00000
	s_cbranch_vccnz .LBB0_528
	v_lshl_add_u32 v59, v220, 2, 0
	v_add_u32_e32 v59, 0x18300, v59
	ds_read_b32 v60, v59
.LBB0_528:
	s_waitcnt vmcnt(2)
	v_pk_add_f32 v[24:25], v[24:25], 1.0 op_sel_hi:[1,0]
	v_pk_add_f32 v[22:23], v[22:23], 1.0 op_sel_hi:[1,0]
	v_pk_add_f32 v[14:15], v[14:15], 1.0 op_sel_hi:[1,0]
	v_pk_add_f32 v[16:17], v[16:17], 1.0 op_sel_hi:[1,0]
	v_pk_mul_f32 v[20:21], v[20:21], v[24:25]
	v_pk_mul_f32 v[18:19], v[18:19], v[22:23]
	v_pk_mul_f32 v[12:13], v[12:13], v[16:17]
	v_pk_mul_f32 v[10:11], v[10:11], v[14:15]
	s_waitcnt lgkmcnt(0)
	v_pk_mul_f32 v[14:15], v[60:61], v[80:81] op_sel_hi:[0,1]
	v_pk_mul_f32 v[16:17], v[60:61], v[78:79] op_sel_hi:[0,1]
	s_waitcnt vmcnt(0)
	v_pk_fma_f32 v[22:23], v[20:21], v[14:15], v[8:9]
	v_pk_fma_f32 v[14:15], v[18:19], v[16:17], v[6:7]
	v_pk_mul_f32 v[16:17], v[60:61], v[76:77] op_sel_hi:[0,1]
	v_pk_mul_f32 v[24:25], v[60:61], v[74:75] op_sel_hi:[0,1]
	v_pk_fma_f32 v[60:61], v[12:13], v[16:17], v[4:5]
	v_pk_fma_f32 v[16:17], v[10:11], v[24:25], v[2:3]
	v_cvt_pk_bf16_f32 v14, v14, v15
	v_cvt_pk_bf16_f32 v15, v22, v23
	v_cvt_pk_bf16_f32 v16, v16, v17
	v_cvt_pk_bf16_f32 v17, v60, v61
	s_and_b64 vcc, exec, s[8:9]
	global_store_dwordx4 v[64:65], v[14:17], off offset:256 sc1
	s_cbranch_vccnz .LBB0_530
	s_nop 0
	v_lshl_add_u32 v14, v90, 2, 0
	v_add_u32_e32 v14, 0x18300, v14
	ds_read_b32 v58, v14
.LBB0_530:
	s_waitcnt lgkmcnt(0)
	v_pk_mul_f32 v[14:15], v[58:59], v[54:55] op_sel_hi:[0,1]
	v_pk_mul_f32 v[16:17], v[58:59], v[82:83] op_sel_hi:[0,1]
	v_pk_fma_f32 v[22:23], v[20:21], v[14:15], v[8:9]
	v_pk_fma_f32 v[14:15], v[18:19], v[16:17], v[6:7]
	v_pk_mul_f32 v[16:17], v[58:59], v[52:53] op_sel_hi:[0,1]
	v_pk_mul_f32 v[24:25], v[58:59], v[50:51] op_sel_hi:[0,1]
	v_pk_fma_f32 v[50:51], v[12:13], v[16:17], v[4:5]
	v_pk_fma_f32 v[16:17], v[10:11], v[24:25], v[2:3]
	v_cvt_pk_bf16_f32 v14, v14, v15
	v_cvt_pk_bf16_f32 v15, v22, v23
	v_cvt_pk_bf16_f32 v16, v16, v17
	v_cvt_pk_bf16_f32 v17, v50, v51
	global_store_dwordx4 v[66:67], v[14:17], off offset:256 sc1
	s_and_b64 vcc, exec, s[8:9]
	s_nop 0
	v_mov_b32_e32 v14, 0x7fc00000
	v_mov_b32_e32 v16, 0x7fc00000
	s_cbranch_vccnz .LBB0_532
	v_lshl_add_u32 v15, v91, 2, 0
	v_add_u32_e32 v15, 0x18300, v15
	ds_read_b32 v16, v15
; __device__ __forceinline__ u32x4 pack8(const f32x4 a, const f32x4 b) { u32x4 w; w.x = cvt_pk_bf16(a[0], a[1]); w.y = cvt_pk_bf16(a[2], a[3]); w.z = cvt_pk_bf16(b[0], b[1]); w.w = cvt_pk_bf16(b[2], b[3]); return w; }
; #define PG8_BAR __builtin_amdgcn_s_barrier()
;     ...
;         if (!has_next) break;
; #pragma unroll
;         for (int a = 0; a < 2; ++a)
; #pragma unroll
;             for (int b = 0; b < 2; ++b)
; #pragma unroll
;                 for (int m = 0; m < 4; ++m)
; #pragma unroll
;                     for (int n = 0; n < 2; ++n) acc[a][b][m][n] = (f32x4){0.f, 0.f, 0.f, 0.f};
;         cur = nxt; cA = nA; cB = nB; ++ui;
; #pragma unroll
;         for (int hh = 0; hh < 2; ++hh)
; #pragma unroll
;             for (int i = 0; i < 2; ++i) voffA[hh][i] = voffN[hh][i];
;         if (wr == 1) PG8_BAR;
;     __device__ __forceinline__ void fused(f32x4 (&acc)[2][2][4][2], const pg8::Unit& u_, int wr_, int wc_, int fr_, int fq_, LAS unsigned char* lds, int tid_) const {
;     ...
; #pragma unroll
;         for (int bj = 0; bj < 2; ++bj) { f32x4 G[2], SH[2];
; #pragma unroll
;             for (int n = 0; n < 2; ++n) { const int c = col0 + bj * HALF + 4 * n; const f32x4 gg = *(const f32x4*)(g2 + c), sc = *(const f32x4*)(mrow + 4 * D + c);
;                 G[n] = gg * (sc + 1.f); SH[n] = *(const f32x4*)(mrow + 3 * D + c); }
; #pragma unroll
;             for (int ai = 0; ai < 2; ++ai)
; #pragma unroll
;                 for (int m = 0; m < 4; ++m) { const int rl = ai * HALF + wr * 64 + m * 16 + fr; const float r = bad ? __builtin_nanf("") : Sr[rl];
;                     *(u32x4*)(HB + (size_t)(u.pm * BM + rl) * D + col0 + bj * HALF) = pack8(acc[ai][bj][m][0] * r * G[0] + SH[0], acc[ai][bj][m][1] * r * G[1] + SH[1]); }
;             asm volatile("" ::: "memory"); }
.LBB0_532:
	s_waitcnt lgkmcnt(0)
	v_pk_mul_f32 v[22:23], v[16:17], v[46:47] op_sel_hi:[0,1]
	v_pk_mul_f32 v[24:25], v[16:17], v[56:57] op_sel_hi:[0,1]
	v_pk_fma_f32 v[46:47], v[20:21], v[22:23], v[8:9]
	v_pk_fma_f32 v[22:23], v[18:19], v[24:25], v[6:7]
	v_pk_mul_f32 v[24:25], v[16:17], v[44:45] op_sel_hi:[0,1]
	v_pk_mul_f32 v[16:17], v[16:17], v[42:43] op_sel_hi:[0,1]
	v_pk_fma_f32 v[42:43], v[12:13], v[24:25], v[4:5]
	v_pk_fma_f32 v[16:17], v[10:11], v[16:17], v[2:3]
	v_cvt_pk_bf16_f32 v22, v22, v23
	v_cvt_pk_bf16_f32 v23, v46, v47
	v_cvt_pk_bf16_f32 v24, v16, v17
	v_cvt_pk_bf16_f32 v25, v42, v43
	s_and_b64 vcc, exec, s[8:9]
	global_store_dwordx4 v[68:69], v[22:25], off offset:256 sc1
	s_cbranch_vccnz .LBB0_534
	v_lshl_add_u32 v14, v92, 2, 0
	v_add_u32_e32 v14, 0x18300, v14
	ds_read_b32 v14, v14
.LBB0_534:
	s_waitcnt lgkmcnt(0)
	v_pk_mul_f32 v[16:17], v[14:15], v[38:39] op_sel_hi:[0,1]
	v_pk_mul_f32 v[22:23], v[14:15], v[48:49] op_sel_hi:[0,1]
	v_pk_mul_f32 v[24:25], v[14:15], v[36:37] op_sel_hi:[0,1]
	v_pk_mul_f32 v[14:15], v[14:15], v[34:35] op_sel_hi:[0,1]
	v_pk_fma_f32 v[16:17], v[20:21], v[16:17], v[8:9]
	v_pk_fma_f32 v[22:23], v[18:19], v[22:23], v[6:7]
	v_pk_fma_f32 v[24:25], v[12:13], v[24:25], v[4:5]
	v_pk_fma_f32 v[34:35], v[10:11], v[14:15], v[2:3]
	v_cvt_pk_bf16_f32 v14, v22, v23
	v_cvt_pk_bf16_f32 v15, v16, v17
	v_cvt_pk_bf16_f32 v16, v34, v35
	v_cvt_pk_bf16_f32 v17, v24, v25
	global_store_dwordx4 v[70:71], v[14:17], off offset:256 sc1
	s_and_b64 vcc, exec, s[8:9]
	s_nop 0
	v_mov_b32_e32 v14, 0x7fc00000
	v_mov_b32_e32 v16, 0x7fc00000
	s_cbranch_vccnz .LBB0_536
	v_lshl_add_u32 v15, v93, 2, 0
	v_add_u32_e32 v15, 0x18300, v15
	ds_read_b32 v16, v15
.LBB0_536:
	s_waitcnt lgkmcnt(0)
	v_pk_mul_f32 v[22:23], v[16:17], v[30:31] op_sel_hi:[0,1]
	v_pk_mul_f32 v[24:25], v[16:17], v[40:41] op_sel_hi:[0,1]
	v_pk_fma_f32 v[30:31], v[20:21], v[22:23], v[8:9]
	v_pk_fma_f32 v[22:23], v[18:19], v[24:25], v[6:7]
	v_pk_mul_f32 v[24:25], v[16:17], v[28:29] op_sel_hi:[0,1]
	v_pk_mul_f32 v[16:17], v[16:17], v[26:27] op_sel_hi:[0,1]
	v_pk_fma_f32 v[26:27], v[12:13], v[24:25], v[4:5]
	v_pk_fma_f32 v[16:17], v[10:11], v[16:17], v[2:3]
	v_cvt_pk_bf16_f32 v22, v22, v23
	v_cvt_pk_bf16_f32 v23, v30, v31
	v_cvt_pk_bf16_f32 v24, v16, v17
	v_cvt_pk_bf16_f32 v25, v26, v27
	s_and_b64 vcc, exec, s[8:9]
	global_store_dwordx4 v[84:85], v[22:25], off offset:256 sc1
	s_cbranch_vccnz .LBB0_538
	v_lshl_add_u32 v14, v94, 2, 0
	v_add_u32_e32 v14, 0x18300, v14
	ds_read_b32 v14, v14
.LBB0_538:
	s_waitcnt lgkmcnt(0)
	v_pk_mul_f32 v[16:17], v[14:15], v[104:105] op_sel_hi:[0,1]
	v_pk_mul_f32 v[22:23], v[14:15], v[100:101] op_sel_hi:[0,1]
	v_pk_mul_f32 v[24:25], v[14:15], v[96:97] op_sel_hi:[0,1]
	v_pk_mul_f32 v[14:15], v[14:15], v[32:33] op_sel_hi:[0,1]
	v_pk_fma_f32 v[16:17], v[20:21], v[16:17], v[8:9]
	v_pk_fma_f32 v[22:23], v[18:19], v[22:23], v[6:7]
	v_pk_fma_f32 v[24:25], v[12:13], v[24:25], v[4:5]
	v_pk_fma_f32 v[26:27], v[10:11], v[14:15], v[2:3]
	v_cvt_pk_bf16_f32 v14, v22, v23
	v_cvt_pk_bf16_f32 v15, v16, v17
	v_cvt_pk_bf16_f32 v16, v26, v27
	v_cvt_pk_bf16_f32 v17, v24, v25
	global_store_dwordx4 v[86:87], v[14:17], off offset:256 sc1
	s_and_b64 vcc, exec, s[8:9]
	s_nop 0
	v_mov_b32_e32 v14, 0x7fc00000
	v_mov_b32_e32 v16, 0x7fc00000
	s_cbranch_vccnz .LBB0_540
	v_lshl_add_u32 v15, v95, 2, 0
	v_add_u32_e32 v15, 0x18300, v15
	ds_read_b32 v16, v15
.LBB0_540:
	s_waitcnt lgkmcnt(0)
	v_pk_mul_f32 v[22:23], v[16:17], v[120:121] op_sel_hi:[0,1]
	v_pk_mul_f32 v[24:25], v[16:17], v[118:119] op_sel_hi:[0,1]
	v_pk_fma_f32 v[26:27], v[20:21], v[22:23], v[8:9]
	v_pk_fma_f32 v[22:23], v[18:19], v[24:25], v[6:7]
	v_pk_mul_f32 v[24:25], v[16:17], v[116:117] op_sel_hi:[0,1]
	v_pk_mul_f32 v[16:17], v[16:17], v[114:115] op_sel_hi:[0,1]
	v_pk_fma_f32 v[28:29], v[12:13], v[24:25], v[4:5]
	v_pk_fma_f32 v[16:17], v[10:11], v[16:17], v[2:3]
	v_cvt_pk_bf16_f32 v22, v22, v23
	v_cvt_pk_bf16_f32 v23, v26, v27
	v_cvt_pk_bf16_f32 v24, v16, v17
	v_cvt_pk_bf16_f32 v25, v28, v29
	s_and_b64 vcc, exec, s[8:9]
	global_store_dwordx4 v[88:89], v[22:25], off offset:256 sc1
	s_cbranch_vccnz .LBB0_542
	v_lshl_add_u32 v14, v98, 2, 0
	v_add_u32_e32 v14, 0x18300, v14
	ds_read_b32 v14, v14
.LBB0_542:
	s_waitcnt lgkmcnt(0)
	v_pk_mul_f32 v[16:17], v[14:15], v[136:137] op_sel_hi:[0,1]
	v_pk_mul_f32 v[22:23], v[14:15], v[134:135] op_sel_hi:[0,1]
	v_pk_fma_f32 v[8:9], v[20:21], v[16:17], v[8:9]
	v_pk_mul_f32 v[16:17], v[14:15], v[132:133] op_sel_hi:[0,1]
	v_pk_mul_f32 v[14:15], v[14:15], v[130:131] op_sel_hi:[0,1]
	v_pk_fma_f32 v[6:7], v[18:19], v[22:23], v[6:7]
	v_pk_fma_f32 v[12:13], v[12:13], v[16:17], v[4:5]
	v_pk_fma_f32 v[4:5], v[10:11], v[14:15], v[2:3]
	v_cvt_pk_bf16_f32 v2, v6, v7
	v_cvt_pk_bf16_f32 v3, v8, v9
	v_cvt_pk_bf16_f32 v4, v4, v5
	v_cvt_pk_bf16_f32 v5, v12, v13
	global_store_dwordx4 v[72:73], v[2:5], off offset:256 sc1
	s_andn2_b64 vcc, exec, s[0:1]
	s_mov_b64 s[0:1], -1
	s_cbranch_vccnz .LBB0_452
	v_readlane_b32 s0, v250, 32
	v_readlane_b32 s1, v250, 33
	s_andn2_b64 vcc, exec, s[0:1]
	s_cbranch_vccnz .LBB0_451
	s_barrier
	s_branch .LBB0_451

; __device__ __forceinline__ u32x4 pack8(const f32x4 a, const f32x4 b) { u32x4 w; w.x = cvt_pk_bf16(a[0], a[1]); w.y = cvt_pk_bf16(a[2], a[3]); w.z = cvt_pk_bf16(b[0], b[1]); w.w = cvt_pk_bf16(b[2], b[3]); return w; }
;     __device__ __forceinline__ void fused(f32x4 (&acc)[2][2][4][2], const pg8::Unit& u_, int wr_, int wc_, int fr_, int fq_, LAS unsigned char* lds, int tid_) const {
;     ...
;         {   const float* gp = gate + bidx * MODW + col0; f32x4 gv[2][2];
; #pragma unroll
;             for (int bj = 0; bj < 2; ++bj)
; #pragma unroll
;                 for (int n = 0; n < 2; ++n) gv[bj][n] = *(const f32x4*)(gp + bj * HALF + 4 * n);
; #pragma unroll
;             for (int ai = 0; ai < 2; ++ai)
; #pragma unroll
;                 for (int m = 0; m < 4; ++m) { bf16_t* rowp = X + (size_t)(row0 + ai * HALF + m * 16) * D + col0;
; #pragma unroll
;                     for (int bj = 0; bj < 2; ++bj) { f32x4 s0, s1;
;                         if (LAYER == 0) { const float* sp = (isctx ? srcC + (size_t)(row0 - ML + ai * HALF + m * 16) * D : srcL + (size_t)(row0 + ai * HALF + m * 16) * D) + col0 + bj * HALF;
;                             s0 = __builtin_nontemporal_load((const f32x4*)sp); s1 = __builtin_nontemporal_load((const f32x4*)(sp + 4)); }
;                         else { const u32x4 xb = *(const u32x4*)(rowp + bj * HALF);
;                             s0 = (f32x4){__uint_as_float(xb.x << 16), __uint_as_float(xb.x & 0xffff0000u), __uint_as_float(xb.y << 16), __uint_as_float(xb.y & 0xffff0000u)};
;                             s1 = (f32x4){__uint_as_float(xb.z << 16), __uint_as_float(xb.z & 0xffff0000u), __uint_as_float(xb.w << 16), __uint_as_float(xb.w & 0xffff0000u)}; }
;                         const u32x4 w = pack8(s0 + gv[bj][0] * acc[ai][bj][m][0], s1 + gv[bj][1] * acc[ai][bj][m][1]);
;                         *(u32x4*)(rowp + bj * HALF) = w;
;                         acc[ai][bj][m][0] = (f32x4){__uint_as_float(w.x << 16), __uint_as_float(w.x & 0xffff0000u), __uint_as_float(w.y << 16), __uint_as_float(w.y & 0xffff0000u)};
;                         acc[ai][bj][m][1] = (f32x4){__uint_as_float(w.z << 16), __uint_as_float(w.z & 0xffff0000u), __uint_as_float(w.w << 16), __uint_as_float(w.w & 0xffff0000u)}; } }
.LBB0_562:
	s_lshl_b32 s27, s6, 8
	v_lshlrev_b32_e64 v179, 5, s42
	v_lshlrev_b32_e32 v178, 3, v176
	s_lshl_b32 s25, s36, 8
	v_lshl_add_u32 v216, s4, 6, v177
	v_add3_u32 v164, v178, v179, s27
	s_lshl_b64 s[2:3], s[2:3], 2
	v_add_u32_e32 v170, s25, v216
	s_add_u32 s4, s57, s2
	v_ashrrev_i32_e32 v165, 31, v164
	s_addc_u32 s5, s58, s3
	v_lshlrev_b64 v[168:169], 2, v[164:165]
	v_ashrrev_i32_e32 v171, 31, v170
	v_readlane_b32 s8, v250, 10
	v_lshl_add_u64 v[134:135], s[4:5], 0, v[168:169]
	v_lshlrev_b64 v[130:131], 12, v[170:171]
	v_readlane_b32 s12, v250, 14
	v_readlane_b32 s13, v250, 15
	s_brev_b32 s4, 63
	v_readlane_b32 s9, v250, 11
	v_lshl_add_u64 v[174:175], s[12:13], 0, v[130:131]
	s_mov_b32 s5, -1
	v_lshl_add_u64 v[132:133], v[174:175], 0, s[4:5]
	v_lshl_add_u64 v[130:131], s[8:9], 0, v[130:131]
	v_cndmask_b32_e64 v131, v131, v133, s[0:1]
	v_cndmask_b32_e64 v130, v130, v132, s[0:1]
	v_lshl_add_u64 v[188:189], v[130:131], 0, v[168:169]
	global_load_dwordx4 v[180:183], v[188:189], off nt
	global_load_dwordx4 v[142:145], v[134:135], off
	global_load_dwordx4 v[138:141], v[134:135], off offset:16
	global_load_dwordx4 v[184:187], v[188:189], off offset:16 nt
	v_lshl_add_u64 v[172:173], v[164:165], 1, s[96:97]
	v_lshlrev_b64 v[166:167], 11, v[170:171]
	v_lshl_add_u64 v[190:191], v[172:173], 0, v[166:167]
	global_load_dwordx4 v[130:133], v[134:135], off offset:528
	s_nop 0
	global_load_dwordx4 v[134:137], v[134:135], off offset:512
	s_mov_b32 s4, 0xfc010000
	s_mov_b32 s5, -1
	s_add_u32 s38, s84, s2
	v_readlane_b32 s22, v250, 24
	v_readlane_b32 s23, v250, 25
	s_addc_u32 s39, s85, s3
	v_and_b32_e32 v158, 15, v217
	v_readlane_b32 s10, v250, 12
	v_readlane_b32 s11, v250, 13
	v_readlane_b32 s14, v250, 16
	v_readlane_b32 s15, v250, 17
	v_readlane_b32 s16, v250, 18
	v_readlane_b32 s17, v250, 19
	v_readlane_b32 s18, v250, 20
	v_readlane_b32 s19, v250, 21
	v_readlane_b32 s20, v250, 22
	v_readlane_b32 s21, v250, 23
	s_waitcnt vmcnt(0)
	v_pk_fma_f32 v[128:129], v[128:129], v[144:145], v[182:183]
	v_pk_fma_f32 v[126:127], v[126:127], v[142:143], v[180:181]
	v_pk_fma_f32 v[180:181], v[60:61], v[140:141], v[186:187]
	v_pk_fma_f32 v[60:61], v[58:59], v[138:139], v[184:185]
	v_cvt_pk_bf16_f32 v58, v126, v127
	v_cvt_pk_bf16_f32 v59, v128, v129
	v_cvt_pk_bf16_f32 v60, v60, v61
	v_cvt_pk_bf16_f32 v61, v180, v181
	global_store_dwordx4 v[190:191], v[58:61], off sc1
	global_load_dwordx4 v[126:129], v[188:189], off offset:512 nt
	global_load_dwordx4 v[180:183], v[188:189], off offset:528 nt
	v_add_u32_e32 v184, 16, v170
	v_ashrrev_i32_e32 v185, 31, v184
	v_lshlrev_b64 v[186:187], 12, v[184:185]
	v_lshl_add_u64 v[188:189], v[174:175], 0, s[4:5]
	v_lshl_add_u64 v[186:187], s[8:9], 0, v[186:187]
	v_cndmask_b32_e64 v187, v187, v189, s[0:1]
	v_cndmask_b32_e64 v186, v186, v188, s[0:1]
	v_lshl_add_u64 v[186:187], v[186:187], 0, v[168:169]
	s_mov_b32 s4, 0xfc020000
	s_mov_b32 s5, -1
	s_waitcnt vmcnt(1)
	v_pk_fma_f32 v[68:69], v[68:69], v[136:137], v[128:129]
	v_pk_fma_f32 v[66:67], v[66:67], v[134:135], v[126:127]
	s_waitcnt vmcnt(0)
	v_pk_fma_f32 v[52:53], v[52:53], v[132:133], v[182:183]
	v_pk_fma_f32 v[50:51], v[50:51], v[130:131], v[180:181]
	v_cvt_pk_bf16_f32 v66, v66, v67
	v_cvt_pk_bf16_f32 v67, v68, v69
	v_cvt_pk_bf16_f32 v68, v50, v51
	v_cvt_pk_bf16_f32 v69, v52, v53
	global_store_dwordx4 v[190:191], v[66:69], off offset:256 sc1
	global_load_dwordx4 v[50:53], v[186:187], off nt
	global_load_dwordx4 v[126:129], v[186:187], off offset:16 nt
	v_lshlrev_b64 v[180:181], 11, v[184:185]
	v_lshl_add_u64 v[180:181], v[172:173], 0, v[180:181]
	v_lshl_add_u64 v[182:183], v[174:175], 0, s[4:5]
	s_mov_b32 s4, 0xfc030000
	s_mov_b32 s5, -1
	s_waitcnt vmcnt(1)
	v_pk_fma_f32 v[52:53], v[124:125], v[144:145], v[52:53]
	v_pk_fma_f32 v[50:51], v[122:123], v[142:143], v[50:51]
	s_waitcnt vmcnt(0)
	v_pk_fma_f32 v[120:121], v[120:121], v[140:141], v[128:129]
	v_pk_fma_f32 v[118:119], v[118:119], v[138:139], v[126:127]
	v_cvt_pk_bf16_f32 v50, v50, v51
	v_cvt_pk_bf16_f32 v51, v52, v53
	v_cvt_pk_bf16_f32 v52, v118, v119
	v_cvt_pk_bf16_f32 v53, v120, v121
	global_store_dwordx4 v[180:181], v[50:53], off sc1
	global_load_dwordx4 v[118:121], v[186:187], off offset:512 nt
	global_load_dwordx4 v[122:125], v[186:187], off offset:528 nt
	v_add_u32_e32 v126, 32, v170
	v_ashrrev_i32_e32 v127, 31, v126
	v_lshlrev_b64 v[128:129], 12, v[126:127]
	v_lshl_add_u64 v[128:129], s[8:9], 0, v[128:129]
	v_cndmask_b32_e64 v129, v129, v183, s[0:1]
	v_cndmask_b32_e64 v128, v128, v182, s[0:1]
	v_lshl_add_u64 v[128:129], v[128:129], 0, v[168:169]
	s_waitcnt vmcnt(1)
	v_pk_fma_f32 v[56:57], v[56:57], v[136:137], v[120:121]
	v_pk_fma_f32 v[54:55], v[54:55], v[134:135], v[118:119]
	s_waitcnt vmcnt(0)
	v_pk_fma_f32 v[44:45], v[44:45], v[132:133], v[124:125]
	v_pk_fma_f32 v[42:43], v[42:43], v[130:131], v[122:123]
	v_cvt_pk_bf16_f32 v54, v54, v55
	v_cvt_pk_bf16_f32 v55, v56, v57
	v_cvt_pk_bf16_f32 v56, v42, v43
	v_cvt_pk_bf16_f32 v57, v44, v45
	global_store_dwordx4 v[180:181], v[54:57], off offset:256 sc1
	global_load_dwordx4 v[42:45], v[128:129], off nt
	global_load_dwordx4 v[118:121], v[128:129], off offset:16 nt
	v_lshlrev_b64 v[122:123], 11, v[126:127]
	v_lshl_add_u64 v[122:123], v[172:173], 0, v[122:123]
	v_lshl_add_u64 v[124:125], v[174:175], 0, s[4:5]
	s_mov_b32 s4, 0xfc080000
	s_mov_b32 s5, -1
	s_waitcnt vmcnt(1)
	v_pk_fma_f32 v[44:45], v[116:117], v[144:145], v[44:45]
	v_pk_fma_f32 v[42:43], v[114:115], v[142:143], v[42:43]
	s_waitcnt vmcnt(0)
; __device__ __forceinline__ u32x4 pack8(const f32x4 a, const f32x4 b) { u32x4 w; w.x = cvt_pk_bf16(a[0], a[1]); w.y = cvt_pk_bf16(a[2], a[3]); w.z = cvt_pk_bf16(b[0], b[1]); w.w = cvt_pk_bf16(b[2], b[3]); return w; }
;     __device__ __forceinline__ void fused(f32x4 (&acc)[2][2][4][2], const pg8::Unit& u_, int wr_, int wc_, int fr_, int fq_, LAS unsigned char* lds, int tid_) const {
;     ...
;             for (int ai = 0; ai < 2; ++ai)
; #pragma unroll
;                 for (int m = 0; m < 4; ++m) { bf16_t* rowp = X + (size_t)(row0 + ai * HALF + m * 16) * D + col0;
; #pragma unroll
;                     for (int bj = 0; bj < 2; ++bj) { f32x4 s0, s1;
;                         if (LAYER == 0) { const float* sp = (isctx ? srcC + (size_t)(row0 - ML + ai * HALF + m * 16) * D : srcL + (size_t)(row0 + ai * HALF + m * 16) * D) + col0 + bj * HALF;
;                             s0 = __builtin_nontemporal_load((const f32x4*)sp); s1 = __builtin_nontemporal_load((const f32x4*)(sp + 4)); }
;                         else { const u32x4 xb = *(const u32x4*)(rowp + bj * HALF);
;                             s0 = (f32x4){__uint_as_float(xb.x << 16), __uint_as_float(xb.x & 0xffff0000u), __uint_as_float(xb.y << 16), __uint_as_float(xb.y & 0xffff0000u)};
;                             s1 = (f32x4){__uint_as_float(xb.z << 16), __uint_as_float(xb.z & 0xffff0000u), __uint_as_float(xb.w << 16), __uint_as_float(xb.w & 0xffff0000u)}; }
;                         const u32x4 w = pack8(s0 + gv[bj][0] * acc[ai][bj][m][0], s1 + gv[bj][1] * acc[ai][bj][m][1]);
;                         *(u32x4*)(rowp + bj * HALF) = w;
;                         acc[ai][bj][m][0] = (f32x4){__uint_as_float(w.x << 16), __uint_as_float(w.x & 0xffff0000u), __uint_as_float(w.y << 16), __uint_as_float(w.y & 0xffff0000u)};
;                         acc[ai][bj][m][1] = (f32x4){__uint_as_float(w.z << 16), __uint_as_float(w.z & 0xffff0000u), __uint_as_float(w.w << 16), __uint_as_float(w.w & 0xffff0000u)}; } }
	v_pk_fma_f32 v[112:113], v[112:113], v[140:141], v[120:121]
	v_pk_fma_f32 v[110:111], v[110:111], v[138:139], v[118:119]
	v_cvt_pk_bf16_f32 v42, v42, v43
	v_cvt_pk_bf16_f32 v43, v44, v45
	v_cvt_pk_bf16_f32 v44, v110, v111
	v_cvt_pk_bf16_f32 v45, v112, v113
	global_store_dwordx4 v[122:123], v[42:45], off sc1
	global_load_dwordx4 v[110:113], v[128:129], off offset:512 nt
	global_load_dwordx4 v[114:117], v[128:129], off offset:528 nt
	v_add_u32_e32 v118, 48, v170
	v_ashrrev_i32_e32 v119, 31, v118
	v_lshlrev_b64 v[120:121], 12, v[118:119]
	v_lshl_add_u64 v[120:121], s[8:9], 0, v[120:121]
	v_cndmask_b32_e64 v121, v121, v125, s[0:1]
	v_cndmask_b32_e64 v120, v120, v124, s[0:1]
	v_lshl_add_u64 v[120:121], v[120:121], 0, v[168:169]
	s_waitcnt vmcnt(1)
	v_pk_fma_f32 v[48:49], v[48:49], v[136:137], v[112:113]
	v_pk_fma_f32 v[46:47], v[46:47], v[134:135], v[110:111]
	s_waitcnt vmcnt(0)
	v_pk_fma_f32 v[36:37], v[36:37], v[132:133], v[116:117]
	v_pk_fma_f32 v[34:35], v[34:35], v[130:131], v[114:115]
	v_cvt_pk_bf16_f32 v46, v46, v47
	v_cvt_pk_bf16_f32 v47, v48, v49
	v_cvt_pk_bf16_f32 v48, v34, v35
	v_cvt_pk_bf16_f32 v49, v36, v37
	global_store_dwordx4 v[122:123], v[46:49], off offset:256 sc1
	global_load_dwordx4 v[34:37], v[120:121], off nt
	global_load_dwordx4 v[110:113], v[120:121], off offset:16 nt
	v_lshlrev_b64 v[114:115], 11, v[118:119]
	v_lshl_add_u64 v[114:115], v[172:173], 0, v[114:115]
	v_lshl_add_u64 v[116:117], v[174:175], 0, s[4:5]
	s_mov_b32 s4, 0xfc090000
	s_mov_b32 s5, -1
	s_waitcnt vmcnt(1)
	v_pk_fma_f32 v[36:37], v[108:109], v[144:145], v[36:37]
	v_pk_fma_f32 v[34:35], v[106:107], v[142:143], v[34:35]
	s_waitcnt vmcnt(0)
	v_pk_fma_f32 v[104:105], v[104:105], v[140:141], v[112:113]
	v_pk_fma_f32 v[102:103], v[102:103], v[138:139], v[110:111]
	v_cvt_pk_bf16_f32 v34, v34, v35
	v_cvt_pk_bf16_f32 v35, v36, v37
	v_cvt_pk_bf16_f32 v36, v102, v103
	v_cvt_pk_bf16_f32 v37, v104, v105
	global_store_dwordx4 v[114:115], v[34:37], off sc1
	global_load_dwordx4 v[102:105], v[120:121], off offset:512 nt
	global_load_dwordx4 v[106:109], v[120:121], off offset:528 nt
	v_add_u32_e32 v110, 0x80, v170
	v_ashrrev_i32_e32 v111, 31, v110
	v_lshlrev_b64 v[112:113], 12, v[110:111]
	v_lshl_add_u64 v[112:113], s[8:9], 0, v[112:113]
	v_cndmask_b32_e64 v113, v113, v117, s[0:1]
	v_cndmask_b32_e64 v112, v112, v116, s[0:1]
	v_lshl_add_u64 v[112:113], v[112:113], 0, v[168:169]
	s_waitcnt vmcnt(1)
	v_pk_fma_f32 v[100:101], v[100:101], v[136:137], v[104:105]
	v_pk_fma_f32 v[98:99], v[98:99], v[134:135], v[102:103]
	s_waitcnt vmcnt(0)
	v_pk_fma_f32 v[102:103], v[40:41], v[132:133], v[108:109]
	v_pk_fma_f32 v[40:41], v[38:39], v[130:131], v[106:107]
	v_cvt_pk_bf16_f32 v38, v98, v99
	v_cvt_pk_bf16_f32 v39, v100, v101
	v_cvt_pk_bf16_f32 v40, v40, v41
	v_cvt_pk_bf16_f32 v41, v102, v103
	global_store_dwordx4 v[114:115], v[38:41], off offset:256 sc1
	global_load_dwordx4 v[98:101], v[112:113], off nt
	global_load_dwordx4 v[102:105], v[112:113], off offset:16 nt
	v_lshlrev_b64 v[106:107], 11, v[110:111]
	v_lshl_add_u64 v[106:107], v[172:173], 0, v[106:107]
	v_lshl_add_u64 v[108:109], v[174:175], 0, s[4:5]
	s_mov_b32 s4, 0xfc0a0000
	s_mov_b32 s5, -1
	s_waitcnt vmcnt(1)
	v_pk_fma_f32 v[96:97], v[96:97], v[144:145], v[100:101]
	v_pk_fma_f32 v[94:95], v[94:95], v[142:143], v[98:99]
	s_waitcnt vmcnt(0)
	v_pk_fma_f32 v[98:99], v[28:29], v[140:141], v[104:105]
	v_pk_fma_f32 v[28:29], v[26:27], v[138:139], v[102:103]
	v_cvt_pk_bf16_f32 v26, v94, v95
	v_cvt_pk_bf16_f32 v27, v96, v97
	v_cvt_pk_bf16_f32 v28, v28, v29
	v_cvt_pk_bf16_f32 v29, v98, v99
	global_store_dwordx4 v[106:107], v[26:29], off sc1
	global_load_dwordx4 v[94:97], v[112:113], off offset:512 nt
	global_load_dwordx4 v[98:101], v[112:113], off offset:528 nt
	v_add_u32_e32 v102, 0x90, v170
	v_ashrrev_i32_e32 v103, 31, v102
	v_lshlrev_b64 v[104:105], 12, v[102:103]
	v_lshl_add_u64 v[104:105], s[8:9], 0, v[104:105]
	v_cndmask_b32_e64 v105, v105, v109, s[0:1]
	v_cndmask_b32_e64 v104, v104, v108, s[0:1]
	v_lshl_add_u64 v[104:105], v[104:105], 0, v[168:169]
	s_waitcnt vmcnt(1)
	v_pk_fma_f32 v[32:33], v[32:33], v[136:137], v[96:97]
	v_pk_fma_f32 v[30:31], v[30:31], v[134:135], v[94:95]
	s_waitcnt vmcnt(0)
	v_pk_fma_f32 v[20:21], v[20:21], v[132:133], v[100:101]
	v_pk_fma_f32 v[18:19], v[18:19], v[130:131], v[98:99]
	v_cvt_pk_bf16_f32 v30, v30, v31
	v_cvt_pk_bf16_f32 v31, v32, v33
	v_cvt_pk_bf16_f32 v32, v18, v19
	v_cvt_pk_bf16_f32 v33, v20, v21
	global_store_dwordx4 v[106:107], v[30:33], off offset:256 sc1
	global_load_dwordx4 v[18:21], v[104:105], off nt
	global_load_dwordx4 v[94:97], v[104:105], off offset:16 nt
	v_lshlrev_b64 v[98:99], 11, v[102:103]
	v_lshl_add_u64 v[98:99], v[172:173], 0, v[98:99]
	v_lshl_add_u64 v[100:101], v[174:175], 0, s[4:5]
	s_mov_b32 s4, 0xfc0b0000
	s_mov_b32 s5, -1
	s_waitcnt vmcnt(1)
; #define LAS __attribute__((address_space(3)))
;     __device__ __forceinline__ void fused(f32x4 (&acc)[2][2][4][2], const pg8::Unit& u_, int wr_, int wc_, int fr_, int fq_, LAS unsigned char* lds, int tid_) const {
;     ...
;             for (int ai = 0; ai < 2; ++ai)
; #pragma unroll
;                 for (int m = 0; m < 4; ++m) { bf16_t* rowp = X + (size_t)(row0 + ai * HALF + m * 16) * D + col0;
; #pragma unroll
;                     for (int bj = 0; bj < 2; ++bj) { f32x4 s0, s1;
;                         if (LAYER == 0) { const float* sp = (isctx ? srcC + (size_t)(row0 - ML + ai * HALF + m * 16) * D : srcL + (size_t)(row0 + ai * HALF + m * 16) * D) + col0 + bj * HALF;
;                             s0 = __builtin_nontemporal_load((const f32x4*)sp); s1 = __builtin_nontemporal_load((const f32x4*)(sp + 4)); }
;                         else { const u32x4 xb = *(const u32x4*)(rowp + bj * HALF);
;                             s0 = (f32x4){__uint_as_float(xb.x << 16), __uint_as_float(xb.x & 0xffff0000u), __uint_as_float(xb.y << 16), __uint_as_float(xb.y & 0xffff0000u)};
;                             s1 = (f32x4){__uint_as_float(xb.z << 16), __uint_as_float(xb.z & 0xffff0000u), __uint_as_float(xb.w << 16), __uint_as_float(xb.w & 0xffff0000u)}; }
;                         const u32x4 w = pack8(s0 + gv[bj][0] * acc[ai][bj][m][0], s1 + gv[bj][1] * acc[ai][bj][m][1]);
;                         *(u32x4*)(rowp + bj * HALF) = w;
;                         acc[ai][bj][m][0] = (f32x4){__uint_as_float(w.x << 16), __uint_as_float(w.x & 0xffff0000u), __uint_as_float(w.y << 16), __uint_as_float(w.y & 0xffff0000u)};
;                         acc[ai][bj][m][1] = (f32x4){__uint_as_float(w.z << 16), __uint_as_float(w.z & 0xffff0000u), __uint_as_float(w.w << 16), __uint_as_float(w.w & 0xffff0000u)}; } }
;         }
;         asm volatile("s_waitcnt vmcnt(0)" ::: "memory"); __builtin_amdgcn_s_barrier(); asm volatile("" ::: "memory");
;         LAS bf16_t* WLh = (LAS bf16_t*)lds;
;         LAS bf16_t* WLl = WLh + 16 * 264;
;         LAS float* CSH = (LAS float*)(WLl + 16 * 264);
;         LAS float* P = CSH + 64;
;         LAS float* Sr = P + 256 * 4 * 20;
;         LAS float* LG = Sr + 256;
;         LAS unsigned* flag = (LAS unsigned*)(LG + 1024);
;         const float* mrow = mod + bidx * MODW;
	v_pk_fma_f32 v[20:21], v[92:93], v[144:145], v[20:21]
	v_pk_fma_f32 v[18:19], v[90:91], v[142:143], v[18:19]
	s_waitcnt vmcnt(0)
	v_pk_fma_f32 v[88:89], v[88:89], v[140:141], v[96:97]
	v_pk_fma_f32 v[86:87], v[86:87], v[138:139], v[94:95]
	v_cvt_pk_bf16_f32 v18, v18, v19
	v_cvt_pk_bf16_f32 v19, v20, v21
	v_cvt_pk_bf16_f32 v20, v86, v87
	v_cvt_pk_bf16_f32 v21, v88, v89
	global_store_dwordx4 v[98:99], v[18:21], off sc1
	global_load_dwordx4 v[86:89], v[104:105], off offset:512 nt
	global_load_dwordx4 v[90:93], v[104:105], off offset:528 nt
	v_add_u32_e32 v94, 0xa0, v170
	v_ashrrev_i32_e32 v95, 31, v94
	v_lshlrev_b64 v[96:97], 12, v[94:95]
	v_lshl_add_u64 v[96:97], s[8:9], 0, v[96:97]
	v_cndmask_b32_e64 v97, v97, v101, s[0:1]
	v_cndmask_b32_e64 v96, v96, v100, s[0:1]
	v_lshl_add_u64 v[96:97], v[96:97], 0, v[168:169]
	s_waitcnt vmcnt(1)
	v_pk_fma_f32 v[24:25], v[24:25], v[136:137], v[88:89]
	v_pk_fma_f32 v[22:23], v[22:23], v[134:135], v[86:87]
	s_waitcnt vmcnt(0)
	v_pk_fma_f32 v[12:13], v[12:13], v[132:133], v[92:93]
	v_pk_fma_f32 v[10:11], v[10:11], v[130:131], v[90:91]
	v_cvt_pk_bf16_f32 v22, v22, v23
	v_cvt_pk_bf16_f32 v23, v24, v25
	v_cvt_pk_bf16_f32 v24, v10, v11
	v_cvt_pk_bf16_f32 v25, v12, v13
	global_store_dwordx4 v[98:99], v[22:25], off offset:256 sc1
	global_load_dwordx4 v[10:13], v[96:97], off nt
	global_load_dwordx4 v[86:89], v[96:97], off offset:16 nt
	v_lshlrev_b64 v[90:91], 11, v[94:95]
	v_lshl_add_u64 v[90:91], v[172:173], 0, v[90:91]
	v_lshl_add_u64 v[92:93], v[174:175], 0, s[4:5]
	s_waitcnt vmcnt(1)
	v_pk_fma_f32 v[12:13], v[84:85], v[144:145], v[12:13]
	v_pk_fma_f32 v[10:11], v[82:83], v[142:143], v[10:11]
	s_waitcnt vmcnt(0)
	v_pk_fma_f32 v[80:81], v[80:81], v[140:141], v[88:89]
	v_pk_fma_f32 v[78:79], v[78:79], v[138:139], v[86:87]
	v_cvt_pk_bf16_f32 v10, v10, v11
	v_cvt_pk_bf16_f32 v11, v12, v13
	v_cvt_pk_bf16_f32 v12, v78, v79
	v_cvt_pk_bf16_f32 v13, v80, v81
	global_store_dwordx4 v[90:91], v[10:13], off sc1
	global_load_dwordx4 v[78:81], v[96:97], off offset:512 nt
	global_load_dwordx4 v[82:85], v[96:97], off offset:528 nt
	v_add_u32_e32 v86, 0xb0, v170
	v_ashrrev_i32_e32 v87, 31, v86
	v_lshlrev_b64 v[88:89], 12, v[86:87]
	v_lshl_add_u64 v[88:89], s[8:9], 0, v[88:89]
	v_cndmask_b32_e64 v89, v89, v93, s[0:1]
	v_cndmask_b32_e64 v88, v88, v92, s[0:1]
	v_lshl_add_u64 v[88:89], v[88:89], 0, v[168:169]
	s_movk_i32 s0, 0x1000
	v_cmp_gt_i32_e32 vcc, s0, v217
	s_waitcnt vmcnt(1)
	v_pk_fma_f32 v[16:17], v[16:17], v[136:137], v[80:81]
	v_pk_fma_f32 v[14:15], v[14:15], v[134:135], v[78:79]
	s_waitcnt vmcnt(0)
	v_pk_fma_f32 v[4:5], v[4:5], v[132:133], v[84:85]
	v_pk_fma_f32 v[2:3], v[2:3], v[130:131], v[82:83]
	v_cvt_pk_bf16_f32 v14, v14, v15
	v_cvt_pk_bf16_f32 v15, v16, v17
	v_cvt_pk_bf16_f32 v16, v2, v3
	v_cvt_pk_bf16_f32 v17, v4, v5
	global_store_dwordx4 v[90:91], v[14:17], off offset:256 sc1
	global_load_dwordx4 v[2:5], v[88:89], off nt
	global_load_dwordx4 v[78:81], v[88:89], off offset:16 nt
	v_lshlrev_b64 v[82:83], 11, v[86:87]
	v_lshl_add_u64 v[82:83], v[172:173], 0, v[82:83]
	s_waitcnt vmcnt(1)
	v_pk_fma_f32 v[4:5], v[76:77], v[144:145], v[4:5]
	v_pk_fma_f32 v[2:3], v[74:75], v[142:143], v[2:3]
	s_waitcnt vmcnt(0)
	v_pk_fma_f32 v[72:73], v[72:73], v[140:141], v[80:81]
	v_pk_fma_f32 v[70:71], v[70:71], v[138:139], v[78:79]
	v_cvt_pk_bf16_f32 v2, v2, v3
	v_cvt_pk_bf16_f32 v3, v4, v5
	v_cvt_pk_bf16_f32 v4, v70, v71
	v_cvt_pk_bf16_f32 v5, v72, v73
	global_store_dwordx4 v[82:83], v[2:5], off sc1
	global_load_dwordx4 v[70:73], v[88:89], off offset:512 nt
	global_load_dwordx4 v[74:77], v[88:89], off offset:528 nt
	s_waitcnt vmcnt(1)
	v_pk_fma_f32 v[64:65], v[64:65], v[136:137], v[72:73]
	v_pk_fma_f32 v[62:63], v[62:63], v[134:135], v[70:71]
	s_waitcnt vmcnt(0)
	v_pk_fma_f32 v[70:71], v[8:9], v[132:133], v[76:77]
	v_pk_fma_f32 v[8:9], v[6:7], v[130:131], v[74:75]
	v_cvt_pk_bf16_f32 v6, v62, v63
	v_cvt_pk_bf16_f32 v7, v64, v65
	v_cvt_pk_bf16_f32 v8, v8, v9
	v_cvt_pk_bf16_f32 v9, v70, v71
	global_store_dwordx4 v[82:83], v[6:9], off offset:256 sc1
	s_waitcnt vmcnt(0)
	s_barrier
	s_and_saveexec_b64 s[0:1], vcc
	s_cbranch_execz .LBB0_565
	v_mul_u32_u24_e32 v62, 0x108, v158
	s_mov_b64 s[4:5], 0
	v_mov_b32_e32 v63, v217

; __device__ __forceinline__ u32x4 pack8(const f32x4 a, const f32x4 b) { u32x4 w; w.x = cvt_pk_bf16(a[0], a[1]); w.y = cvt_pk_bf16(a[2], a[3]); w.z = cvt_pk_bf16(b[0], b[1]); w.w = cvt_pk_bf16(b[2], b[3]); return w; }
;     __device__ __forceinline__ void fused(f32x4 (&acc)[2][2][4][2], const pg8::Unit& u_, int wr_, int wc_, int fr_, int fq_, LAS unsigned char* lds, int tid_) const {
;     ...
;         for (int bj = 0; bj < 2; ++bj) { f32x4 G[2], SH[2];
; #pragma unroll
;             for (int n = 0; n < 2; ++n) { const int c = col0 + bj * HALF + 4 * n; const f32x4 gg = *(const f32x4*)(g2 + c), sc = *(const f32x4*)(mrow + 4 * D + c);
;                 G[n] = gg * (sc + 1.f); SH[n] = *(const f32x4*)(mrow + 3 * D + c); }
; #pragma unroll
;             for (int ai = 0; ai < 2; ++ai)
; #pragma unroll
;                 for (int m = 0; m < 4; ++m) { const int rl = ai * HALF + wr * 64 + m * 16 + fr; const float r = bad ? __builtin_nanf("") : Sr[rl];
;                     *(u32x4*)(HB + (size_t)(u.pm * BM + rl) * D + col0 + bj * HALF) = pack8(acc[ai][bj][m][0] * r * G[0] + SH[0], acc[ai][bj][m][1] * r * G[1] + SH[1]); }
;             asm volatile("" ::: "memory"); }
.LBB0_609:
	s_waitcnt vmcnt(3)
	v_pk_add_f32 v[24:25], v[24:25], 1.0 op_sel_hi:[1,0]
	v_pk_add_f32 v[22:23], v[22:23], 1.0 op_sel_hi:[1,0]
	s_waitcnt vmcnt(1)
	v_pk_add_f32 v[18:19], v[18:19], 1.0 op_sel_hi:[1,0]
	v_pk_add_f32 v[20:21], v[20:21], 1.0 op_sel_hi:[1,0]
	v_pk_mul_f32 v[16:17], v[16:17], v[24:25]
	v_pk_mul_f32 v[14:15], v[14:15], v[22:23]
	v_pk_mul_f32 v[12:13], v[12:13], v[20:21]
	v_pk_mul_f32 v[10:11], v[10:11], v[18:19]
	s_waitcnt lgkmcnt(0)
	v_pk_mul_f32 v[18:19], v[64:65], v[90:91] op_sel_hi:[0,1]
	v_pk_mul_f32 v[20:21], v[64:65], v[88:89] op_sel_hi:[0,1]
	v_pk_fma_f32 v[22:23], v[16:17], v[18:19], v[8:9]
	v_pk_fma_f32 v[18:19], v[14:15], v[20:21], v[6:7]
	v_pk_mul_f32 v[20:21], v[64:65], v[86:87] op_sel_hi:[0,1]
	v_pk_mul_f32 v[24:25], v[64:65], v[84:85] op_sel_hi:[0,1]
	v_lshl_add_u64 v[72:73], v[164:165], 1, s[82:83]
	s_waitcnt vmcnt(0)
	v_pk_fma_f32 v[64:65], v[12:13], v[20:21], v[4:5]
	v_pk_fma_f32 v[20:21], v[10:11], v[24:25], v[2:3]
	v_cvt_pk_bf16_f32 v18, v18, v19
	v_cvt_pk_bf16_f32 v19, v22, v23
	v_cvt_pk_bf16_f32 v20, v20, v21
	v_cvt_pk_bf16_f32 v21, v64, v65
	v_lshl_add_u64 v[64:65], v[72:73], 0, v[166:167]
	s_and_b64 vcc, exec, s[6:7]
	v_add_u32_e32 v90, 16, v216
	global_store_dwordx4 v[64:65], v[18:21], off sc1
	s_cbranch_vccnz .LBB0_611
	s_nop 0
	v_lshl_add_u32 v18, v90, 2, 0
	v_add_u32_e32 v18, 0x18300, v18
	ds_read_b32 v66, v18
.LBB0_611:
	s_waitcnt lgkmcnt(0)
	v_pk_mul_f32 v[18:19], v[66:67], v[102:103] op_sel_hi:[0,1]
	v_pk_mul_f32 v[20:21], v[66:67], v[98:99] op_sel_hi:[0,1]
	v_pk_fma_f32 v[22:23], v[16:17], v[18:19], v[8:9]
	v_pk_fma_f32 v[18:19], v[14:15], v[20:21], v[6:7]
	v_pk_mul_f32 v[20:21], v[66:67], v[94:95] op_sel_hi:[0,1]
	v_cvt_pk_bf16_f32 v18, v18, v19
	v_cvt_pk_bf16_f32 v19, v22, v23
	v_add_u32_e32 v22, s25, v90
	v_pk_mul_f32 v[24:25], v[66:67], v[92:93] op_sel_hi:[0,1]
	v_ashrrev_i32_e32 v23, 31, v22
	v_pk_fma_f32 v[66:67], v[12:13], v[20:21], v[4:5]
	v_pk_fma_f32 v[20:21], v[10:11], v[24:25], v[2:3]
	v_lshlrev_b64 v[22:23], 11, v[22:23]
	v_cvt_pk_bf16_f32 v20, v20, v21
	v_cvt_pk_bf16_f32 v21, v66, v67
	v_lshl_add_u64 v[66:67], v[72:73], 0, v[22:23]
	global_store_dwordx4 v[66:67], v[18:21], off sc1
	v_add_u32_e32 v91, 32, v216
	s_and_b64 vcc, exec, s[6:7]
	v_mov_b32_e32 v18, 0x7fc00000
	v_mov_b32_e32 v20, 0x7fc00000
	s_cbranch_vccnz .LBB0_613
	v_lshl_add_u32 v19, v91, 2, 0
	v_add_u32_e32 v19, 0x18300, v19
	ds_read_b32 v20, v19
.LBB0_613:
	s_waitcnt lgkmcnt(0)
	v_pk_mul_f32 v[24:25], v[20:21], v[110:111] op_sel_hi:[0,1]
	v_pk_mul_f32 v[22:23], v[20:21], v[112:113] op_sel_hi:[0,1]
	v_pk_fma_f32 v[24:25], v[14:15], v[24:25], v[6:7]
	v_pk_mul_f32 v[68:69], v[20:21], v[108:109] op_sel_hi:[0,1]
	v_pk_mul_f32 v[20:21], v[20:21], v[106:107] op_sel_hi:[0,1]
	v_pk_fma_f32 v[70:71], v[10:11], v[20:21], v[2:3]
	v_cvt_pk_bf16_f32 v20, v24, v25
	v_add_u32_e32 v24, s25, v91
	v_ashrrev_i32_e32 v25, 31, v24
	v_pk_fma_f32 v[22:23], v[16:17], v[22:23], v[8:9]
	v_pk_fma_f32 v[68:69], v[12:13], v[68:69], v[4:5]
	v_lshlrev_b64 v[24:25], 11, v[24:25]
	v_cvt_pk_bf16_f32 v21, v22, v23
	v_cvt_pk_bf16_f32 v22, v70, v71
	v_cvt_pk_bf16_f32 v23, v68, v69
	v_lshl_add_u64 v[68:69], v[72:73], 0, v[24:25]
	s_and_b64 vcc, exec, s[6:7]
	v_add_u32_e32 v92, 48, v216
	global_store_dwordx4 v[68:69], v[20:23], off sc1
	s_cbranch_vccnz .LBB0_615
	v_lshl_add_u32 v18, v92, 2, 0
	v_add_u32_e32 v18, 0x18300, v18
	ds_read_b32 v18, v18
.LBB0_615:
	s_waitcnt lgkmcnt(0)
	v_pk_mul_f32 v[22:23], v[18:19], v[126:127] op_sel_hi:[0,1]
	v_pk_mul_f32 v[20:21], v[18:19], v[128:129] op_sel_hi:[0,1]
	v_pk_fma_f32 v[22:23], v[14:15], v[22:23], v[6:7]
	v_pk_mul_f32 v[24:25], v[18:19], v[124:125] op_sel_hi:[0,1]
	v_pk_mul_f32 v[18:19], v[18:19], v[122:123] op_sel_hi:[0,1]
	v_pk_fma_f32 v[70:71], v[10:11], v[18:19], v[2:3]
	v_cvt_pk_bf16_f32 v18, v22, v23
	v_add_u32_e32 v22, s25, v92
	v_ashrrev_i32_e32 v23, 31, v22
	v_pk_fma_f32 v[20:21], v[16:17], v[20:21], v[8:9]
	v_pk_fma_f32 v[24:25], v[12:13], v[24:25], v[4:5]
	v_lshlrev_b64 v[22:23], 11, v[22:23]
	v_cvt_pk_bf16_f32 v19, v20, v21
	v_cvt_pk_bf16_f32 v20, v70, v71
	v_cvt_pk_bf16_f32 v21, v24, v25
	v_lshl_add_u64 v[70:71], v[72:73], 0, v[22:23]
	global_store_dwordx4 v[70:71], v[18:21], off sc1
	v_add_u32_e32 v93, 0x80, v216
	s_and_b64 vcc, exec, s[6:7]
	v_mov_b32_e32 v18, 0x7fc00000
	v_mov_b32_e32 v20, 0x7fc00000
	s_cbranch_vccnz .LBB0_617
	v_lshl_add_u32 v19, v93, 2, 0
	v_add_u32_e32 v19, 0x18300, v19
	ds_read_b32 v20, v19
.LBB0_617:
	s_waitcnt lgkmcnt(0)
	v_pk_mul_f32 v[24:25], v[20:21], v[142:143] op_sel_hi:[0,1]
	v_pk_mul_f32 v[22:23], v[20:21], v[144:145] op_sel_hi:[0,1]
	v_pk_fma_f32 v[24:25], v[14:15], v[24:25], v[6:7]
	v_pk_mul_f32 v[84:85], v[20:21], v[140:141] op_sel_hi:[0,1]
	v_pk_mul_f32 v[20:21], v[20:21], v[138:139] op_sel_hi:[0,1]
	v_pk_fma_f32 v[86:87], v[10:11], v[20:21], v[2:3]
	v_cvt_pk_bf16_f32 v20, v24, v25
	v_add_u32_e32 v24, s25, v93
	v_ashrrev_i32_e32 v25, 31, v24
	v_pk_fma_f32 v[22:23], v[16:17], v[22:23], v[8:9]
	v_pk_fma_f32 v[84:85], v[12:13], v[84:85], v[4:5]
	v_lshlrev_b64 v[24:25], 11, v[24:25]
	v_cvt_pk_bf16_f32 v21, v22, v23
	v_cvt_pk_bf16_f32 v22, v86, v87
	v_cvt_pk_bf16_f32 v23, v84, v85
	v_lshl_add_u64 v[84:85], v[72:73], 0, v[24:25]
	s_and_b64 vcc, exec, s[6:7]
	v_add_u32_e32 v94, 0x90, v216
	global_store_dwordx4 v[84:85], v[20:23], off sc1
	s_cbranch_vccnz .LBB0_619
	v_lshl_add_u32 v18, v94, 2, 0
	v_add_u32_e32 v18, 0x18300, v18
	ds_read_b32 v18, v18
; __device__ __forceinline__ u32x4 pack8(const f32x4 a, const f32x4 b) { u32x4 w; w.x = cvt_pk_bf16(a[0], a[1]); w.y = cvt_pk_bf16(a[2], a[3]); w.z = cvt_pk_bf16(b[0], b[1]); w.w = cvt_pk_bf16(b[2], b[3]); return w; }
;     __device__ __forceinline__ void fused(f32x4 (&acc)[2][2][4][2], const pg8::Unit& u_, int wr_, int wc_, int fr_, int fq_, LAS unsigned char* lds, int tid_) const {
;     ...
;         for (int bj = 0; bj < 2; ++bj) { f32x4 G[2], SH[2];
; #pragma unroll
;             for (int n = 0; n < 2; ++n) { const int c = col0 + bj * HALF + 4 * n; const f32x4 gg = *(const f32x4*)(g2 + c), sc = *(const f32x4*)(mrow + 4 * D + c);
;                 G[n] = gg * (sc + 1.f); SH[n] = *(const f32x4*)(mrow + 3 * D + c); }
; #pragma unroll
;             for (int ai = 0; ai < 2; ++ai)
; #pragma unroll
;                 for (int m = 0; m < 4; ++m) { const int rl = ai * HALF + wr * 64 + m * 16 + fr; const float r = bad ? __builtin_nanf("") : Sr[rl];
;                     *(u32x4*)(HB + (size_t)(u.pm * BM + rl) * D + col0 + bj * HALF) = pack8(acc[ai][bj][m][0] * r * G[0] + SH[0], acc[ai][bj][m][1] * r * G[1] + SH[1]); }
;             asm volatile("" ::: "memory"); }
.LBB0_619:
	s_waitcnt lgkmcnt(0)
	v_pk_mul_f32 v[22:23], v[18:19], v[174:175] op_sel_hi:[0,1]
	v_pk_mul_f32 v[20:21], v[18:19], v[176:177] op_sel_hi:[0,1]
	v_pk_fma_f32 v[22:23], v[14:15], v[22:23], v[6:7]
	v_pk_mul_f32 v[24:25], v[18:19], v[172:173] op_sel_hi:[0,1]
	v_pk_mul_f32 v[18:19], v[18:19], v[170:171] op_sel_hi:[0,1]
	v_pk_fma_f32 v[86:87], v[10:11], v[18:19], v[2:3]
	v_cvt_pk_bf16_f32 v18, v22, v23
	v_add_u32_e32 v22, s25, v94
	v_ashrrev_i32_e32 v23, 31, v22
	v_pk_fma_f32 v[20:21], v[16:17], v[20:21], v[8:9]
	v_pk_fma_f32 v[24:25], v[12:13], v[24:25], v[4:5]
	v_lshlrev_b64 v[22:23], 11, v[22:23]
	v_cvt_pk_bf16_f32 v19, v20, v21
	v_cvt_pk_bf16_f32 v20, v86, v87
	v_cvt_pk_bf16_f32 v21, v24, v25
	v_lshl_add_u64 v[86:87], v[72:73], 0, v[22:23]
	global_store_dwordx4 v[86:87], v[18:21], off sc1
	v_add_u32_e32 v95, 0xa0, v216
	s_and_b64 vcc, exec, s[6:7]
	v_mov_b32_e32 v18, 0x7fc00000
	v_mov_b32_e32 v20, 0x7fc00000
	s_cbranch_vccnz .LBB0_621
	v_lshl_add_u32 v19, v95, 2, 0
	v_add_u32_e32 v19, 0x18300, v19
	ds_read_b32 v20, v19
.LBB0_621:
	s_waitcnt lgkmcnt(0)
	v_pk_mul_f32 v[24:25], v[20:21], v[182:183] op_sel_hi:[0,1]
	v_pk_mul_f32 v[22:23], v[20:21], v[184:185] op_sel_hi:[0,1]
	v_pk_fma_f32 v[24:25], v[14:15], v[24:25], v[6:7]
	v_pk_mul_f32 v[88:89], v[20:21], v[180:181] op_sel_hi:[0,1]
	v_pk_mul_f32 v[20:21], v[20:21], v[178:179] op_sel_hi:[0,1]
	v_pk_fma_f32 v[98:99], v[10:11], v[20:21], v[2:3]
	v_cvt_pk_bf16_f32 v20, v24, v25
	v_add_u32_e32 v24, s25, v95
	v_ashrrev_i32_e32 v25, 31, v24
	v_pk_fma_f32 v[22:23], v[16:17], v[22:23], v[8:9]
	v_pk_fma_f32 v[88:89], v[12:13], v[88:89], v[4:5]
	v_lshlrev_b64 v[24:25], 11, v[24:25]
	v_cvt_pk_bf16_f32 v21, v22, v23
	v_cvt_pk_bf16_f32 v22, v98, v99
	v_cvt_pk_bf16_f32 v23, v88, v89
	v_lshl_add_u64 v[88:89], v[72:73], 0, v[24:25]
	s_and_b64 vcc, exec, s[6:7]
	v_add_u32_e32 v98, 0xb0, v216
	global_store_dwordx4 v[88:89], v[20:23], off sc1
	s_cbranch_vccnz .LBB0_623
	v_lshl_add_u32 v18, v98, 2, 0
	v_add_u32_e32 v18, 0x18300, v18
	ds_read_b32 v18, v18
.LBB0_623:
	s_waitcnt lgkmcnt(0)
	v_pk_mul_f32 v[20:21], v[18:19], v[192:193] op_sel_hi:[0,1]
	v_pk_mul_f32 v[22:23], v[18:19], v[190:191] op_sel_hi:[0,1]
	v_pk_fma_f32 v[8:9], v[16:17], v[20:21], v[8:9]
	v_pk_fma_f32 v[6:7], v[14:15], v[22:23], v[6:7]
	v_pk_mul_f32 v[14:15], v[18:19], v[188:189] op_sel_hi:[0,1]
	v_pk_mul_f32 v[16:17], v[18:19], v[186:187] op_sel_hi:[0,1]
	v_pk_fma_f32 v[12:13], v[12:13], v[14:15], v[4:5]
	v_pk_fma_f32 v[4:5], v[10:11], v[16:17], v[2:3]
	v_cvt_pk_bf16_f32 v2, v6, v7
	v_add_u32_e32 v6, s25, v98
	v_ashrrev_i32_e32 v7, 31, v6
	v_lshlrev_b64 v[6:7], 11, v[6:7]
	v_cvt_pk_bf16_f32 v3, v8, v9
	v_cvt_pk_bf16_f32 v4, v4, v5
	v_cvt_pk_bf16_f32 v5, v12, v13
	v_lshl_add_u64 v[72:73], v[72:73], 0, v[6:7]
	global_store_dwordx4 v[72:73], v[2:5], off sc1
	global_load_dwordx4 v[10:13], v[58:59], off offset:528
	global_load_dwordx4 v[18:21], v[58:59], off offset:512
	global_load_dwordx4 v[14:17], v[60:61], off offset:528
	global_load_dwordx4 v[22:25], v[60:61], off offset:512
	global_load_dwordx4 v[2:5], v[62:63], off offset:528
	global_load_dwordx4 v[6:9], v[62:63], off offset:512
	v_mov_b32_e32 v58, 0x7fc00000
	s_and_b64 vcc, exec, s[6:7]
	v_mov_b32_e32 v60, 0x7fc00000
	s_cbranch_vccnz .LBB0_625
	v_lshl_add_u32 v59, v216, 2, 0
	v_add_u32_e32 v59, 0x18300, v59
	ds_read_b32 v60, v59
.LBB0_625:
	s_waitcnt vmcnt(2)
	v_pk_add_f32 v[24:25], v[24:25], 1.0 op_sel_hi:[1,0]
	v_pk_add_f32 v[22:23], v[22:23], 1.0 op_sel_hi:[1,0]
	v_pk_add_f32 v[14:15], v[14:15], 1.0 op_sel_hi:[1,0]
	v_pk_add_f32 v[16:17], v[16:17], 1.0 op_sel_hi:[1,0]
	v_pk_mul_f32 v[20:21], v[20:21], v[24:25]
	v_pk_mul_f32 v[18:19], v[18:19], v[22:23]
	v_pk_mul_f32 v[12:13], v[12:13], v[16:17]
	v_pk_mul_f32 v[10:11], v[10:11], v[14:15]
	s_waitcnt lgkmcnt(0)
	v_pk_mul_f32 v[14:15], v[60:61], v[80:81] op_sel_hi:[0,1]
	v_pk_mul_f32 v[16:17], v[60:61], v[78:79] op_sel_hi:[0,1]
	s_waitcnt vmcnt(0)
	v_pk_fma_f32 v[22:23], v[20:21], v[14:15], v[8:9]
	v_pk_fma_f32 v[14:15], v[18:19], v[16:17], v[6:7]
	v_pk_mul_f32 v[16:17], v[60:61], v[76:77] op_sel_hi:[0,1]
	v_pk_mul_f32 v[24:25], v[60:61], v[74:75] op_sel_hi:[0,1]
	v_pk_fma_f32 v[60:61], v[12:13], v[16:17], v[4:5]
	v_pk_fma_f32 v[16:17], v[10:11], v[24:25], v[2:3]
	v_cvt_pk_bf16_f32 v14, v14, v15
	v_cvt_pk_bf16_f32 v15, v22, v23
	v_cvt_pk_bf16_f32 v16, v16, v17
	v_cvt_pk_bf16_f32 v17, v60, v61
	s_and_b64 vcc, exec, s[6:7]
	global_store_dwordx4 v[64:65], v[14:17], off offset:256 sc1
	s_cbranch_vccnz .LBB0_627
	s_nop 0
	v_lshl_add_u32 v14, v90, 2, 0
	v_add_u32_e32 v14, 0x18300, v14
	ds_read_b32 v58, v14
.LBB0_627:
	s_waitcnt lgkmcnt(0)
	v_pk_mul_f32 v[14:15], v[58:59], v[54:55] op_sel_hi:[0,1]
	v_pk_mul_f32 v[16:17], v[58:59], v[82:83] op_sel_hi:[0,1]
	v_pk_fma_f32 v[22:23], v[20:21], v[14:15], v[8:9]
	v_pk_fma_f32 v[14:15], v[18:19], v[16:17], v[6:7]
	v_pk_mul_f32 v[16:17], v[58:59], v[52:53] op_sel_hi:[0,1]
	v_pk_mul_f32 v[24:25], v[58:59], v[50:51] op_sel_hi:[0,1]
	v_pk_fma_f32 v[50:51], v[12:13], v[16:17], v[4:5]
	v_pk_fma_f32 v[16:17], v[10:11], v[24:25], v[2:3]
	v_cvt_pk_bf16_f32 v14, v14, v15
	v_cvt_pk_bf16_f32 v15, v22, v23
	v_cvt_pk_bf16_f32 v16, v16, v17
	v_cvt_pk_bf16_f32 v17, v50, v51
	global_store_dwordx4 v[66:67], v[14:17], off offset:256 sc1
	s_and_b64 vcc, exec, s[6:7]
	s_nop 0
	v_mov_b32_e32 v14, 0x7fc00000
	v_mov_b32_e32 v16, 0x7fc00000
	s_cbranch_vccnz .LBB0_629
	v_lshl_add_u32 v15, v91, 2, 0
	v_add_u32_e32 v15, 0x18300, v15
	ds_read_b32 v16, v15
; __device__ __forceinline__ u32x4 pack8(const f32x4 a, const f32x4 b) { u32x4 w; w.x = cvt_pk_bf16(a[0], a[1]); w.y = cvt_pk_bf16(a[2], a[3]); w.z = cvt_pk_bf16(b[0], b[1]); w.w = cvt_pk_bf16(b[2], b[3]); return w; }
; #define PG8_BAR __builtin_amdgcn_s_barrier()
;     ...
;         if (!has_next) break;
; #pragma unroll
;         for (int a = 0; a < 2; ++a)
; #pragma unroll
;             for (int b = 0; b < 2; ++b)
; #pragma unroll
;                 for (int m = 0; m < 4; ++m)
; #pragma unroll
;                     for (int n = 0; n < 2; ++n) acc[a][b][m][n] = (f32x4){0.f, 0.f, 0.f, 0.f};
;         cur = nxt; cA = nA; cB = nB; ++ui;
; #pragma unroll
;         for (int hh = 0; hh < 2; ++hh)
; #pragma unroll
;             for (int i = 0; i < 2; ++i) voffA[hh][i] = voffN[hh][i];
;         if (wr == 1) PG8_BAR;
;     __device__ __forceinline__ void fused(f32x4 (&acc)[2][2][4][2], const pg8::Unit& u_, int wr_, int wc_, int fr_, int fq_, LAS unsigned char* lds, int tid_) const {
;     ...
;         for (int bj = 0; bj < 2; ++bj) { f32x4 G[2], SH[2];
; #pragma unroll
;             for (int n = 0; n < 2; ++n) { const int c = col0 + bj * HALF + 4 * n; const f32x4 gg = *(const f32x4*)(g2 + c), sc = *(const f32x4*)(mrow + 4 * D + c);
;                 G[n] = gg * (sc + 1.f); SH[n] = *(const f32x4*)(mrow + 3 * D + c); }
; #pragma unroll
;             for (int ai = 0; ai < 2; ++ai)
; #pragma unroll
;                 for (int m = 0; m < 4; ++m) { const int rl = ai * HALF + wr * 64 + m * 16 + fr; const float r = bad ? __builtin_nanf("") : Sr[rl];
;                     *(u32x4*)(HB + (size_t)(u.pm * BM + rl) * D + col0 + bj * HALF) = pack8(acc[ai][bj][m][0] * r * G[0] + SH[0], acc[ai][bj][m][1] * r * G[1] + SH[1]); }
;             asm volatile("" ::: "memory"); }
.LBB0_629:
	s_waitcnt lgkmcnt(0)
	v_pk_mul_f32 v[22:23], v[16:17], v[46:47] op_sel_hi:[0,1]
	v_pk_mul_f32 v[24:25], v[16:17], v[56:57] op_sel_hi:[0,1]
	v_pk_fma_f32 v[46:47], v[20:21], v[22:23], v[8:9]
	v_pk_fma_f32 v[22:23], v[18:19], v[24:25], v[6:7]
	v_pk_mul_f32 v[24:25], v[16:17], v[44:45] op_sel_hi:[0,1]
	v_pk_mul_f32 v[16:17], v[16:17], v[42:43] op_sel_hi:[0,1]
	v_pk_fma_f32 v[42:43], v[12:13], v[24:25], v[4:5]
	v_pk_fma_f32 v[16:17], v[10:11], v[16:17], v[2:3]
	v_cvt_pk_bf16_f32 v22, v22, v23
	v_cvt_pk_bf16_f32 v23, v46, v47
	v_cvt_pk_bf16_f32 v24, v16, v17
	v_cvt_pk_bf16_f32 v25, v42, v43
	s_and_b64 vcc, exec, s[6:7]
	global_store_dwordx4 v[68:69], v[22:25], off offset:256 sc1
	s_cbranch_vccnz .LBB0_631
	v_lshl_add_u32 v14, v92, 2, 0
	v_add_u32_e32 v14, 0x18300, v14
	ds_read_b32 v14, v14
.LBB0_631:
	s_waitcnt lgkmcnt(0)
	v_pk_mul_f32 v[16:17], v[14:15], v[38:39] op_sel_hi:[0,1]
	v_pk_mul_f32 v[22:23], v[14:15], v[48:49] op_sel_hi:[0,1]
	v_pk_mul_f32 v[24:25], v[14:15], v[36:37] op_sel_hi:[0,1]
	v_pk_mul_f32 v[14:15], v[14:15], v[34:35] op_sel_hi:[0,1]
	v_pk_fma_f32 v[16:17], v[20:21], v[16:17], v[8:9]
	v_pk_fma_f32 v[22:23], v[18:19], v[22:23], v[6:7]
	v_pk_fma_f32 v[24:25], v[12:13], v[24:25], v[4:5]
	v_pk_fma_f32 v[34:35], v[10:11], v[14:15], v[2:3]
	v_cvt_pk_bf16_f32 v14, v22, v23
	v_cvt_pk_bf16_f32 v15, v16, v17
	v_cvt_pk_bf16_f32 v16, v34, v35
	v_cvt_pk_bf16_f32 v17, v24, v25
	global_store_dwordx4 v[70:71], v[14:17], off offset:256 sc1
	s_and_b64 vcc, exec, s[6:7]
	s_nop 0
	v_mov_b32_e32 v14, 0x7fc00000
	v_mov_b32_e32 v16, 0x7fc00000
	s_cbranch_vccnz .LBB0_633
	v_lshl_add_u32 v15, v93, 2, 0
	v_add_u32_e32 v15, 0x18300, v15
	ds_read_b32 v16, v15
.LBB0_633:
	s_waitcnt lgkmcnt(0)
	v_pk_mul_f32 v[22:23], v[16:17], v[30:31] op_sel_hi:[0,1]
	v_pk_mul_f32 v[24:25], v[16:17], v[40:41] op_sel_hi:[0,1]
	v_pk_fma_f32 v[30:31], v[20:21], v[22:23], v[8:9]
	v_pk_fma_f32 v[22:23], v[18:19], v[24:25], v[6:7]
	v_pk_mul_f32 v[24:25], v[16:17], v[28:29] op_sel_hi:[0,1]
	v_pk_mul_f32 v[16:17], v[16:17], v[26:27] op_sel_hi:[0,1]
	v_pk_fma_f32 v[26:27], v[12:13], v[24:25], v[4:5]
	v_pk_fma_f32 v[16:17], v[10:11], v[16:17], v[2:3]
	v_cvt_pk_bf16_f32 v22, v22, v23
	v_cvt_pk_bf16_f32 v23, v30, v31
	v_cvt_pk_bf16_f32 v24, v16, v17
	v_cvt_pk_bf16_f32 v25, v26, v27
	s_and_b64 vcc, exec, s[6:7]
	global_store_dwordx4 v[84:85], v[22:25], off offset:256 sc1
	s_cbranch_vccnz .LBB0_635
	v_lshl_add_u32 v14, v94, 2, 0
	v_add_u32_e32 v14, 0x18300, v14
	ds_read_b32 v14, v14
.LBB0_635:
	s_waitcnt lgkmcnt(0)
	v_pk_mul_f32 v[16:17], v[14:15], v[104:105] op_sel_hi:[0,1]
	v_pk_mul_f32 v[22:23], v[14:15], v[100:101] op_sel_hi:[0,1]
	v_pk_mul_f32 v[24:25], v[14:15], v[96:97] op_sel_hi:[0,1]
	v_pk_mul_f32 v[14:15], v[14:15], v[32:33] op_sel_hi:[0,1]
	v_pk_fma_f32 v[16:17], v[20:21], v[16:17], v[8:9]
	v_pk_fma_f32 v[22:23], v[18:19], v[22:23], v[6:7]
	v_pk_fma_f32 v[24:25], v[12:13], v[24:25], v[4:5]
	v_pk_fma_f32 v[26:27], v[10:11], v[14:15], v[2:3]
	v_cvt_pk_bf16_f32 v14, v22, v23
	v_cvt_pk_bf16_f32 v15, v16, v17
	v_cvt_pk_bf16_f32 v16, v26, v27
	v_cvt_pk_bf16_f32 v17, v24, v25
	global_store_dwordx4 v[86:87], v[14:17], off offset:256 sc1
	s_and_b64 vcc, exec, s[6:7]
	s_nop 0
	v_mov_b32_e32 v14, 0x7fc00000
	v_mov_b32_e32 v16, 0x7fc00000
	s_cbranch_vccnz .LBB0_637
	v_lshl_add_u32 v15, v95, 2, 0
	v_add_u32_e32 v15, 0x18300, v15
	ds_read_b32 v16, v15
.LBB0_637:
	s_waitcnt lgkmcnt(0)
	v_pk_mul_f32 v[22:23], v[16:17], v[120:121] op_sel_hi:[0,1]
	v_pk_mul_f32 v[24:25], v[16:17], v[118:119] op_sel_hi:[0,1]
	v_pk_fma_f32 v[26:27], v[20:21], v[22:23], v[8:9]
	v_pk_fma_f32 v[22:23], v[18:19], v[24:25], v[6:7]
	v_pk_mul_f32 v[24:25], v[16:17], v[116:117] op_sel_hi:[0,1]
	v_pk_mul_f32 v[16:17], v[16:17], v[114:115] op_sel_hi:[0,1]
	v_pk_fma_f32 v[28:29], v[12:13], v[24:25], v[4:5]
	v_pk_fma_f32 v[16:17], v[10:11], v[16:17], v[2:3]
	v_cvt_pk_bf16_f32 v22, v22, v23
	v_cvt_pk_bf16_f32 v23, v26, v27
	v_cvt_pk_bf16_f32 v24, v16, v17
	v_cvt_pk_bf16_f32 v25, v28, v29
	s_and_b64 vcc, exec, s[6:7]
	global_store_dwordx4 v[88:89], v[22:25], off offset:256 sc1
	s_cbranch_vccnz .LBB0_639
	v_lshl_add_u32 v14, v98, 2, 0
	v_add_u32_e32 v14, 0x18300, v14
	ds_read_b32 v14, v14
.LBB0_639:
	s_waitcnt lgkmcnt(0)
	v_pk_mul_f32 v[16:17], v[14:15], v[136:137] op_sel_hi:[0,1]
	v_pk_mul_f32 v[22:23], v[14:15], v[134:135] op_sel_hi:[0,1]
	v_pk_fma_f32 v[8:9], v[20:21], v[16:17], v[8:9]
	v_pk_mul_f32 v[16:17], v[14:15], v[132:133] op_sel_hi:[0,1]
	v_pk_mul_f32 v[14:15], v[14:15], v[130:131] op_sel_hi:[0,1]
	v_pk_fma_f32 v[6:7], v[18:19], v[22:23], v[6:7]
	v_pk_fma_f32 v[12:13], v[12:13], v[16:17], v[4:5]
	v_pk_fma_f32 v[4:5], v[10:11], v[14:15], v[2:3]
	v_cvt_pk_bf16_f32 v2, v6, v7
	v_cvt_pk_bf16_f32 v3, v8, v9
	v_cvt_pk_bf16_f32 v4, v4, v5
	v_cvt_pk_bf16_f32 v5, v12, v13
	global_store_dwordx4 v[72:73], v[2:5], off offset:256 sc1
	s_andn2_b64 vcc, exec, s[30:31]
	s_mov_b64 s[0:1], -1
	s_cbranch_vccnz .LBB0_553
	v_readlane_b32 s0, v250, 32
	v_readlane_b32 s1, v250, 33
	s_andn2_b64 vcc, exec, s[0:1]
	s_cbranch_vccnz .LBB0_552
	s_barrier
	s_branch .LBB0_552

; template <int VPT>
; __device__ __forceinline__ void topk_list(const Params& p, LAS unsigned char* lds, const float* a, int N, int cap, int rowbase, int mbase, int e) {
;     ...
;     if (active) {
; #pragma unroll
;         for (int j = 0; j < VPT; ++j) {
;             const int i = tid * VPT + j, row = rowbase + i; int slot = -1;
;             if (k[j] > T) slot = gtb++;
;             else if (k[j] == T) { if (eqb < need) slot = G + eqb; ++eqb; }
;             if (slot >= 0) { const int m = mbase + slot; WSP(int, OFF_RIDX)[e * MEXP + m] = row; WSP(float, OFF_GATE)[e * MEXP + m] = __uint_as_float(k[j] >> 2); WSP(int, OFF_SLOT)[row * 16 + e] = m; }
;             else WSP(int, OFF_SLOT)[row * 16 + e] = -1;
;         }
.LBB0_926:
	s_or_b64 exec, exec, s[0:1]
	v_mov_b32_e32 v231, v3
	s_mul_i32 s98, s92, 0x4200
	v_subrev_u32_e32 v4, 15, v4
	v_add_u32_e32 v4, s98, v4
	v_ashrrev_i32_e32 v5, 31, v4
	v_lshl_add_u64 v[4:5], v[4:5], 2, s[80:81]
	global_store_dwordx4 v[4:5], v[216:219], off sc1
	global_store_dwordx4 v[4:5], v[220:223], off offset:16 sc1
	global_store_dwordx4 v[4:5], v[224:227], off offset:32 sc1
	global_store_dwordx4 v[4:5], v[228:231], off offset:48 sc1

; __device__ __forceinline__ float silu_fast(float v) { return v * __builtin_amdgcn_rcpf(1.f + __builtin_amdgcn_exp2f(-1.4426950408889634f * v)); }
; __device__ __forceinline__ u32x4 pack8(const f32x4 a, const f32x4 b) { u32x4 w; w.x = cvt_pk_bf16(a[0], a[1]); w.y = cvt_pk_bf16(a[2], a[3]); w.z = cvt_pk_bf16(b[0], b[1]); w.w = cvt_pk_bf16(b[2], b[3]); return w; }
;     __device__ __forceinline__ void operator()(const f32x4 (&acc)[2][2][4][2], const Unit& u, int wr, int wc, int fr, int fq) const {
;         const int row0 = u.pm * BM + wr * 64 + fr, col0 = u.pn * HALF + wc * 32 + 8 * fq;
;         bf16_t* base = HID + (size_t)u.z * MEXP * FF;
; #pragma unroll
;         for (int ai = 0; ai < 2; ++ai)
; #pragma unroll
;             for (int m = 0; m < 4; ++m) { f32x4 h[2];
; #pragma unroll
;                 for (int n = 0; n < 2; ++n)
; #pragma unroll
;                     for (int j = 0; j < 4; ++j) h[n][j] = silu_fast(acc[ai][0][m][n][j]) * acc[ai][1][m][n][j];
;                 const int row = row0 + ai * HALF + m * 16;
;                 *(u32x4*)(base + ((size_t)(row >> 7) * (FF / 64) + (col0 >> 6)) * 8192 + (row & 127) * 64 + (col0 & 63)) = pack8(h[0], h[1]); }
.LBB0_1018:
	v_mul_f32_e32 v2, 0xbfb8aa3b, v130
	v_exp_f32_e32 v2, v2
	v_mul_f32_e32 v136, 0xbfb8aa3b, v131
	v_exp_f32_e32 v136, v136
	s_lshl_b32 s6, s63, 8
	v_add_f32_e32 v2, 1.0, v2
	v_rcp_f32_e32 v138, v2
	v_add_f32_e32 v2, 1.0, v136
	v_rcp_f32_e32 v139, v2
	v_mul_f32_e32 v2, 0xbfb8aa3b, v132
	v_exp_f32_e32 v2, v2
	s_add_i32 s6, s6, s45
	v_pk_mul_f32 v[130:131], v[130:131], v[138:139]
	v_mul_f32_e32 v138, 0xbfb8aa3b, v133
	v_exp_f32_e32 v138, v138
	v_add_f32_e32 v2, 1.0, v2
	v_pk_mul_f32 v[122:123], v[122:123], v[130:131]
	v_rcp_f32_e32 v130, v2
	v_add_f32_e32 v2, 1.0, v138
	v_rcp_f32_e32 v131, v2
	v_mul_f32_e32 v2, 0xbfb8aa3b, v126
	v_exp_f32_e32 v2, v2
	v_mul_f32_e32 v138, 0xbfb8aa3b, v127
	v_exp_f32_e32 v138, v138
	v_pk_mul_f32 v[130:131], v[132:133], v[130:131]
	v_add_f32_e32 v2, 1.0, v2
	v_mul_f32_e32 v133, 0xbfb8aa3b, v128
	v_rcp_f32_e32 v132, v2
	v_add_f32_e32 v2, 1.0, v138
	v_exp_f32_e32 v138, v133
	v_mul_f32_e32 v133, 0xbfb8aa3b, v129
	v_exp_f32_e32 v139, v133
	v_rcp_f32_e32 v133, v2
	v_add_f32_e32 v2, 1.0, v138
	v_rcp_f32_e32 v138, v2
	v_add_f32_e32 v2, 1.0, v139
	v_rcp_f32_e32 v139, v2
	s_lshl_b32 s4, s22, 7
	v_pk_mul_f32 v[126:127], v[126:127], v[132:133]
	s_or_b32 s4, s4, s46
	s_ashr_i32 s7, s6, 7
	v_pk_mul_f32 v[126:127], v[118:119], v[126:127]
	v_pk_mul_f32 v[118:119], v[128:129], v[138:139]
	v_mul_f32_e32 v2, 0xbfb8aa3b, v114
	s_ashr_i32 s5, s4, 6
	v_mad_i64_i32 v[134:135], s[8:9], s62, v230, v[206:207]
	s_mul_i32 s7, s7, 44
	v_pk_mul_f32 v[128:129], v[120:121], v[118:119]
	v_exp_f32_e32 v2, v2
	v_mul_f32_e32 v121, 0xbfb8aa3b, v115
	s_ashr_i32 s4, s5, 31
	s_ashr_i32 s9, s7, 31
	v_cvt_pk_bf16_f32 v118, v122, v123
	v_exp_f32_e32 v123, v121
	s_add_u32 s8, s7, s5
	s_addc_u32 s9, s9, s4
	s_lshl_b64 s[8:9], s[8:9], 14
	v_add_f32_e32 v2, 1.0, v2
	v_lshl_add_u64 v[136:137], v[134:135], 0, s[8:9]
	v_pk_mul_f32 v[124:125], v[124:125], v[130:131]
	v_rcp_f32_e32 v122, v2
	v_add_f32_e32 v2, 1.0, v123
	v_mov_b32_e32 v209, v3
	v_cvt_pk_bf16_f32 v119, v124, v125
	v_cvt_pk_bf16_f32 v120, v126, v127
	v_cvt_pk_bf16_f32 v121, v128, v129
	v_rcp_f32_e32 v123, v2
	v_lshl_add_u64 v[124:125], v[136:137], 0, v[208:209]
	v_mul_f32_e32 v2, 0xbfb8aa3b, v116
	global_store_dwordx4 v[124:125], v[118:121], off sc1
	v_exp_f32_e32 v2, v2
	v_pk_mul_f32 v[114:115], v[114:115], v[122:123]
	v_mul_f32_e32 v118, 0xbfb8aa3b, v117
	v_exp_f32_e32 v118, v118
	v_add_f32_e32 v2, 1.0, v2
	v_pk_mul_f32 v[106:107], v[106:107], v[114:115]
	v_rcp_f32_e32 v114, v2
	v_add_f32_e32 v2, 1.0, v118
	v_rcp_f32_e32 v115, v2
	v_mul_f32_e32 v2, 0xbfb8aa3b, v110
	v_exp_f32_e32 v2, v2
	v_mul_f32_e32 v118, 0xbfb8aa3b, v111
	v_exp_f32_e32 v118, v118
	v_pk_mul_f32 v[114:115], v[116:117], v[114:115]
	v_add_f32_e32 v2, 1.0, v2
	v_mul_f32_e32 v117, 0xbfb8aa3b, v112
	v_rcp_f32_e32 v116, v2
	v_add_f32_e32 v2, 1.0, v118
	v_exp_f32_e32 v118, v117
	v_mul_f32_e32 v117, 0xbfb8aa3b, v113
	v_exp_f32_e32 v119, v117
	v_rcp_f32_e32 v117, v2
	v_add_f32_e32 v2, 1.0, v118
	v_rcp_f32_e32 v118, v2
	v_add_f32_e32 v2, 1.0, v119
	v_rcp_f32_e32 v119, v2
	v_pk_mul_f32 v[110:111], v[110:111], v[116:117]
	v_mul_f32_e32 v2, 0xbfb8aa3b, v98
	v_pk_mul_f32 v[110:111], v[102:103], v[110:111]
	v_pk_mul_f32 v[102:103], v[112:113], v[118:119]
	v_exp_f32_e32 v2, v2
	v_pk_mul_f32 v[112:113], v[104:105], v[102:103]
	v_mul_f32_e32 v103, 0xbfb8aa3b, v99
	v_exp_f32_e32 v104, v103
	v_add_f32_e32 v2, 1.0, v2
	v_pk_mul_f32 v[108:109], v[108:109], v[114:115]
	v_cvt_pk_bf16_f32 v102, v106, v107
	v_rcp_f32_e32 v106, v2
	v_add_f32_e32 v2, 1.0, v104
	v_cvt_pk_bf16_f32 v103, v108, v109
	v_rcp_f32_e32 v107, v2
	v_cvt_pk_bf16_f32 v104, v110, v111
	v_cvt_pk_bf16_f32 v105, v112, v113
	v_mul_f32_e32 v2, 0xbfb8aa3b, v100
	global_store_dwordx4 v[124:125], v[102:105], off offset:2048 sc1
	v_exp_f32_e32 v2, v2
	v_pk_mul_f32 v[98:99], v[98:99], v[106:107]
	v_mul_f32_e32 v102, 0xbfb8aa3b, v101
	v_exp_f32_e32 v102, v102
	v_add_f32_e32 v2, 1.0, v2
	v_pk_mul_f32 v[90:91], v[90:91], v[98:99]
	v_rcp_f32_e32 v98, v2
	v_add_f32_e32 v2, 1.0, v102
	v_rcp_f32_e32 v99, v2
	v_mul_f32_e32 v2, 0xbfb8aa3b, v94
	v_exp_f32_e32 v2, v2
	v_mul_f32_e32 v102, 0xbfb8aa3b, v95
	v_exp_f32_e32 v102, v102
	v_pk_mul_f32 v[98:99], v[100:101], v[98:99]
	v_add_f32_e32 v2, 1.0, v2
	v_mul_f32_e32 v101, 0xbfb8aa3b, v96
	v_rcp_f32_e32 v100, v2
	v_add_f32_e32 v2, 1.0, v102
	v_exp_f32_e32 v102, v101
	v_mul_f32_e32 v101, 0xbfb8aa3b, v97
	v_exp_f32_e32 v103, v101
	v_rcp_f32_e32 v101, v2
	v_add_f32_e32 v2, 1.0, v102
	v_rcp_f32_e32 v102, v2
	v_add_f32_e32 v2, 1.0, v103
	v_rcp_f32_e32 v103, v2
	v_pk_mul_f32 v[94:95], v[94:95], v[100:101]
	v_mul_f32_e32 v2, 0xbfb8aa3b, v82
	v_pk_mul_f32 v[94:95], v[86:87], v[94:95]
	v_pk_mul_f32 v[86:87], v[96:97], v[102:103]
	v_exp_f32_e32 v2, v2
	v_pk_mul_f32 v[96:97], v[88:89], v[86:87]
	v_mul_f32_e32 v89, 0xbfb8aa3b, v83
	v_cvt_pk_bf16_f32 v86, v90, v91
	v_exp_f32_e32 v91, v89
	v_add_f32_e32 v2, 1.0, v2
	v_pk_mul_f32 v[92:93], v[92:93], v[98:99]
	v_rcp_f32_e32 v90, v2
	v_add_f32_e32 v2, 1.0, v91
	v_mov_b32_e32 v211, v3
	v_cvt_pk_bf16_f32 v87, v92, v93
	v_cvt_pk_bf16_f32 v88, v94, v95
	v_cvt_pk_bf16_f32 v89, v96, v97
	v_rcp_f32_e32 v91, v2
	v_lshl_add_u64 v[92:93], v[136:137], 0, v[210:211]
	v_mul_f32_e32 v2, 0xbfb8aa3b, v84
	global_store_dwordx4 v[92:93], v[86:89], off sc1
	v_exp_f32_e32 v2, v2
	v_pk_mul_f32 v[82:83], v[82:83], v[90:91]
	v_mul_f32_e32 v86, 0xbfb8aa3b, v85
	v_exp_f32_e32 v86, v86
	v_add_f32_e32 v2, 1.0, v2
	v_pk_mul_f32 v[74:75], v[74:75], v[82:83]
	v_rcp_f32_e32 v82, v2
	v_add_f32_e32 v2, 1.0, v86
	v_rcp_f32_e32 v83, v2
	v_mul_f32_e32 v2, 0xbfb8aa3b, v78
	v_exp_f32_e32 v2, v2
	v_mul_f32_e32 v86, 0xbfb8aa3b, v79
	v_exp_f32_e32 v86, v86
; __device__ __forceinline__ float silu_fast(float v) { return v * __builtin_amdgcn_rcpf(1.f + __builtin_amdgcn_exp2f(-1.4426950408889634f * v)); }
; __device__ __forceinline__ u32x4 pack8(const f32x4 a, const f32x4 b) { u32x4 w; w.x = cvt_pk_bf16(a[0], a[1]); w.y = cvt_pk_bf16(a[2], a[3]); w.z = cvt_pk_bf16(b[0], b[1]); w.w = cvt_pk_bf16(b[2], b[3]); return w; }
;     __device__ __forceinline__ void operator()(const f32x4 (&acc)[2][2][4][2], const Unit& u, int wr, int wc, int fr, int fq) const {
;         const int row0 = u.pm * BM + wr * 64 + fr, col0 = u.pn * HALF + wc * 32 + 8 * fq;
;         bf16_t* base = HID + (size_t)u.z * MEXP * FF;
; #pragma unroll
;         for (int ai = 0; ai < 2; ++ai)
; #pragma unroll
;             for (int m = 0; m < 4; ++m) { f32x4 h[2];
; #pragma unroll
;                 for (int n = 0; n < 2; ++n)
; #pragma unroll
;                     for (int j = 0; j < 4; ++j) h[n][j] = silu_fast(acc[ai][0][m][n][j]) * acc[ai][1][m][n][j];
;                 const int row = row0 + ai * HALF + m * 16;
;                 *(u32x4*)(base + ((size_t)(row >> 7) * (FF / 64) + (col0 >> 6)) * 8192 + (row & 127) * 64 + (col0 & 63)) = pack8(h[0], h[1]); }
	v_pk_mul_f32 v[82:83], v[84:85], v[82:83]
	v_add_f32_e32 v2, 1.0, v2
	v_mul_f32_e32 v85, 0xbfb8aa3b, v80
	v_rcp_f32_e32 v84, v2
	v_add_f32_e32 v2, 1.0, v86
	v_exp_f32_e32 v86, v85
	v_mul_f32_e32 v85, 0xbfb8aa3b, v81
	v_exp_f32_e32 v87, v85
	v_rcp_f32_e32 v85, v2
	v_add_f32_e32 v2, 1.0, v86
	v_rcp_f32_e32 v86, v2
	v_add_f32_e32 v2, 1.0, v87
	v_rcp_f32_e32 v87, v2
	v_pk_mul_f32 v[78:79], v[78:79], v[84:85]
	v_pk_mul_f32 v[76:77], v[76:77], v[82:83]
	v_pk_mul_f32 v[78:79], v[70:71], v[78:79]
	v_pk_mul_f32 v[70:71], v[80:81], v[86:87]
	v_mov_b32_e32 v213, v3
	v_pk_mul_f32 v[80:81], v[72:73], v[70:71]
	v_cvt_pk_bf16_f32 v70, v74, v75
	v_cvt_pk_bf16_f32 v71, v76, v77
	v_cvt_pk_bf16_f32 v72, v78, v79
	v_cvt_pk_bf16_f32 v73, v80, v81
	v_lshl_add_u64 v[74:75], v[136:137], 0, v[212:213]
	v_mul_f32_e32 v2, 0xbfb8aa3b, v66
	global_store_dwordx4 v[74:75], v[70:73], off sc1
	v_exp_f32_e32 v2, v2
	s_addk_i32 s6, 0x80
	v_mul_f32_e32 v70, 0xbfb8aa3b, v67
	v_exp_f32_e32 v70, v70
	v_add_f32_e32 v2, 1.0, v2
	v_rcp_f32_e32 v72, v2
	s_ashr_i32 s6, s6, 7
	v_add_f32_e32 v2, 1.0, v70
	v_rcp_f32_e32 v73, v2
	v_mul_f32_e32 v2, 0xbfb8aa3b, v68
	v_exp_f32_e32 v2, v2
	s_mul_i32 s6, s6, 44
	v_pk_mul_f32 v[66:67], v[66:67], v[72:73]
	v_mul_f32_e32 v72, 0xbfb8aa3b, v69
	v_exp_f32_e32 v72, v72
	v_add_f32_e32 v2, 1.0, v2
	v_pk_mul_f32 v[58:59], v[58:59], v[66:67]
	v_rcp_f32_e32 v66, v2
	v_add_f32_e32 v2, 1.0, v72
	v_rcp_f32_e32 v67, v2
	v_mul_f32_e32 v2, 0xbfb8aa3b, v62
	v_exp_f32_e32 v2, v2
	v_mul_f32_e32 v72, 0xbfb8aa3b, v63
	v_exp_f32_e32 v72, v72
	v_pk_mul_f32 v[66:67], v[68:69], v[66:67]
	v_add_f32_e32 v2, 1.0, v2
	v_mul_f32_e32 v69, 0xbfb8aa3b, v64
	v_rcp_f32_e32 v68, v2
	v_add_f32_e32 v2, 1.0, v72
	v_exp_f32_e32 v72, v69
	v_mul_f32_e32 v69, 0xbfb8aa3b, v65
	v_exp_f32_e32 v73, v69
	v_rcp_f32_e32 v69, v2
	v_add_f32_e32 v2, 1.0, v72
	v_rcp_f32_e32 v72, v2
	v_add_f32_e32 v2, 1.0, v73
	v_rcp_f32_e32 v73, v2
	v_pk_mul_f32 v[62:63], v[62:63], v[68:69]
	v_mul_f32_e32 v2, 0xbfb8aa3b, v50
	v_pk_mul_f32 v[62:63], v[54:55], v[62:63]
	v_pk_mul_f32 v[54:55], v[64:65], v[72:73]
	v_exp_f32_e32 v2, v2
	v_pk_mul_f32 v[64:65], v[56:57], v[54:55]
	v_mul_f32_e32 v56, 0xbfb8aa3b, v51
	s_ashr_i32 s7, s6, 31
	v_exp_f32_e32 v57, v56
	s_add_u32 s6, s6, s5
	s_addc_u32 s7, s7, s4
	s_lshl_b64 s[4:5], s[6:7], 14
	v_add_f32_e32 v2, 1.0, v2
	v_lshl_add_u64 v[70:71], v[134:135], 0, s[4:5]
	v_pk_mul_f32 v[60:61], v[60:61], v[66:67]
	v_cvt_pk_bf16_f32 v54, v58, v59
	v_rcp_f32_e32 v58, v2
	v_add_f32_e32 v2, 1.0, v57
	v_cvt_pk_bf16_f32 v55, v60, v61
	v_cvt_pk_bf16_f32 v56, v62, v63
	v_rcp_f32_e32 v59, v2
	v_cvt_pk_bf16_f32 v57, v64, v65
	v_lshl_add_u64 v[60:61], v[70:71], 0, v[208:209]
	v_mul_f32_e32 v2, 0xbfb8aa3b, v52
	global_store_dwordx4 v[60:61], v[54:57], off sc1
	v_exp_f32_e32 v2, v2
	v_pk_mul_f32 v[50:51], v[50:51], v[58:59]
	v_mul_f32_e32 v54, 0xbfb8aa3b, v53
	v_exp_f32_e32 v54, v54
	v_add_f32_e32 v2, 1.0, v2
	v_pk_mul_f32 v[42:43], v[42:43], v[50:51]
	v_rcp_f32_e32 v50, v2
	v_add_f32_e32 v2, 1.0, v54
	v_rcp_f32_e32 v51, v2
	v_mul_f32_e32 v2, 0xbfb8aa3b, v46
	v_exp_f32_e32 v2, v2
	v_mul_f32_e32 v54, 0xbfb8aa3b, v47
	v_exp_f32_e32 v54, v54
	v_pk_mul_f32 v[50:51], v[52:53], v[50:51]
	v_add_f32_e32 v2, 1.0, v2
	v_mul_f32_e32 v53, 0xbfb8aa3b, v48
	v_rcp_f32_e32 v52, v2
	v_add_f32_e32 v2, 1.0, v54
	v_exp_f32_e32 v54, v53
	v_mul_f32_e32 v53, 0xbfb8aa3b, v49
	v_exp_f32_e32 v55, v53
	v_rcp_f32_e32 v53, v2
	v_add_f32_e32 v2, 1.0, v54
	v_rcp_f32_e32 v54, v2
	v_add_f32_e32 v2, 1.0, v55
	v_rcp_f32_e32 v55, v2
	v_pk_mul_f32 v[46:47], v[46:47], v[52:53]
	v_mul_f32_e32 v2, 0xbfb8aa3b, v34
	v_pk_mul_f32 v[46:47], v[38:39], v[46:47]
	v_pk_mul_f32 v[38:39], v[48:49], v[54:55]
	v_exp_f32_e32 v2, v2
	v_pk_mul_f32 v[48:49], v[40:41], v[38:39]
	v_mul_f32_e32 v39, 0xbfb8aa3b, v35
	v_exp_f32_e32 v40, v39
	v_add_f32_e32 v2, 1.0, v2
	v_pk_mul_f32 v[44:45], v[44:45], v[50:51]
	v_cvt_pk_bf16_f32 v38, v42, v43
	v_rcp_f32_e32 v42, v2
	v_add_f32_e32 v2, 1.0, v40
	v_cvt_pk_bf16_f32 v39, v44, v45
	v_rcp_f32_e32 v43, v2
	v_cvt_pk_bf16_f32 v40, v46, v47
	v_cvt_pk_bf16_f32 v41, v48, v49
	v_mul_f32_e32 v2, 0xbfb8aa3b, v36
	global_store_dwordx4 v[60:61], v[38:41], off offset:2048 sc1
	v_exp_f32_e32 v2, v2
	v_pk_mul_f32 v[34:35], v[34:35], v[42:43]
	v_mul_f32_e32 v38, 0xbfb8aa3b, v37
	v_exp_f32_e32 v38, v38
	v_add_f32_e32 v2, 1.0, v2
	v_pk_mul_f32 v[26:27], v[26:27], v[34:35]
	v_rcp_f32_e32 v34, v2
	v_add_f32_e32 v2, 1.0, v38
	v_rcp_f32_e32 v35, v2
	v_mul_f32_e32 v2, 0xbfb8aa3b, v30
	v_exp_f32_e32 v2, v2
	v_mul_f32_e32 v38, 0xbfb8aa3b, v31
	v_exp_f32_e32 v38, v38
	v_pk_mul_f32 v[34:35], v[36:37], v[34:35]
	v_add_f32_e32 v2, 1.0, v2
	v_mul_f32_e32 v37, 0xbfb8aa3b, v32
	v_rcp_f32_e32 v36, v2
	v_add_f32_e32 v2, 1.0, v38
	v_exp_f32_e32 v38, v37
	v_mul_f32_e32 v37, 0xbfb8aa3b, v33
	v_exp_f32_e32 v39, v37
	v_rcp_f32_e32 v37, v2
	v_add_f32_e32 v2, 1.0, v38
	v_rcp_f32_e32 v38, v2
	v_add_f32_e32 v2, 1.0, v39
	v_rcp_f32_e32 v39, v2
	v_pk_mul_f32 v[30:31], v[30:31], v[36:37]
	v_mul_f32_e32 v2, 0xbfb8aa3b, v18
	v_pk_mul_f32 v[30:31], v[22:23], v[30:31]
	v_pk_mul_f32 v[22:23], v[32:33], v[38:39]
	v_exp_f32_e32 v2, v2
	v_pk_mul_f32 v[32:33], v[24:25], v[22:23]
	v_mul_f32_e32 v24, 0xbfb8aa3b, v19
	v_exp_f32_e32 v25, v24
	v_add_f32_e32 v2, 1.0, v2
	v_pk_mul_f32 v[28:29], v[28:29], v[34:35]
	v_cvt_pk_bf16_f32 v22, v26, v27
	v_rcp_f32_e32 v26, v2
	v_add_f32_e32 v2, 1.0, v25
	v_cvt_pk_bf16_f32 v23, v28, v29
	v_cvt_pk_bf16_f32 v24, v30, v31
	v_rcp_f32_e32 v27, v2
	v_cvt_pk_bf16_f32 v25, v32, v33
	v_lshl_add_u64 v[28:29], v[70:71], 0, v[210:211]
	v_mul_f32_e32 v2, 0xbfb8aa3b, v20
	global_store_dwordx4 v[28:29], v[22:25], off sc1
	v_exp_f32_e32 v2, v2
	v_pk_mul_f32 v[18:19], v[18:19], v[26:27]
	v_mul_f32_e32 v22, 0xbfb8aa3b, v21
	v_exp_f32_e32 v22, v22
	v_add_f32_e32 v2, 1.0, v2
	v_pk_mul_f32 v[10:11], v[10:11], v[18:19]
	v_rcp_f32_e32 v18, v2
	v_add_f32_e32 v2, 1.0, v22
	v_rcp_f32_e32 v19, v2
	v_mul_f32_e32 v2, 0xbfb8aa3b, v14
	v_exp_f32_e32 v2, v2
	v_mul_f32_e32 v22, 0xbfb8aa3b, v15
	v_exp_f32_e32 v22, v22
	v_pk_mul_f32 v[18:19], v[20:21], v[18:19]
	v_add_f32_e32 v2, 1.0, v2
	v_mul_f32_e32 v21, 0xbfb8aa3b, v16
	v_rcp_f32_e32 v20, v2
	v_add_f32_e32 v2, 1.0, v22
	v_exp_f32_e32 v22, v21
	v_mul_f32_e32 v21, 0xbfb8aa3b, v17
	v_exp_f32_e32 v23, v21
	v_rcp_f32_e32 v21, v2
	v_add_f32_e32 v2, 1.0, v22
	v_rcp_f32_e32 v22, v2
	v_add_f32_e32 v2, 1.0, v23
	v_rcp_f32_e32 v23, v2
	v_pk_mul_f32 v[14:15], v[14:15], v[20:21]
	v_pk_mul_f32 v[12:13], v[12:13], v[18:19]
	v_pk_mul_f32 v[14:15], v[6:7], v[14:15]
	v_pk_mul_f32 v[6:7], v[16:17], v[22:23]
	s_and_b64 vcc, exec, s[0:1]
	v_pk_mul_f32 v[16:17], v[8:9], v[6:7]
	v_cvt_pk_bf16_f32 v6, v10, v11
	v_cvt_pk_bf16_f32 v7, v12, v13
	v_cvt_pk_bf16_f32 v8, v14, v15
	v_cvt_pk_bf16_f32 v9, v16, v17
	v_lshl_add_u64 v[10:11], v[70:71], 0, v[212:213]
	s_mov_b64 s[0:1], -1
	global_store_dwordx4 v[10:11], v[6:9], off sc1
	s_cbranch_vccnz .LBB0_999
	s_andn2_b64 vcc, exec, s[2:3]
	s_cbranch_vccnz .LBB0_998
	s_barrier
	s_branch .LBB0_998

; __device__ __forceinline__ u32x4 pack8(const f32x4 a, const f32x4 b) { u32x4 w; w.x = cvt_pk_bf16(a[0], a[1]); w.y = cvt_pk_bf16(a[2], a[3]); w.z = cvt_pk_bf16(b[0], b[1]); w.w = cvt_pk_bf16(b[2], b[3]); return w; }
;     __device__ __forceinline__ void operator()(const f32x4 (&acc)[2][2][4][2], const Unit& u, int wr, int wc, int fr, int fq) const {
;     ...
; #pragma unroll
;         for (int ai = 0; ai < 2; ++ai)
; #pragma unroll
;             for (int m = 0; m < 4; ++m) { const int row = row0 + ai * HALF + m * 16; const float gsc = gvp[row];
; #pragma unroll
;                 for (int bj = 0; bj < 2; ++bj) *(u32x4*)(base + (size_t)row * D + col0 + bj * HALF) = pack8(acc[ai][bj][m][0] * gsc, acc[ai][bj][m][1] * gsc); }
.LBB0_1110:
	s_mul_i32 s6, s57, 0x480000
	s_mul_hi_i32 s7, s57, 0x480000
	s_add_u32 s6, s84, s6
	s_mul_i32 s8, s57, 0x900
	s_addc_u32 s7, s85, s7
	s_ashr_i32 s9, s8, 31
	s_lshl_b64 s[8:9], s[8:9], 2
	s_add_u32 s8, s96, s8
	v_lshl_add_u32 v4, s58, 8, v1
	s_addc_u32 s9, s97, s9
	s_andn2_b64 vcc, exec, s[4:5]
	v_lshl_or_b32 v134, s56, 8, v217
	s_cbranch_vccnz .LBB0_1112
	v_ashrrev_i32_e32 v5, 31, v4
	v_lshl_add_u64 v[138:139], v[4:5], 2, s[8:9]
	global_load_dword v140, v[138:139], off
	v_ashrrev_i32_e32 v135, 31, v134
	v_lshl_add_u64 v[148:149], v[134:135], 1, s[6:7]
	v_lshlrev_b64 v[136:137], 11, v[4:5]
	v_lshl_add_u64 v[136:137], v[148:149], 0, v[136:137]
	s_mov_b32 s18, 0x40000
	s_mov_b64 s[4:5], 0x40000
	s_waitcnt vmcnt(0)
	v_pk_mul_f32 v[142:143], v[68:69], v[140:141] op_sel_hi:[1,0]
	v_pk_mul_f32 v[144:145], v[66:67], v[140:141] op_sel_hi:[1,0]
	v_pk_mul_f32 v[146:147], v[64:65], v[140:141] op_sel_hi:[1,0]
	v_pk_mul_f32 v[150:151], v[62:63], v[140:141] op_sel_hi:[1,0]
	v_pk_mul_f32 v[152:153], v[60:61], v[140:141] op_sel_hi:[1,0]
	v_pk_mul_f32 v[154:155], v[58:59], v[140:141] op_sel_hi:[1,0]
	v_pk_mul_f32 v[156:157], v[56:57], v[140:141] op_sel_hi:[1,0]
	v_pk_mul_f32 v[158:159], v[54:55], v[140:141] op_sel_hi:[1,0]
	v_cvt_pk_bf16_f32 v140, v144, v145
	v_cvt_pk_bf16_f32 v141, v142, v143
	v_cvt_pk_bf16_f32 v142, v150, v151
	v_cvt_pk_bf16_f32 v143, v146, v147
	v_cvt_pk_bf16_f32 v144, v154, v155
	v_cvt_pk_bf16_f32 v145, v152, v153
	v_cvt_pk_bf16_f32 v146, v158, v159
	v_cvt_pk_bf16_f32 v147, v156, v157
	global_store_dwordx4 v[136:137], v[140:143], off sc1
	global_store_dwordx4 v[136:137], v[144:147], off offset:256 sc1
	global_load_dword v140, v[138:139], off offset:64
	v_or_b32_e32 v142, 16, v4
	v_ashrrev_i32_e32 v143, 31, v142
	v_lshlrev_b64 v[142:143], 11, v[142:143]
	v_lshl_add_u64 v[150:151], v[148:149], 0, v[142:143]
	s_waitcnt vmcnt(0)
	v_pk_mul_f32 v[142:143], v[52:53], v[140:141] op_sel_hi:[1,0]
	v_pk_mul_f32 v[144:145], v[50:51], v[140:141] op_sel_hi:[1,0]
	v_pk_mul_f32 v[146:147], v[48:49], v[140:141] op_sel_hi:[1,0]
	v_pk_mul_f32 v[152:153], v[46:47], v[140:141] op_sel_hi:[1,0]
	v_pk_mul_f32 v[154:155], v[44:45], v[140:141] op_sel_hi:[1,0]
	v_pk_mul_f32 v[156:157], v[42:43], v[140:141] op_sel_hi:[1,0]
	v_pk_mul_f32 v[158:159], v[40:41], v[140:141] op_sel_hi:[1,0]
	v_pk_mul_f32 v[160:161], v[38:39], v[140:141] op_sel_hi:[1,0]
	v_cvt_pk_bf16_f32 v140, v144, v145
	v_cvt_pk_bf16_f32 v141, v142, v143
	v_cvt_pk_bf16_f32 v142, v152, v153
	v_cvt_pk_bf16_f32 v143, v146, v147
	v_cvt_pk_bf16_f32 v144, v156, v157
	v_cvt_pk_bf16_f32 v145, v154, v155
	v_cvt_pk_bf16_f32 v146, v160, v161
	v_cvt_pk_bf16_f32 v147, v158, v159
	global_store_dwordx4 v[150:151], v[140:143], off sc1
	global_store_dwordx4 v[150:151], v[144:147], off offset:256 sc1
	global_load_dword v140, v[138:139], off offset:128
	v_or_b32_e32 v142, 32, v4
	v_ashrrev_i32_e32 v143, 31, v142
	v_lshlrev_b64 v[142:143], 11, v[142:143]
	v_lshl_add_u64 v[150:151], v[148:149], 0, v[142:143]
	s_waitcnt vmcnt(0)
	v_pk_mul_f32 v[142:143], v[36:37], v[140:141] op_sel_hi:[1,0]
	v_pk_mul_f32 v[144:145], v[34:35], v[140:141] op_sel_hi:[1,0]
	v_pk_mul_f32 v[146:147], v[32:33], v[140:141] op_sel_hi:[1,0]
	v_pk_mul_f32 v[152:153], v[30:31], v[140:141] op_sel_hi:[1,0]
	v_pk_mul_f32 v[154:155], v[28:29], v[140:141] op_sel_hi:[1,0]
	v_pk_mul_f32 v[156:157], v[26:27], v[140:141] op_sel_hi:[1,0]
	v_pk_mul_f32 v[158:159], v[24:25], v[140:141] op_sel_hi:[1,0]
	v_pk_mul_f32 v[160:161], v[22:23], v[140:141] op_sel_hi:[1,0]
	v_cvt_pk_bf16_f32 v140, v144, v145
	v_cvt_pk_bf16_f32 v141, v142, v143
	v_cvt_pk_bf16_f32 v142, v152, v153
	v_cvt_pk_bf16_f32 v143, v146, v147
	v_cvt_pk_bf16_f32 v144, v156, v157
	v_cvt_pk_bf16_f32 v145, v154, v155
	v_cvt_pk_bf16_f32 v146, v160, v161
	v_cvt_pk_bf16_f32 v147, v158, v159
	global_store_dwordx4 v[150:151], v[140:143], off sc1
	global_store_dwordx4 v[150:151], v[144:147], off offset:256 sc1
	global_load_dword v140, v[138:139], off offset:192
	v_or_b32_e32 v142, 48, v4
	v_ashrrev_i32_e32 v143, 31, v142
	v_lshlrev_b64 v[142:143], 11, v[142:143]
	v_lshl_add_u64 v[148:149], v[148:149], 0, v[142:143]
	s_waitcnt vmcnt(0)
; __device__ __forceinline__ u32x4 pack8(const f32x4 a, const f32x4 b) { u32x4 w; w.x = cvt_pk_bf16(a[0], a[1]); w.y = cvt_pk_bf16(a[2], a[3]); w.z = cvt_pk_bf16(b[0], b[1]); w.w = cvt_pk_bf16(b[2], b[3]); return w; }
;     __device__ __forceinline__ void operator()(const f32x4 (&acc)[2][2][4][2], const Unit& u, int wr, int wc, int fr, int fq) const {
;     ...
; #pragma unroll
;         for (int ai = 0; ai < 2; ++ai)
; #pragma unroll
;             for (int m = 0; m < 4; ++m) { const int row = row0 + ai * HALF + m * 16; const float gsc = gvp[row];
; #pragma unroll
;                 for (int bj = 0; bj < 2; ++bj) *(u32x4*)(base + (size_t)row * D + col0 + bj * HALF) = pack8(acc[ai][bj][m][0] * gsc, acc[ai][bj][m][1] * gsc); }
	v_pk_mul_f32 v[142:143], v[20:21], v[140:141] op_sel_hi:[1,0]
	v_pk_mul_f32 v[144:145], v[18:19], v[140:141] op_sel_hi:[1,0]
	v_pk_mul_f32 v[146:147], v[16:17], v[140:141] op_sel_hi:[1,0]
	v_pk_mul_f32 v[150:151], v[14:15], v[140:141] op_sel_hi:[1,0]
	v_pk_mul_f32 v[152:153], v[12:13], v[140:141] op_sel_hi:[1,0]
	v_pk_mul_f32 v[154:155], v[10:11], v[140:141] op_sel_hi:[1,0]
	v_pk_mul_f32 v[156:157], v[8:9], v[140:141] op_sel_hi:[1,0]
	v_pk_mul_f32 v[158:159], v[6:7], v[140:141] op_sel_hi:[1,0]
	v_cvt_pk_bf16_f32 v140, v144, v145
	v_cvt_pk_bf16_f32 v141, v142, v143
	v_cvt_pk_bf16_f32 v142, v150, v151
	v_cvt_pk_bf16_f32 v143, v146, v147
	v_cvt_pk_bf16_f32 v144, v154, v155
	v_cvt_pk_bf16_f32 v145, v152, v153
	v_cvt_pk_bf16_f32 v146, v158, v159
	v_cvt_pk_bf16_f32 v147, v156, v157
	global_store_dwordx4 v[148:149], v[140:143], off sc1
	global_store_dwordx4 v[148:149], v[144:147], off offset:256 sc1
	global_load_dword v140, v[138:139], off offset:512
	v_lshl_add_u64 v[142:143], v[136:137], 0, s[4:5]
	v_add_co_u32_e32 v144, vcc, s18, v136
	s_mov_b32 s18, 0x48000
	s_nop 0
	v_addc_co_u32_e32 v145, vcc, 0, v137, vcc
	s_mov_b64 s[4:5], 0x48000
	s_waitcnt vmcnt(0)
	v_pk_mul_f32 v[132:133], v[132:133], v[140:141] op_sel_hi:[1,0]
	v_pk_mul_f32 v[130:131], v[130:131], v[140:141] op_sel_hi:[1,0]
	v_pk_mul_f32 v[128:129], v[128:129], v[140:141] op_sel_hi:[1,0]
	v_pk_mul_f32 v[126:127], v[126:127], v[140:141] op_sel_hi:[1,0]
	v_pk_mul_f32 v[124:125], v[124:125], v[140:141] op_sel_hi:[1,0]
	v_pk_mul_f32 v[122:123], v[122:123], v[140:141] op_sel_hi:[1,0]
	v_pk_mul_f32 v[146:147], v[120:121], v[140:141] op_sel_hi:[1,0]
	v_pk_mul_f32 v[140:141], v[118:119], v[140:141] op_sel_hi:[1,0]
	v_cvt_pk_bf16_f32 v118, v130, v131
	v_cvt_pk_bf16_f32 v119, v132, v133
	v_cvt_pk_bf16_f32 v120, v126, v127
	v_cvt_pk_bf16_f32 v121, v128, v129
	v_cvt_pk_bf16_f32 v122, v122, v123
	v_cvt_pk_bf16_f32 v123, v124, v125
	v_cvt_pk_bf16_f32 v124, v140, v141
	v_cvt_pk_bf16_f32 v125, v146, v147
	global_store_dwordx4 v[144:145], v[118:121], off sc1
	global_store_dwordx4 v[142:143], v[122:125], off offset:256 sc1
	global_load_dword v118, v[138:139], off offset:576
	v_lshl_add_u64 v[120:121], v[136:137], 0, s[4:5]
	v_add_co_u32_e32 v122, vcc, s18, v136
	s_mov_b64 s[4:5], 0x50000
	s_nop 0
	v_addc_co_u32_e32 v123, vcc, 0, v137, vcc
	s_waitcnt vmcnt(0)
	v_pk_mul_f32 v[116:117], v[116:117], v[118:119] op_sel_hi:[1,0]
	v_pk_mul_f32 v[114:115], v[114:115], v[118:119] op_sel_hi:[1,0]
	v_pk_mul_f32 v[112:113], v[112:113], v[118:119] op_sel_hi:[1,0]
	v_pk_mul_f32 v[110:111], v[110:111], v[118:119] op_sel_hi:[1,0]
	v_pk_mul_f32 v[108:109], v[108:109], v[118:119] op_sel_hi:[1,0]
	v_pk_mul_f32 v[106:107], v[106:107], v[118:119] op_sel_hi:[1,0]
	v_pk_mul_f32 v[124:125], v[104:105], v[118:119] op_sel_hi:[1,0]
	v_pk_mul_f32 v[118:119], v[102:103], v[118:119] op_sel_hi:[1,0]
	v_cvt_pk_bf16_f32 v102, v114, v115
	v_cvt_pk_bf16_f32 v103, v116, v117
	v_cvt_pk_bf16_f32 v104, v110, v111
	v_cvt_pk_bf16_f32 v105, v112, v113
	v_cvt_pk_bf16_f32 v106, v106, v107
	v_cvt_pk_bf16_f32 v107, v108, v109
	v_cvt_pk_bf16_f32 v108, v118, v119
	v_cvt_pk_bf16_f32 v109, v124, v125
	global_store_dwordx4 v[122:123], v[102:105], off sc1
	global_store_dwordx4 v[120:121], v[106:109], off offset:256 sc1
	global_load_dword v102, v[138:139], off offset:640
	v_lshl_add_u64 v[104:105], v[136:137], 0, s[4:5]
	v_add_co_u32_e32 v106, vcc, s50, v136
	s_mov_b64 s[4:5], -1
	s_nop 0
	v_addc_co_u32_e32 v107, vcc, 0, v137, vcc
	s_waitcnt vmcnt(0)
	v_pk_mul_f32 v[100:101], v[100:101], v[102:103] op_sel_hi:[1,0]
	v_pk_mul_f32 v[98:99], v[98:99], v[102:103] op_sel_hi:[1,0]
	v_pk_mul_f32 v[96:97], v[96:97], v[102:103] op_sel_hi:[1,0]
	v_pk_mul_f32 v[94:95], v[94:95], v[102:103] op_sel_hi:[1,0]
	v_pk_mul_f32 v[92:93], v[92:93], v[102:103] op_sel_hi:[1,0]
	v_pk_mul_f32 v[90:91], v[90:91], v[102:103] op_sel_hi:[1,0]
	v_pk_mul_f32 v[108:109], v[88:89], v[102:103] op_sel_hi:[1,0]
	v_pk_mul_f32 v[102:103], v[86:87], v[102:103] op_sel_hi:[1,0]
	v_cvt_pk_bf16_f32 v86, v98, v99
	v_cvt_pk_bf16_f32 v87, v100, v101
	v_cvt_pk_bf16_f32 v88, v94, v95
	v_cvt_pk_bf16_f32 v89, v96, v97
	v_cvt_pk_bf16_f32 v90, v90, v91
	v_cvt_pk_bf16_f32 v91, v92, v93
	v_cvt_pk_bf16_f32 v92, v102, v103
	v_cvt_pk_bf16_f32 v93, v108, v109
	global_store_dwordx4 v[106:107], v[86:89], off sc1
	global_store_dwordx4 v[104:105], v[90:93], off offset:256 sc1
	global_load_dword v88, v[138:139], off offset:704
	v_lshl_add_u64 v[86:87], v[136:137], 0, s[12:13]
	v_add_co_u32_e32 v90, vcc, s51, v136
	s_waitcnt vmcnt(0)
	v_pk_mul_f32 v[84:85], v[84:85], v[88:89] op_sel_hi:[1,0]
	v_pk_mul_f32 v[82:83], v[82:83], v[88:89] op_sel_hi:[1,0]
	v_pk_mul_f32 v[92:93], v[80:81], v[88:89] op_sel_hi:[1,0]
	v_pk_mul_f32 v[80:81], v[78:79], v[88:89] op_sel_hi:[1,0]
	v_addc_co_u32_e32 v91, vcc, 0, v137, vcc
	v_pk_mul_f32 v[76:77], v[76:77], v[88:89] op_sel_hi:[1,0]
	v_pk_mul_f32 v[74:75], v[74:75], v[88:89] op_sel_hi:[1,0]
	v_pk_mul_f32 v[72:73], v[72:73], v[88:89] op_sel_hi:[1,0]
	v_pk_mul_f32 v[70:71], v[70:71], v[88:89] op_sel_hi:[1,0]
	v_cvt_pk_bf16_f32 v78, v82, v83
	v_cvt_pk_bf16_f32 v79, v84, v85
	v_cvt_pk_bf16_f32 v80, v80, v81
	v_cvt_pk_bf16_f32 v81, v92, v93
	global_store_dwordx4 v[90:91], v[78:81], off sc1
	s_cbranch_execz .LBB0_1113
	s_branch .LBB0_1115

; __device__ __forceinline__ u32x4 pack8(const f32x4 a, const f32x4 b) { u32x4 w; w.x = cvt_pk_bf16(a[0], a[1]); w.y = cvt_pk_bf16(a[2], a[3]); w.z = cvt_pk_bf16(b[0], b[1]); w.w = cvt_pk_bf16(b[2], b[3]); return w; }
;     __device__ __forceinline__ void operator()(const f32x4 (&acc)[2][2][4][2], const Unit& u, int wr, int wc, int fr, int fq) const {
;     ...
;         if (u.kq >= 0) {
;             if (wr == 0) {
; #pragma unroll
;                 for (int m = 0; m < 4; ++m) { const int row = row0 + m * 16; const float gsc = gvp[row];
; #pragma unroll
;                     for (int bj = 0; bj < 2; ++bj) *(u32x4*)(base + (size_t)(row + 64 * u.kq) * D + col0 + bj * HALF) = pack8(acc[0][bj][m][0] * gsc, acc[0][bj][m][1] * gsc); }
;             }
;             return;
;         }
; #pragma unroll
;         for (int ai = 0; ai < 2; ++ai)
; #pragma unroll
;             for (int m = 0; m < 4; ++m) { const int row = row0 + ai * HALF + m * 16; const float gsc = gvp[row];
; #pragma unroll
;                 for (int bj = 0; bj < 2; ++bj) *(u32x4*)(base + (size_t)row * D + col0 + bj * HALF) = pack8(acc[ai][bj][m][0] * gsc, acc[ai][bj][m][1] * gsc); }
.LBB0_1113:
	s_and_b64 vcc, exec, s[10:11]
	s_cbranch_vccz .LBB0_1115
	v_ashrrev_i32_e32 v5, 31, v4
	v_lshl_add_u64 v[70:71], v[4:5], 2, s[8:9]
	global_load_dword v72, v[70:71], off
	v_lshl_add_u32 v4, s45, 6, v4
	v_ashrrev_i32_e32 v135, 31, v134
	v_ashrrev_i32_e32 v5, 31, v4
	v_lshl_add_u64 v[74:75], v[134:135], 1, s[6:7]
	v_lshlrev_b64 v[76:77], 11, v[4:5]
	v_lshl_add_u64 v[76:77], v[74:75], 0, v[76:77]
	s_mov_b64 s[4:5], -1
	s_waitcnt vmcnt(0)
	v_pk_mul_f32 v[68:69], v[68:69], v[72:73] op_sel_hi:[1,0]
	v_pk_mul_f32 v[66:67], v[66:67], v[72:73] op_sel_hi:[1,0]
	v_pk_mul_f32 v[64:65], v[64:65], v[72:73] op_sel_hi:[1,0]
	v_pk_mul_f32 v[62:63], v[62:63], v[72:73] op_sel_hi:[1,0]
	v_pk_mul_f32 v[60:61], v[60:61], v[72:73] op_sel_hi:[1,0]
	v_pk_mul_f32 v[58:59], v[58:59], v[72:73] op_sel_hi:[1,0]
	v_pk_mul_f32 v[78:79], v[56:57], v[72:73] op_sel_hi:[1,0]
	v_pk_mul_f32 v[72:73], v[54:55], v[72:73] op_sel_hi:[1,0]
	v_cvt_pk_bf16_f32 v54, v66, v67
	v_cvt_pk_bf16_f32 v55, v68, v69
	v_cvt_pk_bf16_f32 v56, v62, v63
	v_cvt_pk_bf16_f32 v57, v64, v65
	v_cvt_pk_bf16_f32 v58, v58, v59
	v_cvt_pk_bf16_f32 v59, v60, v61
	v_cvt_pk_bf16_f32 v60, v72, v73
	v_cvt_pk_bf16_f32 v61, v78, v79
	global_store_dwordx4 v[76:77], v[54:57], off sc1
	global_store_dwordx4 v[76:77], v[58:61], off offset:256 sc1
	global_load_dword v54, v[70:71], off offset:64
	v_add_u32_e32 v56, 16, v4
	v_ashrrev_i32_e32 v57, 31, v56
	v_lshlrev_b64 v[56:57], 11, v[56:57]
	v_lshl_add_u64 v[56:57], v[74:75], 0, v[56:57]
	s_waitcnt vmcnt(0)
	v_pk_mul_f32 v[52:53], v[52:53], v[54:55] op_sel_hi:[1,0]
	v_pk_mul_f32 v[50:51], v[50:51], v[54:55] op_sel_hi:[1,0]
	v_pk_mul_f32 v[48:49], v[48:49], v[54:55] op_sel_hi:[1,0]
	v_pk_mul_f32 v[46:47], v[46:47], v[54:55] op_sel_hi:[1,0]
	v_pk_mul_f32 v[44:45], v[44:45], v[54:55] op_sel_hi:[1,0]
	v_pk_mul_f32 v[42:43], v[42:43], v[54:55] op_sel_hi:[1,0]
	v_pk_mul_f32 v[58:59], v[40:41], v[54:55] op_sel_hi:[1,0]
	v_pk_mul_f32 v[54:55], v[38:39], v[54:55] op_sel_hi:[1,0]
	v_cvt_pk_bf16_f32 v38, v50, v51
	v_cvt_pk_bf16_f32 v39, v52, v53
	v_cvt_pk_bf16_f32 v40, v46, v47
	v_cvt_pk_bf16_f32 v41, v48, v49
	v_cvt_pk_bf16_f32 v42, v42, v43
	v_cvt_pk_bf16_f32 v43, v44, v45
	v_cvt_pk_bf16_f32 v44, v54, v55
	v_cvt_pk_bf16_f32 v45, v58, v59
	global_store_dwordx4 v[56:57], v[38:41], off sc1
	global_store_dwordx4 v[56:57], v[42:45], off offset:256 sc1
	global_load_dword v38, v[70:71], off offset:128
	v_add_u32_e32 v40, 32, v4
	v_ashrrev_i32_e32 v41, 31, v40
	v_lshlrev_b64 v[40:41], 11, v[40:41]
	v_lshl_add_u64 v[40:41], v[74:75], 0, v[40:41]
	v_add_u32_e32 v4, 48, v4
	v_ashrrev_i32_e32 v5, 31, v4
	v_lshlrev_b64 v[4:5], 11, v[4:5]
	v_lshl_add_u64 v[86:87], v[74:75], 0, v[4:5]
	s_waitcnt vmcnt(0)
	v_pk_mul_f32 v[36:37], v[36:37], v[38:39] op_sel_hi:[1,0]
	v_pk_mul_f32 v[34:35], v[34:35], v[38:39] op_sel_hi:[1,0]
	v_pk_mul_f32 v[32:33], v[32:33], v[38:39] op_sel_hi:[1,0]
	v_pk_mul_f32 v[30:31], v[30:31], v[38:39] op_sel_hi:[1,0]
	v_pk_mul_f32 v[28:29], v[28:29], v[38:39] op_sel_hi:[1,0]
	v_pk_mul_f32 v[26:27], v[26:27], v[38:39] op_sel_hi:[1,0]
	v_pk_mul_f32 v[42:43], v[24:25], v[38:39] op_sel_hi:[1,0]
	v_pk_mul_f32 v[38:39], v[22:23], v[38:39] op_sel_hi:[1,0]
	v_cvt_pk_bf16_f32 v22, v34, v35
	v_cvt_pk_bf16_f32 v23, v36, v37
	v_cvt_pk_bf16_f32 v24, v30, v31
	v_cvt_pk_bf16_f32 v25, v32, v33
	v_cvt_pk_bf16_f32 v26, v26, v27
	v_cvt_pk_bf16_f32 v27, v28, v29
	v_cvt_pk_bf16_f32 v28, v38, v39
	v_cvt_pk_bf16_f32 v29, v42, v43
	global_store_dwordx4 v[40:41], v[22:25], off sc1
	global_store_dwordx4 v[40:41], v[26:29], off offset:256 sc1
	global_load_dword v22, v[70:71], off offset:192
	s_waitcnt vmcnt(0)
	v_pk_mul_f32 v[20:21], v[20:21], v[22:23] op_sel_hi:[1,0]
	v_pk_mul_f32 v[4:5], v[18:19], v[22:23] op_sel_hi:[1,0]
	v_pk_mul_f32 v[16:17], v[16:17], v[22:23] op_sel_hi:[1,0]
	v_pk_mul_f32 v[14:15], v[14:15], v[22:23] op_sel_hi:[1,0]
	v_pk_mul_f32 v[76:77], v[12:13], v[22:23] op_sel_hi:[1,0]
	v_pk_mul_f32 v[74:75], v[10:11], v[22:23] op_sel_hi:[1,0]
	v_pk_mul_f32 v[72:73], v[8:9], v[22:23] op_sel_hi:[1,0]
	v_pk_mul_f32 v[70:71], v[6:7], v[22:23] op_sel_hi:[1,0]
	v_cvt_pk_bf16_f32 v4, v4, v5
	v_cvt_pk_bf16_f32 v5, v20, v21
	v_cvt_pk_bf16_f32 v6, v14, v15
	v_cvt_pk_bf16_f32 v7, v16, v17
	global_store_dwordx4 v[86:87], v[4:7], off sc1
.LBB0_1115:
	s_and_b64 vcc, exec, s[4:5]
	s_cbranch_vccz .LBB0_1117
	v_cvt_pk_bf16_f32 v4, v74, v75
	v_cvt_pk_bf16_f32 v5, v76, v77
	v_cvt_pk_bf16_f32 v6, v70, v71
	v_cvt_pk_bf16_f32 v7, v72, v73
	global_store_dwordx4 v[86:87], v[4:7], off offset:256 sc1

; __device__ __forceinline__ u32x4 pack8(const f32x4 a, const f32x4 b) { u32x4 w; w.x = cvt_pk_bf16(a[0], a[1]); w.y = cvt_pk_bf16(a[2], a[3]); w.z = cvt_pk_bf16(b[0], b[1]); w.w = cvt_pk_bf16(b[2], b[3]); return w; }
;     __device__ __forceinline__ void operator()(const f32x4 (&acc)[2][2][4][2], const Unit& u, int wr, int wc, int fr, int fq) const {
;     ...
;         } else {
;             const bool isv = u.pn < 16; bf16_t* O = isv ? V : Gs; const int ct = (isv ? u.pn - 8 : u.pn - 16) * BM + cl;
; #pragma unroll
;             for (int ai = 0; ai < 2; ++ai)
; #pragma unroll
;                 for (int m = 0; m < 4; ++m) { bf16_t* rowp = O + (size_t)(row0 + ai * HALF + m * 16) * 2048 + ct;
; #pragma unroll
;                     for (int bj = 0; bj < 2; ++bj) { f32x4 v0 = acc[ai][bj][m][0], v1 = acc[ai][bj][m][1];
;                         if (isv) *(u32x4*)(rowp + bj * HALF) = pack8(v0, v1); else __builtin_nontemporal_store(pack8(v0, v1), (u32x4*)(rowp + bj * HALF)); } }
.LBB0_1260:
	s_lshl_b32 s29, s10, 8
	s_add_i32 s29, s29, s51
	v_or_b32_e32 v156, s29, v1
	s_cmp_gt_i32 s2, 7
	s_mov_b64 s[38:39], -1
	s_cbranch_scc0 .LBB0_1263
	s_cmp_lt_u32 s2, 16
	s_cselect_b64 s[38:39], -1, 0
	s_and_b64 s[38:39], s[38:39], exec
	s_cselect_b32 s3, 0, s17
	v_mov_b32_e32 v159, s3
	s_cselect_b32 s3, -8, -16
	s_cselect_b32 s11, 0, s16
	s_add_i32 s3, s3, s2
	v_mov_b32_e32 v158, s11
	v_lshl_or_b32 v142, s3, 8, v175
	v_ashrrev_i32_e32 v157, 31, v156
	v_lshl_add_u64 v[162:163], v[142:143], 1, v[158:159]
	v_lshlrev_b64 v[158:159], 12, v[156:157]
	v_lshl_add_u64 v[164:165], v[162:163], 0, v[158:159]
	v_cvt_pk_bf16_f32 v158, v126, v127
	v_cvt_pk_bf16_f32 v159, v128, v129
	v_cvt_pk_bf16_f32 v160, v118, v119
	v_cvt_pk_bf16_f32 v161, v120, v121
	global_store_dwordx4 v[164:165], v[158:161], off sc1
	s_mov_b32 s3, 0x80000
	s_mov_b64 s[38:39], 0x80000
	v_cvt_pk_bf16_f32 v158, v122, v123
	v_cvt_pk_bf16_f32 v159, v124, v125
	v_cvt_pk_bf16_f32 v160, v114, v115
	v_cvt_pk_bf16_f32 v161, v116, v117
	global_store_dwordx4 v[164:165], v[158:161], off offset:256 sc1
	s_nop 1
	v_or_b32_e32 v158, 16, v156
	v_ashrrev_i32_e32 v159, 31, v158
	v_lshlrev_b64 v[158:159], 12, v[158:159]
	v_lshl_add_u64 v[166:167], v[162:163], 0, v[158:159]
	v_cvt_pk_bf16_f32 v158, v110, v111
	v_cvt_pk_bf16_f32 v159, v112, v113
	v_cvt_pk_bf16_f32 v160, v102, v103
	v_cvt_pk_bf16_f32 v161, v104, v105
	global_store_dwordx4 v[166:167], v[158:161], off sc1
	s_nop 1
	v_cvt_pk_bf16_f32 v158, v106, v107
	v_cvt_pk_bf16_f32 v159, v108, v109
	v_cvt_pk_bf16_f32 v160, v98, v99
	v_cvt_pk_bf16_f32 v161, v100, v101
	global_store_dwordx4 v[166:167], v[158:161], off offset:256 sc1
	s_nop 1
	v_or_b32_e32 v158, 32, v156
	v_ashrrev_i32_e32 v159, 31, v158
	v_lshlrev_b64 v[158:159], 12, v[158:159]
	v_lshl_add_u64 v[166:167], v[162:163], 0, v[158:159]
	v_cvt_pk_bf16_f32 v158, v94, v95
	v_cvt_pk_bf16_f32 v159, v96, v97
	v_cvt_pk_bf16_f32 v160, v86, v87
	v_cvt_pk_bf16_f32 v161, v88, v89
	global_store_dwordx4 v[166:167], v[158:161], off sc1
	s_nop 1
	v_cvt_pk_bf16_f32 v158, v90, v91
	v_cvt_pk_bf16_f32 v159, v92, v93
	v_cvt_pk_bf16_f32 v160, v82, v83
	v_cvt_pk_bf16_f32 v161, v84, v85
	global_store_dwordx4 v[166:167], v[158:161], off offset:256 sc1
	v_add_co_u32_e32 v166, vcc, s3, v164
	s_nop 0
	v_or_b32_e32 v158, 48, v156
	v_ashrrev_i32_e32 v159, 31, v158
	v_lshlrev_b64 v[158:159], 12, v[158:159]
	v_lshl_add_u64 v[162:163], v[162:163], 0, v[158:159]
	v_cvt_pk_bf16_f32 v158, v78, v79
	v_cvt_pk_bf16_f32 v159, v80, v81
	v_cvt_pk_bf16_f32 v160, v70, v71
	v_cvt_pk_bf16_f32 v161, v72, v73
	global_store_dwordx4 v[162:163], v[158:161], off sc1
	v_addc_co_u32_e32 v167, vcc, 0, v165, vcc
	s_nop 0
	v_cvt_pk_bf16_f32 v158, v74, v75
	v_cvt_pk_bf16_f32 v159, v76, v77
	v_cvt_pk_bf16_f32 v160, v66, v67
	v_cvt_pk_bf16_f32 v161, v68, v69
	global_store_dwordx4 v[162:163], v[158:161], off offset:256 sc1
	s_mov_b32 s3, 0x90000
	v_lshl_add_u64 v[162:163], v[164:165], 0, s[38:39]
	v_cvt_pk_bf16_f32 v158, v62, v63
	v_cvt_pk_bf16_f32 v159, v64, v65
	v_cvt_pk_bf16_f32 v160, v54, v55
	v_cvt_pk_bf16_f32 v161, v56, v57
	global_store_dwordx4 v[166:167], v[158:161], off sc1
	v_add_co_u32_e32 v166, vcc, s3, v164
	s_nop 0
	v_cvt_pk_bf16_f32 v158, v58, v59
	v_cvt_pk_bf16_f32 v159, v60, v61
	v_cvt_pk_bf16_f32 v160, v50, v51
	v_cvt_pk_bf16_f32 v161, v52, v53
	global_store_dwordx4 v[162:163], v[158:161], off offset:256 sc1
	s_mov_b64 s[38:39], 0x90000
	v_addc_co_u32_e32 v167, vcc, 0, v165, vcc
	v_cvt_pk_bf16_f32 v158, v46, v47
	v_cvt_pk_bf16_f32 v159, v48, v49
	v_cvt_pk_bf16_f32 v160, v38, v39
	v_cvt_pk_bf16_f32 v161, v40, v41
	v_lshl_add_u64 v[162:163], v[164:165], 0, s[38:39]
	global_store_dwordx4 v[166:167], v[158:161], off sc1
	v_add_co_u32_e32 v166, vcc, s58, v164
	s_nop 0
	v_cvt_pk_bf16_f32 v158, v42, v43
	v_cvt_pk_bf16_f32 v159, v44, v45
	v_cvt_pk_bf16_f32 v160, v34, v35
	v_cvt_pk_bf16_f32 v161, v36, v37
	global_store_dwordx4 v[162:163], v[158:161], off offset:256 sc1
	v_addc_co_u32_e32 v167, vcc, 0, v165, vcc
	s_nop 0
	v_cvt_pk_bf16_f32 v158, v30, v31
	v_cvt_pk_bf16_f32 v159, v32, v33
	v_cvt_pk_bf16_f32 v160, v22, v23
	v_cvt_pk_bf16_f32 v161, v24, v25
	v_lshl_add_u64 v[162:163], v[164:165], 0, s[24:25]
	global_store_dwordx4 v[166:167], v[158:161], off sc1
	s_nop 1
	v_cvt_pk_bf16_f32 v158, v26, v27
	v_cvt_pk_bf16_f32 v159, v28, v29
	v_cvt_pk_bf16_f32 v160, v18, v19
	v_cvt_pk_bf16_f32 v161, v20, v21
	global_store_dwordx4 v[162:163], v[158:161], off offset:256 sc1
	v_lshl_add_u64 v[162:163], v[164:165], 0, s[26:27]
	v_add_co_u32_e32 v164, vcc, s59, v164
	v_cvt_pk_bf16_f32 v158, v14, v15
	v_cvt_pk_bf16_f32 v159, v16, v17
	v_cvt_pk_bf16_f32 v160, v6, v7
	v_cvt_pk_bf16_f32 v161, v8, v9
	v_addc_co_u32_e32 v165, vcc, 0, v165, vcc
	global_store_dwordx4 v[164:165], v[158:161], off sc1
	s_nop 1
	v_cvt_pk_bf16_f32 v158, v10, v11
	v_cvt_pk_bf16_f32 v159, v12, v13
	v_cvt_pk_bf16_f32 v160, v2, v3
	v_cvt_pk_bf16_f32 v161, v4, v5
	global_store_dwordx4 v[162:163], v[158:161], off offset:256 sc1
	s_cbranch_execz .LBB0_1264

; __device__ __forceinline__ u32x4 pack8(const f32x4 a, const f32x4 b) { u32x4 w; w.x = cvt_pk_bf16(a[0], a[1]); w.y = cvt_pk_bf16(a[2], a[3]); w.z = cvt_pk_bf16(b[0], b[1]); w.w = cvt_pk_bf16(b[2], b[3]); return w; }
;     __device__ __forceinline__ void operator()(const f32x4 (&acc)[2][2][4][2], const Unit& u, int wr, int wc, int fr, int fq) const {
;     ...
;         if (u.pn < 8) {
;             const bool isq = u.pn < 4; const int head = isq ? u.pn : u.pn - 4; bf16_t* O = isq ? Q : Kb; const float sc = isq ? 1.f : 0.0625f;
;             const bool lat = u.pm < 64;
; #pragma unroll
;             for (int ai = 0; ai < 2; ++ai)
; #pragma unroll
;                 for (int m = 0; m < 4; ++m) {
;                     const int row = row0 + ai * HALF + m * 16; const int t = row & (SEQ - 1);
;                     const int pos = wc < 2 ? (t >> 6) : (t & 63);
;                     const f32x4* tp = (const f32x4*)(rope + pos * 64 + (wc & 1) * 32 + 8 * fq);
;                     f32x4 o1[2], o2[2];
; #pragma unroll
;                     for (int n = 0; n < 2; ++n) {
;                         const f32x4 x1 = acc[ai][0][m][n], x2 = acc[ai][1][m][n];
;                         if (lat) { const f32x4 cs0 = tp[2 * n], cs1 = tp[2 * n + 1];
;                             o1[n][0] = (x1[0] * cs0[0] - x2[0] * cs0[1]) * sc; o2[n][0] = (x1[0] * cs0[1] + x2[0] * cs0[0]) * sc;
;                             o1[n][1] = (x1[1] * cs0[2] - x2[1] * cs0[3]) * sc; o2[n][1] = (x1[1] * cs0[3] + x2[1] * cs0[2]) * sc;
;                             o1[n][2] = (x1[2] * cs1[0] - x2[2] * cs1[1]) * sc; o2[n][2] = (x1[2] * cs1[1] + x2[2] * cs1[0]) * sc;
;                             o1[n][3] = (x1[3] * cs1[2] - x2[3] * cs1[3]) * sc; o2[n][3] = (x1[3] * cs1[3] + x2[3] * cs1[2]) * sc;
;                         } else { o1[n] = x1 * sc; o2[n] = x2 * sc; }
;                     }
;                     bf16_t* fp = O + ((((size_t)(row >> 13) * 4 + head) * 512 + (t >> 4)) * 8 + wc) * 512 + ((t & 15) + 16 * fq) * 8;
;                     *(u32x4*)(fp) = pack8(o1[0], o1[1]);
;                     *(u32x4*)(fp + 4 * 512) = pack8(o2[0], o2[1]);
.LBB0_1272:
	s_add_i32 s3, s2, -4
	s_and_b64 s[38:39], s[38:39], exec
	s_cselect_b32 s2, s2, s3
	s_cselect_b32 s12, s60, 0x8313600
	s_ashr_i32 s38, s29, 13
	s_ashr_i32 s3, s2, 31
	s_ashr_i32 s39, s38, 31
	s_lshl_b64 s[2:3], s[2:3], 9
	s_lshl_b64 s[38:39], s[38:39], 11
	v_and_b32_e32 v116, 0x1fcf, v156
	v_lshl_add_u64 v[114:115], v[144:145], 0, s[12:13]
	s_add_u32 s12, s2, s38
	s_addc_u32 s29, s3, s39
	v_lshrrev_b32_e32 v168, 4, v116
	v_or_b32_e32 v116, s12, v168
	v_mov_b32_e32 v117, s29
	v_lshlrev_b64 v[116:117], 13, v[116:117]
	v_lshl_add_u64 v[120:121], v[114:115], 0, v[116:117]
	v_cvt_pk_bf16_f32 v116, v164, v165
	v_cvt_pk_bf16_f32 v117, v166, v167
	v_cvt_pk_bf16_f32 v118, v128, v129
	v_cvt_pk_bf16_f32 v119, v122, v123
	global_store_dwordx4 v[120:121], v[116:119], off sc1
	v_add_co_u32_e32 v120, vcc, 0x1000, v120
	s_nop 0
	v_cvt_pk_bf16_f32 v116, v160, v161
	v_addc_co_u32_e32 v121, vcc, 0, v121, vcc
	v_cvt_pk_bf16_f32 v117, v162, v163
	v_cvt_pk_bf16_f32 v118, v126, v127
	v_cvt_pk_bf16_f32 v119, v124, v125
	s_and_b64 vcc, exec, s[10:11]
	s_mov_b64 s[38:39], -1
	global_store_dwordx4 v[120:121], v[116:119], off sc1
	s_cbranch_vccnz .LBB0_1274
	s_nop 0
	v_mov_b32_e32 v116, v158
	v_mov_b32_e32 v117, v158
	v_pk_mul_f32 v[120:121], v[116:117], v[112:113]
	v_pk_mul_f32 v[122:123], v[158:159], v[110:111]
	v_pk_mul_f32 v[116:117], v[116:117], v[108:109]
	v_pk_mul_f32 v[118:119], v[158:159], v[106:107]
	s_mov_b64 s[38:39], 0

; __device__ __forceinline__ u32x4 pack8(const f32x4 a, const f32x4 b) { u32x4 w; w.x = cvt_pk_bf16(a[0], a[1]); w.y = cvt_pk_bf16(a[2], a[3]); w.z = cvt_pk_bf16(b[0], b[1]); w.w = cvt_pk_bf16(b[2], b[3]); return w; }
;     __device__ __forceinline__ void operator()(const f32x4 (&acc)[2][2][4][2], const Unit& u, int wr, int wc, int fr, int fq) const {
;     ...
;             for (int ai = 0; ai < 2; ++ai)
; #pragma unroll
;                 for (int m = 0; m < 4; ++m) {
;                     const int row = row0 + ai * HALF + m * 16; const int t = row & (SEQ - 1);
;                     const int pos = wc < 2 ? (t >> 6) : (t & 63);
;                     const f32x4* tp = (const f32x4*)(rope + pos * 64 + (wc & 1) * 32 + 8 * fq);
;                     f32x4 o1[2], o2[2];
; #pragma unroll
;                     for (int n = 0; n < 2; ++n) {
;                         const f32x4 x1 = acc[ai][0][m][n], x2 = acc[ai][1][m][n];
;                         if (lat) { const f32x4 cs0 = tp[2 * n], cs1 = tp[2 * n + 1];
;                             o1[n][0] = (x1[0] * cs0[0] - x2[0] * cs0[1]) * sc; o2[n][0] = (x1[0] * cs0[1] + x2[0] * cs0[0]) * sc;
;                             o1[n][1] = (x1[1] * cs0[2] - x2[1] * cs0[3]) * sc; o2[n][1] = (x1[1] * cs0[3] + x2[1] * cs0[2]) * sc;
;                             o1[n][2] = (x1[2] * cs1[0] - x2[2] * cs1[1]) * sc; o2[n][2] = (x1[2] * cs1[1] + x2[2] * cs1[0]) * sc;
;                             o1[n][3] = (x1[3] * cs1[2] - x2[3] * cs1[3]) * sc; o2[n][3] = (x1[3] * cs1[3] + x2[3] * cs1[2]) * sc;
;                         } else { o1[n] = x1 * sc; o2[n] = x2 * sc; }
;                     }
;                     bf16_t* fp = O + ((((size_t)(row >> 13) * 4 + head) * 512 + (t >> 4)) * 8 + wc) * 512 + ((t & 15) + 16 * fq) * 8;
;                     *(u32x4*)(fp) = pack8(o1[0], o1[1]);
;                     *(u32x4*)(fp + 4 * 512) = pack8(o2[0], o2[1]);
.LBB0_1280:
	v_or3_b32 v98, v168, s12, 1
	v_mov_b32_e32 v99, s29
	v_lshlrev_b64 v[98:99], 13, v[98:99]
	v_lshl_add_u64 v[102:103], v[114:115], 0, v[98:99]
	v_cvt_pk_bf16_f32 v98, v122, v123
	v_cvt_pk_bf16_f32 v99, v120, v121
	v_cvt_pk_bf16_f32 v100, v112, v113
	v_cvt_pk_bf16_f32 v101, v106, v107
	global_store_dwordx4 v[102:103], v[98:101], off sc1
	v_add_co_u32_e32 v102, vcc, 0x1000, v102
	s_nop 0
	v_cvt_pk_bf16_f32 v98, v118, v119
	v_addc_co_u32_e32 v103, vcc, 0, v103, vcc
	v_cvt_pk_bf16_f32 v99, v116, v117
	v_cvt_pk_bf16_f32 v100, v110, v111
	v_cvt_pk_bf16_f32 v101, v108, v109
	s_and_b64 vcc, exec, s[10:11]
	s_mov_b64 s[38:39], -1
	global_store_dwordx4 v[102:103], v[98:101], off sc1
	s_cbranch_vccnz .LBB0_1282
	s_nop 0
	v_mov_b32_e32 v98, v158
	v_mov_b32_e32 v99, v158
	v_pk_mul_f32 v[102:103], v[98:99], v[96:97]
	v_pk_mul_f32 v[104:105], v[158:159], v[94:95]
	v_pk_mul_f32 v[98:99], v[98:99], v[92:93]
	v_pk_mul_f32 v[100:101], v[158:159], v[90:91]
	s_mov_b64 s[38:39], 0

; __device__ __forceinline__ u32x4 pack8(const f32x4 a, const f32x4 b) { u32x4 w; w.x = cvt_pk_bf16(a[0], a[1]); w.y = cvt_pk_bf16(a[2], a[3]); w.z = cvt_pk_bf16(b[0], b[1]); w.w = cvt_pk_bf16(b[2], b[3]); return w; }
;     __device__ __forceinline__ void operator()(const f32x4 (&acc)[2][2][4][2], const Unit& u, int wr, int wc, int fr, int fq) const {
;     ...
;             for (int ai = 0; ai < 2; ++ai)
; #pragma unroll
;                 for (int m = 0; m < 4; ++m) {
;                     const int row = row0 + ai * HALF + m * 16; const int t = row & (SEQ - 1);
;                     const int pos = wc < 2 ? (t >> 6) : (t & 63);
;                     const f32x4* tp = (const f32x4*)(rope + pos * 64 + (wc & 1) * 32 + 8 * fq);
;                     f32x4 o1[2], o2[2];
; #pragma unroll
;                     for (int n = 0; n < 2; ++n) {
;                         const f32x4 x1 = acc[ai][0][m][n], x2 = acc[ai][1][m][n];
;                         if (lat) { const f32x4 cs0 = tp[2 * n], cs1 = tp[2 * n + 1];
;                             o1[n][0] = (x1[0] * cs0[0] - x2[0] * cs0[1]) * sc; o2[n][0] = (x1[0] * cs0[1] + x2[0] * cs0[0]) * sc;
;                             o1[n][1] = (x1[1] * cs0[2] - x2[1] * cs0[3]) * sc; o2[n][1] = (x1[1] * cs0[3] + x2[1] * cs0[2]) * sc;
;                             o1[n][2] = (x1[2] * cs1[0] - x2[2] * cs1[1]) * sc; o2[n][2] = (x1[2] * cs1[1] + x2[2] * cs1[0]) * sc;
;                             o1[n][3] = (x1[3] * cs1[2] - x2[3] * cs1[3]) * sc; o2[n][3] = (x1[3] * cs1[3] + x2[3] * cs1[2]) * sc;
;                         } else { o1[n] = x1 * sc; o2[n] = x2 * sc; }
;                     }
;                     bf16_t* fp = O + ((((size_t)(row >> 13) * 4 + head) * 512 + (t >> 4)) * 8 + wc) * 512 + ((t & 15) + 16 * fq) * 8;
;                     *(u32x4*)(fp) = pack8(o1[0], o1[1]);
;                     *(u32x4*)(fp + 4 * 512) = pack8(o2[0], o2[1]);
.LBB0_1288:
	v_or3_b32 v82, v168, s12, 2
	v_mov_b32_e32 v83, s29
	v_lshlrev_b64 v[82:83], 13, v[82:83]
	v_lshl_add_u64 v[86:87], v[114:115], 0, v[82:83]
	v_cvt_pk_bf16_f32 v82, v104, v105
	v_cvt_pk_bf16_f32 v83, v102, v103
	v_cvt_pk_bf16_f32 v84, v96, v97
	v_cvt_pk_bf16_f32 v85, v90, v91
	global_store_dwordx4 v[86:87], v[82:85], off sc1
	v_add_co_u32_e32 v86, vcc, 0x1000, v86
	s_nop 0
	v_cvt_pk_bf16_f32 v82, v100, v101
	v_addc_co_u32_e32 v87, vcc, 0, v87, vcc
	v_cvt_pk_bf16_f32 v83, v98, v99
	v_cvt_pk_bf16_f32 v84, v94, v95
	v_cvt_pk_bf16_f32 v85, v92, v93
	s_and_b64 vcc, exec, s[10:11]
	s_mov_b64 s[38:39], -1
	global_store_dwordx4 v[86:87], v[82:85], off sc1
	s_cbranch_vccnz .LBB0_1290
	s_nop 0
	v_mov_b32_e32 v82, v158
	v_mov_b32_e32 v83, v158
	v_pk_mul_f32 v[86:87], v[82:83], v[80:81]
	v_pk_mul_f32 v[88:89], v[158:159], v[78:79]
	v_pk_mul_f32 v[82:83], v[82:83], v[76:77]
	v_pk_mul_f32 v[84:85], v[158:159], v[74:75]
	s_mov_b64 s[38:39], 0

; __device__ __forceinline__ u32x4 pack8(const f32x4 a, const f32x4 b) { u32x4 w; w.x = cvt_pk_bf16(a[0], a[1]); w.y = cvt_pk_bf16(a[2], a[3]); w.z = cvt_pk_bf16(b[0], b[1]); w.w = cvt_pk_bf16(b[2], b[3]); return w; }
;     __device__ __forceinline__ void operator()(const f32x4 (&acc)[2][2][4][2], const Unit& u, int wr, int wc, int fr, int fq) const {
;     ...
;             for (int ai = 0; ai < 2; ++ai)
; #pragma unroll
;                 for (int m = 0; m < 4; ++m) {
;                     const int row = row0 + ai * HALF + m * 16; const int t = row & (SEQ - 1);
;                     const int pos = wc < 2 ? (t >> 6) : (t & 63);
;                     const f32x4* tp = (const f32x4*)(rope + pos * 64 + (wc & 1) * 32 + 8 * fq);
;                     f32x4 o1[2], o2[2];
; #pragma unroll
;                     for (int n = 0; n < 2; ++n) {
;                         const f32x4 x1 = acc[ai][0][m][n], x2 = acc[ai][1][m][n];
;                         if (lat) { const f32x4 cs0 = tp[2 * n], cs1 = tp[2 * n + 1];
;                             o1[n][0] = (x1[0] * cs0[0] - x2[0] * cs0[1]) * sc; o2[n][0] = (x1[0] * cs0[1] + x2[0] * cs0[0]) * sc;
;                             o1[n][1] = (x1[1] * cs0[2] - x2[1] * cs0[3]) * sc; o2[n][1] = (x1[1] * cs0[3] + x2[1] * cs0[2]) * sc;
;                             o1[n][2] = (x1[2] * cs1[0] - x2[2] * cs1[1]) * sc; o2[n][2] = (x1[2] * cs1[1] + x2[2] * cs1[0]) * sc;
;                             o1[n][3] = (x1[3] * cs1[2] - x2[3] * cs1[3]) * sc; o2[n][3] = (x1[3] * cs1[3] + x2[3] * cs1[2]) * sc;
;                         } else { o1[n] = x1 * sc; o2[n] = x2 * sc; }
;                     }
;                     bf16_t* fp = O + ((((size_t)(row >> 13) * 4 + head) * 512 + (t >> 4)) * 8 + wc) * 512 + ((t & 15) + 16 * fq) * 8;
;                     *(u32x4*)(fp) = pack8(o1[0], o1[1]);
;                     *(u32x4*)(fp + 4 * 512) = pack8(o2[0], o2[1]);
.LBB0_1296:
	v_or3_b32 v66, v168, s12, 3
	v_mov_b32_e32 v67, s29
	v_lshlrev_b64 v[66:67], 13, v[66:67]
	v_lshl_add_u64 v[70:71], v[114:115], 0, v[66:67]
	v_cvt_pk_bf16_f32 v66, v88, v89
	v_cvt_pk_bf16_f32 v67, v86, v87
	v_cvt_pk_bf16_f32 v68, v80, v81
	v_cvt_pk_bf16_f32 v69, v74, v75
	global_store_dwordx4 v[70:71], v[66:69], off sc1
	v_add_co_u32_e32 v70, vcc, 0x1000, v70
	s_nop 0
	v_cvt_pk_bf16_f32 v66, v84, v85
	v_addc_co_u32_e32 v71, vcc, 0, v71, vcc
	v_cvt_pk_bf16_f32 v67, v82, v83
	v_cvt_pk_bf16_f32 v68, v78, v79
	v_cvt_pk_bf16_f32 v69, v76, v77
	s_and_b64 vcc, exec, s[10:11]
	s_mov_b64 s[38:39], -1
	global_store_dwordx4 v[70:71], v[66:69], off sc1
	s_cbranch_vccnz .LBB0_1298
	s_nop 0
	v_mov_b32_e32 v66, v158
	v_mov_b32_e32 v67, v158
	v_pk_mul_f32 v[70:71], v[66:67], v[64:65]
	v_pk_mul_f32 v[72:73], v[158:159], v[62:63]
	v_pk_mul_f32 v[66:67], v[66:67], v[60:61]
	v_pk_mul_f32 v[68:69], v[158:159], v[58:59]
	s_mov_b64 s[38:39], 0

; __device__ __forceinline__ u32x4 pack8(const f32x4 a, const f32x4 b) { u32x4 w; w.x = cvt_pk_bf16(a[0], a[1]); w.y = cvt_pk_bf16(a[2], a[3]); w.z = cvt_pk_bf16(b[0], b[1]); w.w = cvt_pk_bf16(b[2], b[3]); return w; }
;     __device__ __forceinline__ void operator()(const f32x4 (&acc)[2][2][4][2], const Unit& u, int wr, int wc, int fr, int fq) const {
;     ...
;             for (int ai = 0; ai < 2; ++ai)
; #pragma unroll
;                 for (int m = 0; m < 4; ++m) {
;                     const int row = row0 + ai * HALF + m * 16; const int t = row & (SEQ - 1);
;                     const int pos = wc < 2 ? (t >> 6) : (t & 63);
;                     const f32x4* tp = (const f32x4*)(rope + pos * 64 + (wc & 1) * 32 + 8 * fq);
;                     f32x4 o1[2], o2[2];
; #pragma unroll
;                     for (int n = 0; n < 2; ++n) {
;                         const f32x4 x1 = acc[ai][0][m][n], x2 = acc[ai][1][m][n];
;                         if (lat) { const f32x4 cs0 = tp[2 * n], cs1 = tp[2 * n + 1];
;                             o1[n][0] = (x1[0] * cs0[0] - x2[0] * cs0[1]) * sc; o2[n][0] = (x1[0] * cs0[1] + x2[0] * cs0[0]) * sc;
;                             o1[n][1] = (x1[1] * cs0[2] - x2[1] * cs0[3]) * sc; o2[n][1] = (x1[1] * cs0[3] + x2[1] * cs0[2]) * sc;
;                             o1[n][2] = (x1[2] * cs1[0] - x2[2] * cs1[1]) * sc; o2[n][2] = (x1[2] * cs1[1] + x2[2] * cs1[0]) * sc;
;                             o1[n][3] = (x1[3] * cs1[2] - x2[3] * cs1[3]) * sc; o2[n][3] = (x1[3] * cs1[3] + x2[3] * cs1[2]) * sc;
;                         } else { o1[n] = x1 * sc; o2[n] = x2 * sc; }
;                     }
;                     bf16_t* fp = O + ((((size_t)(row >> 13) * 4 + head) * 512 + (t >> 4)) * 8 + wc) * 512 + ((t & 15) + 16 * fq) * 8;
;                     *(u32x4*)(fp) = pack8(o1[0], o1[1]);
;                     *(u32x4*)(fp + 4 * 512) = pack8(o2[0], o2[1]);
.LBB0_1304:
	v_ashrrev_i32_e32 v50, 13, v76
	v_ashrrev_i32_e32 v51, 31, v50
	v_and_b32_e32 v52, 0x1fcf, v76
	v_lshlrev_b64 v[50:51], 11, v[50:51]
	v_lshl_add_u64 v[50:51], v[50:51], 0, s[2:3]
	v_lshrrev_b32_e32 v52, 4, v52
	v_or_b32_e32 v52, v50, v52
	v_mov_b32_e32 v53, v51
	v_lshlrev_b64 v[52:53], 13, v[52:53]
	v_lshl_add_u64 v[56:57], v[114:115], 0, v[52:53]
	v_cvt_pk_bf16_f32 v52, v72, v73
	v_cvt_pk_bf16_f32 v53, v70, v71
	v_cvt_pk_bf16_f32 v54, v64, v65
	v_cvt_pk_bf16_f32 v55, v58, v59
	global_store_dwordx4 v[56:57], v[52:55], off sc1
	v_add_co_u32_e32 v56, vcc, 0x1000, v56
	s_nop 0
	v_cvt_pk_bf16_f32 v52, v68, v69
	v_addc_co_u32_e32 v57, vcc, 0, v57, vcc
	v_cvt_pk_bf16_f32 v53, v66, v67
	v_cvt_pk_bf16_f32 v54, v62, v63
	v_cvt_pk_bf16_f32 v55, v60, v61
	s_and_b64 vcc, exec, s[10:11]
	s_mov_b64 s[2:3], -1
	global_store_dwordx4 v[56:57], v[52:55], off sc1
	s_cbranch_vccnz .LBB0_1306
	s_nop 0
	v_mov_b32_e32 v52, v158
	v_mov_b32_e32 v53, v158
	v_pk_mul_f32 v[56:57], v[52:53], v[48:49]
	v_pk_mul_f32 v[58:59], v[158:159], v[46:47]
	v_pk_mul_f32 v[52:53], v[52:53], v[44:45]
	v_pk_mul_f32 v[54:55], v[158:159], v[42:43]
	s_mov_b64 s[2:3], 0

; __device__ __forceinline__ u32x4 pack8(const f32x4 a, const f32x4 b) { u32x4 w; w.x = cvt_pk_bf16(a[0], a[1]); w.y = cvt_pk_bf16(a[2], a[3]); w.z = cvt_pk_bf16(b[0], b[1]); w.w = cvt_pk_bf16(b[2], b[3]); return w; }
;     __device__ __forceinline__ void operator()(const f32x4 (&acc)[2][2][4][2], const Unit& u, int wr, int wc, int fr, int fq) const {
;     ...
;             for (int ai = 0; ai < 2; ++ai)
; #pragma unroll
;                 for (int m = 0; m < 4; ++m) {
;                     const int row = row0 + ai * HALF + m * 16; const int t = row & (SEQ - 1);
;                     const int pos = wc < 2 ? (t >> 6) : (t & 63);
;                     const f32x4* tp = (const f32x4*)(rope + pos * 64 + (wc & 1) * 32 + 8 * fq);
;                     f32x4 o1[2], o2[2];
; #pragma unroll
;                     for (int n = 0; n < 2; ++n) {
;                         const f32x4 x1 = acc[ai][0][m][n], x2 = acc[ai][1][m][n];
;                         if (lat) { const f32x4 cs0 = tp[2 * n], cs1 = tp[2 * n + 1];
;                             o1[n][0] = (x1[0] * cs0[0] - x2[0] * cs0[1]) * sc; o2[n][0] = (x1[0] * cs0[1] + x2[0] * cs0[0]) * sc;
;                             o1[n][1] = (x1[1] * cs0[2] - x2[1] * cs0[3]) * sc; o2[n][1] = (x1[1] * cs0[3] + x2[1] * cs0[2]) * sc;
;                             o1[n][2] = (x1[2] * cs1[0] - x2[2] * cs1[1]) * sc; o2[n][2] = (x1[2] * cs1[1] + x2[2] * cs1[0]) * sc;
;                             o1[n][3] = (x1[3] * cs1[2] - x2[3] * cs1[3]) * sc; o2[n][3] = (x1[3] * cs1[3] + x2[3] * cs1[2]) * sc;
;                         } else { o1[n] = x1 * sc; o2[n] = x2 * sc; }
;                     }
;                     bf16_t* fp = O + ((((size_t)(row >> 13) * 4 + head) * 512 + (t >> 4)) * 8 + wc) * 512 + ((t & 15) + 16 * fq) * 8;
;                     *(u32x4*)(fp) = pack8(o1[0], o1[1]);
;                     *(u32x4*)(fp + 4 * 512) = pack8(o2[0], o2[1]);
.LBB0_1312:
	v_and_b32_e32 v34, 0x1fdf, v62
	v_lshrrev_b32_e32 v34, 4, v34
	v_or_b32_e32 v34, v50, v34
	v_mov_b32_e32 v35, v51
	v_lshlrev_b64 v[34:35], 13, v[34:35]
	v_lshl_add_u64 v[38:39], v[114:115], 0, v[34:35]
	v_cvt_pk_bf16_f32 v34, v58, v59
	v_cvt_pk_bf16_f32 v35, v56, v57
	v_cvt_pk_bf16_f32 v36, v48, v49
	v_cvt_pk_bf16_f32 v37, v42, v43
	global_store_dwordx4 v[38:39], v[34:37], off sc1
	v_add_co_u32_e32 v38, vcc, 0x1000, v38
	s_nop 0
	v_cvt_pk_bf16_f32 v34, v54, v55
	v_addc_co_u32_e32 v39, vcc, 0, v39, vcc
	v_cvt_pk_bf16_f32 v35, v52, v53
	v_cvt_pk_bf16_f32 v36, v46, v47
	v_cvt_pk_bf16_f32 v37, v44, v45
	s_and_b64 vcc, exec, s[10:11]
	s_mov_b64 s[2:3], -1
	global_store_dwordx4 v[38:39], v[34:37], off sc1
	s_cbranch_vccnz .LBB0_1314
	s_nop 0
	v_mov_b32_e32 v34, v158
	v_mov_b32_e32 v35, v158
	v_pk_mul_f32 v[38:39], v[34:35], v[32:33]
	v_pk_mul_f32 v[40:41], v[158:159], v[30:31]
	v_pk_mul_f32 v[34:35], v[34:35], v[28:29]
	v_pk_mul_f32 v[36:37], v[158:159], v[26:27]
	s_mov_b64 s[2:3], 0

; __device__ __forceinline__ u32x4 pack8(const f32x4 a, const f32x4 b) { u32x4 w; w.x = cvt_pk_bf16(a[0], a[1]); w.y = cvt_pk_bf16(a[2], a[3]); w.z = cvt_pk_bf16(b[0], b[1]); w.w = cvt_pk_bf16(b[2], b[3]); return w; }
;     __device__ __forceinline__ void operator()(const f32x4 (&acc)[2][2][4][2], const Unit& u, int wr, int wc, int fr, int fq) const {
;     ...
;             for (int ai = 0; ai < 2; ++ai)
; #pragma unroll
;                 for (int m = 0; m < 4; ++m) {
;                     const int row = row0 + ai * HALF + m * 16; const int t = row & (SEQ - 1);
;                     const int pos = wc < 2 ? (t >> 6) : (t & 63);
;                     const f32x4* tp = (const f32x4*)(rope + pos * 64 + (wc & 1) * 32 + 8 * fq);
;                     f32x4 o1[2], o2[2];
; #pragma unroll
;                     for (int n = 0; n < 2; ++n) {
;                         const f32x4 x1 = acc[ai][0][m][n], x2 = acc[ai][1][m][n];
;                         if (lat) { const f32x4 cs0 = tp[2 * n], cs1 = tp[2 * n + 1];
;                             o1[n][0] = (x1[0] * cs0[0] - x2[0] * cs0[1]) * sc; o2[n][0] = (x1[0] * cs0[1] + x2[0] * cs0[0]) * sc;
;                             o1[n][1] = (x1[1] * cs0[2] - x2[1] * cs0[3]) * sc; o2[n][1] = (x1[1] * cs0[3] + x2[1] * cs0[2]) * sc;
;                             o1[n][2] = (x1[2] * cs1[0] - x2[2] * cs1[1]) * sc; o2[n][2] = (x1[2] * cs1[1] + x2[2] * cs1[0]) * sc;
;                             o1[n][3] = (x1[3] * cs1[2] - x2[3] * cs1[3]) * sc; o2[n][3] = (x1[3] * cs1[3] + x2[3] * cs1[2]) * sc;
;                         } else { o1[n] = x1 * sc; o2[n] = x2 * sc; }
;                     }
;                     bf16_t* fp = O + ((((size_t)(row >> 13) * 4 + head) * 512 + (t >> 4)) * 8 + wc) * 512 + ((t & 15) + 16 * fq) * 8;
;                     *(u32x4*)(fp) = pack8(o1[0], o1[1]);
;                     *(u32x4*)(fp + 4 * 512) = pack8(o2[0], o2[1]);
.LBB0_1320:
	v_and_b32_e32 v18, 0x1fef, v44
	v_lshrrev_b32_e32 v18, 4, v18
	v_or_b32_e32 v18, v50, v18
	v_mov_b32_e32 v19, v51
	v_lshlrev_b64 v[18:19], 13, v[18:19]
	v_lshl_add_u64 v[22:23], v[114:115], 0, v[18:19]
	v_cvt_pk_bf16_f32 v18, v40, v41
	v_cvt_pk_bf16_f32 v19, v38, v39
	v_cvt_pk_bf16_f32 v20, v32, v33
	v_cvt_pk_bf16_f32 v21, v26, v27
	global_store_dwordx4 v[22:23], v[18:21], off sc1
	v_add_co_u32_e32 v22, vcc, 0x1000, v22
	s_nop 0
	v_cvt_pk_bf16_f32 v18, v36, v37
	v_addc_co_u32_e32 v23, vcc, 0, v23, vcc
	v_cvt_pk_bf16_f32 v19, v34, v35
	v_cvt_pk_bf16_f32 v20, v30, v31
	v_cvt_pk_bf16_f32 v21, v28, v29
	s_and_b64 vcc, exec, s[10:11]
	s_mov_b64 s[2:3], -1
	global_store_dwordx4 v[22:23], v[18:21], off sc1
	s_cbranch_vccnz .LBB0_1322
	s_nop 0
	v_mov_b32_e32 v18, v158
	v_mov_b32_e32 v19, v158
	v_pk_mul_f32 v[22:23], v[18:19], v[16:17]
	v_pk_mul_f32 v[24:25], v[158:159], v[14:15]
	v_pk_mul_f32 v[18:19], v[18:19], v[12:13]
	v_pk_mul_f32 v[20:21], v[158:159], v[10:11]
	s_mov_b64 s[2:3], 0

; __device__ __forceinline__ u32x4 pack8(const f32x4 a, const f32x4 b) { u32x4 w; w.x = cvt_pk_bf16(a[0], a[1]); w.y = cvt_pk_bf16(a[2], a[3]); w.z = cvt_pk_bf16(b[0], b[1]); w.w = cvt_pk_bf16(b[2], b[3]); return w; }
;     __device__ __forceinline__ void operator()(const f32x4 (&acc)[2][2][4][2], const Unit& u, int wr, int wc, int fr, int fq) const {
;     ...
;             for (int ai = 0; ai < 2; ++ai)
; #pragma unroll
;                 for (int m = 0; m < 4; ++m) {
;                     const int row = row0 + ai * HALF + m * 16; const int t = row & (SEQ - 1);
;                     const int pos = wc < 2 ? (t >> 6) : (t & 63);
;                     const f32x4* tp = (const f32x4*)(rope + pos * 64 + (wc & 1) * 32 + 8 * fq);
;                     f32x4 o1[2], o2[2];
; #pragma unroll
;                     for (int n = 0; n < 2; ++n) {
;                         const f32x4 x1 = acc[ai][0][m][n], x2 = acc[ai][1][m][n];
;                         if (lat) { const f32x4 cs0 = tp[2 * n], cs1 = tp[2 * n + 1];
;                             o1[n][0] = (x1[0] * cs0[0] - x2[0] * cs0[1]) * sc; o2[n][0] = (x1[0] * cs0[1] + x2[0] * cs0[0]) * sc;
;                             o1[n][1] = (x1[1] * cs0[2] - x2[1] * cs0[3]) * sc; o2[n][1] = (x1[1] * cs0[3] + x2[1] * cs0[2]) * sc;
;                             o1[n][2] = (x1[2] * cs1[0] - x2[2] * cs1[1]) * sc; o2[n][2] = (x1[2] * cs1[1] + x2[2] * cs1[0]) * sc;
;                             o1[n][3] = (x1[3] * cs1[2] - x2[3] * cs1[3]) * sc; o2[n][3] = (x1[3] * cs1[3] + x2[3] * cs1[2]) * sc;
;                         } else { o1[n] = x1 * sc; o2[n] = x2 * sc; }
;                     }
;                     bf16_t* fp = O + ((((size_t)(row >> 13) * 4 + head) * 512 + (t >> 4)) * 8 + wc) * 512 + ((t & 15) + 16 * fq) * 8;
;                     *(u32x4*)(fp) = pack8(o1[0], o1[1]);
;                     *(u32x4*)(fp + 4 * 512) = pack8(o2[0], o2[1]);
.LBB0_1328:
	v_and_b32_e32 v2, 0x1fff, v28
	v_lshrrev_b32_e32 v2, 4, v2
	v_or_b32_e32 v50, v50, v2
	v_lshlrev_b64 v[2:3], 13, v[50:51]
	v_lshl_add_u64 v[6:7], v[114:115], 0, v[2:3]
	v_cvt_pk_bf16_f32 v2, v24, v25
	v_cvt_pk_bf16_f32 v3, v22, v23
	v_cvt_pk_bf16_f32 v4, v16, v17
	v_cvt_pk_bf16_f32 v5, v10, v11
	global_store_dwordx4 v[6:7], v[2:5], off sc1
	v_add_co_u32_e32 v6, vcc, 0x1000, v6
	s_nop 0
	v_cvt_pk_bf16_f32 v2, v20, v21
	v_cvt_pk_bf16_f32 v3, v18, v19
	v_cvt_pk_bf16_f32 v4, v14, v15
	v_cvt_pk_bf16_f32 v5, v12, v13
	v_addc_co_u32_e32 v7, vcc, 0, v7, vcc
	global_store_dwordx4 v[6:7], v[2:5], off sc1
	s_andn2_b64 vcc, exec, s[8:9]
	s_mov_b64 s[2:3], -1
	s_cbranch_vccnz .LBB0_1253

; __device__ __forceinline__ u32x4 pack8(const f32x4 a, const f32x4 b) { u32x4 w; w.x = cvt_pk_bf16(a[0], a[1]); w.y = cvt_pk_bf16(a[2], a[3]); w.z = cvt_pk_bf16(b[0], b[1]); w.w = cvt_pk_bf16(b[2], b[3]); return w; }
;     __device__ __forceinline__ void operator()(const f32x4 (&acc)[2][2][4][2], const Unit& u, int wr, int wc, int fr, int fq) const {
;     ...
;         } else {
;             const int rb = (u.pm - 8) * BM + wr * 64 + fr;
; #pragma unroll
;             for (int ai = 0; ai < 2; ++ai) { if (u.kq >= 0 && u.kq != ai) continue;
; #pragma unroll
;                 for (int m = 0; m < 4; ++m)
; #pragma unroll
;                     for (int bj = 0; bj < 2; ++bj) *(u32x4*)(VT + (size_t)(rb + ai * HALF + m * 16) * MT + col0 + bj * HALF) = pack8(acc[ai][bj][m][0], acc[ai][bj][m][1]); }
.LBB0_1346:
	s_cmp_gt_i32 s54, 7
	s_mov_b64 s[0:1], -1
	v_readlane_b32 s94, v250, 34
	s_cbranch_scc0 .LBB0_1349
	v_readlane_b32 s0, v250, 36
	v_lshl_or_b32 v134, s2, 8, v191
	v_readlane_b32 s1, v250, 37
	v_lshl_add_u32 v140, s54, 8, v163
	v_ashrrev_i32_e32 v135, 31, v134
	v_mov_b64_e32 v[136:137], s[0:1]
	v_mad_i64_i32 v[138:139], s[0:1], v140, s22, v[136:137]
	v_lshlrev_b64 v[134:135], 1, v[134:135]
	v_cvt_pk_bf16_f32 v130, v126, v127
	v_cvt_pk_bf16_f32 v131, v128, v129
	v_cvt_pk_bf16_f32 v132, v122, v123
	v_cvt_pk_bf16_f32 v133, v124, v125
	v_lshl_add_u64 v[138:139], v[138:139], 0, v[134:135]
	global_store_dwordx4 v[138:139], v[130:133], off sc1
	s_nop 1
	v_cvt_pk_bf16_f32 v130, v110, v111
	v_cvt_pk_bf16_f32 v131, v112, v113
	v_cvt_pk_bf16_f32 v132, v106, v107
	v_cvt_pk_bf16_f32 v133, v108, v109
	global_store_dwordx4 v[138:139], v[130:133], off offset:256 sc1
	v_or_b32_e32 v138, 16, v140
	v_mad_i64_i32 v[138:139], s[0:1], v138, s22, v[136:137]
	v_cvt_pk_bf16_f32 v130, v94, v95
	v_cvt_pk_bf16_f32 v131, v96, v97
	v_cvt_pk_bf16_f32 v132, v90, v91
	v_cvt_pk_bf16_f32 v133, v92, v93
	v_lshl_add_u64 v[138:139], v[138:139], 0, v[134:135]
	global_store_dwordx4 v[138:139], v[130:133], off sc1
	s_nop 1
	v_cvt_pk_bf16_f32 v130, v78, v79
	v_cvt_pk_bf16_f32 v131, v80, v81
	v_cvt_pk_bf16_f32 v132, v74, v75
	v_cvt_pk_bf16_f32 v133, v76, v77
	global_store_dwordx4 v[138:139], v[130:133], off offset:256 sc1
	v_or_b32_e32 v138, 32, v140
	v_mad_i64_i32 v[138:139], s[0:1], v138, s22, v[136:137]
	v_cvt_pk_bf16_f32 v130, v62, v63
	v_cvt_pk_bf16_f32 v131, v64, v65
	v_cvt_pk_bf16_f32 v132, v58, v59
	v_cvt_pk_bf16_f32 v133, v60, v61
	v_lshl_add_u64 v[138:139], v[138:139], 0, v[134:135]
	global_store_dwordx4 v[138:139], v[130:133], off sc1
	s_nop 1
	v_cvt_pk_bf16_f32 v130, v46, v47
	v_cvt_pk_bf16_f32 v131, v48, v49
	v_cvt_pk_bf16_f32 v132, v42, v43
	v_cvt_pk_bf16_f32 v133, v44, v45
	global_store_dwordx4 v[138:139], v[130:133], off offset:256 sc1
	v_or_b32_e32 v138, 48, v140
	v_mad_i64_i32 v[138:139], s[0:1], v138, s22, v[136:137]
	v_cvt_pk_bf16_f32 v130, v30, v31
	v_cvt_pk_bf16_f32 v131, v32, v33
	v_cvt_pk_bf16_f32 v132, v26, v27
	v_cvt_pk_bf16_f32 v133, v28, v29
	v_lshl_add_u64 v[138:139], v[138:139], 0, v[134:135]
	global_store_dwordx4 v[138:139], v[130:133], off sc1
	s_nop 1
	v_cvt_pk_bf16_f32 v130, v14, v15
	v_cvt_pk_bf16_f32 v131, v16, v17
	v_cvt_pk_bf16_f32 v132, v10, v11
	v_cvt_pk_bf16_f32 v133, v12, v13
	global_store_dwordx4 v[138:139], v[130:133], off offset:256 sc1
	v_add_u32_e32 v138, 0x80, v140
	v_mad_i64_i32 v[138:139], s[0:1], v138, s22, v[136:137]
	v_cvt_pk_bf16_f32 v130, v118, v119
	v_cvt_pk_bf16_f32 v131, v120, v121
	v_cvt_pk_bf16_f32 v132, v114, v115
	v_cvt_pk_bf16_f32 v133, v116, v117
	v_lshl_add_u64 v[138:139], v[138:139], 0, v[134:135]
	global_store_dwordx4 v[138:139], v[130:133], off sc1
	s_nop 1
	v_cvt_pk_bf16_f32 v130, v102, v103
	v_cvt_pk_bf16_f32 v131, v104, v105
	v_cvt_pk_bf16_f32 v132, v98, v99
	v_cvt_pk_bf16_f32 v133, v100, v101
	global_store_dwordx4 v[138:139], v[130:133], off offset:256 sc1
	v_add_u32_e32 v138, 0x90, v140
	v_mad_i64_i32 v[138:139], s[0:1], v138, s22, v[136:137]
	v_cvt_pk_bf16_f32 v130, v86, v87
	v_cvt_pk_bf16_f32 v131, v88, v89
	v_cvt_pk_bf16_f32 v132, v82, v83
	v_cvt_pk_bf16_f32 v133, v84, v85
	v_lshl_add_u64 v[138:139], v[138:139], 0, v[134:135]
	global_store_dwordx4 v[138:139], v[130:133], off sc1
	s_nop 1
	v_cvt_pk_bf16_f32 v130, v70, v71
	v_cvt_pk_bf16_f32 v131, v72, v73
	v_cvt_pk_bf16_f32 v132, v66, v67
	v_cvt_pk_bf16_f32 v133, v68, v69
	global_store_dwordx4 v[138:139], v[130:133], off offset:256 sc1
	v_add_u32_e32 v138, 0xa0, v140
	v_mad_i64_i32 v[138:139], s[0:1], v138, s22, v[136:137]
	v_cvt_pk_bf16_f32 v130, v54, v55
	v_cvt_pk_bf16_f32 v131, v56, v57
	v_cvt_pk_bf16_f32 v132, v50, v51
	v_cvt_pk_bf16_f32 v133, v52, v53
	v_lshl_add_u64 v[138:139], v[138:139], 0, v[134:135]
	global_store_dwordx4 v[138:139], v[130:133], off sc1
	s_nop 1
	v_cvt_pk_bf16_f32 v130, v38, v39
	v_cvt_pk_bf16_f32 v131, v40, v41
	v_cvt_pk_bf16_f32 v132, v34, v35
	v_cvt_pk_bf16_f32 v133, v36, v37
	global_store_dwordx4 v[138:139], v[130:133], off offset:256 sc1
	v_add_u32_e32 v138, 0xb0, v140
	v_mad_i64_i32 v[136:137], s[0:1], v138, s22, v[136:137]
	v_cvt_pk_bf16_f32 v130, v22, v23
	v_cvt_pk_bf16_f32 v131, v24, v25
	v_cvt_pk_bf16_f32 v132, v18, v19
	v_cvt_pk_bf16_f32 v133, v20, v21
	v_lshl_add_u64 v[134:135], v[136:137], 0, v[134:135]
	global_store_dwordx4 v[134:135], v[130:133], off sc1
	s_nop 1
	v_cvt_pk_bf16_f32 v130, v6, v7
	v_cvt_pk_bf16_f32 v131, v8, v9
	v_cvt_pk_bf16_f32 v132, v2, v3
	v_cvt_pk_bf16_f32 v133, v4, v5
	global_store_dwordx4 v[134:135], v[130:133], off offset:256 sc1
	s_cbranch_execz .LBB0_1350

;     __device__ __forceinline__ void operator()(const f32x4 (&acc)[2][2][4][2], const Unit& u, int wr, int wc, int fr, int fq) const {
;         const int col0 = u.pn * BM + wc * 32 + 8 * fq;
;         if (u.pm < 8) {
;             const int head = u.pm - 4; const bool lat = u.pn < 64;
; #pragma unroll
;             for (int m = 0; m < 4; ++m) {
;                 const int f = 16 * m + fr, r1 = head * 256 + wr * 64 + f;
; #pragma unroll
;                 for (int bj = 0; bj < 2; ++bj) {
;                     f32x4 o1[2], o2[2];
; #pragma unroll
;                     for (int n = 0; n < 2; ++n) {
;                         const f32x4 x1 = acc[0][bj][m][n], x2 = acc[1][bj][m][n];
;                         if (lat) {
;                             f32x4 cc, ss;
;                             if (wr == 0) { const int pos = ((u.pn * BM + bj * HALF + wc * 32) & (SEQ - 1)) >> 6; const f32x2 cs = rope[pos * 64 + f];
;                                 cc = (f32x4){cs.x, cs.x, cs.x, cs.x}; ss = (f32x4){cs.y, cs.y, cs.y, cs.y}; }
;                             else { const f32x4* tp = (const f32x4*)(rope2 + f * 128 + (wc & 1) * 32 + 8 * fq + 4 * n); const f32x4 a = tp[0], b = tp[1];
;                                 cc = (f32x4){a[0], a[2], b[0], b[2]}; ss = (f32x4){a[1], a[3], b[1], b[3]}; }
;                             o1[n] = (x1 * cc - x2 * ss) * 0.0625f; o2[n] = (x1 * ss + x2 * cc) * 0.0625f;
;                         } else { o1[n] = x1 * 0.0625f; o2[n] = x2 * 0.0625f; }
;                     }
;                     const int dk = wr * 64 + f; bf16_t* fp = KT + ((((size_t)head * 132 + 2 * u.pn + bj) * 8 + (dk >> 5)) * 8 + 2 * wc + (fq >> 1)) * 512 + (32 * (fq & 1) + (dk & 31)) * 8;
;                     if (u.kq != 1) *(u32x4*)(fp) = pack8(o1[0], o1[1]);
;                     if (u.kq != 0) *(u32x4*)(fp + (size_t)4 * 8 * 512) = pack8(o2[0], o2[1]);
;                     if (lat) {
;                         LAS bf16_t* tl = (LAS bf16_t*)(scr + (wr * 4 + wc) * 2048);
;                         *(LAS u32x4*)(tl + fr * 32 + 8 * fq) = pack8(o1[0], o1[1]);
;                         *(LAS u32x4*)(tl + 512 + fr * 32 + 8 * fq) = pack8(o2[0], o2[1]);
;                         asm volatile("s_waitcnt lgkmcnt(0)" ::: "memory");
;                         const int L = fr + 16 * fq, tt = L & 31, hf = L >> 5, T = u.pn * BM + bj * HALF + wc * 32 + tt, t = T & (SEQ - 1);
.LBB0_1358:
	s_add_i32 s56, s54, -4
	s_ashr_i32 s57, s56, 31
	s_lshl_b32 s45, s2, 1
	s_mul_i32 s19, s56, 0x84
	s_lshl_b64 s[58:59], s[56:57], 9
	s_ashr_i32 s47, s45, 31
	s_mul_hi_i32 s18, s56, 0x84
	s_add_u32 s56, s19, s45
	s_addc_u32 s57, s18, s47
	s_lshl_b64 s[56:57], s[56:57], 16
	v_readlane_b32 s18, v250, 8
	s_add_u32 s45, s18, s56
	v_readlane_b32 s18, v250, 6
	s_addc_u32 s47, s18, s57
	v_pk_mul_f32 v[142:143], v[118:119], v[136:137]
	v_pk_mul_f32 v[118:119], v[118:119], v[182:183]
	s_add_u32 s56, s45, s26
	v_pk_mul_f32 v[138:139], v[120:121], v[132:133]
	v_pk_fma_f32 v[142:143], v[126:127], v[182:183], v[142:143] neg_lo:[0,0,1] neg_hi:[0,0,1]
	v_pk_mul_f32 v[120:121], v[120:121], v[184:185]
	v_pk_fma_f32 v[118:119], v[126:127], v[136:137], v[118:119]
	v_pk_mul_f32 v[126:127], v[116:117], v[140:141]
	v_pk_mul_f32 v[116:117], v[116:117], v[134:135]
	s_addc_u32 s57, s47, s27
	v_pk_fma_f32 v[138:139], v[128:129], v[184:185], v[138:139] neg_lo:[0,0,1] neg_hi:[0,0,1]
	v_pk_fma_f32 v[120:121], v[128:129], v[132:133], v[120:121]
	v_pk_mul_f32 v[128:129], v[114:115], v[144:145]
	v_pk_fma_f32 v[126:127], v[124:125], v[134:135], v[126:127] neg_lo:[0,0,1] neg_hi:[0,0,1]
	v_pk_mul_f32 v[114:115], v[114:115], v[130:131]
	v_pk_fma_f32 v[116:117], v[124:125], v[140:141], v[116:117]
	v_lshl_add_u64 v[134:135], s[56:57], 0, v[164:165]
	v_lshlrev_b32_e32 v158, 1, v160
	v_pk_mul_f32 v[120:121], v[120:121], s[6:7] op_sel_hi:[1,0]
	v_pk_mul_f32 v[118:119], v[118:119], s[6:7] op_sel_hi:[1,0]
	v_pk_fma_f32 v[128:129], v[122:123], v[130:131], v[128:129] neg_lo:[0,0,1] neg_hi:[0,0,1]
	v_pk_fma_f32 v[114:115], v[122:123], v[144:145], v[114:115]
	v_pk_mul_f32 v[122:123], v[116:117], s[6:7] op_sel_hi:[1,0]
	v_lshl_add_u64 v[130:131], v[134:135], 0, v[158:159]
	v_pk_mul_f32 v[138:139], v[138:139], s[6:7] op_sel_hi:[1,0]
	v_pk_mul_f32 v[142:143], v[142:143], s[6:7] op_sel_hi:[1,0]
	v_pk_mul_f32 v[126:127], v[126:127], s[6:7] op_sel_hi:[1,0]
	v_pk_mul_f32 v[128:129], v[128:129], s[6:7] op_sel_hi:[1,0]
	v_pk_mul_f32 v[124:125], v[114:115], s[6:7] op_sel_hi:[1,0]
	v_cvt_pk_bf16_f32 v118, v118, v119
	v_cvt_pk_bf16_f32 v119, v120, v121
	v_cvt_pk_bf16_f32 v121, v122, v123
	v_add_co_u32_e32 v122, vcc, s69, v130
	v_cvt_pk_bf16_f32 v114, v142, v143
	v_cvt_pk_bf16_f32 v115, v138, v139
	v_cvt_pk_bf16_f32 v116, v128, v129
	v_cvt_pk_bf16_f32 v117, v126, v127
	v_cvt_pk_bf16_f32 v120, v124, v125
	v_addc_co_u32_e32 v123, vcc, 0, v131, vcc
	s_and_b32 s3, s3, 0x1f00
	s_ashr_i32 s2, s2, 5
	global_store_dwordx4 v[130:131], v[114:117], off sc1
	global_store_dwordx4 v[122:123], v[118:121], off sc1
	ds_write_b128 v189, v[114:117]
	ds_write_b128 v189, v[118:121] offset:1024
	v_or_b32_e32 v114, s3, v192
	s_ashr_i32 s3, s2, 31
	s_lshl_b64 s[2:3], s[2:3], 11
	s_waitcnt lgkmcnt(0)
	s_add_u32 s57, s2, s58
	s_addc_u32 s58, s3, s59
	v_lshrrev_b32_e32 v142, 4, v114
	ds_read_u16 v116, v190
	ds_read_u16 v117, v190 offset:64
	ds_read_u16 v120, v190 offset:128
	ds_read_u16 v121, v190 offset:192
	ds_read_u16 v122, v190 offset:256
	ds_read_u16 v123, v190 offset:320
	ds_read_u16 v124, v190 offset:384
	ds_read_u16 v125, v190 offset:448
	v_or_b32_e32 v114, s57, v142
	v_mov_b32_e32 v115, s58
	v_lshlrev_b64 v[118:119], 13, v[114:115]
	v_lshl_add_u64 v[132:133], s[20:21], 0, v[118:119]
	v_lshl_add_u64 v[118:119], v[132:133], 0, s[28:29]
	v_lshlrev_b32_e32 v130, 1, v162
	v_mov_b32_e32 v131, v159
	s_waitcnt lgkmcnt(0)
	v_lshl_or_b32 v114, v117, 16, v116
	v_lshl_or_b32 v115, v121, 16, v120
	v_lshl_or_b32 v116, v123, 16, v122
	v_lshl_or_b32 v117, v125, 16, v124
	v_lshl_add_u64 v[136:137], v[118:119], 0, v[130:131]
	ds_read_u16 v118, v190 offset:1024
	ds_read_u16 v119, v190 offset:1088
	ds_read_u16 v120, v190 offset:1152
	ds_read_u16 v121, v190 offset:1216
	ds_read_u16 v122, v190 offset:1280
	ds_read_u16 v123, v190 offset:1344
	ds_read_u16 v124, v190 offset:1408
	ds_read_u16 v125, v190 offset:1472
	global_store_dwordx4 v[136:137], v[114:117], off sc1
	s_and_b64 vcc, exec, s[0:1]
	s_mov_b64 s[2:3], -1
	s_waitcnt lgkmcnt(0)
	v_lshl_or_b32 v114, v119, 16, v118
	v_lshl_add_u64 v[118:119], v[132:133], 0, s[30:31]
	v_lshl_or_b32 v115, v121, 16, v120
	v_lshl_or_b32 v116, v123, 16, v122
	v_lshl_or_b32 v117, v125, 16, v124
	v_lshl_add_u64 v[118:119], v[118:119], 0, v[130:131]
	global_store_dwordx4 v[118:119], v[114:117], off sc1
	s_waitcnt lgkmcnt(0)
	s_cbranch_vccnz .LBB0_1360
	global_load_dwordx4 v[114:117], v[168:169], off offset:16
	global_load_dwordx4 v[118:121], v[168:169], off
	s_waitcnt vmcnt(0)
	v_mov_b32_e32 v141, v116
	v_mov_b32_e32 v140, v114
	v_mov_b32_e32 v139, v120
	v_mov_b32_e32 v138, v118
	v_mov_b32_e32 v116, v115
	v_mov_b32_e32 v120, v119
	s_cbranch_execnz .LBB0_1362
	s_branch .LBB0_1361

;     __device__ __forceinline__ void operator()(const f32x4 (&acc)[2][2][4][2], const Unit& u, int wr, int wc, int fr, int fq) const {
;     ...
;             for (int m = 0; m < 4; ++m) {
;                 const int f = 16 * m + fr, r1 = head * 256 + wr * 64 + f;
; #pragma unroll
;                 for (int bj = 0; bj < 2; ++bj) {
;                     f32x4 o1[2], o2[2];
; #pragma unroll
;                     for (int n = 0; n < 2; ++n) {
;                         const f32x4 x1 = acc[0][bj][m][n], x2 = acc[1][bj][m][n];
;                         if (lat) {
;                             f32x4 cc, ss;
;                             if (wr == 0) { const int pos = ((u.pn * BM + bj * HALF + wc * 32) & (SEQ - 1)) >> 6; const f32x2 cs = rope[pos * 64 + f];
;                                 cc = (f32x4){cs.x, cs.x, cs.x, cs.x}; ss = (f32x4){cs.y, cs.y, cs.y, cs.y}; }
;                             else { const f32x4* tp = (const f32x4*)(rope2 + f * 128 + (wc & 1) * 32 + 8 * fq + 4 * n); const f32x4 a = tp[0], b = tp[1];
;                                 cc = (f32x4){a[0], a[2], b[0], b[2]}; ss = (f32x4){a[1], a[3], b[1], b[3]}; }
;                             o1[n] = (x1 * cc - x2 * ss) * 0.0625f; o2[n] = (x1 * ss + x2 * cc) * 0.0625f;
;                         } else { o1[n] = x1 * 0.0625f; o2[n] = x2 * 0.0625f; }
;                     }
;                     const int dk = wr * 64 + f; bf16_t* fp = KT + ((((size_t)head * 132 + 2 * u.pn + bj) * 8 + (dk >> 5)) * 8 + 2 * wc + (fq >> 1)) * 512 + (32 * (fq & 1) + (dk & 31)) * 8;
;                     if (u.kq != 1) *(u32x4*)(fp) = pack8(o1[0], o1[1]);
;                     if (u.kq != 0) *(u32x4*)(fp + (size_t)4 * 8 * 512) = pack8(o2[0], o2[1]);
;                     if (lat) {
;                         LAS bf16_t* tl = (LAS bf16_t*)(scr + (wr * 4 + wc) * 2048);
;                         *(LAS u32x4*)(tl + fr * 32 + 8 * fq) = pack8(o1[0], o1[1]);
;                         *(LAS u32x4*)(tl + 512 + fr * 32 + 8 * fq) = pack8(o2[0], o2[1]);
;                         asm volatile("s_waitcnt lgkmcnt(0)" ::: "memory");
;                         const int L = fr + 16 * fq, tt = L & 31, hf = L >> 5, T = u.pn * BM + bj * HALF + wc * 32 + tt, t = T & (SEQ - 1);
; #pragma unroll
;                         for (int part = 0; part < 2; ++part) { const LAS bf16_t* sp = tl + part * 512 + (hf * 8) * 32 + tt; u32x4 w8;
.LBB0_1366:
	s_add_u32 s54, s45, 0x10000
	s_addc_u32 s56, s47, 0
	v_pk_mul_f32 v[126:127], v[102:103], v[120:121]
	v_pk_mul_f32 v[102:103], v[102:103], v[138:139]
	s_add_u32 s2, s54, s26
	v_pk_mul_f32 v[122:123], v[104:105], v[116:117]
	v_pk_fma_f32 v[126:127], v[110:111], v[138:139], v[126:127] neg_lo:[0,0,1] neg_hi:[0,0,1]
	v_pk_mul_f32 v[104:105], v[104:105], v[140:141]
	v_pk_fma_f32 v[102:103], v[110:111], v[120:121], v[102:103]
	v_pk_mul_f32 v[110:111], v[100:101], v[124:125]
	v_pk_mul_f32 v[100:101], v[100:101], v[118:119]
	s_addc_u32 s3, s56, s27
	v_pk_fma_f32 v[122:123], v[112:113], v[140:141], v[122:123] neg_lo:[0,0,1] neg_hi:[0,0,1]
	v_pk_fma_f32 v[104:105], v[112:113], v[116:117], v[104:105]
	v_pk_mul_f32 v[112:113], v[98:99], v[128:129]
	v_pk_mul_f32 v[98:99], v[98:99], v[114:115]
	v_pk_fma_f32 v[100:101], v[108:109], v[124:125], v[100:101]
	v_lshl_add_u64 v[116:117], s[2:3], 0, v[164:165]
	v_pk_mul_f32 v[104:105], v[104:105], s[6:7] op_sel_hi:[1,0]
	v_pk_mul_f32 v[102:103], v[102:103], s[6:7] op_sel_hi:[1,0]
	v_pk_fma_f32 v[112:113], v[106:107], v[114:115], v[112:113] neg_lo:[0,0,1] neg_hi:[0,0,1]
	v_pk_fma_f32 v[110:111], v[108:109], v[118:119], v[110:111] neg_lo:[0,0,1] neg_hi:[0,0,1]
	v_pk_fma_f32 v[98:99], v[106:107], v[128:129], v[98:99]
	v_pk_mul_f32 v[106:107], v[100:101], s[6:7] op_sel_hi:[1,0]
	v_lshl_add_u64 v[114:115], v[116:117], 0, v[158:159]
	v_pk_mul_f32 v[122:123], v[122:123], s[6:7] op_sel_hi:[1,0]
	v_pk_mul_f32 v[126:127], v[126:127], s[6:7] op_sel_hi:[1,0]
	v_pk_mul_f32 v[110:111], v[110:111], s[6:7] op_sel_hi:[1,0]
	v_pk_mul_f32 v[112:113], v[112:113], s[6:7] op_sel_hi:[1,0]
	v_pk_mul_f32 v[108:109], v[98:99], s[6:7] op_sel_hi:[1,0]
	v_cvt_pk_bf16_f32 v102, v102, v103
	v_cvt_pk_bf16_f32 v103, v104, v105
	v_cvt_pk_bf16_f32 v105, v106, v107
	v_add_co_u32_e32 v106, vcc, s69, v114
	v_cvt_pk_bf16_f32 v98, v126, v127
	v_cvt_pk_bf16_f32 v99, v122, v123
	v_cvt_pk_bf16_f32 v100, v112, v113
	v_cvt_pk_bf16_f32 v101, v110, v111
	v_cvt_pk_bf16_f32 v104, v108, v109
	v_addc_co_u32_e32 v107, vcc, 0, v115, vcc
	global_store_dwordx4 v[114:115], v[98:101], off sc1
	global_store_dwordx4 v[106:107], v[102:105], off sc1
	ds_write_b128 v189, v[98:101]
	ds_write_b128 v189, v[102:105] offset:1024
	s_waitcnt lgkmcnt(0)
	ds_read_u16 v100, v190
	ds_read_u16 v101, v190 offset:64
	ds_read_u16 v104, v190 offset:128
	ds_read_u16 v105, v190 offset:192
	ds_read_u16 v106, v190 offset:256
	ds_read_u16 v107, v190 offset:320
	ds_read_u16 v108, v190 offset:384
	ds_read_u16 v109, v190 offset:448
	v_or3_b32 v98, v142, s57, 8
	v_mov_b32_e32 v99, s58
	v_lshlrev_b64 v[102:103], 13, v[98:99]
	v_lshl_add_u64 v[114:115], s[20:21], 0, v[102:103]
	v_lshl_add_u64 v[102:103], v[114:115], 0, s[28:29]
	v_mov_b32_e32 v131, v159
	s_waitcnt lgkmcnt(0)
	v_lshl_or_b32 v98, v101, 16, v100
	v_lshl_or_b32 v99, v105, 16, v104
	v_lshl_or_b32 v100, v107, 16, v106
	v_lshl_or_b32 v101, v109, 16, v108
	v_lshl_add_u64 v[118:119], v[102:103], 0, v[130:131]
	ds_read_u16 v102, v190 offset:1024
	ds_read_u16 v103, v190 offset:1088
	ds_read_u16 v104, v190 offset:1152
	ds_read_u16 v105, v190 offset:1216
	ds_read_u16 v106, v190 offset:1280
	ds_read_u16 v107, v190 offset:1344
	ds_read_u16 v108, v190 offset:1408
	ds_read_u16 v109, v190 offset:1472
	global_store_dwordx4 v[118:119], v[98:101], off sc1
	s_and_b64 vcc, exec, s[0:1]
	s_mov_b64 s[2:3], -1
	s_waitcnt lgkmcnt(0)
	v_lshl_or_b32 v98, v103, 16, v102
	v_lshl_add_u64 v[102:103], v[114:115], 0, s[30:31]
	v_lshl_or_b32 v99, v105, 16, v104
	v_lshl_or_b32 v100, v107, 16, v106
	v_lshl_or_b32 v101, v109, 16, v108
	v_lshl_add_u64 v[102:103], v[102:103], 0, v[130:131]
	global_store_dwordx4 v[102:103], v[98:101], off sc1
	s_waitcnt lgkmcnt(0)
	s_cbranch_vccnz .LBB0_1368
	global_load_dwordx4 v[98:101], v[170:171], off offset:16
	global_load_dwordx4 v[102:105], v[170:171], off
	s_mov_b64 s[2:3], 0
	s_waitcnt vmcnt(0)
	v_mov_b32_e32 v123, v100
	v_mov_b32_e32 v122, v98
	v_mov_b32_e32 v121, v104
	v_mov_b32_e32 v120, v102
	v_mov_b32_e32 v100, v99
	v_mov_b32_e32 v104, v103

;     __device__ __forceinline__ void operator()(const f32x4 (&acc)[2][2][4][2], const Unit& u, int wr, int wc, int fr, int fq) const {
;     ...
;             for (int m = 0; m < 4; ++m) {
;                 const int f = 16 * m + fr, r1 = head * 256 + wr * 64 + f;
; #pragma unroll
;                 for (int bj = 0; bj < 2; ++bj) {
;                     f32x4 o1[2], o2[2];
; #pragma unroll
;                     for (int n = 0; n < 2; ++n) {
;                         const f32x4 x1 = acc[0][bj][m][n], x2 = acc[1][bj][m][n];
;                         if (lat) {
;                             f32x4 cc, ss;
;                             if (wr == 0) { const int pos = ((u.pn * BM + bj * HALF + wc * 32) & (SEQ - 1)) >> 6; const f32x2 cs = rope[pos * 64 + f];
;                                 cc = (f32x4){cs.x, cs.x, cs.x, cs.x}; ss = (f32x4){cs.y, cs.y, cs.y, cs.y}; }
;                             else { const f32x4* tp = (const f32x4*)(rope2 + f * 128 + (wc & 1) * 32 + 8 * fq + 4 * n); const f32x4 a = tp[0], b = tp[1];
;                                 cc = (f32x4){a[0], a[2], b[0], b[2]}; ss = (f32x4){a[1], a[3], b[1], b[3]}; }
;                             o1[n] = (x1 * cc - x2 * ss) * 0.0625f; o2[n] = (x1 * ss + x2 * cc) * 0.0625f;
;                         } else { o1[n] = x1 * 0.0625f; o2[n] = x2 * 0.0625f; }
;                     }
;                     const int dk = wr * 64 + f; bf16_t* fp = KT + ((((size_t)head * 132 + 2 * u.pn + bj) * 8 + (dk >> 5)) * 8 + 2 * wc + (fq >> 1)) * 512 + (32 * (fq & 1) + (dk & 31)) * 8;
;                     if (u.kq != 1) *(u32x4*)(fp) = pack8(o1[0], o1[1]);
;                     if (u.kq != 0) *(u32x4*)(fp + (size_t)4 * 8 * 512) = pack8(o2[0], o2[1]);
;                     if (lat) {
;                         LAS bf16_t* tl = (LAS bf16_t*)(scr + (wr * 4 + wc) * 2048);
;                         *(LAS u32x4*)(tl + fr * 32 + 8 * fq) = pack8(o1[0], o1[1]);
;                         *(LAS u32x4*)(tl + 512 + fr * 32 + 8 * fq) = pack8(o2[0], o2[1]);
;                         asm volatile("s_waitcnt lgkmcnt(0)" ::: "memory");
;                         const int L = fr + 16 * fq, tt = L & 31, hf = L >> 5, T = u.pn * BM + bj * HALF + wc * 32 + tt, t = T & (SEQ - 1);
; #pragma unroll
;                         for (int part = 0; part < 2; ++part) { const LAS bf16_t* sp = tl + part * 512 + (hf * 8) * 32 + tt; u32x4 w8;
.LBB0_1374:
	v_pk_mul_f32 v[110:111], v[86:87], v[104:105]
	v_pk_mul_f32 v[86:87], v[86:87], v[120:121]
	v_pk_mul_f32 v[106:107], v[88:89], v[100:101]
	v_pk_fma_f32 v[110:111], v[94:95], v[120:121], v[110:111] neg_lo:[0,0,1] neg_hi:[0,0,1]
	v_pk_mul_f32 v[88:89], v[88:89], v[122:123]
	v_pk_fma_f32 v[86:87], v[94:95], v[104:105], v[86:87]
	v_pk_mul_f32 v[94:95], v[84:85], v[108:109]
	v_pk_mul_f32 v[84:85], v[84:85], v[124:125]
	v_pk_fma_f32 v[106:107], v[96:97], v[122:123], v[106:107] neg_lo:[0,0,1] neg_hi:[0,0,1]
	v_pk_fma_f32 v[88:89], v[96:97], v[100:101], v[88:89]
	v_pk_mul_f32 v[96:97], v[82:83], v[112:113]
	v_pk_mul_f32 v[82:83], v[82:83], v[102:103]
	v_pk_fma_f32 v[84:85], v[92:93], v[108:109], v[84:85]
	v_lshlrev_b32_e32 v100, 1, v166
	v_mov_b32_e32 v101, v159
	v_pk_mul_f32 v[88:89], v[88:89], s[6:7] op_sel_hi:[1,0]
	v_pk_mul_f32 v[86:87], v[86:87], s[6:7] op_sel_hi:[1,0]
	v_pk_fma_f32 v[96:97], v[90:91], v[102:103], v[96:97] neg_lo:[0,0,1] neg_hi:[0,0,1]
	v_pk_fma_f32 v[94:95], v[92:93], v[124:125], v[94:95] neg_lo:[0,0,1] neg_hi:[0,0,1]
	v_pk_fma_f32 v[82:83], v[90:91], v[112:113], v[82:83]
	v_pk_mul_f32 v[90:91], v[84:85], s[6:7] op_sel_hi:[1,0]
	v_lshl_add_u64 v[102:103], v[134:135], 0, v[100:101]
	v_pk_mul_f32 v[106:107], v[106:107], s[6:7] op_sel_hi:[1,0]
	v_pk_mul_f32 v[110:111], v[110:111], s[6:7] op_sel_hi:[1,0]
	v_pk_mul_f32 v[94:95], v[94:95], s[6:7] op_sel_hi:[1,0]
	v_pk_mul_f32 v[96:97], v[96:97], s[6:7] op_sel_hi:[1,0]
	v_pk_mul_f32 v[92:93], v[82:83], s[6:7] op_sel_hi:[1,0]
	v_cvt_pk_bf16_f32 v86, v86, v87
	v_cvt_pk_bf16_f32 v87, v88, v89
	v_cvt_pk_bf16_f32 v89, v90, v91
	v_add_co_u32_e32 v90, vcc, s69, v102
	v_cvt_pk_bf16_f32 v82, v110, v111
	v_cvt_pk_bf16_f32 v83, v106, v107
	v_cvt_pk_bf16_f32 v84, v96, v97
	v_cvt_pk_bf16_f32 v85, v94, v95
	v_cvt_pk_bf16_f32 v88, v92, v93
	v_addc_co_u32_e32 v91, vcc, 0, v103, vcc
	global_store_dwordx4 v[102:103], v[82:85], off sc1
	global_store_dwordx4 v[90:91], v[86:89], off sc1
	ds_write_b128 v189, v[82:85]
	ds_write_b128 v189, v[86:89] offset:1024
	s_waitcnt lgkmcnt(0)
	ds_read_u16 v82, v190
	ds_read_u16 v83, v190 offset:64
	ds_read_u16 v84, v190 offset:128
	ds_read_u16 v85, v190 offset:192
	ds_read_u16 v86, v190 offset:256
	ds_read_u16 v87, v190 offset:320
	ds_read_u16 v88, v190 offset:384
	ds_read_u16 v89, v190 offset:448
	s_waitcnt lgkmcnt(0)
	v_lshl_or_b32 v82, v83, 16, v82
	v_lshl_or_b32 v83, v85, 16, v84
	v_lshl_or_b32 v84, v87, 16, v86
	v_mov_b32_e32 v131, v159
	v_lshl_or_b32 v85, v89, 16, v88
	ds_read_u16 v86, v190 offset:1024
	ds_read_u16 v87, v190 offset:1088
	ds_read_u16 v88, v190 offset:1152
	ds_read_u16 v89, v190 offset:1216
	ds_read_u16 v90, v190 offset:1280
	ds_read_u16 v91, v190 offset:1344
	ds_read_u16 v92, v190 offset:1408
	ds_read_u16 v93, v190 offset:1472
	global_store_dwordx4 v[136:137], v[82:85], off offset:512 sc1
	s_and_b64 vcc, exec, s[0:1]
	s_mov_b64 s[2:3], -1
	s_waitcnt lgkmcnt(0)
	v_lshl_or_b32 v82, v87, 16, v86
	v_lshl_add_u64 v[86:87], v[132:133], 0, s[34:35]
	v_lshl_or_b32 v83, v89, 16, v88
	v_lshl_or_b32 v84, v91, 16, v90
	v_lshl_or_b32 v85, v93, 16, v92
	v_lshl_add_u64 v[86:87], v[86:87], 0, v[130:131]
	global_store_dwordx4 v[86:87], v[82:85], off offset:512 sc1
	s_waitcnt lgkmcnt(0)
	s_cbranch_vccnz .LBB0_1376
	global_load_dwordx4 v[82:85], v[170:171], off offset:16
	global_load_dwordx4 v[86:89], v[170:171], off
	s_waitcnt vmcnt(0)
	v_mov_b32_e32 v105, v84
	v_mov_b32_e32 v104, v82
	v_mov_b32_e32 v103, v88
	v_mov_b32_e32 v102, v86
	v_mov_b32_e32 v84, v83
	v_mov_b32_e32 v88, v87
	s_cbranch_execnz .LBB0_1378
	s_branch .LBB0_1377

;     __device__ __forceinline__ void operator()(const f32x4 (&acc)[2][2][4][2], const Unit& u, int wr, int wc, int fr, int fq) const {
;     ...
;             for (int m = 0; m < 4; ++m) {
;                 const int f = 16 * m + fr, r1 = head * 256 + wr * 64 + f;
; #pragma unroll
;                 for (int bj = 0; bj < 2; ++bj) {
;                     f32x4 o1[2], o2[2];
; #pragma unroll
;                     for (int n = 0; n < 2; ++n) {
;                         const f32x4 x1 = acc[0][bj][m][n], x2 = acc[1][bj][m][n];
;                         if (lat) {
;                             f32x4 cc, ss;
;                             if (wr == 0) { const int pos = ((u.pn * BM + bj * HALF + wc * 32) & (SEQ - 1)) >> 6; const f32x2 cs = rope[pos * 64 + f];
;                                 cc = (f32x4){cs.x, cs.x, cs.x, cs.x}; ss = (f32x4){cs.y, cs.y, cs.y, cs.y}; }
;                             else { const f32x4* tp = (const f32x4*)(rope2 + f * 128 + (wc & 1) * 32 + 8 * fq + 4 * n); const f32x4 a = tp[0], b = tp[1];
;                                 cc = (f32x4){a[0], a[2], b[0], b[2]}; ss = (f32x4){a[1], a[3], b[1], b[3]}; }
;                             o1[n] = (x1 * cc - x2 * ss) * 0.0625f; o2[n] = (x1 * ss + x2 * cc) * 0.0625f;
;                         } else { o1[n] = x1 * 0.0625f; o2[n] = x2 * 0.0625f; }
;                     }
;                     const int dk = wr * 64 + f; bf16_t* fp = KT + ((((size_t)head * 132 + 2 * u.pn + bj) * 8 + (dk >> 5)) * 8 + 2 * wc + (fq >> 1)) * 512 + (32 * (fq & 1) + (dk & 31)) * 8;
;                     if (u.kq != 1) *(u32x4*)(fp) = pack8(o1[0], o1[1]);
;                     if (u.kq != 0) *(u32x4*)(fp + (size_t)4 * 8 * 512) = pack8(o2[0], o2[1]);
;                     if (lat) {
;                         LAS bf16_t* tl = (LAS bf16_t*)(scr + (wr * 4 + wc) * 2048);
;                         *(LAS u32x4*)(tl + fr * 32 + 8 * fq) = pack8(o1[0], o1[1]);
;                         *(LAS u32x4*)(tl + 512 + fr * 32 + 8 * fq) = pack8(o2[0], o2[1]);
;                         asm volatile("s_waitcnt lgkmcnt(0)" ::: "memory");
;                         const int L = fr + 16 * fq, tt = L & 31, hf = L >> 5, T = u.pn * BM + bj * HALF + wc * 32 + tt, t = T & (SEQ - 1);
; #pragma unroll
;                         for (int part = 0; part < 2; ++part) { const LAS bf16_t* sp = tl + part * 512 + (hf * 8) * 32 + tt; u32x4 w8;
.LBB0_1382:
	v_pk_mul_f32 v[94:95], v[70:71], v[88:89]
	v_pk_mul_f32 v[70:71], v[70:71], v[102:103]
	v_pk_mul_f32 v[90:91], v[72:73], v[84:85]
	v_pk_fma_f32 v[94:95], v[78:79], v[102:103], v[94:95] neg_lo:[0,0,1] neg_hi:[0,0,1]
	v_pk_mul_f32 v[72:73], v[72:73], v[104:105]
	v_pk_fma_f32 v[70:71], v[78:79], v[88:89], v[70:71]
	v_pk_mul_f32 v[78:79], v[68:69], v[92:93]
	v_pk_mul_f32 v[68:69], v[68:69], v[86:87]
	v_pk_fma_f32 v[90:91], v[80:81], v[104:105], v[90:91] neg_lo:[0,0,1] neg_hi:[0,0,1]
	v_pk_fma_f32 v[72:73], v[80:81], v[84:85], v[72:73]
	v_pk_mul_f32 v[80:81], v[66:67], v[96:97]
	v_pk_mul_f32 v[66:67], v[66:67], v[82:83]
	v_pk_fma_f32 v[68:69], v[76:77], v[92:93], v[68:69]
	v_mov_b32_e32 v101, v159
	v_pk_mul_f32 v[72:73], v[72:73], s[6:7] op_sel_hi:[1,0]
	v_pk_mul_f32 v[70:71], v[70:71], s[6:7] op_sel_hi:[1,0]
	v_pk_fma_f32 v[80:81], v[74:75], v[82:83], v[80:81] neg_lo:[0,0,1] neg_hi:[0,0,1]
	v_pk_fma_f32 v[78:79], v[76:77], v[86:87], v[78:79] neg_lo:[0,0,1] neg_hi:[0,0,1]
	v_pk_fma_f32 v[66:67], v[74:75], v[96:97], v[66:67]
	v_pk_mul_f32 v[74:75], v[68:69], s[6:7] op_sel_hi:[1,0]
	v_lshl_add_u64 v[82:83], v[116:117], 0, v[100:101]
	v_pk_mul_f32 v[90:91], v[90:91], s[6:7] op_sel_hi:[1,0]
	v_pk_mul_f32 v[94:95], v[94:95], s[6:7] op_sel_hi:[1,0]
	v_pk_mul_f32 v[78:79], v[78:79], s[6:7] op_sel_hi:[1,0]
	v_pk_mul_f32 v[80:81], v[80:81], s[6:7] op_sel_hi:[1,0]
	v_pk_mul_f32 v[76:77], v[66:67], s[6:7] op_sel_hi:[1,0]
	v_cvt_pk_bf16_f32 v70, v70, v71
	v_cvt_pk_bf16_f32 v71, v72, v73
	v_cvt_pk_bf16_f32 v73, v74, v75
	v_add_co_u32_e32 v74, vcc, s69, v82
	v_cvt_pk_bf16_f32 v66, v94, v95
	v_cvt_pk_bf16_f32 v67, v90, v91
	v_cvt_pk_bf16_f32 v68, v80, v81
	v_cvt_pk_bf16_f32 v69, v78, v79
	v_cvt_pk_bf16_f32 v72, v76, v77
	v_addc_co_u32_e32 v75, vcc, 0, v83, vcc
	global_store_dwordx4 v[82:83], v[66:69], off sc1
	global_store_dwordx4 v[74:75], v[70:73], off sc1
	ds_write_b128 v189, v[66:69]
	ds_write_b128 v189, v[70:73] offset:1024
	s_waitcnt lgkmcnt(0)
	ds_read_u16 v66, v190
	ds_read_u16 v67, v190 offset:64
	ds_read_u16 v68, v190 offset:128
	ds_read_u16 v69, v190 offset:192
	ds_read_u16 v70, v190 offset:256
	ds_read_u16 v71, v190 offset:320
	ds_read_u16 v72, v190 offset:384
	ds_read_u16 v73, v190 offset:448
	s_waitcnt lgkmcnt(0)
	v_lshl_or_b32 v66, v67, 16, v66
	v_lshl_or_b32 v67, v69, 16, v68
	v_lshl_or_b32 v68, v71, 16, v70
	v_mov_b32_e32 v131, v159
	v_lshl_or_b32 v69, v73, 16, v72
	ds_read_u16 v70, v190 offset:1024
	ds_read_u16 v71, v190 offset:1088
	ds_read_u16 v72, v190 offset:1152
	ds_read_u16 v73, v190 offset:1216
	ds_read_u16 v74, v190 offset:1280
	ds_read_u16 v75, v190 offset:1344
	ds_read_u16 v76, v190 offset:1408
	ds_read_u16 v77, v190 offset:1472
	global_store_dwordx4 v[118:119], v[66:69], off offset:512 sc1
	s_and_b64 vcc, exec, s[0:1]
	s_mov_b64 s[2:3], -1
	s_waitcnt lgkmcnt(0)
	v_lshl_or_b32 v66, v71, 16, v70
	v_lshl_add_u64 v[70:71], v[114:115], 0, s[34:35]
	v_lshl_or_b32 v67, v73, 16, v72
	v_lshl_or_b32 v68, v75, 16, v74
	v_lshl_or_b32 v69, v77, 16, v76
	v_lshl_add_u64 v[70:71], v[70:71], 0, v[130:131]
	global_store_dwordx4 v[70:71], v[66:69], off offset:512 sc1
	s_waitcnt lgkmcnt(0)
	s_cbranch_vccnz .LBB0_1384
	global_load_dwordx4 v[66:69], v[172:173], off offset:16
	global_load_dwordx4 v[70:73], v[172:173], off
	s_mov_b64 s[2:3], 0
	s_waitcnt vmcnt(0)
	v_mov_b32_e32 v87, v68
	v_mov_b32_e32 v86, v66
	v_mov_b32_e32 v85, v72
	v_mov_b32_e32 v84, v70
	v_mov_b32_e32 v68, v67
	v_mov_b32_e32 v72, v71

;     __device__ __forceinline__ void operator()(const f32x4 (&acc)[2][2][4][2], const Unit& u, int wr, int wc, int fr, int fq) const {
;     ...
;             for (int m = 0; m < 4; ++m) {
;                 const int f = 16 * m + fr, r1 = head * 256 + wr * 64 + f;
; #pragma unroll
;                 for (int bj = 0; bj < 2; ++bj) {
;                     f32x4 o1[2], o2[2];
; #pragma unroll
;                     for (int n = 0; n < 2; ++n) {
;                         const f32x4 x1 = acc[0][bj][m][n], x2 = acc[1][bj][m][n];
;                         if (lat) {
;                             f32x4 cc, ss;
;                             if (wr == 0) { const int pos = ((u.pn * BM + bj * HALF + wc * 32) & (SEQ - 1)) >> 6; const f32x2 cs = rope[pos * 64 + f];
;                                 cc = (f32x4){cs.x, cs.x, cs.x, cs.x}; ss = (f32x4){cs.y, cs.y, cs.y, cs.y}; }
;                             else { const f32x4* tp = (const f32x4*)(rope2 + f * 128 + (wc & 1) * 32 + 8 * fq + 4 * n); const f32x4 a = tp[0], b = tp[1];
;                                 cc = (f32x4){a[0], a[2], b[0], b[2]}; ss = (f32x4){a[1], a[3], b[1], b[3]}; }
;                             o1[n] = (x1 * cc - x2 * ss) * 0.0625f; o2[n] = (x1 * ss + x2 * cc) * 0.0625f;
;                         } else { o1[n] = x1 * 0.0625f; o2[n] = x2 * 0.0625f; }
;                     }
;                     const int dk = wr * 64 + f; bf16_t* fp = KT + ((((size_t)head * 132 + 2 * u.pn + bj) * 8 + (dk >> 5)) * 8 + 2 * wc + (fq >> 1)) * 512 + (32 * (fq & 1) + (dk & 31)) * 8;
;                     if (u.kq != 1) *(u32x4*)(fp) = pack8(o1[0], o1[1]);
;                     if (u.kq != 0) *(u32x4*)(fp + (size_t)4 * 8 * 512) = pack8(o2[0], o2[1]);
;                     if (lat) {
;                         LAS bf16_t* tl = (LAS bf16_t*)(scr + (wr * 4 + wc) * 2048);
;                         *(LAS u32x4*)(tl + fr * 32 + 8 * fq) = pack8(o1[0], o1[1]);
;                         *(LAS u32x4*)(tl + 512 + fr * 32 + 8 * fq) = pack8(o2[0], o2[1]);
;                         asm volatile("s_waitcnt lgkmcnt(0)" ::: "memory");
;                         const int L = fr + 16 * fq, tt = L & 31, hf = L >> 5, T = u.pn * BM + bj * HALF + wc * 32 + tt, t = T & (SEQ - 1);
; #pragma unroll
;                         for (int part = 0; part < 2; ++part) { const LAS bf16_t* sp = tl + part * 512 + (hf * 8) * 32 + tt; u32x4 w8;
.LBB0_1390:
	v_pk_mul_f32 v[74:75], v[56:57], v[68:69]
	v_pk_mul_f32 v[56:57], v[56:57], v[86:87]
	v_pk_mul_f32 v[78:79], v[54:55], v[72:73]
	v_pk_fma_f32 v[74:75], v[64:65], v[86:87], v[74:75] neg_lo:[0,0,1] neg_hi:[0,0,1]
	v_pk_mul_f32 v[54:55], v[54:55], v[84:85]
	v_pk_fma_f32 v[56:57], v[64:65], v[68:69], v[56:57]
	v_pk_mul_f32 v[64:65], v[50:51], v[80:81]
	v_pk_mul_f32 v[50:51], v[50:51], v[66:67]
	s_add_u32 s2, s45, s36
	v_pk_fma_f32 v[78:79], v[62:63], v[84:85], v[78:79] neg_lo:[0,0,1] neg_hi:[0,0,1]
	v_pk_fma_f32 v[54:55], v[62:63], v[72:73], v[54:55]
	v_pk_mul_f32 v[62:63], v[52:53], v[76:77]
	v_pk_mul_f32 v[52:53], v[52:53], v[70:71]
	v_pk_fma_f32 v[50:51], v[58:59], v[80:81], v[50:51]
	s_addc_u32 s3, s47, s37
	v_pk_fma_f32 v[62:63], v[60:61], v[70:71], v[62:63] neg_lo:[0,0,1] neg_hi:[0,0,1]
	v_pk_fma_f32 v[52:53], v[60:61], v[76:77], v[52:53]
	v_pk_mul_f32 v[60:61], v[50:51], s[6:7] op_sel_hi:[1,0]
	v_lshl_add_u64 v[50:51], s[2:3], 0, v[164:165]
	v_pk_fma_f32 v[64:65], v[58:59], v[66:67], v[64:65] neg_lo:[0,0,1] neg_hi:[0,0,1]
	v_lshl_add_u64 v[66:67], v[50:51], 0, v[158:159]
	v_pk_mul_f32 v[74:75], v[74:75], s[6:7] op_sel_hi:[1,0]
	v_pk_mul_f32 v[78:79], v[78:79], s[6:7] op_sel_hi:[1,0]
	v_pk_mul_f32 v[56:57], v[56:57], s[6:7] op_sel_hi:[1,0]
	v_pk_mul_f32 v[54:55], v[54:55], s[6:7] op_sel_hi:[1,0]
	v_pk_mul_f32 v[62:63], v[62:63], s[6:7] op_sel_hi:[1,0]
	v_pk_mul_f32 v[64:65], v[64:65], s[6:7] op_sel_hi:[1,0]
	v_pk_mul_f32 v[58:59], v[52:53], s[6:7] op_sel_hi:[1,0]
	v_add_co_u32_e32 v70, vcc, s69, v66
	v_cvt_pk_bf16_f32 v50, v78, v79
	v_cvt_pk_bf16_f32 v51, v74, v75
	v_cvt_pk_bf16_f32 v52, v64, v65
	v_cvt_pk_bf16_f32 v53, v62, v63
	v_cvt_pk_bf16_f32 v54, v54, v55
	v_cvt_pk_bf16_f32 v55, v56, v57
	v_cvt_pk_bf16_f32 v56, v60, v61
	v_cvt_pk_bf16_f32 v57, v58, v59
	v_addc_co_u32_e32 v71, vcc, 0, v67, vcc
	global_store_dwordx4 v[66:67], v[50:53], off sc1
	global_store_dwordx4 v[70:71], v[54:57], off sc1
	ds_write_b128 v189, v[50:53]
	ds_write_b128 v189, v[54:57] offset:1024
	s_waitcnt lgkmcnt(0)
	ds_read_u16 v50, v190
	ds_read_u16 v51, v190 offset:64
	ds_read_u16 v52, v190 offset:128
	ds_read_u16 v53, v190 offset:192
	ds_read_u16 v54, v190 offset:256
	ds_read_u16 v55, v190 offset:320
	ds_read_u16 v56, v190 offset:384
	ds_read_u16 v57, v190 offset:448
	s_waitcnt lgkmcnt(0)
	v_lshl_or_b32 v50, v51, 16, v50
	v_lshl_or_b32 v51, v53, 16, v52
	v_lshl_or_b32 v52, v55, 16, v54
	v_lshl_add_u64 v[54:55], v[132:133], 0, s[38:39]
	v_mov_b32_e32 v131, v159
	v_lshl_or_b32 v53, v57, 16, v56
	v_lshl_add_u64 v[68:69], v[54:55], 0, v[130:131]
	ds_read_u16 v54, v190 offset:1024
	ds_read_u16 v55, v190 offset:1088
	ds_read_u16 v56, v190 offset:1152
	ds_read_u16 v57, v190 offset:1216
	ds_read_u16 v58, v190 offset:1280
	ds_read_u16 v59, v190 offset:1344
	ds_read_u16 v60, v190 offset:1408
	ds_read_u16 v61, v190 offset:1472
	global_store_dwordx4 v[68:69], v[50:53], off sc1
	s_and_b64 vcc, exec, s[0:1]
	s_mov_b64 s[2:3], -1
	s_waitcnt lgkmcnt(0)
	v_lshl_or_b32 v50, v55, 16, v54
	v_lshl_add_u64 v[54:55], v[132:133], 0, s[40:41]
	v_lshl_or_b32 v51, v57, 16, v56
	v_lshl_or_b32 v52, v59, 16, v58
	v_lshl_or_b32 v53, v61, 16, v60
	v_lshl_add_u64 v[54:55], v[54:55], 0, v[130:131]
	global_store_dwordx4 v[54:55], v[50:53], off sc1
	s_waitcnt lgkmcnt(0)
	s_cbranch_vccnz .LBB0_1392
	global_load_dwordx4 v[50:53], v[172:173], off offset:16
	global_load_dwordx4 v[54:57], v[172:173], off
	s_waitcnt vmcnt(0)
	v_mov_b32_e32 v75, v52
	v_mov_b32_e32 v74, v50
	v_mov_b32_e32 v73, v56
	v_mov_b32_e32 v72, v54
	v_mov_b32_e32 v52, v51
	v_mov_b32_e32 v56, v55
	s_cbranch_execnz .LBB0_1394
	s_branch .LBB0_1393

;     __device__ __forceinline__ void operator()(const f32x4 (&acc)[2][2][4][2], const Unit& u, int wr, int wc, int fr, int fq) const {
;     ...
;             for (int m = 0; m < 4; ++m) {
;                 const int f = 16 * m + fr, r1 = head * 256 + wr * 64 + f;
; #pragma unroll
;                 for (int bj = 0; bj < 2; ++bj) {
;                     f32x4 o1[2], o2[2];
; #pragma unroll
;                     for (int n = 0; n < 2; ++n) {
;                         const f32x4 x1 = acc[0][bj][m][n], x2 = acc[1][bj][m][n];
;                         if (lat) {
;                             f32x4 cc, ss;
;                             if (wr == 0) { const int pos = ((u.pn * BM + bj * HALF + wc * 32) & (SEQ - 1)) >> 6; const f32x2 cs = rope[pos * 64 + f];
;                                 cc = (f32x4){cs.x, cs.x, cs.x, cs.x}; ss = (f32x4){cs.y, cs.y, cs.y, cs.y}; }
;                             else { const f32x4* tp = (const f32x4*)(rope2 + f * 128 + (wc & 1) * 32 + 8 * fq + 4 * n); const f32x4 a = tp[0], b = tp[1];
;                                 cc = (f32x4){a[0], a[2], b[0], b[2]}; ss = (f32x4){a[1], a[3], b[1], b[3]}; }
;                             o1[n] = (x1 * cc - x2 * ss) * 0.0625f; o2[n] = (x1 * ss + x2 * cc) * 0.0625f;
;                         } else { o1[n] = x1 * 0.0625f; o2[n] = x2 * 0.0625f; }
;                     }
;                     const int dk = wr * 64 + f; bf16_t* fp = KT + ((((size_t)head * 132 + 2 * u.pn + bj) * 8 + (dk >> 5)) * 8 + 2 * wc + (fq >> 1)) * 512 + (32 * (fq & 1) + (dk & 31)) * 8;
;                     if (u.kq != 1) *(u32x4*)(fp) = pack8(o1[0], o1[1]);
;                     if (u.kq != 0) *(u32x4*)(fp + (size_t)4 * 8 * 512) = pack8(o2[0], o2[1]);
;                     if (lat) {
;                         LAS bf16_t* tl = (LAS bf16_t*)(scr + (wr * 4 + wc) * 2048);
;                         *(LAS u32x4*)(tl + fr * 32 + 8 * fq) = pack8(o1[0], o1[1]);
;                         *(LAS u32x4*)(tl + 512 + fr * 32 + 8 * fq) = pack8(o2[0], o2[1]);
;                         asm volatile("s_waitcnt lgkmcnt(0)" ::: "memory");
;                         const int L = fr + 16 * fq, tt = L & 31, hf = L >> 5, T = u.pn * BM + bj * HALF + wc * 32 + tt, t = T & (SEQ - 1);
; #pragma unroll
;                         for (int part = 0; part < 2; ++part) { const LAS bf16_t* sp = tl + part * 512 + (hf * 8) * 32 + tt; u32x4 w8;
.LBB0_1398:
	v_pk_mul_f32 v[58:59], v[40:41], v[52:53]
	v_pk_mul_f32 v[40:41], v[40:41], v[74:75]
	v_pk_mul_f32 v[62:63], v[38:39], v[56:57]
	v_pk_fma_f32 v[58:59], v[48:49], v[74:75], v[58:59] neg_lo:[0,0,1] neg_hi:[0,0,1]
	v_pk_mul_f32 v[38:39], v[38:39], v[72:73]
	v_pk_fma_f32 v[40:41], v[48:49], v[52:53], v[40:41]
	v_pk_mul_f32 v[48:49], v[34:35], v[64:65]
	v_pk_mul_f32 v[34:35], v[34:35], v[50:51]
	s_add_u32 s2, s54, s36
	v_pk_fma_f32 v[62:63], v[46:47], v[72:73], v[62:63] neg_lo:[0,0,1] neg_hi:[0,0,1]
	v_pk_fma_f32 v[38:39], v[46:47], v[56:57], v[38:39]
	v_pk_mul_f32 v[46:47], v[36:37], v[60:61]
	v_pk_mul_f32 v[36:37], v[36:37], v[54:55]
	v_pk_fma_f32 v[34:35], v[42:43], v[64:65], v[34:35]
	s_addc_u32 s3, s56, s37
	v_pk_fma_f32 v[46:47], v[44:45], v[54:55], v[46:47] neg_lo:[0,0,1] neg_hi:[0,0,1]
	v_pk_fma_f32 v[36:37], v[44:45], v[60:61], v[36:37]
	v_pk_mul_f32 v[44:45], v[34:35], s[6:7] op_sel_hi:[1,0]
	v_lshl_add_u64 v[34:35], s[2:3], 0, v[164:165]
	v_pk_fma_f32 v[48:49], v[42:43], v[50:51], v[48:49] neg_lo:[0,0,1] neg_hi:[0,0,1]
	v_lshl_add_u64 v[50:51], v[34:35], 0, v[158:159]
	v_pk_mul_f32 v[58:59], v[58:59], s[6:7] op_sel_hi:[1,0]
	v_pk_mul_f32 v[62:63], v[62:63], s[6:7] op_sel_hi:[1,0]
	v_pk_mul_f32 v[40:41], v[40:41], s[6:7] op_sel_hi:[1,0]
	v_pk_mul_f32 v[38:39], v[38:39], s[6:7] op_sel_hi:[1,0]
	v_pk_mul_f32 v[46:47], v[46:47], s[6:7] op_sel_hi:[1,0]
	v_pk_mul_f32 v[48:49], v[48:49], s[6:7] op_sel_hi:[1,0]
	v_pk_mul_f32 v[42:43], v[36:37], s[6:7] op_sel_hi:[1,0]
	v_add_co_u32_e32 v54, vcc, s69, v50
	v_cvt_pk_bf16_f32 v34, v62, v63
	v_cvt_pk_bf16_f32 v35, v58, v59
	v_cvt_pk_bf16_f32 v36, v48, v49
	v_cvt_pk_bf16_f32 v37, v46, v47
	v_cvt_pk_bf16_f32 v38, v38, v39
	v_cvt_pk_bf16_f32 v39, v40, v41
	v_cvt_pk_bf16_f32 v40, v44, v45
	v_cvt_pk_bf16_f32 v41, v42, v43
	v_addc_co_u32_e32 v55, vcc, 0, v51, vcc
	global_store_dwordx4 v[50:51], v[34:37], off sc1
	global_store_dwordx4 v[54:55], v[38:41], off sc1
	ds_write_b128 v189, v[34:37]
	ds_write_b128 v189, v[38:41] offset:1024
	s_waitcnt lgkmcnt(0)
	ds_read_u16 v34, v190
	ds_read_u16 v35, v190 offset:64
	ds_read_u16 v36, v190 offset:128
	ds_read_u16 v37, v190 offset:192
	ds_read_u16 v38, v190 offset:256
	ds_read_u16 v39, v190 offset:320
	ds_read_u16 v40, v190 offset:384
	ds_read_u16 v41, v190 offset:448
	s_waitcnt lgkmcnt(0)
	v_lshl_or_b32 v34, v35, 16, v34
	v_lshl_or_b32 v35, v37, 16, v36
	v_lshl_or_b32 v36, v39, 16, v38
	v_lshl_add_u64 v[38:39], v[114:115], 0, s[38:39]
	v_mov_b32_e32 v131, v159
	v_lshl_or_b32 v37, v41, 16, v40
	v_lshl_add_u64 v[52:53], v[38:39], 0, v[130:131]
	ds_read_u16 v38, v190 offset:1024
	ds_read_u16 v39, v190 offset:1088
	ds_read_u16 v40, v190 offset:1152
	ds_read_u16 v41, v190 offset:1216
	ds_read_u16 v42, v190 offset:1280
	ds_read_u16 v43, v190 offset:1344
	ds_read_u16 v44, v190 offset:1408
	ds_read_u16 v45, v190 offset:1472
	global_store_dwordx4 v[52:53], v[34:37], off sc1
	s_and_b64 vcc, exec, s[0:1]
	s_mov_b64 s[2:3], -1
	s_waitcnt lgkmcnt(0)
	v_lshl_or_b32 v34, v39, 16, v38
	v_lshl_add_u64 v[38:39], v[114:115], 0, s[40:41]
	v_lshl_or_b32 v35, v41, 16, v40
	v_lshl_or_b32 v36, v43, 16, v42
	v_lshl_or_b32 v37, v45, 16, v44
	v_lshl_add_u64 v[38:39], v[38:39], 0, v[130:131]
	global_store_dwordx4 v[38:39], v[34:37], off sc1
	s_waitcnt lgkmcnt(0)
	s_cbranch_vccnz .LBB0_1400
	global_load_dwordx4 v[34:37], v[174:175], off offset:16
	global_load_dwordx4 v[38:41], v[174:175], off
	s_mov_b64 s[2:3], 0
	s_waitcnt vmcnt(0)
	v_mov_b32_e32 v59, v36
	v_mov_b32_e32 v58, v34
	v_mov_b32_e32 v57, v40
	v_mov_b32_e32 v56, v38
	v_mov_b32_e32 v36, v35
	v_mov_b32_e32 v40, v39

;     __device__ __forceinline__ void operator()(const f32x4 (&acc)[2][2][4][2], const Unit& u, int wr, int wc, int fr, int fq) const {
;     ...
;             for (int m = 0; m < 4; ++m) {
;                 const int f = 16 * m + fr, r1 = head * 256 + wr * 64 + f;
; #pragma unroll
;                 for (int bj = 0; bj < 2; ++bj) {
;                     f32x4 o1[2], o2[2];
; #pragma unroll
;                     for (int n = 0; n < 2; ++n) {
;                         const f32x4 x1 = acc[0][bj][m][n], x2 = acc[1][bj][m][n];
;                         if (lat) {
;                             f32x4 cc, ss;
;                             if (wr == 0) { const int pos = ((u.pn * BM + bj * HALF + wc * 32) & (SEQ - 1)) >> 6; const f32x2 cs = rope[pos * 64 + f];
;                                 cc = (f32x4){cs.x, cs.x, cs.x, cs.x}; ss = (f32x4){cs.y, cs.y, cs.y, cs.y}; }
;                             else { const f32x4* tp = (const f32x4*)(rope2 + f * 128 + (wc & 1) * 32 + 8 * fq + 4 * n); const f32x4 a = tp[0], b = tp[1];
;                                 cc = (f32x4){a[0], a[2], b[0], b[2]}; ss = (f32x4){a[1], a[3], b[1], b[3]}; }
;                             o1[n] = (x1 * cc - x2 * ss) * 0.0625f; o2[n] = (x1 * ss + x2 * cc) * 0.0625f;
;                         } else { o1[n] = x1 * 0.0625f; o2[n] = x2 * 0.0625f; }
;                     }
;                     const int dk = wr * 64 + f; bf16_t* fp = KT + ((((size_t)head * 132 + 2 * u.pn + bj) * 8 + (dk >> 5)) * 8 + 2 * wc + (fq >> 1)) * 512 + (32 * (fq & 1) + (dk & 31)) * 8;
;                     if (u.kq != 1) *(u32x4*)(fp) = pack8(o1[0], o1[1]);
;                     if (u.kq != 0) *(u32x4*)(fp + (size_t)4 * 8 * 512) = pack8(o2[0], o2[1]);
;                     if (lat) {
;                         LAS bf16_t* tl = (LAS bf16_t*)(scr + (wr * 4 + wc) * 2048);
;                         *(LAS u32x4*)(tl + fr * 32 + 8 * fq) = pack8(o1[0], o1[1]);
;                         *(LAS u32x4*)(tl + 512 + fr * 32 + 8 * fq) = pack8(o2[0], o2[1]);
;                         asm volatile("s_waitcnt lgkmcnt(0)" ::: "memory");
;                         const int L = fr + 16 * fq, tt = L & 31, hf = L >> 5, T = u.pn * BM + bj * HALF + wc * 32 + tt, t = T & (SEQ - 1);
; #pragma unroll
;                         for (int part = 0; part < 2; ++part) { const LAS bf16_t* sp = tl + part * 512 + (hf * 8) * 32 + tt; u32x4 w8;
.LBB0_1406:
	v_pk_mul_f32 v[42:43], v[24:25], v[36:37]
	v_pk_mul_f32 v[46:47], v[22:23], v[40:41]
	v_pk_mul_f32 v[24:25], v[24:25], v[58:59]
	v_pk_mul_f32 v[22:23], v[22:23], v[56:57]
	v_pk_fma_f32 v[46:47], v[30:31], v[56:57], v[46:47] neg_lo:[0,0,1] neg_hi:[0,0,1]
	v_pk_fma_f32 v[42:43], v[32:33], v[58:59], v[42:43] neg_lo:[0,0,1] neg_hi:[0,0,1]
	v_pk_fma_f32 v[22:23], v[30:31], v[40:41], v[22:23]
	v_pk_fma_f32 v[24:25], v[32:33], v[36:37], v[24:25]
	v_pk_mul_f32 v[30:31], v[20:21], v[44:45]
	v_pk_mul_f32 v[32:33], v[18:19], v[48:49]
	v_pk_mul_f32 v[20:21], v[20:21], v[60:61]
	v_pk_mul_f32 v[18:19], v[18:19], v[38:39]
	v_pk_fma_f32 v[32:33], v[26:27], v[38:39], v[32:33] neg_lo:[0,0,1] neg_hi:[0,0,1]
	v_pk_fma_f32 v[30:31], v[28:29], v[60:61], v[30:31] neg_lo:[0,0,1] neg_hi:[0,0,1]
	v_pk_fma_f32 v[18:19], v[26:27], v[48:49], v[18:19]
	v_pk_fma_f32 v[20:21], v[28:29], v[44:45], v[20:21]
	v_pk_mul_f32 v[42:43], v[42:43], s[6:7] op_sel_hi:[1,0]
	v_pk_mul_f32 v[46:47], v[46:47], s[6:7] op_sel_hi:[1,0]
	v_pk_mul_f32 v[24:25], v[24:25], s[6:7] op_sel_hi:[1,0]
	v_pk_mul_f32 v[22:23], v[22:23], s[6:7] op_sel_hi:[1,0]
	v_pk_mul_f32 v[30:31], v[30:31], s[6:7] op_sel_hi:[1,0]
	v_pk_mul_f32 v[32:33], v[32:33], s[6:7] op_sel_hi:[1,0]
	v_pk_mul_f32 v[26:27], v[20:21], s[6:7] op_sel_hi:[1,0]
	v_pk_mul_f32 v[28:29], v[18:19], s[6:7] op_sel_hi:[1,0]
	v_cvt_pk_bf16_f32 v18, v46, v47
	v_cvt_pk_bf16_f32 v19, v42, v43
	v_cvt_pk_bf16_f32 v20, v32, v33
	v_cvt_pk_bf16_f32 v21, v30, v31
	v_cvt_pk_bf16_f32 v22, v22, v23
	v_cvt_pk_bf16_f32 v23, v24, v25
	v_cvt_pk_bf16_f32 v24, v28, v29
	v_cvt_pk_bf16_f32 v25, v26, v27
	global_store_dwordx4 v[66:67], v[18:21], off offset:256 sc1
	global_store_dwordx4 v[70:71], v[22:25], off offset:256 sc1
	ds_write_b128 v189, v[18:21]
	ds_write_b128 v189, v[22:25] offset:1024
	s_waitcnt lgkmcnt(0)
	ds_read_u16 v18, v190
	ds_read_u16 v19, v190 offset:64
	ds_read_u16 v20, v190 offset:128
	ds_read_u16 v21, v190 offset:192
	ds_read_u16 v22, v190 offset:256
	ds_read_u16 v23, v190 offset:320
	ds_read_u16 v24, v190 offset:384
	ds_read_u16 v25, v190 offset:448
	s_waitcnt lgkmcnt(0)
	v_lshl_or_b32 v18, v19, 16, v18
	v_lshl_or_b32 v19, v21, 16, v20
	v_lshl_or_b32 v20, v23, 16, v22
	v_mov_b32_e32 v131, v159
	v_lshl_or_b32 v21, v25, 16, v24
	ds_read_u16 v22, v190 offset:1024
	ds_read_u16 v23, v190 offset:1088
	ds_read_u16 v24, v190 offset:1152
	ds_read_u16 v25, v190 offset:1216
	ds_read_u16 v26, v190 offset:1280
	ds_read_u16 v27, v190 offset:1344
	ds_read_u16 v28, v190 offset:1408
	ds_read_u16 v29, v190 offset:1472
	global_store_dwordx4 v[68:69], v[18:21], off offset:512 sc1
	s_and_b64 vcc, exec, s[0:1]
	s_mov_b64 s[2:3], -1
	s_waitcnt lgkmcnt(0)
	v_lshl_or_b32 v18, v23, 16, v22
	v_lshl_add_u64 v[22:23], v[132:133], 0, s[42:43]
	v_lshl_or_b32 v19, v25, 16, v24
	v_lshl_or_b32 v20, v27, 16, v26
	v_lshl_or_b32 v21, v29, 16, v28
	v_lshl_add_u64 v[22:23], v[22:23], 0, v[130:131]
	global_store_dwordx4 v[22:23], v[18:21], off offset:512 sc1
	s_waitcnt lgkmcnt(0)
	s_cbranch_vccnz .LBB0_1408
	global_load_dwordx4 v[18:21], v[174:175], off offset:16
	global_load_dwordx4 v[22:25], v[174:175], off
	s_waitcnt vmcnt(0)
	v_mov_b32_e32 v39, v20
	v_mov_b32_e32 v38, v18
	v_mov_b32_e32 v37, v24
	v_mov_b32_e32 v36, v22
	v_mov_b32_e32 v20, v19
	v_mov_b32_e32 v24, v23
	s_cbranch_execnz .LBB0_1410
	s_branch .LBB0_1409

;     __device__ __forceinline__ void operator()(const f32x4 (&acc)[2][2][4][2], const Unit& u, int wr, int wc, int fr, int fq) const {
;     ...
;             for (int m = 0; m < 4; ++m) {
;                 const int f = 16 * m + fr, r1 = head * 256 + wr * 64 + f;
; #pragma unroll
;                 for (int bj = 0; bj < 2; ++bj) {
;                     f32x4 o1[2], o2[2];
; #pragma unroll
;                     for (int n = 0; n < 2; ++n) {
;                         const f32x4 x1 = acc[0][bj][m][n], x2 = acc[1][bj][m][n];
;                         if (lat) {
;                             f32x4 cc, ss;
;                             if (wr == 0) { const int pos = ((u.pn * BM + bj * HALF + wc * 32) & (SEQ - 1)) >> 6; const f32x2 cs = rope[pos * 64 + f];
;                                 cc = (f32x4){cs.x, cs.x, cs.x, cs.x}; ss = (f32x4){cs.y, cs.y, cs.y, cs.y}; }
;                             else { const f32x4* tp = (const f32x4*)(rope2 + f * 128 + (wc & 1) * 32 + 8 * fq + 4 * n); const f32x4 a = tp[0], b = tp[1];
;                                 cc = (f32x4){a[0], a[2], b[0], b[2]}; ss = (f32x4){a[1], a[3], b[1], b[3]}; }
;                             o1[n] = (x1 * cc - x2 * ss) * 0.0625f; o2[n] = (x1 * ss + x2 * cc) * 0.0625f;
;                         } else { o1[n] = x1 * 0.0625f; o2[n] = x2 * 0.0625f; }
;                     }
;                     const int dk = wr * 64 + f; bf16_t* fp = KT + ((((size_t)head * 132 + 2 * u.pn + bj) * 8 + (dk >> 5)) * 8 + 2 * wc + (fq >> 1)) * 512 + (32 * (fq & 1) + (dk & 31)) * 8;
;                     if (u.kq != 1) *(u32x4*)(fp) = pack8(o1[0], o1[1]);
;                     if (u.kq != 0) *(u32x4*)(fp + (size_t)4 * 8 * 512) = pack8(o2[0], o2[1]);
;                     if (lat) {
;                         LAS bf16_t* tl = (LAS bf16_t*)(scr + (wr * 4 + wc) * 2048);
;                         *(LAS u32x4*)(tl + fr * 32 + 8 * fq) = pack8(o1[0], o1[1]);
;                         *(LAS u32x4*)(tl + 512 + fr * 32 + 8 * fq) = pack8(o2[0], o2[1]);
;                         asm volatile("s_waitcnt lgkmcnt(0)" ::: "memory");
;                         const int L = fr + 16 * fq, tt = L & 31, hf = L >> 5, T = u.pn * BM + bj * HALF + wc * 32 + tt, t = T & (SEQ - 1);
; #pragma unroll
;                         for (int part = 0; part < 2; ++part) { const LAS bf16_t* sp = tl + part * 512 + (hf * 8) * 32 + tt; u32x4 w8;
.LBB0_1414:
	v_pk_mul_f32 v[26:27], v[8:9], v[20:21]
	v_pk_mul_f32 v[30:31], v[6:7], v[24:25]
	v_pk_mul_f32 v[8:9], v[8:9], v[38:39]
	v_pk_mul_f32 v[6:7], v[6:7], v[36:37]
	v_pk_fma_f32 v[30:31], v[14:15], v[36:37], v[30:31] neg_lo:[0,0,1] neg_hi:[0,0,1]
	v_pk_fma_f32 v[26:27], v[16:17], v[38:39], v[26:27] neg_lo:[0,0,1] neg_hi:[0,0,1]
	v_pk_fma_f32 v[6:7], v[14:15], v[24:25], v[6:7]
	v_pk_fma_f32 v[8:9], v[16:17], v[20:21], v[8:9]
	v_pk_mul_f32 v[14:15], v[4:5], v[22:23]
	v_pk_mul_f32 v[16:17], v[2:3], v[18:19]
	v_pk_mul_f32 v[4:5], v[4:5], v[32:33]
	v_pk_mul_f32 v[2:3], v[2:3], v[28:29]
	v_pk_fma_f32 v[16:17], v[10:11], v[28:29], v[16:17]
	v_pk_fma_f32 v[14:15], v[12:13], v[32:33], v[14:15]
	v_pk_fma_f32 v[2:3], v[10:11], v[18:19], v[2:3] neg_lo:[0,0,1] neg_hi:[0,0,1]
	v_pk_fma_f32 v[4:5], v[12:13], v[22:23], v[4:5] neg_lo:[0,0,1] neg_hi:[0,0,1]
	v_pk_mul_f32 v[26:27], v[26:27], s[6:7] op_sel_hi:[1,0]
	v_pk_mul_f32 v[30:31], v[30:31], s[6:7] op_sel_hi:[1,0]
	v_pk_mul_f32 v[8:9], v[8:9], s[6:7] op_sel_hi:[1,0]
	v_pk_mul_f32 v[6:7], v[6:7], s[6:7] op_sel_hi:[1,0]
	v_pk_mul_f32 v[10:11], v[4:5], s[6:7] op_sel_hi:[1,0]
	v_pk_mul_f32 v[4:5], v[2:3], s[6:7] op_sel_hi:[1,0]
	v_pk_mul_f32 v[12:13], v[14:15], s[6:7] op_sel_hi:[1,0]
	v_pk_mul_f32 v[14:15], v[16:17], s[6:7] op_sel_hi:[1,0]
	v_cvt_pk_bf16_f32 v2, v30, v31
	v_cvt_pk_bf16_f32 v3, v26, v27
	v_cvt_pk_bf16_f32 v4, v4, v5
	v_cvt_pk_bf16_f32 v5, v10, v11
	v_cvt_pk_bf16_f32 v6, v6, v7
	v_cvt_pk_bf16_f32 v7, v8, v9
	v_cvt_pk_bf16_f32 v8, v14, v15
	v_cvt_pk_bf16_f32 v9, v12, v13
	global_store_dwordx4 v[50:51], v[2:5], off offset:256 sc1
	global_store_dwordx4 v[54:55], v[6:9], off offset:256 sc1
	ds_write_b128 v189, v[2:5]
	ds_write_b128 v189, v[6:9] offset:1024
	s_waitcnt lgkmcnt(0)
	ds_read_u16 v2, v190
	ds_read_u16 v3, v190 offset:64
	ds_read_u16 v4, v190 offset:128
	ds_read_u16 v5, v190 offset:192
	ds_read_u16 v6, v190 offset:256
	ds_read_u16 v7, v190 offset:320
	ds_read_u16 v8, v190 offset:384
	ds_read_u16 v9, v190 offset:448
	s_waitcnt lgkmcnt(0)
	v_lshl_or_b32 v2, v3, 16, v2
	v_lshl_or_b32 v3, v5, 16, v4
	v_lshl_or_b32 v4, v7, 16, v6
	v_mov_b32_e32 v131, v159
	v_lshl_or_b32 v5, v9, 16, v8
	ds_read_u16 v6, v190 offset:1024
	ds_read_u16 v7, v190 offset:1088
	ds_read_u16 v8, v190 offset:1152
	ds_read_u16 v9, v190 offset:1216
	ds_read_u16 v10, v190 offset:1280
	ds_read_u16 v11, v190 offset:1344
	ds_read_u16 v12, v190 offset:1408
	ds_read_u16 v13, v190 offset:1472
	global_store_dwordx4 v[52:53], v[2:5], off offset:512 sc1
	s_waitcnt lgkmcnt(0)
	s_nop 0
	v_lshl_or_b32 v2, v7, 16, v6
	v_lshl_add_u64 v[6:7], v[114:115], 0, s[42:43]
	v_lshl_or_b32 v3, v9, 16, v8
	v_lshl_or_b32 v4, v11, 16, v10
	v_lshl_or_b32 v5, v13, 16, v12
	v_lshl_add_u64 v[6:7], v[6:7], 0, v[130:131]
	global_store_dwordx4 v[6:7], v[2:5], off offset:512 sc1
	s_waitcnt lgkmcnt(0)
	s_andn2_b64 vcc, exec, s[50:51]
	s_mov_b64 s[0:1], -1
	s_cbranch_vccnz .LBB0_1339

; __device__ __forceinline__ u32x4 pack8(const f32x4 a, const f32x4 b) { u32x4 w; w.x = cvt_pk_bf16(a[0], a[1]); w.y = cvt_pk_bf16(a[2], a[3]); w.z = cvt_pk_bf16(b[0], b[1]); w.w = cvt_pk_bf16(b[2], b[3]); return w; }
;     __device__ __forceinline__ void operator()(const f32x4 (&acc)[2][2][4][2], const Unit& u, int wr, int wc, int fr, int fq) const {
;     ...
;         } else {
;             const int rb = (u.pm - 8) * BM + wr * 64 + fr;
; #pragma unroll
;             for (int ai = 0; ai < 2; ++ai) { if (u.kq >= 0 && u.kq != ai) continue;
; #pragma unroll
;                 for (int m = 0; m < 4; ++m)
; #pragma unroll
;                     for (int bj = 0; bj < 2; ++bj) *(u32x4*)(VT + (size_t)(rb + ai * HALF + m * 16) * MT + col0 + bj * HALF) = pack8(acc[ai][bj][m][0], acc[ai][bj][m][1]); }
.LBB0_1503:
	v_readlane_b32 s0, v250, 36
	v_lshl_or_b32 v134, s2, 8, v187
	v_readlane_b32 s1, v250, 37
	v_lshl_add_u32 v150, s8, 8, v155
	v_ashrrev_i32_e32 v135, 31, v134
	v_mov_b64_e32 v[136:137], s[0:1]
	v_mad_i64_i32 v[172:173], s[0:1], v150, s36, v[136:137]
	v_lshlrev_b64 v[134:135], 1, v[134:135]
	v_cvt_pk_bf16_f32 v130, v126, v127
	v_cvt_pk_bf16_f32 v131, v128, v129
	v_cvt_pk_bf16_f32 v132, v122, v123
	v_cvt_pk_bf16_f32 v133, v124, v125
	v_lshl_add_u64 v[172:173], v[172:173], 0, v[134:135]
	global_store_dwordx4 v[172:173], v[130:133], off sc1
	s_nop 1
	v_cvt_pk_bf16_f32 v130, v110, v111
	v_cvt_pk_bf16_f32 v131, v112, v113
	v_cvt_pk_bf16_f32 v132, v106, v107
	v_cvt_pk_bf16_f32 v133, v108, v109
	global_store_dwordx4 v[172:173], v[130:133], off offset:256 sc1
	v_or_b32_e32 v172, 16, v150
	v_mad_i64_i32 v[172:173], s[0:1], v172, s36, v[136:137]
	v_cvt_pk_bf16_f32 v130, v94, v95
	v_cvt_pk_bf16_f32 v131, v96, v97
	v_cvt_pk_bf16_f32 v132, v90, v91
	v_cvt_pk_bf16_f32 v133, v92, v93
	v_lshl_add_u64 v[172:173], v[172:173], 0, v[134:135]
	global_store_dwordx4 v[172:173], v[130:133], off sc1
	s_nop 1
	v_cvt_pk_bf16_f32 v130, v78, v79
	v_cvt_pk_bf16_f32 v131, v80, v81
	v_cvt_pk_bf16_f32 v132, v74, v75
	v_cvt_pk_bf16_f32 v133, v76, v77
	global_store_dwordx4 v[172:173], v[130:133], off offset:256 sc1
	v_or_b32_e32 v172, 32, v150
	v_mad_i64_i32 v[172:173], s[0:1], v172, s36, v[136:137]
	v_cvt_pk_bf16_f32 v130, v62, v63
	v_cvt_pk_bf16_f32 v131, v64, v65
	v_cvt_pk_bf16_f32 v132, v58, v59
	v_cvt_pk_bf16_f32 v133, v60, v61
	v_lshl_add_u64 v[172:173], v[172:173], 0, v[134:135]
	global_store_dwordx4 v[172:173], v[130:133], off sc1
	s_nop 1
	v_cvt_pk_bf16_f32 v130, v46, v47
	v_cvt_pk_bf16_f32 v131, v48, v49
	v_cvt_pk_bf16_f32 v132, v42, v43
	v_cvt_pk_bf16_f32 v133, v44, v45
	global_store_dwordx4 v[172:173], v[130:133], off offset:256 sc1
	v_or_b32_e32 v172, 48, v150
	v_mad_i64_i32 v[172:173], s[0:1], v172, s36, v[136:137]
	v_cvt_pk_bf16_f32 v130, v30, v31
	v_cvt_pk_bf16_f32 v131, v32, v33
	v_cvt_pk_bf16_f32 v132, v26, v27
	v_cvt_pk_bf16_f32 v133, v28, v29
	v_lshl_add_u64 v[172:173], v[172:173], 0, v[134:135]
	global_store_dwordx4 v[172:173], v[130:133], off sc1
	s_nop 1
	v_cvt_pk_bf16_f32 v130, v14, v15
	v_cvt_pk_bf16_f32 v131, v16, v17
	v_cvt_pk_bf16_f32 v132, v10, v11
	v_cvt_pk_bf16_f32 v133, v12, v13
	global_store_dwordx4 v[172:173], v[130:133], off offset:256 sc1
	v_add_u32_e32 v172, 0x80, v150
	v_mad_i64_i32 v[172:173], s[0:1], v172, s36, v[136:137]
	v_cvt_pk_bf16_f32 v130, v118, v119
	v_cvt_pk_bf16_f32 v131, v120, v121
	v_cvt_pk_bf16_f32 v132, v114, v115
	v_cvt_pk_bf16_f32 v133, v116, v117
	v_lshl_add_u64 v[172:173], v[172:173], 0, v[134:135]
	global_store_dwordx4 v[172:173], v[130:133], off sc1
	s_nop 1
	v_cvt_pk_bf16_f32 v130, v102, v103
	v_cvt_pk_bf16_f32 v131, v104, v105
	v_cvt_pk_bf16_f32 v132, v98, v99
	v_cvt_pk_bf16_f32 v133, v100, v101
	global_store_dwordx4 v[172:173], v[130:133], off offset:256 sc1
	v_add_u32_e32 v172, 0x90, v150
	v_mad_i64_i32 v[172:173], s[0:1], v172, s36, v[136:137]
	v_cvt_pk_bf16_f32 v130, v86, v87
	v_cvt_pk_bf16_f32 v131, v88, v89
	v_cvt_pk_bf16_f32 v132, v82, v83
	v_cvt_pk_bf16_f32 v133, v84, v85
	v_lshl_add_u64 v[172:173], v[172:173], 0, v[134:135]
	global_store_dwordx4 v[172:173], v[130:133], off sc1
	s_nop 1
	v_cvt_pk_bf16_f32 v130, v70, v71
	v_cvt_pk_bf16_f32 v131, v72, v73
	v_cvt_pk_bf16_f32 v132, v66, v67
	v_cvt_pk_bf16_f32 v133, v68, v69
	global_store_dwordx4 v[172:173], v[130:133], off offset:256 sc1
	v_add_u32_e32 v172, 0xa0, v150
	v_mad_i64_i32 v[172:173], s[0:1], v172, s36, v[136:137]
	v_cvt_pk_bf16_f32 v130, v54, v55
	v_cvt_pk_bf16_f32 v131, v56, v57
	v_cvt_pk_bf16_f32 v132, v50, v51
	v_cvt_pk_bf16_f32 v133, v52, v53
	v_lshl_add_u64 v[172:173], v[172:173], 0, v[134:135]
	v_add_u32_e32 v150, 0xb0, v150
	global_store_dwordx4 v[172:173], v[130:133], off sc1
	v_mad_i64_i32 v[136:137], s[0:1], v150, s36, v[136:137]
	s_nop 0
	v_cvt_pk_bf16_f32 v130, v38, v39
	v_cvt_pk_bf16_f32 v131, v40, v41
	v_cvt_pk_bf16_f32 v132, v34, v35
	v_cvt_pk_bf16_f32 v133, v36, v37
	global_store_dwordx4 v[172:173], v[130:133], off offset:256 sc1
	v_lshl_add_u64 v[134:135], v[136:137], 0, v[134:135]
	s_nop 0
	v_cvt_pk_bf16_f32 v130, v22, v23
	v_cvt_pk_bf16_f32 v131, v24, v25
	v_cvt_pk_bf16_f32 v132, v18, v19
	v_cvt_pk_bf16_f32 v133, v20, v21
	global_store_dwordx4 v[134:135], v[130:133], off sc1
	s_nop 1
	v_cvt_pk_bf16_f32 v130, v6, v7
	v_cvt_pk_bf16_f32 v131, v8, v9
	v_cvt_pk_bf16_f32 v132, v2, v3
	v_cvt_pk_bf16_f32 v133, v4, v5
	global_store_dwordx4 v[134:135], v[130:133], off offset:256 sc1
	s_cbranch_execnz .LBB0_1648

; #define LAS __attribute__((address_space(3)))
; __device__ __forceinline__ u32x4 pack8(const f32x4 a, const f32x4 b) { u32x4 w; w.x = cvt_pk_bf16(a[0], a[1]); w.y = cvt_pk_bf16(a[2], a[3]); w.z = cvt_pk_bf16(b[0], b[1]); w.w = cvt_pk_bf16(b[2], b[3]); return w; }
;     __device__ __forceinline__ void operator()(const f32x4 (&acc)[2][2][4][2], const Unit& u, int wr, int wc, int fr, int fq) const {
;     ...
;                     const int dk = wr * 64 + f; bf16_t* fp = KT + ((((size_t)head * 132 + 2 * u.pn + bj) * 8 + (dk >> 5)) * 8 + 2 * wc + (fq >> 1)) * 512 + (32 * (fq & 1) + (dk & 31)) * 8;
;                     if (u.kq != 1) *(u32x4*)(fp) = pack8(o1[0], o1[1]);
;                     if (u.kq != 0) *(u32x4*)(fp + (size_t)4 * 8 * 512) = pack8(o2[0], o2[1]);
;                     if (lat) {
;                         LAS bf16_t* tl = (LAS bf16_t*)(scr + (wr * 4 + wc) * 2048);
;                         *(LAS u32x4*)(tl + fr * 32 + 8 * fq) = pack8(o1[0], o1[1]);
;                         *(LAS u32x4*)(tl + 512 + fr * 32 + 8 * fq) = pack8(o2[0], o2[1]);
;                         asm volatile("s_waitcnt lgkmcnt(0)" ::: "memory");
;                         const int L = fr + 16 * fq, tt = L & 31, hf = L >> 5, T = u.pn * BM + bj * HALF + wc * 32 + tt, t = T & (SEQ - 1);
; #pragma unroll
;                         for (int part = 0; part < 2; ++part) { const LAS bf16_t* sp = tl + part * 512 + (hf * 8) * 32 + tt; u32x4 w8;
;                             w8.x = (unsigned)sp[0] | ((unsigned)sp[32] << 16); w8.y = (unsigned)sp[64] | ((unsigned)sp[96] << 16); w8.z = (unsigned)sp[128] | ((unsigned)sp[160] << 16); w8.w = (unsigned)sp[192] | ((unsigned)sp[224] << 16);
;                             const int dk0 = wr * 64 + 16 * m + 8 * hf + 128 * part;
;                             *(u32x4*)(KF + ((((size_t)(T >> 13) * 4 + head) * 512 + (t >> 4)) * 8 + (dk0 >> 5)) * 512 + ((t & 15) + 16 * ((dk0 >> 3) & 3)) * 8) = w8; }
.LBB0_1520:
	s_add_i32 s8, s8, -4
	s_ashr_i32 s9, s8, 31
	s_lshl_b32 s2, s2, 1
	s_mul_hi_i32 s3, s8, 0x84
	s_mul_i32 s18, s8, 0x84
	s_lshl_b64 s[56:57], s[8:9], 9
	s_ashr_i32 s8, s2, 31
	s_add_u32 s2, s18, s2
	s_addc_u32 s3, s3, s8
	s_lshl_b64 s[2:3], s[2:3], 16
	v_readlane_b32 s8, v250, 8
	s_add_u32 s49, s8, s2
	v_readlane_b32 s2, v250, 6
	s_addc_u32 s62, s2, s3
	s_add_u32 s2, s49, s30
	s_addc_u32 s3, s62, s31
	v_lshl_add_u64 v[126:127], s[2:3], 0, v[156:157]
	v_lshlrev_b32_e32 v124, 1, v152
	v_mov_b32_e32 v125, v151
	v_pk_mul_f32 v[120:121], v[120:121], s[10:11] op_sel_hi:[1,0]
	v_pk_mul_f32 v[118:119], v[118:119], s[10:11] op_sel_hi:[1,0]
	v_pk_mul_f32 v[122:123], v[116:117], s[10:11] op_sel_hi:[1,0]
	v_lshl_add_u64 v[134:135], v[126:127], 0, v[124:125]
	v_pk_mul_f32 v[128:129], v[114:115], s[10:11] op_sel_hi:[1,0]
	v_cvt_pk_bf16_f32 v118, v118, v119
	v_cvt_pk_bf16_f32 v119, v120, v121
	v_cvt_pk_bf16_f32 v121, v122, v123
	v_add_co_u32_e32 v122, vcc, 0x8000, v134
	v_cvt_pk_bf16_f32 v120, v128, v129
	s_nop 0
	v_addc_co_u32_e32 v123, vcc, 0, v135, vcc
	global_store_dwordx4 v[122:123], v[118:121], off sc1
	v_cndmask_b32_e64 v122, 0, 1, s[58:59]
	v_cvt_pk_bf16_f32 v114, v176, v177
	v_cvt_pk_bf16_f32 v115, v174, v175
	v_cvt_pk_bf16_f32 v116, v130, v131
	v_cvt_pk_bf16_f32 v117, v132, v133
	v_cmp_ne_u32_e64 s[8:9], 1, v122
	s_andn2_b64 vcc, exec, s[58:59]
	v_lshlrev_b32_e32 v122, 1, v154
	global_store_dwordx4 v[134:135], v[114:117], off sc1
	s_cbranch_vccnz .LBB0_1522
	s_and_b32 s2, s23, 0x1f00
	ds_write_b128 v185, v[114:117]
	ds_write_b128 v185, v[118:121] offset:1024
	v_or_b32_e32 v114, s2, v188
	s_add_u32 s2, s56, 0x800
	s_addc_u32 s3, s57, 0
	v_lshrrev_b32_e32 v114, 4, v114
	s_waitcnt lgkmcnt(0)
	v_or_b32_e32 v114, s2, v114
	v_mov_b32_e32 v115, s3
	v_lshlrev_b64 v[118:119], 13, v[114:115]
	ds_read_u16 v114, v186
	ds_read_u16 v115, v186 offset:64
	v_lshl_add_u64 v[118:119], s[20:21], 0, v[118:119]
	v_mov_b32_e32 v123, v151
	v_readlane_b32 s2, v250, 39
	v_readlane_b32 s3, v250, 40
	s_waitcnt lgkmcnt(0)
	v_lshl_or_b32 v114, v115, 16, v114
	ds_read_u16 v115, v186 offset:128
	ds_read_u16 v116, v186 offset:192
	s_waitcnt lgkmcnt(0)
	v_lshl_or_b32 v115, v116, 16, v115
	ds_read_u16 v116, v186 offset:256
	ds_read_u16 v117, v186 offset:320
	s_waitcnt lgkmcnt(0)
	v_lshl_or_b32 v116, v117, 16, v116
	ds_read_u16 v117, v186 offset:384
	ds_read_u16 v120, v186 offset:448
	s_waitcnt lgkmcnt(0)
	v_lshl_or_b32 v117, v120, 16, v117
	v_lshl_add_u64 v[120:121], v[118:119], 0, s[34:35]
	v_lshl_add_u64 v[120:121], v[120:121], 0, v[122:123]
	global_store_dwordx4 v[120:121], v[114:117], off sc1
	ds_read_u16 v114, v186 offset:1024
	ds_read_u16 v115, v186 offset:1088
	v_lshl_add_u64 v[118:119], v[118:119], 0, s[2:3]
	v_lshl_add_u64 v[118:119], v[118:119], 0, v[122:123]
	s_waitcnt lgkmcnt(0)
	v_lshl_or_b32 v114, v115, 16, v114
	ds_read_u16 v115, v186 offset:1152
	ds_read_u16 v116, v186 offset:1216
	s_waitcnt lgkmcnt(0)
	v_lshl_or_b32 v115, v116, 16, v115
	ds_read_u16 v116, v186 offset:1280
	ds_read_u16 v117, v186 offset:1344
	s_waitcnt lgkmcnt(0)
	v_lshl_or_b32 v116, v117, 16, v116
	ds_read_u16 v117, v186 offset:1408
	ds_read_u16 v120, v186 offset:1472
	s_waitcnt lgkmcnt(0)
	v_lshl_or_b32 v117, v120, 16, v117
	global_store_dwordx4 v[118:119], v[114:117], off sc1
	s_waitcnt lgkmcnt(0)

; #define LAS __attribute__((address_space(3)))
; __device__ __forceinline__ u32x4 pack8(const f32x4 a, const f32x4 b) { u32x4 w; w.x = cvt_pk_bf16(a[0], a[1]); w.y = cvt_pk_bf16(a[2], a[3]); w.z = cvt_pk_bf16(b[0], b[1]); w.w = cvt_pk_bf16(b[2], b[3]); return w; }
;     __device__ __forceinline__ void operator()(const f32x4 (&acc)[2][2][4][2], const Unit& u, int wr, int wc, int fr, int fq) const {
;     ...
;                             o1[n] = (x1 * cc - x2 * ss) * 0.0625f; o2[n] = (x1 * ss + x2 * cc) * 0.0625f;
;                         } else { o1[n] = x1 * 0.0625f; o2[n] = x2 * 0.0625f; }
;                     }
;                     const int dk = wr * 64 + f; bf16_t* fp = KT + ((((size_t)head * 132 + 2 * u.pn + bj) * 8 + (dk >> 5)) * 8 + 2 * wc + (fq >> 1)) * 512 + (32 * (fq & 1) + (dk & 31)) * 8;
;                     if (u.kq != 1) *(u32x4*)(fp) = pack8(o1[0], o1[1]);
;                     if (u.kq != 0) *(u32x4*)(fp + (size_t)4 * 8 * 512) = pack8(o2[0], o2[1]);
;                     if (lat) {
;                         LAS bf16_t* tl = (LAS bf16_t*)(scr + (wr * 4 + wc) * 2048);
;                         *(LAS u32x4*)(tl + fr * 32 + 8 * fq) = pack8(o1[0], o1[1]);
;                         *(LAS u32x4*)(tl + 512 + fr * 32 + 8 * fq) = pack8(o2[0], o2[1]);
;                         asm volatile("s_waitcnt lgkmcnt(0)" ::: "memory");
;                         const int L = fr + 16 * fq, tt = L & 31, hf = L >> 5, T = u.pn * BM + bj * HALF + wc * 32 + tt, t = T & (SEQ - 1);
; #pragma unroll
;                         for (int part = 0; part < 2; ++part) { const LAS bf16_t* sp = tl + part * 512 + (hf * 8) * 32 + tt; u32x4 w8;
;                             w8.x = (unsigned)sp[0] | ((unsigned)sp[32] << 16); w8.y = (unsigned)sp[64] | ((unsigned)sp[96] << 16); w8.z = (unsigned)sp[128] | ((unsigned)sp[160] << 16); w8.w = (unsigned)sp[192] | ((unsigned)sp[224] << 16);
;                             const int dk0 = wr * 64 + 16 * m + 8 * hf + 128 * part;
;                             *(u32x4*)(KF + ((((size_t)(T >> 13) * 4 + head) * 512 + (t >> 4)) * 8 + (dk0 >> 5)) * 512 + ((t & 15) + 16 * ((dk0 >> 3) & 3)) * 8) = w8; }
;                         asm volatile("s_waitcnt lgkmcnt(0)" ::: "memory");
.LBB0_1538:
	s_add_u32 s58, s49, 0x10000
	s_addc_u32 s59, s62, 0
	s_add_u32 s2, s58, s30
	s_addc_u32 s3, s59, s31
	v_lshl_add_u64 v[106:107], s[2:3], 0, v[156:157]
	v_mov_b32_e32 v125, v151
	v_pk_mul_f32 v[104:105], v[104:105], s[10:11] op_sel_hi:[1,0]
	v_pk_mul_f32 v[102:103], v[102:103], s[10:11] op_sel_hi:[1,0]
	v_pk_mul_f32 v[108:109], v[100:101], s[10:11] op_sel_hi:[1,0]
	v_lshl_add_u64 v[112:113], v[106:107], 0, v[124:125]
	v_cvt_pk_bf16_f32 v102, v102, v103
	v_cvt_pk_bf16_f32 v103, v104, v105
	v_cvt_pk_bf16_f32 v105, v108, v109
	v_add_co_u32_e32 v108, vcc, 0x8000, v112
	v_pk_mul_f32 v[110:111], v[98:99], s[10:11] op_sel_hi:[1,0]
	s_nop 0
	v_addc_co_u32_e32 v109, vcc, 0, v113, vcc
	v_cvt_pk_bf16_f32 v98, v130, v131
	v_cvt_pk_bf16_f32 v99, v128, v129
	v_cvt_pk_bf16_f32 v100, v118, v119
	v_cvt_pk_bf16_f32 v101, v120, v121
	v_cvt_pk_bf16_f32 v104, v110, v111
	s_and_b64 vcc, exec, s[8:9]
	global_store_dwordx4 v[112:113], v[98:101], off sc1
	global_store_dwordx4 v[108:109], v[102:105], off sc1
	s_cbranch_vccnz .LBB0_1540
	s_and_b32 s2, s23, 0x1f00
	ds_write_b128 v185, v[98:101]
	ds_write_b128 v185, v[102:105] offset:1024
	v_or_b32_e32 v98, s2, v188
	s_add_u32 s2, s56, 0x800
	s_addc_u32 s3, s57, 0
	v_lshrrev_b32_e32 v98, 4, v98
	s_waitcnt lgkmcnt(0)
	v_or3_b32 v98, v98, s2, 8
	v_mov_b32_e32 v99, s3
	v_lshlrev_b64 v[102:103], 13, v[98:99]
	ds_read_u16 v98, v186
	ds_read_u16 v99, v186 offset:64
	v_lshl_add_u64 v[102:103], s[20:21], 0, v[102:103]
	v_mov_b32_e32 v123, v151
	v_readlane_b32 s2, v250, 39
	v_readlane_b32 s3, v250, 40
	s_waitcnt lgkmcnt(0)
	v_lshl_or_b32 v98, v99, 16, v98
	ds_read_u16 v99, v186 offset:128
	ds_read_u16 v100, v186 offset:192
	s_waitcnt lgkmcnt(0)
	v_lshl_or_b32 v99, v100, 16, v99
	ds_read_u16 v100, v186 offset:256
	ds_read_u16 v101, v186 offset:320
	s_waitcnt lgkmcnt(0)
	v_lshl_or_b32 v100, v101, 16, v100
	ds_read_u16 v101, v186 offset:384
	ds_read_u16 v104, v186 offset:448
	s_waitcnt lgkmcnt(0)
	v_lshl_or_b32 v101, v104, 16, v101
	v_lshl_add_u64 v[104:105], v[102:103], 0, s[34:35]
	v_lshl_add_u64 v[104:105], v[104:105], 0, v[122:123]
	global_store_dwordx4 v[104:105], v[98:101], off sc1
	ds_read_u16 v98, v186 offset:1024
	ds_read_u16 v99, v186 offset:1088
	v_lshl_add_u64 v[102:103], v[102:103], 0, s[2:3]
	v_lshl_add_u64 v[102:103], v[102:103], 0, v[122:123]
	s_waitcnt lgkmcnt(0)
	v_lshl_or_b32 v98, v99, 16, v98
	ds_read_u16 v99, v186 offset:1152
	ds_read_u16 v100, v186 offset:1216
	s_waitcnt lgkmcnt(0)
	v_lshl_or_b32 v99, v100, 16, v99
	ds_read_u16 v100, v186 offset:1280
	ds_read_u16 v101, v186 offset:1344
	s_waitcnt lgkmcnt(0)
	v_lshl_or_b32 v100, v101, 16, v100
	ds_read_u16 v101, v186 offset:1408
	ds_read_u16 v104, v186 offset:1472
	s_waitcnt lgkmcnt(0)
	v_lshl_or_b32 v101, v104, 16, v101
	global_store_dwordx4 v[102:103], v[98:101], off sc1
	s_waitcnt lgkmcnt(0)

; #define LAS __attribute__((address_space(3)))
; __device__ __forceinline__ u32x4 pack8(const f32x4 a, const f32x4 b) { u32x4 w; w.x = cvt_pk_bf16(a[0], a[1]); w.y = cvt_pk_bf16(a[2], a[3]); w.z = cvt_pk_bf16(b[0], b[1]); w.w = cvt_pk_bf16(b[2], b[3]); return w; }
;     __device__ __forceinline__ void operator()(const f32x4 (&acc)[2][2][4][2], const Unit& u, int wr, int wc, int fr, int fq) const {
;     ...
;                             o1[n] = (x1 * cc - x2 * ss) * 0.0625f; o2[n] = (x1 * ss + x2 * cc) * 0.0625f;
;                         } else { o1[n] = x1 * 0.0625f; o2[n] = x2 * 0.0625f; }
;                     }
;                     const int dk = wr * 64 + f; bf16_t* fp = KT + ((((size_t)head * 132 + 2 * u.pn + bj) * 8 + (dk >> 5)) * 8 + 2 * wc + (fq >> 1)) * 512 + (32 * (fq & 1) + (dk & 31)) * 8;
;                     if (u.kq != 1) *(u32x4*)(fp) = pack8(o1[0], o1[1]);
;                     if (u.kq != 0) *(u32x4*)(fp + (size_t)4 * 8 * 512) = pack8(o2[0], o2[1]);
;                     if (lat) {
;                         LAS bf16_t* tl = (LAS bf16_t*)(scr + (wr * 4 + wc) * 2048);
;                         *(LAS u32x4*)(tl + fr * 32 + 8 * fq) = pack8(o1[0], o1[1]);
;                         *(LAS u32x4*)(tl + 512 + fr * 32 + 8 * fq) = pack8(o2[0], o2[1]);
;                         asm volatile("s_waitcnt lgkmcnt(0)" ::: "memory");
;                         const int L = fr + 16 * fq, tt = L & 31, hf = L >> 5, T = u.pn * BM + bj * HALF + wc * 32 + tt, t = T & (SEQ - 1);
; #pragma unroll
;                         for (int part = 0; part < 2; ++part) { const LAS bf16_t* sp = tl + part * 512 + (hf * 8) * 32 + tt; u32x4 w8;
;                             w8.x = (unsigned)sp[0] | ((unsigned)sp[32] << 16); w8.y = (unsigned)sp[64] | ((unsigned)sp[96] << 16); w8.z = (unsigned)sp[128] | ((unsigned)sp[160] << 16); w8.w = (unsigned)sp[192] | ((unsigned)sp[224] << 16);
;                             const int dk0 = wr * 64 + 16 * m + 8 * hf + 128 * part;
;                             *(u32x4*)(KF + ((((size_t)(T >> 13) * 4 + head) * 512 + (t >> 4)) * 8 + (dk0 >> 5)) * 512 + ((t & 15) + 16 * ((dk0 >> 3) & 3)) * 8) = w8; }
;                         asm volatile("s_waitcnt lgkmcnt(0)" ::: "memory");
.LBB0_1556:
	v_lshlrev_b32_e32 v150, 1, v158
	v_pk_mul_f32 v[88:89], v[88:89], s[10:11] op_sel_hi:[1,0]
	v_pk_mul_f32 v[86:87], v[86:87], s[10:11] op_sel_hi:[1,0]
	v_pk_mul_f32 v[90:91], v[84:85], s[10:11] op_sel_hi:[1,0]
	v_lshl_add_u64 v[94:95], v[126:127], 0, v[150:151]
	v_cvt_pk_bf16_f32 v86, v86, v87
	v_cvt_pk_bf16_f32 v87, v88, v89
	v_cvt_pk_bf16_f32 v89, v90, v91
	v_add_co_u32_e32 v90, vcc, 0x8000, v94
	v_pk_mul_f32 v[92:93], v[82:83], s[10:11] op_sel_hi:[1,0]
	s_nop 0
	v_addc_co_u32_e32 v91, vcc, 0, v95, vcc
	v_cvt_pk_bf16_f32 v82, v112, v113
	v_cvt_pk_bf16_f32 v83, v110, v111
	v_cvt_pk_bf16_f32 v84, v102, v103
	v_cvt_pk_bf16_f32 v85, v104, v105
	v_cvt_pk_bf16_f32 v88, v92, v93
	s_and_b64 vcc, exec, s[8:9]
	global_store_dwordx4 v[94:95], v[82:85], off sc1
	global_store_dwordx4 v[90:91], v[86:89], off sc1
	s_cbranch_vccnz .LBB0_1558
	s_and_b32 s2, s23, 0x1f00
	ds_write_b128 v185, v[82:85]
	ds_write_b128 v185, v[86:89] offset:1024
	v_or_b32_e32 v82, s2, v188
	s_add_u32 s2, s56, 0x800
	s_addc_u32 s3, s57, 0
	v_lshrrev_b32_e32 v82, 4, v82
	s_waitcnt lgkmcnt(0)
	v_or_b32_e32 v82, s2, v82
	v_mov_b32_e32 v83, s3
	v_lshlrev_b64 v[86:87], 13, v[82:83]
	ds_read_u16 v82, v186
	ds_read_u16 v83, v186 offset:64
	v_lshl_add_u64 v[86:87], s[20:21], 0, v[86:87]
	v_mov_b32_e32 v123, v151
	s_waitcnt lgkmcnt(0)
	v_lshl_or_b32 v82, v83, 16, v82
	ds_read_u16 v83, v186 offset:128
	ds_read_u16 v84, v186 offset:192
	s_waitcnt lgkmcnt(0)
	v_lshl_or_b32 v83, v84, 16, v83
	ds_read_u16 v84, v186 offset:256
	ds_read_u16 v85, v186 offset:320
	s_waitcnt lgkmcnt(0)
	v_lshl_or_b32 v84, v85, 16, v84
	ds_read_u16 v85, v186 offset:384
	ds_read_u16 v88, v186 offset:448
	s_waitcnt lgkmcnt(0)
	v_lshl_or_b32 v85, v88, 16, v85
	v_lshl_add_u64 v[88:89], v[86:87], 0, s[34:35]
	v_lshl_add_u64 v[88:89], v[88:89], 0, v[122:123]
	global_store_dwordx4 v[88:89], v[82:85], off offset:512 sc1
	ds_read_u16 v82, v186 offset:1024
	ds_read_u16 v83, v186 offset:1088
	v_lshl_add_u64 v[86:87], v[86:87], 0, s[38:39]
	v_lshl_add_u64 v[86:87], v[86:87], 0, v[122:123]
	s_waitcnt lgkmcnt(0)
	v_lshl_or_b32 v82, v83, 16, v82
	ds_read_u16 v83, v186 offset:1152
	ds_read_u16 v84, v186 offset:1216
	s_waitcnt lgkmcnt(0)
	v_lshl_or_b32 v83, v84, 16, v83
	ds_read_u16 v84, v186 offset:1280
	ds_read_u16 v85, v186 offset:1344
	s_waitcnt lgkmcnt(0)
	v_lshl_or_b32 v84, v85, 16, v84
	ds_read_u16 v85, v186 offset:1408
	ds_read_u16 v88, v186 offset:1472
	s_waitcnt lgkmcnt(0)
	v_lshl_or_b32 v85, v88, 16, v85
	global_store_dwordx4 v[86:87], v[82:85], off offset:512 sc1
	s_waitcnt lgkmcnt(0)

; #define LAS __attribute__((address_space(3)))
; __device__ __forceinline__ u32x4 pack8(const f32x4 a, const f32x4 b) { u32x4 w; w.x = cvt_pk_bf16(a[0], a[1]); w.y = cvt_pk_bf16(a[2], a[3]); w.z = cvt_pk_bf16(b[0], b[1]); w.w = cvt_pk_bf16(b[2], b[3]); return w; }
;     __device__ __forceinline__ void operator()(const f32x4 (&acc)[2][2][4][2], const Unit& u, int wr, int wc, int fr, int fq) const {
;     ...
;                             o1[n] = (x1 * cc - x2 * ss) * 0.0625f; o2[n] = (x1 * ss + x2 * cc) * 0.0625f;
;                         } else { o1[n] = x1 * 0.0625f; o2[n] = x2 * 0.0625f; }
;                     }
;                     const int dk = wr * 64 + f; bf16_t* fp = KT + ((((size_t)head * 132 + 2 * u.pn + bj) * 8 + (dk >> 5)) * 8 + 2 * wc + (fq >> 1)) * 512 + (32 * (fq & 1) + (dk & 31)) * 8;
;                     if (u.kq != 1) *(u32x4*)(fp) = pack8(o1[0], o1[1]);
;                     if (u.kq != 0) *(u32x4*)(fp + (size_t)4 * 8 * 512) = pack8(o2[0], o2[1]);
;                     if (lat) {
;                         LAS bf16_t* tl = (LAS bf16_t*)(scr + (wr * 4 + wc) * 2048);
;                         *(LAS u32x4*)(tl + fr * 32 + 8 * fq) = pack8(o1[0], o1[1]);
;                         *(LAS u32x4*)(tl + 512 + fr * 32 + 8 * fq) = pack8(o2[0], o2[1]);
;                         asm volatile("s_waitcnt lgkmcnt(0)" ::: "memory");
;                         const int L = fr + 16 * fq, tt = L & 31, hf = L >> 5, T = u.pn * BM + bj * HALF + wc * 32 + tt, t = T & (SEQ - 1);
; #pragma unroll
;                         for (int part = 0; part < 2; ++part) { const LAS bf16_t* sp = tl + part * 512 + (hf * 8) * 32 + tt; u32x4 w8;
;                             w8.x = (unsigned)sp[0] | ((unsigned)sp[32] << 16); w8.y = (unsigned)sp[64] | ((unsigned)sp[96] << 16); w8.z = (unsigned)sp[128] | ((unsigned)sp[160] << 16); w8.w = (unsigned)sp[192] | ((unsigned)sp[224] << 16);
;                             const int dk0 = wr * 64 + 16 * m + 8 * hf + 128 * part;
;                             *(u32x4*)(KF + ((((size_t)(T >> 13) * 4 + head) * 512 + (t >> 4)) * 8 + (dk0 >> 5)) * 512 + ((t & 15) + 16 * ((dk0 >> 3) & 3)) * 8) = w8; }
;                         asm volatile("s_waitcnt lgkmcnt(0)" ::: "memory");
.LBB0_1574:
	v_pk_mul_f32 v[72:73], v[72:73], s[10:11] op_sel_hi:[1,0]
	v_pk_mul_f32 v[70:71], v[70:71], s[10:11] op_sel_hi:[1,0]
	v_pk_mul_f32 v[74:75], v[68:69], s[10:11] op_sel_hi:[1,0]
	v_lshl_add_u64 v[78:79], v[106:107], 0, v[150:151]
	v_cvt_pk_bf16_f32 v70, v70, v71
	v_cvt_pk_bf16_f32 v71, v72, v73
	v_cvt_pk_bf16_f32 v73, v74, v75
	v_add_co_u32_e32 v74, vcc, 0x8000, v78
	v_pk_mul_f32 v[76:77], v[66:67], s[10:11] op_sel_hi:[1,0]
	s_nop 0
	v_addc_co_u32_e32 v75, vcc, 0, v79, vcc
	v_cvt_pk_bf16_f32 v66, v92, v93
	v_cvt_pk_bf16_f32 v67, v90, v91
	v_cvt_pk_bf16_f32 v68, v86, v87
	v_cvt_pk_bf16_f32 v69, v88, v89
	v_cvt_pk_bf16_f32 v72, v76, v77
	s_and_b64 vcc, exec, s[8:9]
	global_store_dwordx4 v[78:79], v[66:69], off sc1
	global_store_dwordx4 v[74:75], v[70:73], off sc1
	s_cbranch_vccnz .LBB0_1576
	s_and_b32 s2, s23, 0x1f00
	ds_write_b128 v185, v[66:69]
	ds_write_b128 v185, v[70:73] offset:1024
	v_or_b32_e32 v66, s2, v188
	s_add_u32 s2, s56, 0x800
	s_addc_u32 s3, s57, 0
	v_lshrrev_b32_e32 v66, 4, v66
	s_waitcnt lgkmcnt(0)
	v_or3_b32 v66, v66, s2, 8
	v_mov_b32_e32 v67, s3
	v_lshlrev_b64 v[70:71], 13, v[66:67]
	ds_read_u16 v66, v186
	ds_read_u16 v67, v186 offset:64
	v_lshl_add_u64 v[70:71], s[20:21], 0, v[70:71]
	v_mov_b32_e32 v123, v151
	s_waitcnt lgkmcnt(0)
	v_lshl_or_b32 v66, v67, 16, v66
	ds_read_u16 v67, v186 offset:128
	ds_read_u16 v68, v186 offset:192
	s_waitcnt lgkmcnt(0)
	v_lshl_or_b32 v67, v68, 16, v67
	ds_read_u16 v68, v186 offset:256
	ds_read_u16 v69, v186 offset:320
	s_waitcnt lgkmcnt(0)
	v_lshl_or_b32 v68, v69, 16, v68
	ds_read_u16 v69, v186 offset:384
	ds_read_u16 v72, v186 offset:448
	s_waitcnt lgkmcnt(0)
	v_lshl_or_b32 v69, v72, 16, v69
	v_lshl_add_u64 v[72:73], v[70:71], 0, s[34:35]
	v_lshl_add_u64 v[72:73], v[72:73], 0, v[122:123]
	global_store_dwordx4 v[72:73], v[66:69], off offset:512 sc1
	ds_read_u16 v66, v186 offset:1024
	ds_read_u16 v67, v186 offset:1088
	v_lshl_add_u64 v[70:71], v[70:71], 0, s[38:39]
	v_lshl_add_u64 v[70:71], v[70:71], 0, v[122:123]
	s_waitcnt lgkmcnt(0)
	v_lshl_or_b32 v66, v67, 16, v66
	ds_read_u16 v67, v186 offset:1152
	ds_read_u16 v68, v186 offset:1216
	s_waitcnt lgkmcnt(0)
	v_lshl_or_b32 v67, v68, 16, v67
	ds_read_u16 v68, v186 offset:1280
	ds_read_u16 v69, v186 offset:1344
	s_waitcnt lgkmcnt(0)
	v_lshl_or_b32 v68, v69, 16, v68
	ds_read_u16 v69, v186 offset:1408
	ds_read_u16 v72, v186 offset:1472
	s_waitcnt lgkmcnt(0)
	v_lshl_or_b32 v69, v72, 16, v69
	global_store_dwordx4 v[70:71], v[66:69], off offset:512 sc1
	s_waitcnt lgkmcnt(0)

; #define LAS __attribute__((address_space(3)))
; __device__ __forceinline__ u32x4 pack8(const f32x4 a, const f32x4 b) { u32x4 w; w.x = cvt_pk_bf16(a[0], a[1]); w.y = cvt_pk_bf16(a[2], a[3]); w.z = cvt_pk_bf16(b[0], b[1]); w.w = cvt_pk_bf16(b[2], b[3]); return w; }
;     __device__ __forceinline__ void operator()(const f32x4 (&acc)[2][2][4][2], const Unit& u, int wr, int wc, int fr, int fq) const {
;     ...
;                             o1[n] = (x1 * cc - x2 * ss) * 0.0625f; o2[n] = (x1 * ss + x2 * cc) * 0.0625f;
;                         } else { o1[n] = x1 * 0.0625f; o2[n] = x2 * 0.0625f; }
;                     }
;                     const int dk = wr * 64 + f; bf16_t* fp = KT + ((((size_t)head * 132 + 2 * u.pn + bj) * 8 + (dk >> 5)) * 8 + 2 * wc + (fq >> 1)) * 512 + (32 * (fq & 1) + (dk & 31)) * 8;
;                     if (u.kq != 1) *(u32x4*)(fp) = pack8(o1[0], o1[1]);
;                     if (u.kq != 0) *(u32x4*)(fp + (size_t)4 * 8 * 512) = pack8(o2[0], o2[1]);
;                     if (lat) {
;                         LAS bf16_t* tl = (LAS bf16_t*)(scr + (wr * 4 + wc) * 2048);
;                         *(LAS u32x4*)(tl + fr * 32 + 8 * fq) = pack8(o1[0], o1[1]);
;                         *(LAS u32x4*)(tl + 512 + fr * 32 + 8 * fq) = pack8(o2[0], o2[1]);
;                         asm volatile("s_waitcnt lgkmcnt(0)" ::: "memory");
;                         const int L = fr + 16 * fq, tt = L & 31, hf = L >> 5, T = u.pn * BM + bj * HALF + wc * 32 + tt, t = T & (SEQ - 1);
; #pragma unroll
;                         for (int part = 0; part < 2; ++part) { const LAS bf16_t* sp = tl + part * 512 + (hf * 8) * 32 + tt; u32x4 w8;
;                             w8.x = (unsigned)sp[0] | ((unsigned)sp[32] << 16); w8.y = (unsigned)sp[64] | ((unsigned)sp[96] << 16); w8.z = (unsigned)sp[128] | ((unsigned)sp[160] << 16); w8.w = (unsigned)sp[192] | ((unsigned)sp[224] << 16);
;                             const int dk0 = wr * 64 + 16 * m + 8 * hf + 128 * part;
;                             *(u32x4*)(KF + ((((size_t)(T >> 13) * 4 + head) * 512 + (t >> 4)) * 8 + (dk0 >> 5)) * 512 + ((t & 15) + 16 * ((dk0 >> 3) & 3)) * 8) = w8; }
;                         asm volatile("s_waitcnt lgkmcnt(0)" ::: "memory");
.LBB0_1592:
	s_add_u32 s2, s49, s40
	s_addc_u32 s3, s62, s41
	v_pk_mul_f32 v[62:63], v[50:51], s[10:11] op_sel_hi:[1,0]
	v_lshl_add_u64 v[50:51], s[2:3], 0, v[156:157]
	v_mov_b32_e32 v125, v151
	v_pk_mul_f32 v[56:57], v[56:57], s[10:11] op_sel_hi:[1,0]
	v_pk_mul_f32 v[54:55], v[54:55], s[10:11] op_sel_hi:[1,0]
	v_pk_mul_f32 v[60:61], v[52:53], s[10:11] op_sel_hi:[1,0]
	v_lshl_add_u64 v[58:59], v[50:51], 0, v[124:125]
	v_cvt_pk_bf16_f32 v54, v54, v55
	v_cvt_pk_bf16_f32 v55, v56, v57
	v_cvt_pk_bf16_f32 v57, v60, v61
	v_add_co_u32_e32 v60, vcc, 0x8000, v58
	v_cvt_pk_bf16_f32 v50, v78, v79
	s_nop 0
	v_addc_co_u32_e32 v61, vcc, 0, v59, vcc
	v_cvt_pk_bf16_f32 v51, v76, v77
	v_cvt_pk_bf16_f32 v52, v70, v71
	v_cvt_pk_bf16_f32 v53, v72, v73
	v_cvt_pk_bf16_f32 v56, v62, v63
	s_and_b64 vcc, exec, s[8:9]
	global_store_dwordx4 v[58:59], v[50:53], off sc1
	global_store_dwordx4 v[60:61], v[54:57], off sc1
	s_cbranch_vccnz .LBB0_1594
	s_and_b32 s2, s23, 0x1f00
	ds_write_b128 v185, v[50:53]
	ds_write_b128 v185, v[54:57] offset:1024
	v_or_b32_e32 v50, s2, v188
	s_add_u32 s2, s56, 0x800
	s_addc_u32 s3, s57, 0
	v_lshrrev_b32_e32 v50, 4, v50
	s_waitcnt lgkmcnt(0)
	v_or_b32_e32 v50, s2, v50
	v_mov_b32_e32 v51, s3
	v_lshlrev_b64 v[54:55], 13, v[50:51]
	ds_read_u16 v50, v186
	ds_read_u16 v51, v186 offset:64
	v_lshl_add_u64 v[54:55], s[20:21], 0, v[54:55]
	v_mov_b32_e32 v123, v151
	s_waitcnt lgkmcnt(0)
	v_lshl_or_b32 v50, v51, 16, v50
	ds_read_u16 v51, v186 offset:128
	ds_read_u16 v52, v186 offset:192
	s_waitcnt lgkmcnt(0)
	v_lshl_or_b32 v51, v52, 16, v51
	ds_read_u16 v52, v186 offset:256
	ds_read_u16 v53, v186 offset:320
	s_waitcnt lgkmcnt(0)
	v_lshl_or_b32 v52, v53, 16, v52
	ds_read_u16 v53, v186 offset:384
	ds_read_u16 v56, v186 offset:448
	s_waitcnt lgkmcnt(0)
	v_lshl_or_b32 v53, v56, 16, v53
	v_lshl_add_u64 v[56:57], v[54:55], 0, s[42:43]
	v_lshl_add_u64 v[56:57], v[56:57], 0, v[122:123]
	global_store_dwordx4 v[56:57], v[50:53], off sc1
	ds_read_u16 v50, v186 offset:1024
	ds_read_u16 v51, v186 offset:1088
	v_lshl_add_u64 v[54:55], v[54:55], 0, s[44:45]
	v_lshl_add_u64 v[54:55], v[54:55], 0, v[122:123]
	s_waitcnt lgkmcnt(0)
	v_lshl_or_b32 v50, v51, 16, v50
	ds_read_u16 v51, v186 offset:1152
	ds_read_u16 v52, v186 offset:1216
	s_waitcnt lgkmcnt(0)
	v_lshl_or_b32 v51, v52, 16, v51
	ds_read_u16 v52, v186 offset:1280
	ds_read_u16 v53, v186 offset:1344
	s_waitcnt lgkmcnt(0)
	v_lshl_or_b32 v52, v53, 16, v52
	ds_read_u16 v53, v186 offset:1408
	ds_read_u16 v56, v186 offset:1472
	s_waitcnt lgkmcnt(0)
	v_lshl_or_b32 v53, v56, 16, v53
	global_store_dwordx4 v[54:55], v[50:53], off sc1
	s_waitcnt lgkmcnt(0)

; #define LAS __attribute__((address_space(3)))
; __device__ __forceinline__ u32x4 pack8(const f32x4 a, const f32x4 b) { u32x4 w; w.x = cvt_pk_bf16(a[0], a[1]); w.y = cvt_pk_bf16(a[2], a[3]); w.z = cvt_pk_bf16(b[0], b[1]); w.w = cvt_pk_bf16(b[2], b[3]); return w; }
;     __device__ __forceinline__ void operator()(const f32x4 (&acc)[2][2][4][2], const Unit& u, int wr, int wc, int fr, int fq) const {
;     ...
;                             o1[n] = (x1 * cc - x2 * ss) * 0.0625f; o2[n] = (x1 * ss + x2 * cc) * 0.0625f;
;                         } else { o1[n] = x1 * 0.0625f; o2[n] = x2 * 0.0625f; }
;                     }
;                     const int dk = wr * 64 + f; bf16_t* fp = KT + ((((size_t)head * 132 + 2 * u.pn + bj) * 8 + (dk >> 5)) * 8 + 2 * wc + (fq >> 1)) * 512 + (32 * (fq & 1) + (dk & 31)) * 8;
;                     if (u.kq != 1) *(u32x4*)(fp) = pack8(o1[0], o1[1]);
;                     if (u.kq != 0) *(u32x4*)(fp + (size_t)4 * 8 * 512) = pack8(o2[0], o2[1]);
;                     if (lat) {
;                         LAS bf16_t* tl = (LAS bf16_t*)(scr + (wr * 4 + wc) * 2048);
;                         *(LAS u32x4*)(tl + fr * 32 + 8 * fq) = pack8(o1[0], o1[1]);
;                         *(LAS u32x4*)(tl + 512 + fr * 32 + 8 * fq) = pack8(o2[0], o2[1]);
;                         asm volatile("s_waitcnt lgkmcnt(0)" ::: "memory");
;                         const int L = fr + 16 * fq, tt = L & 31, hf = L >> 5, T = u.pn * BM + bj * HALF + wc * 32 + tt, t = T & (SEQ - 1);
; #pragma unroll
;                         for (int part = 0; part < 2; ++part) { const LAS bf16_t* sp = tl + part * 512 + (hf * 8) * 32 + tt; u32x4 w8;
;                             w8.x = (unsigned)sp[0] | ((unsigned)sp[32] << 16); w8.y = (unsigned)sp[64] | ((unsigned)sp[96] << 16); w8.z = (unsigned)sp[128] | ((unsigned)sp[160] << 16); w8.w = (unsigned)sp[192] | ((unsigned)sp[224] << 16);
;                             const int dk0 = wr * 64 + 16 * m + 8 * hf + 128 * part;
;                             *(u32x4*)(KF + ((((size_t)(T >> 13) * 4 + head) * 512 + (t >> 4)) * 8 + (dk0 >> 5)) * 512 + ((t & 15) + 16 * ((dk0 >> 3) & 3)) * 8) = w8; }
;                         asm volatile("s_waitcnt lgkmcnt(0)" ::: "memory");
.LBB0_1610:
	s_add_u32 s2, s58, s40
	s_addc_u32 s3, s59, s41
	v_pk_mul_f32 v[46:47], v[34:35], s[10:11] op_sel_hi:[1,0]
	v_lshl_add_u64 v[34:35], s[2:3], 0, v[156:157]
	v_mov_b32_e32 v125, v151
	v_pk_mul_f32 v[40:41], v[40:41], s[10:11] op_sel_hi:[1,0]
	v_pk_mul_f32 v[38:39], v[38:39], s[10:11] op_sel_hi:[1,0]
	v_pk_mul_f32 v[44:45], v[36:37], s[10:11] op_sel_hi:[1,0]
	v_lshl_add_u64 v[42:43], v[34:35], 0, v[124:125]
	v_cvt_pk_bf16_f32 v38, v38, v39
	v_cvt_pk_bf16_f32 v39, v40, v41
	v_cvt_pk_bf16_f32 v41, v44, v45
	v_add_co_u32_e32 v44, vcc, 0x8000, v42
	v_cvt_pk_bf16_f32 v34, v62, v63
	s_nop 0
	v_addc_co_u32_e32 v45, vcc, 0, v43, vcc
	v_cvt_pk_bf16_f32 v35, v60, v61
	v_cvt_pk_bf16_f32 v36, v54, v55
	v_cvt_pk_bf16_f32 v37, v56, v57
	v_cvt_pk_bf16_f32 v40, v46, v47
	s_and_b64 vcc, exec, s[8:9]
	global_store_dwordx4 v[42:43], v[34:37], off sc1
	global_store_dwordx4 v[44:45], v[38:41], off sc1
	s_cbranch_vccnz .LBB0_1612
	s_and_b32 s2, s23, 0x1f00
	ds_write_b128 v185, v[34:37]
	ds_write_b128 v185, v[38:41] offset:1024
	v_or_b32_e32 v34, s2, v188
	s_add_u32 s2, s56, 0x800
	s_addc_u32 s3, s57, 0
	v_lshrrev_b32_e32 v34, 4, v34
	s_waitcnt lgkmcnt(0)
	v_or3_b32 v34, v34, s2, 8
	v_mov_b32_e32 v35, s3
	v_lshlrev_b64 v[38:39], 13, v[34:35]
	ds_read_u16 v34, v186
	ds_read_u16 v35, v186 offset:64
	v_lshl_add_u64 v[38:39], s[20:21], 0, v[38:39]
	v_mov_b32_e32 v123, v151
	s_waitcnt lgkmcnt(0)
	v_lshl_or_b32 v34, v35, 16, v34
	ds_read_u16 v35, v186 offset:128
	ds_read_u16 v36, v186 offset:192
	s_waitcnt lgkmcnt(0)
	v_lshl_or_b32 v35, v36, 16, v35
	ds_read_u16 v36, v186 offset:256
	ds_read_u16 v37, v186 offset:320
	s_waitcnt lgkmcnt(0)
	v_lshl_or_b32 v36, v37, 16, v36
	ds_read_u16 v37, v186 offset:384
	ds_read_u16 v40, v186 offset:448
	s_waitcnt lgkmcnt(0)
	v_lshl_or_b32 v37, v40, 16, v37
	v_lshl_add_u64 v[40:41], v[38:39], 0, s[42:43]
	v_lshl_add_u64 v[40:41], v[40:41], 0, v[122:123]
	global_store_dwordx4 v[40:41], v[34:37], off sc1
	ds_read_u16 v34, v186 offset:1024
	ds_read_u16 v35, v186 offset:1088
	v_lshl_add_u64 v[38:39], v[38:39], 0, s[44:45]
	v_lshl_add_u64 v[38:39], v[38:39], 0, v[122:123]
	s_waitcnt lgkmcnt(0)
	v_lshl_or_b32 v34, v35, 16, v34
	ds_read_u16 v35, v186 offset:1152
	ds_read_u16 v36, v186 offset:1216
	s_waitcnt lgkmcnt(0)
	v_lshl_or_b32 v35, v36, 16, v35
	ds_read_u16 v36, v186 offset:1280
	ds_read_u16 v37, v186 offset:1344
	s_waitcnt lgkmcnt(0)
	v_lshl_or_b32 v36, v37, 16, v36
	ds_read_u16 v37, v186 offset:1408
	ds_read_u16 v40, v186 offset:1472
	s_waitcnt lgkmcnt(0)
	v_lshl_or_b32 v37, v40, 16, v37
	global_store_dwordx4 v[38:39], v[34:37], off sc1
	s_waitcnt lgkmcnt(0)

; #define LAS __attribute__((address_space(3)))
; __device__ __forceinline__ u32x4 pack8(const f32x4 a, const f32x4 b) { u32x4 w; w.x = cvt_pk_bf16(a[0], a[1]); w.y = cvt_pk_bf16(a[2], a[3]); w.z = cvt_pk_bf16(b[0], b[1]); w.w = cvt_pk_bf16(b[2], b[3]); return w; }
;     __device__ __forceinline__ void operator()(const f32x4 (&acc)[2][2][4][2], const Unit& u, int wr, int wc, int fr, int fq) const {
;     ...
;                             o1[n] = (x1 * cc - x2 * ss) * 0.0625f; o2[n] = (x1 * ss + x2 * cc) * 0.0625f;
;                         } else { o1[n] = x1 * 0.0625f; o2[n] = x2 * 0.0625f; }
;                     }
;                     const int dk = wr * 64 + f; bf16_t* fp = KT + ((((size_t)head * 132 + 2 * u.pn + bj) * 8 + (dk >> 5)) * 8 + 2 * wc + (fq >> 1)) * 512 + (32 * (fq & 1) + (dk & 31)) * 8;
;                     if (u.kq != 1) *(u32x4*)(fp) = pack8(o1[0], o1[1]);
;                     if (u.kq != 0) *(u32x4*)(fp + (size_t)4 * 8 * 512) = pack8(o2[0], o2[1]);
;                     if (lat) {
;                         LAS bf16_t* tl = (LAS bf16_t*)(scr + (wr * 4 + wc) * 2048);
;                         *(LAS u32x4*)(tl + fr * 32 + 8 * fq) = pack8(o1[0], o1[1]);
;                         *(LAS u32x4*)(tl + 512 + fr * 32 + 8 * fq) = pack8(o2[0], o2[1]);
;                         asm volatile("s_waitcnt lgkmcnt(0)" ::: "memory");
;                         const int L = fr + 16 * fq, tt = L & 31, hf = L >> 5, T = u.pn * BM + bj * HALF + wc * 32 + tt, t = T & (SEQ - 1);
; #pragma unroll
;                         for (int part = 0; part < 2; ++part) { const LAS bf16_t* sp = tl + part * 512 + (hf * 8) * 32 + tt; u32x4 w8;
;                             w8.x = (unsigned)sp[0] | ((unsigned)sp[32] << 16); w8.y = (unsigned)sp[64] | ((unsigned)sp[96] << 16); w8.z = (unsigned)sp[128] | ((unsigned)sp[160] << 16); w8.w = (unsigned)sp[192] | ((unsigned)sp[224] << 16);
;                             const int dk0 = wr * 64 + 16 * m + 8 * hf + 128 * part;
;                             *(u32x4*)(KF + ((((size_t)(T >> 13) * 4 + head) * 512 + (t >> 4)) * 8 + (dk0 >> 5)) * 512 + ((t & 15) + 16 * ((dk0 >> 3) & 3)) * 8) = w8; }
;                         asm volatile("s_waitcnt lgkmcnt(0)" ::: "memory");
.LBB0_1628:
	v_pk_mul_f32 v[24:25], v[24:25], s[10:11] op_sel_hi:[1,0]
	v_pk_mul_f32 v[22:23], v[22:23], s[10:11] op_sel_hi:[1,0]
	v_pk_mul_f32 v[26:27], v[20:21], s[10:11] op_sel_hi:[1,0]
	v_cvt_pk_bf16_f32 v22, v22, v23
	v_cvt_pk_bf16_f32 v23, v24, v25
	v_cvt_pk_bf16_f32 v25, v26, v27
	v_add_co_u32_e32 v26, vcc, 0x8000, v58
	v_pk_mul_f32 v[28:29], v[18:19], s[10:11] op_sel_hi:[1,0]
	s_nop 0
	v_addc_co_u32_e32 v27, vcc, 0, v59, vcc
	v_cvt_pk_bf16_f32 v18, v48, v49
	v_cvt_pk_bf16_f32 v19, v46, v47
	v_cvt_pk_bf16_f32 v20, v38, v39
	v_cvt_pk_bf16_f32 v21, v40, v41
	v_cvt_pk_bf16_f32 v24, v28, v29
	s_and_b64 vcc, exec, s[8:9]
	global_store_dwordx4 v[58:59], v[18:21], off offset:256 sc1
	global_store_dwordx4 v[26:27], v[22:25], off offset:256 sc1
	s_cbranch_vccnz .LBB0_1630
	s_and_b32 s2, s23, 0x1f00
	ds_write_b128 v185, v[18:21]
	ds_write_b128 v185, v[22:25] offset:1024
	v_or_b32_e32 v18, s2, v188
	s_add_u32 s2, s56, 0x800
	s_addc_u32 s3, s57, 0
	v_lshrrev_b32_e32 v18, 4, v18
	s_waitcnt lgkmcnt(0)
	v_or_b32_e32 v18, s2, v18
	v_mov_b32_e32 v19, s3
	v_lshlrev_b64 v[22:23], 13, v[18:19]
	ds_read_u16 v18, v186
	ds_read_u16 v19, v186 offset:64
	v_lshl_add_u64 v[22:23], s[20:21], 0, v[22:23]
	v_mov_b32_e32 v123, v151
	s_waitcnt lgkmcnt(0)
	v_lshl_or_b32 v18, v19, 16, v18
	ds_read_u16 v19, v186 offset:128
	ds_read_u16 v20, v186 offset:192
	s_waitcnt lgkmcnt(0)
	v_lshl_or_b32 v19, v20, 16, v19
	ds_read_u16 v20, v186 offset:256
	ds_read_u16 v21, v186 offset:320
	s_waitcnt lgkmcnt(0)
	v_lshl_or_b32 v20, v21, 16, v20
	ds_read_u16 v21, v186 offset:384
	ds_read_u16 v24, v186 offset:448
	s_waitcnt lgkmcnt(0)
	v_lshl_or_b32 v21, v24, 16, v21
	v_lshl_add_u64 v[24:25], v[22:23], 0, s[42:43]
	v_lshl_add_u64 v[24:25], v[24:25], 0, v[122:123]
	global_store_dwordx4 v[24:25], v[18:21], off offset:512 sc1
	ds_read_u16 v18, v186 offset:1024
	ds_read_u16 v19, v186 offset:1088
	v_lshl_add_u64 v[22:23], v[22:23], 0, s[46:47]
	v_lshl_add_u64 v[22:23], v[22:23], 0, v[122:123]
	s_waitcnt lgkmcnt(0)
	v_lshl_or_b32 v18, v19, 16, v18
	ds_read_u16 v19, v186 offset:1152
	ds_read_u16 v20, v186 offset:1216
	s_waitcnt lgkmcnt(0)
	v_lshl_or_b32 v19, v20, 16, v19
	ds_read_u16 v20, v186 offset:1280
	ds_read_u16 v21, v186 offset:1344
	s_waitcnt lgkmcnt(0)
	v_lshl_or_b32 v20, v21, 16, v20
	ds_read_u16 v21, v186 offset:1408
	ds_read_u16 v24, v186 offset:1472
	s_waitcnt lgkmcnt(0)
	v_lshl_or_b32 v21, v24, 16, v21
	global_store_dwordx4 v[22:23], v[18:21], off offset:512 sc1
	s_waitcnt lgkmcnt(0)

; #define LAS __attribute__((address_space(3)))
; __device__ __forceinline__ u32x4 pack8(const f32x4 a, const f32x4 b) { u32x4 w; w.x = cvt_pk_bf16(a[0], a[1]); w.y = cvt_pk_bf16(a[2], a[3]); w.z = cvt_pk_bf16(b[0], b[1]); w.w = cvt_pk_bf16(b[2], b[3]); return w; }
;     __device__ __forceinline__ void operator()(const f32x4 (&acc)[2][2][4][2], const Unit& u, int wr, int wc, int fr, int fq) const {
;     ...
;                             o1[n] = (x1 * cc - x2 * ss) * 0.0625f; o2[n] = (x1 * ss + x2 * cc) * 0.0625f;
;                         } else { o1[n] = x1 * 0.0625f; o2[n] = x2 * 0.0625f; }
;                     }
;                     const int dk = wr * 64 + f; bf16_t* fp = KT + ((((size_t)head * 132 + 2 * u.pn + bj) * 8 + (dk >> 5)) * 8 + 2 * wc + (fq >> 1)) * 512 + (32 * (fq & 1) + (dk & 31)) * 8;
;                     if (u.kq != 1) *(u32x4*)(fp) = pack8(o1[0], o1[1]);
;                     if (u.kq != 0) *(u32x4*)(fp + (size_t)4 * 8 * 512) = pack8(o2[0], o2[1]);
;                     if (lat) {
;                         LAS bf16_t* tl = (LAS bf16_t*)(scr + (wr * 4 + wc) * 2048);
;                         *(LAS u32x4*)(tl + fr * 32 + 8 * fq) = pack8(o1[0], o1[1]);
;                         *(LAS u32x4*)(tl + 512 + fr * 32 + 8 * fq) = pack8(o2[0], o2[1]);
;                         asm volatile("s_waitcnt lgkmcnt(0)" ::: "memory");
;                         const int L = fr + 16 * fq, tt = L & 31, hf = L >> 5, T = u.pn * BM + bj * HALF + wc * 32 + tt, t = T & (SEQ - 1);
; #pragma unroll
;                         for (int part = 0; part < 2; ++part) { const LAS bf16_t* sp = tl + part * 512 + (hf * 8) * 32 + tt; u32x4 w8;
;                             w8.x = (unsigned)sp[0] | ((unsigned)sp[32] << 16); w8.y = (unsigned)sp[64] | ((unsigned)sp[96] << 16); w8.z = (unsigned)sp[128] | ((unsigned)sp[160] << 16); w8.w = (unsigned)sp[192] | ((unsigned)sp[224] << 16);
;                             const int dk0 = wr * 64 + 16 * m + 8 * hf + 128 * part;
;                             *(u32x4*)(KF + ((((size_t)(T >> 13) * 4 + head) * 512 + (t >> 4)) * 8 + (dk0 >> 5)) * 512 + ((t & 15) + 16 * ((dk0 >> 3) & 3)) * 8) = w8; }
;                         asm volatile("s_waitcnt lgkmcnt(0)" ::: "memory");
.LBB0_1646:
	v_pk_mul_f32 v[8:9], v[8:9], s[10:11] op_sel_hi:[1,0]
	v_pk_mul_f32 v[6:7], v[6:7], s[10:11] op_sel_hi:[1,0]
	v_pk_mul_f32 v[10:11], v[4:5], s[10:11] op_sel_hi:[1,0]
	v_cvt_pk_bf16_f32 v6, v6, v7
	v_cvt_pk_bf16_f32 v7, v8, v9
	v_cvt_pk_bf16_f32 v9, v10, v11
	v_add_co_u32_e32 v10, vcc, 0x8000, v42
	v_pk_mul_f32 v[12:13], v[2:3], s[10:11] op_sel_hi:[1,0]
	s_nop 0
	v_addc_co_u32_e32 v11, vcc, 0, v43, vcc
	v_cvt_pk_bf16_f32 v2, v28, v29
	v_cvt_pk_bf16_f32 v3, v26, v27
	v_cvt_pk_bf16_f32 v4, v22, v23
	v_cvt_pk_bf16_f32 v5, v24, v25
	v_cvt_pk_bf16_f32 v8, v12, v13
	s_and_b64 vcc, exec, s[8:9]
	global_store_dwordx4 v[42:43], v[2:5], off offset:256 sc1
	global_store_dwordx4 v[10:11], v[6:9], off offset:256 sc1
	s_cbranch_vccnz .LBB0_1648
	ds_write_b128 v185, v[2:5]
	ds_write_b128 v185, v[6:9] offset:1024
	s_waitcnt lgkmcnt(0)
	ds_read_u16 v4, v186
	ds_read_u16 v5, v186 offset:64
	ds_read_u16 v8, v186 offset:128
	ds_read_u16 v9, v186 offset:192
	ds_read_u16 v10, v186 offset:256
	ds_read_u16 v11, v186 offset:320
	ds_read_u16 v12, v186 offset:384
	ds_read_u16 v13, v186 offset:448
	s_and_b32 s0, s23, 0x1f00
	v_or_b32_e32 v2, s0, v188
	s_add_u32 s0, s56, 0x800
	s_addc_u32 s1, s57, 0
	v_lshrrev_b32_e32 v2, 4, v2
	v_or3_b32 v2, v2, s0, 8
	v_mov_b32_e32 v3, s1
	v_lshlrev_b64 v[6:7], 13, v[2:3]
	s_waitcnt lgkmcnt(0)
	v_lshl_or_b32 v2, v5, 16, v4
	v_lshl_or_b32 v4, v11, 16, v10
	v_lshl_or_b32 v5, v13, 16, v12
	ds_read_u16 v10, v186 offset:1024
	ds_read_u16 v11, v186 offset:1088
	ds_read_u16 v12, v186 offset:1152
	ds_read_u16 v13, v186 offset:1216
	ds_read_u16 v14, v186 offset:1280
	ds_read_u16 v15, v186 offset:1344
	ds_read_u16 v16, v186 offset:1408
	ds_read_u16 v17, v186 offset:1472
	v_lshl_add_u64 v[6:7], s[20:21], 0, v[6:7]
	v_lshl_or_b32 v3, v9, 16, v8
	v_lshl_add_u64 v[8:9], v[6:7], 0, s[42:43]
	v_mov_b32_e32 v123, v151
	v_lshl_add_u64 v[8:9], v[8:9], 0, v[122:123]
	v_lshl_add_u64 v[6:7], v[6:7], 0, s[46:47]
	global_store_dwordx4 v[8:9], v[2:5], off offset:512 sc1
	v_lshl_add_u64 v[6:7], v[6:7], 0, v[122:123]
	s_waitcnt lgkmcnt(0)
	v_lshl_or_b32 v2, v11, 16, v10
	v_lshl_or_b32 v3, v13, 16, v12
	v_lshl_or_b32 v4, v15, 16, v14
	v_lshl_or_b32 v5, v17, 16, v16
	global_store_dwordx4 v[6:7], v[2:5], off offset:512 sc1
	s_waitcnt lgkmcnt(0)

; __device__ __forceinline__ u32x4 pack8(const f32x4 a, const f32x4 b) { u32x4 w; w.x = cvt_pk_bf16(a[0], a[1]); w.y = cvt_pk_bf16(a[2], a[3]); w.z = cvt_pk_bf16(b[0], b[1]); w.w = cvt_pk_bf16(b[2], b[3]); return w; }
;     __device__ __forceinline__ void operator()(const f32x4 (&acc)[2][2][4][2], const Unit& u, int wr, int wc, int fr, int fq) const {
;     ...
;             const int rb = (u.pm - 8) * BM + wr * 64 + fr;
; #pragma unroll
;             for (int ai = 0; ai < 2; ++ai) { if (u.kq >= 0 && u.kq != ai) continue;
; #pragma unroll
;                 for (int m = 0; m < 4; ++m)
; #pragma unroll
;                     for (int bj = 0; bj < 2; ++bj) *(u32x4*)(VT + (size_t)(rb + ai * HALF + m * 16) * MT + col0 + bj * HALF) = pack8(acc[ai][bj][m][0], acc[ai][bj][m][1]); }
.LBB0_1671:
	s_lshl_b32 s0, s28, 8
	v_lshl_or_b32 v130, v199, 3, s0
	s_lshl_b32 s0, s8, 8
	s_addk_i32 s0, 0xf800
	v_or_b32_e32 v133, s43, v130
	v_or_b32_e32 v130, s0, v1
	v_add_u32_e32 v132, s42, v130
	v_mov_b32_e32 v131, 0
	s_mov_b64 s[0:1], -1
	s_and_b64 vcc, exec, s[2:3]
	s_cbranch_vccz .LBB0_1673
	v_readlane_b32 s0, v250, 36
	v_readlane_b32 s1, v250, 37
	v_add_u32_e32 v130, 0x80, v132
	s_mov_b32 s6, 0x8400
	v_mov_b64_e32 v[138:139], s[0:1]
	v_mad_i64_i32 v[140:141], s[0:1], v130, s6, v[138:139]
	v_lshlrev_b32_e32 v130, 1, v133
	v_cvt_pk_bf16_f32 v134, v126, v127
	v_cvt_pk_bf16_f32 v135, v128, v129
	v_cvt_pk_bf16_f32 v136, v122, v123
	v_cvt_pk_bf16_f32 v137, v124, v125
	v_lshl_add_u64 v[140:141], v[140:141], 0, v[130:131]
	global_store_dwordx4 v[140:141], v[134:137], off sc1
	s_nop 1
	v_cvt_pk_bf16_f32 v134, v110, v111
	v_cvt_pk_bf16_f32 v135, v112, v113
	v_cvt_pk_bf16_f32 v136, v106, v107
	v_cvt_pk_bf16_f32 v137, v108, v109
	global_store_dwordx4 v[140:141], v[134:137], off offset:256 sc1
	v_add_u32_e32 v140, 0x90, v132
	v_mad_i64_i32 v[140:141], s[0:1], v140, s6, v[138:139]
	v_cvt_pk_bf16_f32 v134, v94, v95
	v_cvt_pk_bf16_f32 v135, v96, v97
	v_cvt_pk_bf16_f32 v136, v90, v91
	v_cvt_pk_bf16_f32 v137, v92, v93
	v_lshl_add_u64 v[140:141], v[140:141], 0, v[130:131]
	global_store_dwordx4 v[140:141], v[134:137], off sc1
	s_nop 1
	v_cvt_pk_bf16_f32 v134, v78, v79
	v_cvt_pk_bf16_f32 v135, v80, v81
	v_cvt_pk_bf16_f32 v136, v74, v75
	v_cvt_pk_bf16_f32 v137, v76, v77
	global_store_dwordx4 v[140:141], v[134:137], off offset:256 sc1
	v_add_u32_e32 v140, 0xa0, v132
	v_mad_i64_i32 v[140:141], s[0:1], v140, s6, v[138:139]
	v_cvt_pk_bf16_f32 v134, v62, v63
	v_cvt_pk_bf16_f32 v135, v64, v65
	v_cvt_pk_bf16_f32 v136, v58, v59
	v_cvt_pk_bf16_f32 v137, v60, v61
	v_lshl_add_u64 v[140:141], v[140:141], 0, v[130:131]
	global_store_dwordx4 v[140:141], v[134:137], off sc1
	s_nop 1
	v_cvt_pk_bf16_f32 v134, v46, v47
	v_cvt_pk_bf16_f32 v135, v48, v49
	v_cvt_pk_bf16_f32 v136, v42, v43
	v_cvt_pk_bf16_f32 v137, v44, v45
	global_store_dwordx4 v[140:141], v[134:137], off offset:256 sc1
	v_add_u32_e32 v140, 0xb0, v132
	v_mad_i64_i32 v[138:139], s[0:1], v140, s6, v[138:139]
	v_cvt_pk_bf16_f32 v134, v30, v31
	v_cvt_pk_bf16_f32 v135, v32, v33
	v_cvt_pk_bf16_f32 v136, v26, v27
	v_cvt_pk_bf16_f32 v137, v28, v29
	v_lshl_add_u64 v[130:131], v[138:139], 0, v[130:131]
	global_store_dwordx4 v[130:131], v[134:137], off sc1
	s_mov_b64 s[0:1], 0
	s_nop 0
	v_cvt_pk_bf16_f32 v134, v14, v15
	v_cvt_pk_bf16_f32 v135, v16, v17
	v_cvt_pk_bf16_f32 v136, v2, v3
	v_cvt_pk_bf16_f32 v137, v4, v5
	global_store_dwordx4 v[130:131], v[134:137], off offset:256 sc1
.LBB0_1673:
	s_andn2_b64 vcc, exec, s[0:1]
	s_cbranch_vccnz .LBB0_1675
	v_readlane_b32 s0, v250, 36
	v_readlane_b32 s1, v250, 37
	s_mov_b32 s6, 0x8400
	v_lshlrev_b32_e32 v140, 1, v133
	v_mov_b64_e32 v[138:139], s[0:1]
	v_mad_i64_i32 v[130:131], s[0:1], v132, s6, v[138:139]
	v_mov_b32_e32 v141, 0
	v_cvt_pk_bf16_f32 v134, v114, v115
	v_cvt_pk_bf16_f32 v135, v116, v117
	v_cvt_pk_bf16_f32 v136, v118, v119
	v_cvt_pk_bf16_f32 v137, v120, v121
	v_lshl_add_u64 v[130:131], v[130:131], 0, v[140:141]
	global_store_dwordx4 v[130:131], v[134:137], off sc1
	v_cvt_pk_bf16_f32 v133, v24, v25
	s_nop 0
	v_cvt_pk_bf16_f32 v134, v98, v99
	v_cvt_pk_bf16_f32 v135, v100, v101
	v_cvt_pk_bf16_f32 v136, v102, v103
	v_cvt_pk_bf16_f32 v137, v104, v105
	global_store_dwordx4 v[130:131], v[134:137], off offset:256 sc1
	v_or_b32_e32 v130, 16, v132
	v_mad_i64_i32 v[130:131], s[0:1], v130, s6, v[138:139]
	v_cvt_pk_bf16_f32 v134, v82, v83
	v_cvt_pk_bf16_f32 v135, v84, v85
	v_cvt_pk_bf16_f32 v136, v86, v87
	v_cvt_pk_bf16_f32 v137, v88, v89
	v_lshl_add_u64 v[130:131], v[130:131], 0, v[140:141]
	global_store_dwordx4 v[130:131], v[134:137], off sc1
	s_nop 1
	v_cvt_pk_bf16_f32 v134, v66, v67
	v_cvt_pk_bf16_f32 v135, v68, v69
	v_cvt_pk_bf16_f32 v136, v70, v71
	v_cvt_pk_bf16_f32 v137, v72, v73
	global_store_dwordx4 v[130:131], v[134:137], off offset:256 sc1
	v_or_b32_e32 v130, 32, v132
	v_mad_i64_i32 v[130:131], s[0:1], v130, s6, v[138:139]
	v_cvt_pk_bf16_f32 v134, v50, v51
	v_cvt_pk_bf16_f32 v135, v52, v53
	v_cvt_pk_bf16_f32 v136, v54, v55
	v_cvt_pk_bf16_f32 v137, v56, v57
	v_lshl_add_u64 v[130:131], v[130:131], 0, v[140:141]
	global_store_dwordx4 v[130:131], v[134:137], off sc1
	s_nop 1
	v_cvt_pk_bf16_f32 v134, v34, v35
	v_cvt_pk_bf16_f32 v135, v36, v37
	v_cvt_pk_bf16_f32 v136, v38, v39
	v_cvt_pk_bf16_f32 v137, v40, v41
	global_store_dwordx4 v[130:131], v[134:137], off offset:256 sc1
	v_cvt_pk_bf16_f32 v130, v18, v19
	v_cvt_pk_bf16_f32 v131, v20, v21
	v_or_b32_e32 v134, 48, v132
	v_mad_i64_i32 v[134:135], s[0:1], v134, s6, v[138:139]
	v_cvt_pk_bf16_f32 v132, v22, v23
	v_lshl_add_u64 v[134:135], v[134:135], 0, v[140:141]
	global_store_dwordx4 v[134:135], v[130:133], off sc1
	s_nop 1
	v_cvt_pk_bf16_f32 v130, v6, v7
	v_cvt_pk_bf16_f32 v131, v8, v9
	v_cvt_pk_bf16_f32 v132, v10, v11
	v_cvt_pk_bf16_f32 v133, v12, v13
	global_store_dwordx4 v[134:135], v[130:133], off offset:256 sc1

; __device__ __forceinline__ u32x4 pack8(const f32x4 a, const f32x4 b) { u32x4 w; w.x = cvt_pk_bf16(a[0], a[1]); w.y = cvt_pk_bf16(a[2], a[3]); w.z = cvt_pk_bf16(b[0], b[1]); w.w = cvt_pk_bf16(b[2], b[3]); return w; }
;     __device__ __forceinline__ void operator()(const f32x4 (&acc)[2][2][4][2], const Unit& u, int wr, int wc, int fr, int fq) const {
;     ...
;                             o1[n] = (x1 * cc - x2 * ss) * 0.0625f; o2[n] = (x1 * ss + x2 * cc) * 0.0625f;
;                         } else { o1[n] = x1 * 0.0625f; o2[n] = x2 * 0.0625f; }
;                     }
;                     const int dk = wr * 64 + f; bf16_t* fp = KT + ((((size_t)head * 132 + 2 * u.pn + bj) * 8 + (dk >> 5)) * 8 + 2 * wc + (fq >> 1)) * 512 + (32 * (fq & 1) + (dk & 31)) * 8;
;                     if (u.kq != 1) *(u32x4*)(fp) = pack8(o1[0], o1[1]);
;                     if (u.kq != 0) *(u32x4*)(fp + (size_t)4 * 8 * 512) = pack8(o2[0], o2[1]);
.LBB0_1676:
	s_nop 0
	v_lshlrev_b32_e32 v130, 5, v199
	s_lshl_b32 s0, s29, 1
	v_and_b32_e32 v136, 32, v130
	v_lshlrev_b32_e32 v130, 9, v199
	s_ashr_i32 s1, s0, 31
	v_and_b32_e32 v130, 0x400, v130
	s_lshl_b64 s[6:7], s[0:1], 13
	s_add_i32 s1, s8, -4
	v_lshl_or_b32 v130, s9, 11, v130
	s_mul_hi_i32 s9, s1, 0x84
	s_mulk_i32 s1, 0x84
	s_lshl_b32 s8, s28, 1
	s_add_u32 s8, s1, s8
	s_addc_u32 s9, s9, 0
	s_lshl_b64 s[8:9], s[8:9], 16
	v_readlane_b32 s1, v250, 8
	s_add_u32 s10, s1, s8
	v_readlane_b32 s1, v250, 6
	s_addc_u32 s11, s1, s9
	s_add_u32 s8, s10, s6
	v_or_b32_e32 v134, v136, v1
	v_mov_b32_e32 v131, 0
	s_addc_u32 s9, s11, s7
	v_lshlrev_b32_e32 v137, 3, v134
	v_lshl_add_u64 v[132:133], s[8:9], 0, v[130:131]
	v_lshlrev_b32_e32 v134, 4, v134
	v_mov_b32_e32 v135, v131
	v_lshl_add_u64 v[134:135], v[132:133], 0, v[134:135]
	s_mov_b64 s[8:9], -1
	s_and_b64 vcc, exec, s[2:3]
	s_cbranch_vccz .LBB0_1678
	s_mov_b32 s8, 0x3d800000
	v_pk_mul_f32 v[126:127], v[126:127], s[8:9] op_sel_hi:[1,0]
	v_pk_mul_f32 v[128:129], v[128:129], s[8:9] op_sel_hi:[1,0]
	v_pk_mul_f32 v[138:139], v[124:125], s[8:9] op_sel_hi:[1,0]
	v_pk_mul_f32 v[124:125], v[122:123], s[8:9] op_sel_hi:[1,0]
	v_cvt_pk_bf16_f32 v122, v126, v127
	v_add_co_u32_e32 v126, vcc, 0x8000, v134
	v_cvt_pk_bf16_f32 v123, v128, v129
	v_cvt_pk_bf16_f32 v124, v124, v125
	v_cvt_pk_bf16_f32 v125, v138, v139
	v_addc_co_u32_e32 v127, vcc, 0, v135, vcc
	global_store_dwordx4 v[126:127], v[122:125], off sc1
	s_mov_b64 s[8:9], 0
.LBB0_1678:
	s_andn2_b64 vcc, exec, s[8:9]
	s_cbranch_vccnz .LBB0_1680
	s_mov_b32 s8, 0x3d800000
	v_pk_mul_f32 v[120:121], v[120:121], s[8:9] op_sel_hi:[1,0]
	v_pk_mul_f32 v[118:119], v[118:119], s[8:9] op_sel_hi:[1,0]
	v_pk_mul_f32 v[116:117], v[116:117], s[8:9] op_sel_hi:[1,0]
	v_pk_mul_f32 v[114:115], v[114:115], s[8:9] op_sel_hi:[1,0]
	s_nop 0
	v_cvt_pk_bf16_f32 v114, v114, v115
	v_cvt_pk_bf16_f32 v115, v116, v117
	v_cvt_pk_bf16_f32 v116, v118, v119
	v_cvt_pk_bf16_f32 v117, v120, v121
	global_store_dwordx4 v[134:135], v[114:117], off sc1
.LBB0_1680:
	s_add_u32 s8, s10, 0x10000
	s_addc_u32 s9, s11, 0
	s_add_u32 s6, s8, s6
	s_addc_u32 s7, s9, s7
	v_lshl_add_u64 v[116:117], s[6:7], 0, v[130:131]
	v_lshlrev_b32_e32 v114, 1, v137
	v_mov_b32_e32 v115, 0
	v_lshl_add_u64 v[118:119], v[116:117], 0, v[114:115]
	s_mov_b64 s[6:7], -1
	s_and_b64 vcc, exec, s[2:3]
	s_cbranch_vccz .LBB0_1682
	s_mov_b32 s6, 0x3d800000
	v_pk_mul_f32 v[110:111], v[110:111], s[6:7] op_sel_hi:[1,0]
	v_pk_mul_f32 v[112:113], v[112:113], s[6:7] op_sel_hi:[1,0]
	v_pk_mul_f32 v[120:121], v[108:109], s[6:7] op_sel_hi:[1,0]
	v_pk_mul_f32 v[108:109], v[106:107], s[6:7] op_sel_hi:[1,0]
	v_cvt_pk_bf16_f32 v106, v110, v111
	v_add_co_u32_e32 v110, vcc, 0x8000, v118
	v_cvt_pk_bf16_f32 v107, v112, v113
	v_cvt_pk_bf16_f32 v108, v108, v109
	v_cvt_pk_bf16_f32 v109, v120, v121
	v_addc_co_u32_e32 v111, vcc, 0, v119, vcc
	global_store_dwordx4 v[110:111], v[106:109], off sc1
	s_mov_b64 s[6:7], 0
.LBB0_1682:
	s_andn2_b64 vcc, exec, s[6:7]
	s_cbranch_vccnz .LBB0_1684
	s_mov_b32 s6, 0x3d800000
	v_pk_mul_f32 v[104:105], v[104:105], s[6:7] op_sel_hi:[1,0]
	v_pk_mul_f32 v[102:103], v[102:103], s[6:7] op_sel_hi:[1,0]
	v_pk_mul_f32 v[100:101], v[100:101], s[6:7] op_sel_hi:[1,0]
	v_pk_mul_f32 v[98:99], v[98:99], s[6:7] op_sel_hi:[1,0]
	s_nop 0
	v_cvt_pk_bf16_f32 v98, v98, v99
	v_cvt_pk_bf16_f32 v99, v100, v101
	v_cvt_pk_bf16_f32 v100, v102, v103
	v_cvt_pk_bf16_f32 v101, v104, v105
	global_store_dwordx4 v[118:119], v[98:101], off sc1
.LBB0_1684:
	s_nop 1
	v_or3_b32 v98, v1, v136, 16
	v_lshlrev_b32_e32 v1, 3, v98
	v_mov_b32_e32 v99, 0
	v_lshlrev_b32_e32 v98, 4, v98
	v_lshl_add_u64 v[98:99], v[132:133], 0, v[98:99]
	s_mov_b64 s[6:7], -1
	s_and_b64 vcc, exec, s[2:3]
	s_cbranch_vccz .LBB0_1686
	s_mov_b32 s6, 0x3d800000
	v_pk_mul_f32 v[94:95], v[94:95], s[6:7] op_sel_hi:[1,0]
	v_pk_mul_f32 v[96:97], v[96:97], s[6:7] op_sel_hi:[1,0]
	v_pk_mul_f32 v[100:101], v[92:93], s[6:7] op_sel_hi:[1,0]
	v_pk_mul_f32 v[92:93], v[90:91], s[6:7] op_sel_hi:[1,0]
	v_cvt_pk_bf16_f32 v90, v94, v95
	v_add_co_u32_e32 v94, vcc, 0x8000, v98
	v_cvt_pk_bf16_f32 v91, v96, v97
	v_cvt_pk_bf16_f32 v92, v92, v93
	v_cvt_pk_bf16_f32 v93, v100, v101
	v_addc_co_u32_e32 v95, vcc, 0, v99, vcc
	global_store_dwordx4 v[94:95], v[90:93], off sc1
	s_mov_b64 s[6:7], 0
.LBB0_1686:
	s_andn2_b64 vcc, exec, s[6:7]
	s_cbranch_vccnz .LBB0_1688
	s_mov_b32 s6, 0x3d800000
	v_pk_mul_f32 v[88:89], v[88:89], s[6:7] op_sel_hi:[1,0]
	v_pk_mul_f32 v[86:87], v[86:87], s[6:7] op_sel_hi:[1,0]
	v_pk_mul_f32 v[84:85], v[84:85], s[6:7] op_sel_hi:[1,0]
	v_pk_mul_f32 v[82:83], v[82:83], s[6:7] op_sel_hi:[1,0]
	s_nop 0
	v_cvt_pk_bf16_f32 v82, v82, v83
	v_cvt_pk_bf16_f32 v83, v84, v85
	v_cvt_pk_bf16_f32 v84, v86, v87
	v_cvt_pk_bf16_f32 v85, v88, v89
	global_store_dwordx4 v[98:99], v[82:85], off sc1
.LBB0_1688:
	s_nop 1
	v_lshlrev_b32_e32 v82, 1, v1
	v_mov_b32_e32 v83, 0
	v_lshl_add_u64 v[82:83], v[116:117], 0, v[82:83]
	s_mov_b64 s[6:7], -1
	s_and_b64 vcc, exec, s[2:3]
	s_cbranch_vccz .LBB0_1690
	s_mov_b32 s6, 0x3d800000
	v_pk_mul_f32 v[78:79], v[78:79], s[6:7] op_sel_hi:[1,0]
	v_pk_mul_f32 v[80:81], v[80:81], s[6:7] op_sel_hi:[1,0]
	v_pk_mul_f32 v[84:85], v[76:77], s[6:7] op_sel_hi:[1,0]
	v_pk_mul_f32 v[76:77], v[74:75], s[6:7] op_sel_hi:[1,0]
	v_cvt_pk_bf16_f32 v74, v78, v79
	v_add_co_u32_e32 v78, vcc, 0x8000, v82
	v_cvt_pk_bf16_f32 v75, v80, v81
	v_cvt_pk_bf16_f32 v76, v76, v77
	v_cvt_pk_bf16_f32 v77, v84, v85
	v_addc_co_u32_e32 v79, vcc, 0, v83, vcc
	global_store_dwordx4 v[78:79], v[74:77], off sc1
	s_mov_b64 s[6:7], 0
; __device__ __forceinline__ u32x4 pack8(const f32x4 a, const f32x4 b) { u32x4 w; w.x = cvt_pk_bf16(a[0], a[1]); w.y = cvt_pk_bf16(a[2], a[3]); w.z = cvt_pk_bf16(b[0], b[1]); w.w = cvt_pk_bf16(b[2], b[3]); return w; }
;     __device__ __forceinline__ void operator()(const f32x4 (&acc)[2][2][4][2], const Unit& u, int wr, int wc, int fr, int fq) const {
;     ...
;                             o1[n] = (x1 * cc - x2 * ss) * 0.0625f; o2[n] = (x1 * ss + x2 * cc) * 0.0625f;
;                         } else { o1[n] = x1 * 0.0625f; o2[n] = x2 * 0.0625f; }
;                     }
;                     const int dk = wr * 64 + f; bf16_t* fp = KT + ((((size_t)head * 132 + 2 * u.pn + bj) * 8 + (dk >> 5)) * 8 + 2 * wc + (fq >> 1)) * 512 + (32 * (fq & 1) + (dk & 31)) * 8;
;                     if (u.kq != 1) *(u32x4*)(fp) = pack8(o1[0], o1[1]);
;                     if (u.kq != 0) *(u32x4*)(fp + (size_t)4 * 8 * 512) = pack8(o2[0], o2[1]);
.LBB0_1690:
	s_andn2_b64 vcc, exec, s[6:7]
	s_cbranch_vccnz .LBB0_1692
	s_mov_b32 s6, 0x3d800000
	v_pk_mul_f32 v[72:73], v[72:73], s[6:7] op_sel_hi:[1,0]
	v_pk_mul_f32 v[70:71], v[70:71], s[6:7] op_sel_hi:[1,0]
	v_pk_mul_f32 v[68:69], v[68:69], s[6:7] op_sel_hi:[1,0]
	v_pk_mul_f32 v[66:67], v[66:67], s[6:7] op_sel_hi:[1,0]
	s_nop 0
	v_cvt_pk_bf16_f32 v66, v66, v67
	v_cvt_pk_bf16_f32 v67, v68, v69
	v_cvt_pk_bf16_f32 v68, v70, v71
	v_cvt_pk_bf16_f32 v69, v72, v73
	global_store_dwordx4 v[82:83], v[66:69], off sc1
.LBB0_1692:
	s_or_b32 s0, s0, 1
	s_ashr_i32 s1, s0, 31
	s_lshl_b64 s[0:1], s[0:1], 13
	s_add_u32 s6, s10, s0
	s_addc_u32 s7, s11, s1
	v_lshl_add_u64 v[66:67], s[6:7], 0, v[130:131]
	v_mov_b32_e32 v115, 0
	v_lshl_add_u64 v[66:67], v[66:67], 0, v[114:115]
	s_mov_b64 s[6:7], -1
	s_and_b64 vcc, exec, s[2:3]
	s_cbranch_vccz .LBB0_1694
	s_mov_b32 s6, 0x3d800000
	v_pk_mul_f32 v[62:63], v[62:63], s[6:7] op_sel_hi:[1,0]
	v_pk_mul_f32 v[64:65], v[64:65], s[6:7] op_sel_hi:[1,0]
	v_pk_mul_f32 v[68:69], v[60:61], s[6:7] op_sel_hi:[1,0]
	v_pk_mul_f32 v[60:61], v[58:59], s[6:7] op_sel_hi:[1,0]
	v_cvt_pk_bf16_f32 v58, v62, v63
	v_add_co_u32_e32 v62, vcc, 0x8000, v66
	v_cvt_pk_bf16_f32 v59, v64, v65
	v_cvt_pk_bf16_f32 v60, v60, v61
	v_cvt_pk_bf16_f32 v61, v68, v69
	v_addc_co_u32_e32 v63, vcc, 0, v67, vcc
	global_store_dwordx4 v[62:63], v[58:61], off sc1
	s_mov_b64 s[6:7], 0
.LBB0_1694:
	s_andn2_b64 vcc, exec, s[6:7]
	s_cbranch_vccnz .LBB0_1696
	s_mov_b32 s6, 0x3d800000
	v_pk_mul_f32 v[56:57], v[56:57], s[6:7] op_sel_hi:[1,0]
	v_pk_mul_f32 v[54:55], v[54:55], s[6:7] op_sel_hi:[1,0]
	v_pk_mul_f32 v[52:53], v[52:53], s[6:7] op_sel_hi:[1,0]
	v_pk_mul_f32 v[50:51], v[50:51], s[6:7] op_sel_hi:[1,0]
	s_nop 0
	v_cvt_pk_bf16_f32 v50, v50, v51
	v_cvt_pk_bf16_f32 v51, v52, v53
	v_cvt_pk_bf16_f32 v52, v54, v55
	v_cvt_pk_bf16_f32 v53, v56, v57
	global_store_dwordx4 v[66:67], v[50:53], off sc1
.LBB0_1696:
	s_add_u32 s0, s8, s0
	s_addc_u32 s1, s9, s1
	v_lshl_add_u64 v[50:51], s[0:1], 0, v[130:131]
	v_mov_b32_e32 v115, 0
	v_lshl_add_u64 v[50:51], v[50:51], 0, v[114:115]
	s_mov_b64 s[0:1], -1
	s_and_b64 vcc, exec, s[2:3]
	s_cbranch_vccz .LBB0_1698
	s_mov_b32 s0, 0x3d800000
	v_pk_mul_f32 v[46:47], v[46:47], s[0:1] op_sel_hi:[1,0]
	v_pk_mul_f32 v[48:49], v[48:49], s[0:1] op_sel_hi:[1,0]
	v_pk_mul_f32 v[52:53], v[44:45], s[0:1] op_sel_hi:[1,0]
	v_pk_mul_f32 v[44:45], v[42:43], s[0:1] op_sel_hi:[1,0]
	v_cvt_pk_bf16_f32 v42, v46, v47
	v_add_co_u32_e32 v46, vcc, 0x8000, v50
	v_cvt_pk_bf16_f32 v43, v48, v49
	v_cvt_pk_bf16_f32 v44, v44, v45
	v_cvt_pk_bf16_f32 v45, v52, v53
	v_addc_co_u32_e32 v47, vcc, 0, v51, vcc
	global_store_dwordx4 v[46:47], v[42:45], off sc1
	s_mov_b64 s[0:1], 0
.LBB0_1698:
	s_andn2_b64 vcc, exec, s[0:1]
	s_cbranch_vccnz .LBB0_1700
	s_mov_b32 s0, 0x3d800000
	v_pk_mul_f32 v[40:41], v[40:41], s[0:1] op_sel_hi:[1,0]
	v_pk_mul_f32 v[38:39], v[38:39], s[0:1] op_sel_hi:[1,0]
	v_pk_mul_f32 v[36:37], v[36:37], s[0:1] op_sel_hi:[1,0]
	v_pk_mul_f32 v[34:35], v[34:35], s[0:1] op_sel_hi:[1,0]
	s_nop 0
	v_cvt_pk_bf16_f32 v34, v34, v35
	v_cvt_pk_bf16_f32 v35, v36, v37
	v_cvt_pk_bf16_f32 v36, v38, v39
	v_cvt_pk_bf16_f32 v37, v40, v41
	global_store_dwordx4 v[50:51], v[34:37], off sc1
.LBB0_1700:
	s_mov_b64 s[0:1], 0x100
	s_nop 0
	v_lshl_add_u64 v[34:35], v[66:67], 0, s[0:1]
	s_mov_b64 s[0:1], -1
	s_and_b64 vcc, exec, s[2:3]
	s_cbranch_vccz .LBB0_1702
	s_mov_b32 s0, 0x3d800000
	v_pk_mul_f32 v[30:31], v[30:31], s[0:1] op_sel_hi:[1,0]
	v_pk_mul_f32 v[32:33], v[32:33], s[0:1] op_sel_hi:[1,0]
	v_pk_mul_f32 v[36:37], v[28:29], s[0:1] op_sel_hi:[1,0]
	v_pk_mul_f32 v[28:29], v[26:27], s[0:1] op_sel_hi:[1,0]
	v_cvt_pk_bf16_f32 v26, v30, v31
	v_add_co_u32_e32 v30, vcc, 0x8000, v34
	v_cvt_pk_bf16_f32 v27, v32, v33
	v_cvt_pk_bf16_f32 v28, v28, v29
	v_cvt_pk_bf16_f32 v29, v36, v37
	v_addc_co_u32_e32 v31, vcc, 0, v35, vcc
	global_store_dwordx4 v[30:31], v[26:29], off sc1
	s_mov_b64 s[0:1], 0
.LBB0_1702:
	s_andn2_b64 vcc, exec, s[0:1]
	s_cbranch_vccnz .LBB0_1704
	s_mov_b32 s0, 0x3d800000
	v_pk_mul_f32 v[24:25], v[24:25], s[0:1] op_sel_hi:[1,0]
	v_pk_mul_f32 v[22:23], v[22:23], s[0:1] op_sel_hi:[1,0]
	v_pk_mul_f32 v[20:21], v[20:21], s[0:1] op_sel_hi:[1,0]
	v_pk_mul_f32 v[18:19], v[18:19], s[0:1] op_sel_hi:[1,0]
	s_nop 0
	v_cvt_pk_bf16_f32 v18, v18, v19
	v_cvt_pk_bf16_f32 v19, v20, v21
	v_cvt_pk_bf16_f32 v20, v22, v23
	v_cvt_pk_bf16_f32 v21, v24, v25
	global_store_dwordx4 v[34:35], v[18:21], off sc1
.LBB0_1704:
	s_mov_b64 s[0:1], 0x100
	s_nop 0
	v_lshl_add_u64 v[18:19], v[50:51], 0, s[0:1]
	s_mov_b64 s[0:1], -1
	s_and_b64 vcc, exec, s[2:3]
	s_cbranch_vccz .LBB0_1706
	s_mov_b32 s0, 0x3d800000
	v_pk_mul_f32 v[14:15], v[14:15], s[0:1] op_sel_hi:[1,0]
	v_pk_mul_f32 v[16:17], v[16:17], s[0:1] op_sel_hi:[1,0]
	v_pk_mul_f32 v[20:21], v[4:5], s[0:1] op_sel_hi:[1,0]
	v_pk_mul_f32 v[4:5], v[2:3], s[0:1] op_sel_hi:[1,0]
	v_cvt_pk_bf16_f32 v2, v14, v15
	v_add_co_u32_e32 v14, vcc, 0x8000, v18
	v_cvt_pk_bf16_f32 v3, v16, v17
	v_cvt_pk_bf16_f32 v4, v4, v5
	v_cvt_pk_bf16_f32 v5, v20, v21
	v_addc_co_u32_e32 v15, vcc, 0, v19, vcc
	global_store_dwordx4 v[14:15], v[2:5], off sc1
	s_mov_b64 s[0:1], 0
.LBB0_1706:
	s_andn2_b64 vcc, exec, s[0:1]
	s_cbranch_vccnz .LBB0_1708
	s_mov_b32 s0, 0x3d800000
	v_pk_mul_f32 v[12:13], v[12:13], s[0:1] op_sel_hi:[1,0]
	v_pk_mul_f32 v[4:5], v[10:11], s[0:1] op_sel_hi:[1,0]
	v_pk_mul_f32 v[8:9], v[8:9], s[0:1] op_sel_hi:[1,0]
	v_pk_mul_f32 v[2:3], v[6:7], s[0:1] op_sel_hi:[1,0]
	v_cvt_pk_bf16_f32 v4, v4, v5
	v_cvt_pk_bf16_f32 v2, v2, v3
	v_cvt_pk_bf16_f32 v3, v8, v9
	v_cvt_pk_bf16_f32 v5, v12, v13
	global_store_dwordx4 v[18:19], v[2:5], off sc1

; __device__ __forceinline__ float wave_sum(float v) { WAVE_ALLREDUCE(op_add) return v; }
; __device__ __forceinline__ float silu_fast(float v) { return v * __builtin_amdgcn_rcpf(1.f + __builtin_amdgcn_exp2f(-1.4426950408889634f * v)); }
; __device__ __forceinline__ u32x4 pack8(const f32x4 a, const f32x4 b) { u32x4 w; w.x = cvt_pk_bf16(a[0], a[1]); w.y = cvt_pk_bf16(a[2], a[3]); w.z = cvt_pk_bf16(b[0], b[1]); w.w = cvt_pk_bf16(b[2], b[3]); return w; }
; __device__ __forceinline__ void ph_retout(const int vc, const Params& p) {
;     ...
;     for (int it = it0; it < ML * 4; it += its) {
;         const size_t o = off_of(it);
;         const u32x4 a = an, bq = bn, g = gn;
;         { const size_t on = off_of(it + its < ML * 4 ? it + its : it);
;           an = __builtin_nontemporal_load((const u32x4*)(Ob + on)); bn = __builtin_nontemporal_load((const u32x4*)(Ob + (size_t)ML * 2048 + on)); gn = __builtin_nontemporal_load((const u32x4*)(Gs + on)); }
;         const f32x4 s0 = {__uint_as_float(a.x << 16) + __uint_as_float(bq.x << 16), __uint_as_float(a.x & 0xffff0000u) + __uint_as_float(bq.x & 0xffff0000u),
;                           __uint_as_float(a.y << 16) + __uint_as_float(bq.y << 16), __uint_as_float(a.y & 0xffff0000u) + __uint_as_float(bq.y & 0xffff0000u)};
;         const f32x4 s1 = {__uint_as_float(a.z << 16) + __uint_as_float(bq.z << 16), __uint_as_float(a.z & 0xffff0000u) + __uint_as_float(bq.z & 0xffff0000u),
;                           __uint_as_float(a.w << 16) + __uint_as_float(bq.w << 16), __uint_as_float(a.w & 0xffff0000u) + __uint_as_float(bq.w & 0xffff0000u)};
;         const float ss = (s0[0] * s0[0] + s0[1] * s0[1]) + (s0[2] * s0[2] + s0[3] * s0[3]) + (s1[0] * s1[0] + s1[1] * s1[1]) + (s1[2] * s1[2] + s1[3] * s1[3]);
;         const float r = rsqrtf(wave_sum(ss) * (1.f / 512.f) + EPS);
;         f32x4 g0 = {__uint_as_float(g.x << 16), __uint_as_float(g.x & 0xffff0000u), __uint_as_float(g.y << 16), __uint_as_float(g.y & 0xffff0000u)};
;         f32x4 g1 = {__uint_as_float(g.z << 16), __uint_as_float(g.z & 0xffff0000u), __uint_as_float(g.w << 16), __uint_as_float(g.w & 0xffff0000u)};
; #pragma unroll
;         for (int j = 0; j < 4; ++j) { g0[j] = silu_fast(g0[j]); g1[j] = silu_fast(g1[j]); }
;         *(u32x4*)(WSP(bf16_t, OFF_A2B) + o) = pg8::pack8(g0 * s0 * r, g1 * s1 * r);
;     }
.LBB0_1862:
	v_add_u32_e32 v19, s22, v16
	v_cmp_gt_i32_e64 s[0:1], s14, v19
	s_waitcnt vmcnt(1)
	v_lshlrev_b32_e32 v34, 16, v3
	v_and_b32_e32 v35, 0xffff0000, v3
	v_cndmask_b32_e64 v3, v16, v19, s[0:1]
	v_lshlrev_b32_e32 v30, 16, v2
	v_and_b32_e32 v31, 0xffff0000, v2
	v_ashrrev_i32_e32 v2, 2, v3
	v_lshlrev_b32_e32 v32, 16, v4
	v_and_b32_e32 v33, 0xffff0000, v4
	v_lshlrev_b32_e32 v4, 9, v3
	v_ashrrev_i32_e32 v3, 31, v2
	v_and_or_b32 v4, v4, s15, v1
	v_lshlrev_b64 v[2:3], 12, v[2:3]
	s_waitcnt vmcnt(0)
	v_lshlrev_b32_e32 v22, 16, v10
	v_and_b32_e32 v23, 0xffff0000, v10
	v_lshlrev_b32_e32 v24, 16, v6
	v_and_b32_e32 v25, 0xffff0000, v6
	v_lshlrev_b32_e32 v10, 16, v11
	v_and_b32_e32 v11, 0xffff0000, v11
	v_lshlrev_b32_e32 v6, 16, v7
	v_and_b32_e32 v7, 0xffff0000, v7
	v_lshl_or_b32 v2, v4, 1, v2
	v_lshlrev_b32_e32 v26, 16, v12
	v_and_b32_e32 v27, 0xffff0000, v12
	v_lshlrev_b32_e32 v28, 16, v8
	v_and_b32_e32 v29, 0xffff0000, v8
	v_lshlrev_b32_e32 v12, 16, v13
	v_and_b32_e32 v13, 0xffff0000, v13
	v_lshlrev_b32_e32 v8, 16, v9
	v_and_b32_e32 v9, 0xffff0000, v9
	v_lshlrev_b32_e32 v36, 16, v5
	v_and_b32_e32 v37, 0xffff0000, v5
	v_pk_add_f32 v[22:23], v[22:23], v[24:25]
	v_pk_add_f32 v[24:25], v[10:11], v[6:7]
	v_lshl_add_u64 v[4:5], s[6:7], 0, v[2:3]
	v_lshl_add_u64 v[6:7], s[8:9], 0, v[2:3]
	v_lshl_add_u64 v[2:3], s[16:17], 0, v[2:3]
	v_pk_add_f32 v[26:27], v[26:27], v[28:29]
	v_pk_add_f32 v[28:29], v[12:13], v[8:9]
	global_load_dwordx4 v[10:13], v[4:5], off nt
	s_nop 0
	global_load_dwordx4 v[6:9], v[6:7], off nt
	s_nop 0
	global_load_dwordx4 v[2:5], v[2:3], off nt
	v_ashrrev_i32_e32 v20, 2, v16
	v_ashrrev_i32_e32 v21, 31, v20
	v_pk_mul_f32 v[38:39], v[22:23], v[22:23]
	v_pk_mul_f32 v[40:41], v[24:25], v[24:25]
	v_and_or_b32 v14, v17, s15, v1
	v_pk_mul_f32 v[42:43], v[26:27], v[26:27]
	v_lshlrev_b64 v[20:21], 12, v[20:21]
	v_add_f32_e32 v40, v40, v41
	v_add_f32_e32 v38, v38, v39
	v_lshlrev_b32_e32 v14, 1, v14
	v_pk_mul_f32 v[44:45], v[28:29], v[28:29]
	v_add_f32_e32 v41, v42, v43
	v_lshl_add_u64 v[20:21], s[10:11], 0, v[20:21]
	v_add_f32_e32 v40, v38, v40
	v_mul_f32_e32 v46, 0xbfb8aa3b, v30
	v_add_f32_e32 v44, v44, v45
	v_lshl_add_u64 v[38:39], v[20:21], 0, v[14:15]
	v_add_f32_e32 v14, v41, v40
	v_cmp_lt_i32_e32 vcc, s19, v19
	v_mov_b32_e32 v16, v19
	v_exp_f32_e32 v19, v46
	v_add_f32_e32 v14, v44, v14
	v_mul_f32_e32 v47, 0xbfb8aa3b, v31
	v_mul_f32_e32 v48, 0xbfb8aa3b, v32
	v_add_f32_dpp v14, v14, v14 quad_perm:[1,0,3,2] row_mask:0xf bank_mask:0xf bound_ctrl:1
	v_add_f32_e32 v19, 1.0, v19
	v_rcp_f32_e32 v20, v19
	v_add_f32_dpp v14, v14, v14 quad_perm:[2,3,0,1] row_mask:0xf bank_mask:0xf bound_ctrl:1
	v_mul_f32_e32 v49, 0xbfb8aa3b, v33
	v_mul_f32_e32 v50, 0xbfb8aa3b, v34
	v_add_f32_dpp v14, v14, v14 row_half_mirror row_mask:0xf bank_mask:0xf bound_ctrl:1
	v_mul_f32_e32 v51, 0xbfb8aa3b, v35
	v_mul_f32_e32 v52, 0xbfb8aa3b, v36
	v_add_f32_dpp v14, v14, v14 row_mirror row_mask:0xf bank_mask:0xf bound_ctrl:1
	v_mov_b32_e32 v19, v14
	s_nop 1
	v_permlane16_swap_b32_e32 v14, v19
	v_add_f32_e32 v14, v14, v19
	v_mul_f32_e32 v53, 0xbfb8aa3b, v37
	v_mov_b32_e32 v19, v14
	v_exp_f32_e32 v46, v47
	v_exp_f32_e32 v47, v48
	v_exp_f32_e32 v48, v49
	v_exp_f32_e32 v49, v50
	v_exp_f32_e32 v50, v51
	v_exp_f32_e32 v51, v52
	v_exp_f32_e32 v52, v53
	v_permlane32_swap_b32_e32 v14, v19
	v_add_f32_e32 v14, v14, v19
	v_fmamk_f32 v14, v14, 0x3b000000, v18
	s_or_b64 s[12:13], vcc, s[12:13]
	v_mul_f32_e32 v19, 0x4b800000, v14
	v_cmp_gt_f32_e32 vcc, s20, v14
	v_add_f32_e32 v21, 1.0, v46
	v_add_f32_e32 v40, 1.0, v47
	v_add_f32_e32 v41, 1.0, v48
	v_add_f32_e32 v42, 1.0, v49
	v_add_f32_e32 v43, 1.0, v50
	v_add_f32_e32 v44, 1.0, v51
	v_add_f32_e32 v45, 1.0, v52
	v_cndmask_b32_e32 v14, v14, v19, vcc
	v_rcp_f32_e32 v21, v21
	v_rcp_f32_e32 v40, v40
	v_rcp_f32_e32 v41, v41
	v_rcp_f32_e32 v42, v42
	v_rcp_f32_e32 v43, v43
	v_rcp_f32_e32 v44, v44
	v_rcp_f32_e32 v45, v45
	v_rsq_f32_e32 v14, v14
	v_pk_mul_f32 v[20:21], v[20:21], v[30:31]
	v_pk_mul_f32 v[30:31], v[42:43], v[34:35]
	v_pk_mul_f32 v[32:33], v[40:41], v[32:33]
	v_pk_mul_f32 v[34:35], v[44:45], v[36:37]
	v_mul_f32_e32 v19, 0x45800000, v14
	v_pk_mul_f32 v[20:21], v[22:23], v[20:21]
	v_pk_mul_f32 v[22:23], v[24:25], v[30:31]
	v_pk_mul_f32 v[24:25], v[26:27], v[32:33]
	v_pk_mul_f32 v[26:27], v[28:29], v[34:35]
	v_cndmask_b32_e32 v14, v14, v19, vcc
	v_pk_mul_f32 v[22:23], v[22:23], v[14:15] op_sel_hi:[1,0]
	v_pk_mul_f32 v[20:21], v[20:21], v[14:15] op_sel_hi:[1,0]
	v_pk_mul_f32 v[26:27], v[26:27], v[14:15] op_sel_hi:[1,0]
	v_pk_mul_f32 v[24:25], v[24:25], v[14:15] op_sel_hi:[1,0]
	v_add_u32_e32 v17, s18, v17
	v_cvt_pk_bf16_f32 v20, v20, v21
	v_cvt_pk_bf16_f32 v21, v22, v23
	v_cvt_pk_bf16_f32 v22, v24, v25
	v_cvt_pk_bf16_f32 v23, v26, v27
	global_store_dwordx4 v[38:39], v[20:23], off sc1
	s_andn2_b64 exec, exec, s[12:13]
	s_cbranch_execnz .LBB0_1862

; __device__ __forceinline__ u32x4 pack8(const f32x4 a, const f32x4 b) { u32x4 w; w.x = cvt_pk_bf16(a[0], a[1]); w.y = cvt_pk_bf16(a[2], a[3]); w.z = cvt_pk_bf16(b[0], b[1]); w.w = cvt_pk_bf16(b[2], b[3]); return w; }
;     __device__ __forceinline__ void fused(f32x4 (&acc)[2][2][4][2], const pg8::Unit& u_, int wr_, int wc_, int fr_, int fq_, LAS unsigned char* lds, int tid_) const {
;     ...
;                 for (int m = 0; m < 4; ++m) { bf16_t* rowp = X + (size_t)(row0 + ai * HALF + m * 16) * D + col0;
; #pragma unroll
;                     for (int bj = 0; bj < 2; ++bj) { f32x4 s0, s1;
;                         if (LAYER == 0) { const float* sp = (isctx ? srcC + (size_t)(row0 - ML + ai * HALF + m * 16) * D : srcL + (size_t)(row0 + ai * HALF + m * 16) * D) + col0 + bj * HALF;
;                             s0 = __builtin_nontemporal_load((const f32x4*)sp); s1 = __builtin_nontemporal_load((const f32x4*)(sp + 4)); }
;                         else { const u32x4 xb = *(const u32x4*)(rowp + bj * HALF);
;                             s0 = (f32x4){__uint_as_float(xb.x << 16), __uint_as_float(xb.x & 0xffff0000u), __uint_as_float(xb.y << 16), __uint_as_float(xb.y & 0xffff0000u)};
;                             s1 = (f32x4){__uint_as_float(xb.z << 16), __uint_as_float(xb.z & 0xffff0000u), __uint_as_float(xb.w << 16), __uint_as_float(xb.w & 0xffff0000u)}; }
;                         const u32x4 w = pack8(s0 + gv[bj][0] * acc[ai][bj][m][0], s1 + gv[bj][1] * acc[ai][bj][m][1]);
;                         *(u32x4*)(rowp + bj * HALF) = w;
;                         acc[ai][bj][m][0] = (f32x4){__uint_as_float(w.x << 16), __uint_as_float(w.x & 0xffff0000u), __uint_as_float(w.y << 16), __uint_as_float(w.y & 0xffff0000u)};
;                         acc[ai][bj][m][1] = (f32x4){__uint_as_float(w.z << 16), __uint_as_float(w.z & 0xffff0000u), __uint_as_float(w.w << 16), __uint_as_float(w.w & 0xffff0000u)}; } }
;         }
;         asm volatile("s_waitcnt vmcnt(0)" ::: "memory"); __builtin_amdgcn_s_barrier(); asm volatile("" ::: "memory");
.LBB0_1939:
	s_lshl_b32 s27, s36, 8
	s_lshl_b32 s29, s6, 8
	v_lshlrev_b32_e64 v176, 5, s8
	v_lshlrev_b32_e32 v175, 3, v158
	v_lshl_add_u32 v209, s37, 6, v174
	v_add3_u32 v168, v175, v176, s29
	s_lshl_b64 s[0:1], s[0:1], 2
	v_add_u32_e32 v170, s27, v209
	s_add_u32 s40, s61, s0
	v_ashrrev_i32_e32 v169, 31, v168
	v_ashrrev_i32_e32 v171, 31, v170
	s_addc_u32 s41, s62, s1
	v_lshl_add_u64 v[172:173], v[168:169], 1, s[20:21]
	v_lshlrev_b64 v[170:171], 11, v[170:171]
	v_lshl_add_u64 v[78:79], v[168:169], 2, s[40:41]
	v_lshl_add_u64 v[172:173], v[172:173], 0, v[170:171]
	global_load_dwordx4 v[102:105], v[78:79], off offset:16
	global_load_dwordx4 v[106:109], v[78:79], off
	global_load_dwordx4 v[74:77], v[78:79], off offset:528
	s_nop 0
	global_load_dwordx4 v[78:81], v[78:79], off offset:512
	s_mov_b32 s37, 0x8000
	global_load_dwordx4 v[178:181], v[172:173], off
	s_mov_b64 s[40:41], 0x8000
	v_and_b32_e32 v185, 15, v184
	s_waitcnt vmcnt(0)
	v_lshlrev_b32_e32 v182, 16, v178
	v_and_b32_e32 v183, 0xffff0000, v178
	v_lshlrev_b32_e32 v178, 16, v179
	v_and_b32_e32 v179, 0xffff0000, v179
	v_lshlrev_b32_e32 v210, 16, v180
	v_and_b32_e32 v211, 0xffff0000, v180
	v_lshlrev_b32_e32 v180, 16, v181
	v_and_b32_e32 v181, 0xffff0000, v181
	v_pk_fma_f32 v[144:145], v[144:145], v[108:109], v[178:179]
	v_pk_fma_f32 v[142:143], v[142:143], v[106:107], v[182:183]
	v_pk_fma_f32 v[178:179], v[12:13], v[104:105], v[180:181]
	v_pk_fma_f32 v[12:13], v[10:11], v[102:103], v[210:211]
	v_cvt_pk_bf16_f32 v10, v142, v143
	v_cvt_pk_bf16_f32 v11, v144, v145
	global_load_dwordx4 v[142:145], v[172:173], off offset:256
	v_cvt_pk_bf16_f32 v12, v12, v13
	v_cvt_pk_bf16_f32 v13, v178, v179
	global_store_dwordx4 v[172:173], v[10:13], off sc1
	s_waitcnt vmcnt(1)
	v_lshlrev_b32_e32 v178, 16, v142
	v_and_b32_e32 v179, 0xffff0000, v142
	v_lshlrev_b32_e32 v142, 16, v143
	v_and_b32_e32 v143, 0xffff0000, v143
	v_lshlrev_b32_e32 v180, 16, v144
	v_and_b32_e32 v181, 0xffff0000, v144
	v_lshlrev_b32_e32 v144, 16, v145
	v_and_b32_e32 v145, 0xffff0000, v145
	v_pk_fma_f32 v[140:141], v[140:141], v[80:81], v[142:143]
	v_pk_fma_f32 v[142:143], v[16:17], v[76:77], v[144:145]
	v_add_co_u32_e32 v144, vcc, s37, v172
	v_pk_fma_f32 v[16:17], v[14:15], v[74:75], v[180:181]
	s_nop 0
	v_addc_co_u32_e32 v145, vcc, 0, v173, vcc
	v_cvt_pk_bf16_f32 v15, v140, v141
	v_cvt_pk_bf16_f32 v16, v16, v17
	v_cvt_pk_bf16_f32 v17, v142, v143
	global_load_dwordx4 v[140:143], v[144:145], off
	v_pk_fma_f32 v[138:139], v[138:139], v[78:79], v[178:179]
	s_mov_b32 s37, 0x10000
	v_cvt_pk_bf16_f32 v14, v138, v139
	v_lshl_add_u64 v[138:139], v[172:173], 0, s[40:41]
	s_mov_b64 s[40:41], 0x10000
	global_store_dwordx4 v[172:173], v[14:17], off offset:256 sc1
	s_waitcnt vmcnt(1)
	v_lshlrev_b32_e32 v178, 16, v140
	v_and_b32_e32 v179, 0xffff0000, v140
	v_lshlrev_b32_e32 v140, 16, v141
	v_and_b32_e32 v141, 0xffff0000, v141
	v_lshlrev_b32_e32 v180, 16, v142
	v_and_b32_e32 v181, 0xffff0000, v142
	v_lshlrev_b32_e32 v142, 16, v143
	v_and_b32_e32 v143, 0xffff0000, v143
	v_pk_fma_f32 v[136:137], v[136:137], v[108:109], v[140:141]
	v_pk_fma_f32 v[134:135], v[134:135], v[106:107], v[178:179]
	v_pk_fma_f32 v[140:141], v[20:21], v[104:105], v[142:143]
	v_pk_fma_f32 v[20:21], v[18:19], v[102:103], v[180:181]
	v_cvt_pk_bf16_f32 v18, v134, v135
	v_cvt_pk_bf16_f32 v19, v136, v137
	global_load_dwordx4 v[134:137], v[138:139], off offset:256
	v_cvt_pk_bf16_f32 v20, v20, v21
	v_cvt_pk_bf16_f32 v21, v140, v141
	global_store_dwordx4 v[144:145], v[18:21], off sc1
	s_waitcnt vmcnt(1)
	v_lshlrev_b32_e32 v140, 16, v134
	v_and_b32_e32 v141, 0xffff0000, v134
	v_lshlrev_b32_e32 v134, 16, v135
	v_and_b32_e32 v135, 0xffff0000, v135
	v_lshlrev_b32_e32 v142, 16, v136
	v_and_b32_e32 v143, 0xffff0000, v136
	v_lshlrev_b32_e32 v136, 16, v137
	v_and_b32_e32 v137, 0xffff0000, v137
	v_pk_fma_f32 v[132:133], v[132:133], v[80:81], v[134:135]
	v_pk_fma_f32 v[134:135], v[32:33], v[76:77], v[136:137]
	v_add_co_u32_e32 v136, vcc, s37, v172
	v_pk_fma_f32 v[130:131], v[130:131], v[78:79], v[140:141]
	s_nop 0
	v_addc_co_u32_e32 v137, vcc, 0, v173, vcc
	v_pk_fma_f32 v[32:33], v[30:31], v[74:75], v[142:143]
	v_cvt_pk_bf16_f32 v30, v130, v131
	v_cvt_pk_bf16_f32 v31, v132, v133
	global_load_dwordx4 v[130:133], v[136:137], off
	v_cvt_pk_bf16_f32 v32, v32, v33
	v_cvt_pk_bf16_f32 v33, v134, v135
	global_store_dwordx4 v[138:139], v[30:33], off offset:256 sc1
	v_lshl_add_u64 v[134:135], v[172:173], 0, s[40:41]
	s_mov_b32 s37, 0x18000
	s_mov_b64 s[40:41], 0x18000
	s_waitcnt vmcnt(1)
	v_lshlrev_b32_e32 v138, 16, v130
	v_and_b32_e32 v139, 0xffff0000, v130
	v_lshlrev_b32_e32 v130, 16, v131
	v_and_b32_e32 v131, 0xffff0000, v131
	v_lshlrev_b32_e32 v140, 16, v132
	v_and_b32_e32 v141, 0xffff0000, v132
	v_lshlrev_b32_e32 v132, 16, v133
	v_and_b32_e32 v133, 0xffff0000, v133
	v_pk_fma_f32 v[128:129], v[128:129], v[108:109], v[130:131]
	v_pk_fma_f32 v[126:127], v[126:127], v[106:107], v[138:139]
	v_pk_fma_f32 v[130:131], v[24:25], v[104:105], v[132:133]
	v_pk_fma_f32 v[24:25], v[22:23], v[102:103], v[140:141]
	v_cvt_pk_bf16_f32 v22, v126, v127
	v_cvt_pk_bf16_f32 v23, v128, v129
	global_load_dwordx4 v[126:129], v[134:135], off offset:256
	v_cvt_pk_bf16_f32 v24, v24, v25
	v_cvt_pk_bf16_f32 v25, v130, v131
	global_store_dwordx4 v[136:137], v[22:25], off sc1
	s_waitcnt vmcnt(1)
; __device__ __forceinline__ u32x4 pack8(const f32x4 a, const f32x4 b) { u32x4 w; w.x = cvt_pk_bf16(a[0], a[1]); w.y = cvt_pk_bf16(a[2], a[3]); w.z = cvt_pk_bf16(b[0], b[1]); w.w = cvt_pk_bf16(b[2], b[3]); return w; }
;     __device__ __forceinline__ void fused(f32x4 (&acc)[2][2][4][2], const pg8::Unit& u_, int wr_, int wc_, int fr_, int fq_, LAS unsigned char* lds, int tid_) const {
;     ...
;                 for (int m = 0; m < 4; ++m) { bf16_t* rowp = X + (size_t)(row0 + ai * HALF + m * 16) * D + col0;
; #pragma unroll
;                     for (int bj = 0; bj < 2; ++bj) { f32x4 s0, s1;
;                         if (LAYER == 0) { const float* sp = (isctx ? srcC + (size_t)(row0 - ML + ai * HALF + m * 16) * D : srcL + (size_t)(row0 + ai * HALF + m * 16) * D) + col0 + bj * HALF;
;                             s0 = __builtin_nontemporal_load((const f32x4*)sp); s1 = __builtin_nontemporal_load((const f32x4*)(sp + 4)); }
;                         else { const u32x4 xb = *(const u32x4*)(rowp + bj * HALF);
;                             s0 = (f32x4){__uint_as_float(xb.x << 16), __uint_as_float(xb.x & 0xffff0000u), __uint_as_float(xb.y << 16), __uint_as_float(xb.y & 0xffff0000u)};
;                             s1 = (f32x4){__uint_as_float(xb.z << 16), __uint_as_float(xb.z & 0xffff0000u), __uint_as_float(xb.w << 16), __uint_as_float(xb.w & 0xffff0000u)}; }
;                         const u32x4 w = pack8(s0 + gv[bj][0] * acc[ai][bj][m][0], s1 + gv[bj][1] * acc[ai][bj][m][1]);
;                         *(u32x4*)(rowp + bj * HALF) = w;
;                         acc[ai][bj][m][0] = (f32x4){__uint_as_float(w.x << 16), __uint_as_float(w.x & 0xffff0000u), __uint_as_float(w.y << 16), __uint_as_float(w.y & 0xffff0000u)};
;                         acc[ai][bj][m][1] = (f32x4){__uint_as_float(w.z << 16), __uint_as_float(w.z & 0xffff0000u), __uint_as_float(w.w << 16), __uint_as_float(w.w & 0xffff0000u)}; } }
;         }
;         asm volatile("s_waitcnt vmcnt(0)" ::: "memory"); __builtin_amdgcn_s_barrier(); asm volatile("" ::: "memory");
	v_lshlrev_b32_e32 v130, 16, v126
	v_and_b32_e32 v131, 0xffff0000, v126
	v_lshlrev_b32_e32 v126, 16, v127
	v_and_b32_e32 v127, 0xffff0000, v127
	v_lshlrev_b32_e32 v132, 16, v128
	v_and_b32_e32 v133, 0xffff0000, v128
	v_lshlrev_b32_e32 v128, 16, v129
	v_and_b32_e32 v129, 0xffff0000, v129
	v_pk_fma_f32 v[124:125], v[124:125], v[80:81], v[126:127]
	v_pk_fma_f32 v[126:127], v[28:29], v[76:77], v[128:129]
	v_add_co_u32_e32 v128, vcc, s37, v172
	v_pk_fma_f32 v[28:29], v[26:27], v[74:75], v[132:133]
	s_nop 0
	v_addc_co_u32_e32 v129, vcc, 0, v173, vcc
	v_cvt_pk_bf16_f32 v27, v124, v125
	v_cvt_pk_bf16_f32 v28, v28, v29
	v_cvt_pk_bf16_f32 v29, v126, v127
	global_load_dwordx4 v[124:127], v[128:129], off
	v_pk_fma_f32 v[122:123], v[122:123], v[78:79], v[130:131]
	s_mov_b32 s37, 0x40000
	v_cvt_pk_bf16_f32 v26, v122, v123
	v_lshl_add_u64 v[122:123], v[172:173], 0, s[40:41]
	s_mov_b64 s[40:41], 0x40000
	global_store_dwordx4 v[134:135], v[26:29], off offset:256 sc1
	s_waitcnt vmcnt(1)
	v_lshlrev_b32_e32 v130, 16, v124
	v_and_b32_e32 v131, 0xffff0000, v124
	v_lshlrev_b32_e32 v124, 16, v125
	v_and_b32_e32 v125, 0xffff0000, v125
	v_lshlrev_b32_e32 v132, 16, v126
	v_and_b32_e32 v133, 0xffff0000, v126
	v_lshlrev_b32_e32 v126, 16, v127
	v_and_b32_e32 v127, 0xffff0000, v127
	v_pk_fma_f32 v[120:121], v[120:121], v[108:109], v[124:125]
	v_pk_fma_f32 v[118:119], v[118:119], v[106:107], v[130:131]
	v_pk_fma_f32 v[124:125], v[36:37], v[104:105], v[126:127]
	v_pk_fma_f32 v[36:37], v[34:35], v[102:103], v[132:133]
	v_cvt_pk_bf16_f32 v34, v118, v119
	v_cvt_pk_bf16_f32 v35, v120, v121
	global_load_dwordx4 v[118:121], v[122:123], off offset:256
	v_cvt_pk_bf16_f32 v36, v36, v37
	v_cvt_pk_bf16_f32 v37, v124, v125
	global_store_dwordx4 v[128:129], v[34:37], off sc1
	s_waitcnt vmcnt(1)
	v_lshlrev_b32_e32 v124, 16, v118
	v_and_b32_e32 v125, 0xffff0000, v118
	v_lshlrev_b32_e32 v118, 16, v119
	v_and_b32_e32 v119, 0xffff0000, v119
	v_lshlrev_b32_e32 v126, 16, v120
	v_and_b32_e32 v127, 0xffff0000, v120
	v_lshlrev_b32_e32 v120, 16, v121
	v_and_b32_e32 v121, 0xffff0000, v121
	v_pk_fma_f32 v[116:117], v[116:117], v[80:81], v[118:119]
	v_pk_fma_f32 v[118:119], v[48:49], v[76:77], v[120:121]
	v_add_co_u32_e32 v120, vcc, s37, v172
	v_pk_fma_f32 v[48:49], v[46:47], v[74:75], v[126:127]
	s_nop 0
	v_addc_co_u32_e32 v121, vcc, 0, v173, vcc
	v_cvt_pk_bf16_f32 v47, v116, v117
	v_cvt_pk_bf16_f32 v48, v48, v49
	v_cvt_pk_bf16_f32 v49, v118, v119
	global_load_dwordx4 v[116:119], v[120:121], off
	v_pk_fma_f32 v[114:115], v[114:115], v[78:79], v[124:125]
	s_mov_b32 s37, 0x48000
	v_cvt_pk_bf16_f32 v46, v114, v115
	global_store_dwordx4 v[122:123], v[46:49], off offset:256 sc1
	v_lshl_add_u64 v[114:115], v[172:173], 0, s[40:41]
	s_mov_b64 s[40:41], 0x48000
	s_waitcnt vmcnt(1)
	v_lshlrev_b32_e32 v122, 16, v116
	v_and_b32_e32 v123, 0xffff0000, v116
	v_lshlrev_b32_e32 v116, 16, v117
	v_and_b32_e32 v117, 0xffff0000, v117
	v_lshlrev_b32_e32 v124, 16, v118
	v_and_b32_e32 v125, 0xffff0000, v118
	v_lshlrev_b32_e32 v118, 16, v119
	v_and_b32_e32 v119, 0xffff0000, v119
	v_pk_fma_f32 v[112:113], v[112:113], v[108:109], v[116:117]
	v_pk_fma_f32 v[110:111], v[110:111], v[106:107], v[122:123]
	v_pk_fma_f32 v[116:117], v[60:61], v[104:105], v[118:119]
	v_pk_fma_f32 v[60:61], v[58:59], v[102:103], v[124:125]
	v_cvt_pk_bf16_f32 v58, v110, v111
	v_cvt_pk_bf16_f32 v59, v112, v113
	global_load_dwordx4 v[110:113], v[114:115], off offset:256
	v_cvt_pk_bf16_f32 v60, v60, v61
	v_cvt_pk_bf16_f32 v61, v116, v117
	global_store_dwordx4 v[120:121], v[58:61], off sc1
	s_waitcnt vmcnt(1)
	v_lshlrev_b32_e32 v116, 16, v110
	v_and_b32_e32 v117, 0xffff0000, v110
	v_lshlrev_b32_e32 v110, 16, v111
	v_and_b32_e32 v111, 0xffff0000, v111
	v_lshlrev_b32_e32 v118, 16, v112
	v_and_b32_e32 v119, 0xffff0000, v112
	v_lshlrev_b32_e32 v112, 16, v113
	v_and_b32_e32 v113, 0xffff0000, v113
	v_pk_fma_f32 v[100:101], v[100:101], v[80:81], v[110:111]
	v_pk_fma_f32 v[110:111], v[72:73], v[76:77], v[112:113]
	v_pk_fma_f32 v[72:73], v[70:71], v[74:75], v[118:119]
	v_cvt_pk_bf16_f32 v71, v100, v101
	v_add_co_u32_e32 v100, vcc, s37, v172
	v_cvt_pk_bf16_f32 v72, v72, v73
	s_nop 0
	v_addc_co_u32_e32 v101, vcc, 0, v173, vcc
	v_cvt_pk_bf16_f32 v73, v110, v111
	global_load_dwordx4 v[110:113], v[100:101], off
	v_pk_fma_f32 v[98:99], v[98:99], v[78:79], v[116:117]
	s_mov_b32 s37, 0x50000
	v_cvt_pk_bf16_f32 v70, v98, v99
	global_store_dwordx4 v[114:115], v[70:73], off offset:256 sc1
	v_lshl_add_u64 v[98:99], v[172:173], 0, s[40:41]
	s_mov_b64 s[40:41], 0x50000
	s_waitcnt vmcnt(1)
; __device__ __forceinline__ u32x4 pack8(const f32x4 a, const f32x4 b) { u32x4 w; w.x = cvt_pk_bf16(a[0], a[1]); w.y = cvt_pk_bf16(a[2], a[3]); w.z = cvt_pk_bf16(b[0], b[1]); w.w = cvt_pk_bf16(b[2], b[3]); return w; }
;     __device__ __forceinline__ void fused(f32x4 (&acc)[2][2][4][2], const pg8::Unit& u_, int wr_, int wc_, int fr_, int fq_, LAS unsigned char* lds, int tid_) const {
;     ...
;                 for (int m = 0; m < 4; ++m) { bf16_t* rowp = X + (size_t)(row0 + ai * HALF + m * 16) * D + col0;
; #pragma unroll
;                     for (int bj = 0; bj < 2; ++bj) { f32x4 s0, s1;
;                         if (LAYER == 0) { const float* sp = (isctx ? srcC + (size_t)(row0 - ML + ai * HALF + m * 16) * D : srcL + (size_t)(row0 + ai * HALF + m * 16) * D) + col0 + bj * HALF;
;                             s0 = __builtin_nontemporal_load((const f32x4*)sp); s1 = __builtin_nontemporal_load((const f32x4*)(sp + 4)); }
;                         else { const u32x4 xb = *(const u32x4*)(rowp + bj * HALF);
;                             s0 = (f32x4){__uint_as_float(xb.x << 16), __uint_as_float(xb.x & 0xffff0000u), __uint_as_float(xb.y << 16), __uint_as_float(xb.y & 0xffff0000u)};
;                             s1 = (f32x4){__uint_as_float(xb.z << 16), __uint_as_float(xb.z & 0xffff0000u), __uint_as_float(xb.w << 16), __uint_as_float(xb.w & 0xffff0000u)}; }
;                         const u32x4 w = pack8(s0 + gv[bj][0] * acc[ai][bj][m][0], s1 + gv[bj][1] * acc[ai][bj][m][1]);
;                         *(u32x4*)(rowp + bj * HALF) = w;
;                         acc[ai][bj][m][0] = (f32x4){__uint_as_float(w.x << 16), __uint_as_float(w.x & 0xffff0000u), __uint_as_float(w.y << 16), __uint_as_float(w.y & 0xffff0000u)};
;                         acc[ai][bj][m][1] = (f32x4){__uint_as_float(w.z << 16), __uint_as_float(w.z & 0xffff0000u), __uint_as_float(w.w << 16), __uint_as_float(w.w & 0xffff0000u)}; } }
;         }
;         asm volatile("s_waitcnt vmcnt(0)" ::: "memory"); __builtin_amdgcn_s_barrier(); asm volatile("" ::: "memory");
	v_lshlrev_b32_e32 v114, 16, v110
	v_and_b32_e32 v115, 0xffff0000, v110
	v_lshlrev_b32_e32 v110, 16, v111
	v_and_b32_e32 v111, 0xffff0000, v111
	v_lshlrev_b32_e32 v116, 16, v112
	v_and_b32_e32 v117, 0xffff0000, v112
	v_lshlrev_b32_e32 v112, 16, v113
	v_and_b32_e32 v113, 0xffff0000, v113
	v_pk_fma_f32 v[96:97], v[96:97], v[108:109], v[110:111]
	v_pk_fma_f32 v[94:95], v[94:95], v[106:107], v[114:115]
	v_pk_fma_f32 v[110:111], v[84:85], v[104:105], v[112:113]
	v_pk_fma_f32 v[84:85], v[82:83], v[102:103], v[116:117]
	v_cvt_pk_bf16_f32 v82, v94, v95
	v_cvt_pk_bf16_f32 v83, v96, v97
	global_load_dwordx4 v[94:97], v[98:99], off offset:256
	v_cvt_pk_bf16_f32 v84, v84, v85
	v_cvt_pk_bf16_f32 v85, v110, v111
	global_store_dwordx4 v[100:101], v[82:85], off sc1
	s_waitcnt vmcnt(1)
	v_lshlrev_b32_e32 v100, 16, v94
	v_and_b32_e32 v101, 0xffff0000, v94
	v_lshlrev_b32_e32 v94, 16, v95
	v_and_b32_e32 v95, 0xffff0000, v95
	v_lshlrev_b32_e32 v110, 16, v96
	v_and_b32_e32 v111, 0xffff0000, v96
	v_lshlrev_b32_e32 v96, 16, v97
	v_and_b32_e32 v97, 0xffff0000, v97
	v_pk_fma_f32 v[92:93], v[92:93], v[80:81], v[94:95]
	v_pk_fma_f32 v[94:95], v[88:89], v[76:77], v[96:97]
	v_add_co_u32_e32 v96, vcc, s37, v172
	v_pk_fma_f32 v[88:89], v[86:87], v[74:75], v[110:111]
	s_nop 0
	v_addc_co_u32_e32 v97, vcc, 0, v173, vcc
	v_cvt_pk_bf16_f32 v87, v92, v93
	v_cvt_pk_bf16_f32 v88, v88, v89
	v_cvt_pk_bf16_f32 v89, v94, v95
	global_load_dwordx4 v[92:95], v[96:97], off
	v_pk_fma_f32 v[90:91], v[90:91], v[78:79], v[100:101]
	s_mov_b32 s37, 0x58000
	v_cvt_pk_bf16_f32 v86, v90, v91
	global_store_dwordx4 v[98:99], v[86:89], off offset:256 sc1
	v_lshl_add_u64 v[90:91], v[172:173], 0, s[40:41]
	s_mov_b64 s[40:41], 0x58000
	s_waitcnt vmcnt(1)
	v_lshlrev_b32_e32 v98, 16, v92
	v_and_b32_e32 v99, 0xffff0000, v92
	v_lshlrev_b32_e32 v92, 16, v93
	v_and_b32_e32 v93, 0xffff0000, v93
	v_lshlrev_b32_e32 v100, 16, v94
	v_and_b32_e32 v101, 0xffff0000, v94
	v_lshlrev_b32_e32 v94, 16, v95
	v_and_b32_e32 v95, 0xffff0000, v95
	v_pk_fma_f32 v[68:69], v[68:69], v[108:109], v[92:93]
	v_pk_fma_f32 v[66:67], v[66:67], v[106:107], v[98:99]
	v_pk_fma_f32 v[92:93], v[64:65], v[104:105], v[94:95]
	v_pk_fma_f32 v[64:65], v[62:63], v[102:103], v[100:101]
	v_cvt_pk_bf16_f32 v62, v66, v67
	v_cvt_pk_bf16_f32 v63, v68, v69
	global_load_dwordx4 v[66:69], v[90:91], off offset:256
	v_cvt_pk_bf16_f32 v64, v64, v65
	v_cvt_pk_bf16_f32 v65, v92, v93
	global_store_dwordx4 v[96:97], v[62:65], off sc1
	s_waitcnt vmcnt(1)
	v_lshlrev_b32_e32 v92, 16, v66
	v_and_b32_e32 v93, 0xffff0000, v66
	v_lshlrev_b32_e32 v66, 16, v67
	v_and_b32_e32 v67, 0xffff0000, v67
	v_lshlrev_b32_e32 v94, 16, v68
	v_and_b32_e32 v95, 0xffff0000, v68
	v_lshlrev_b32_e32 v68, 16, v69
	v_and_b32_e32 v69, 0xffff0000, v69
	v_pk_fma_f32 v[56:57], v[56:57], v[80:81], v[66:67]
	v_pk_fma_f32 v[66:67], v[52:53], v[76:77], v[68:69]
	v_pk_fma_f32 v[52:53], v[50:51], v[74:75], v[94:95]
	v_cvt_pk_bf16_f32 v51, v56, v57
	v_add_co_u32_e32 v56, vcc, s37, v172
	v_cvt_pk_bf16_f32 v52, v52, v53
	s_nop 0
	v_addc_co_u32_e32 v57, vcc, 0, v173, vcc
	v_cvt_pk_bf16_f32 v53, v66, v67
	global_load_dwordx4 v[66:69], v[56:57], off
	v_pk_fma_f32 v[54:55], v[54:55], v[78:79], v[92:93]
	s_movk_i32 s37, 0x1000
	v_cvt_pk_bf16_f32 v50, v54, v55
	global_store_dwordx4 v[90:91], v[50:53], off offset:256 sc1
	v_lshl_add_u64 v[54:55], v[172:173], 0, s[40:41]
	s_add_u32 s40, s4, s0
	s_addc_u32 s41, s5, s1
	v_cmp_gt_i32_e32 vcc, s37, v184
	s_waitcnt vmcnt(1)
	v_lshlrev_b32_e32 v90, 16, v66
	v_and_b32_e32 v91, 0xffff0000, v66
	v_lshlrev_b32_e32 v66, 16, v67
	v_and_b32_e32 v67, 0xffff0000, v67
	v_lshlrev_b32_e32 v92, 16, v68
	v_and_b32_e32 v93, 0xffff0000, v68
	v_lshlrev_b32_e32 v68, 16, v69
	v_and_b32_e32 v69, 0xffff0000, v69
	v_pk_fma_f32 v[44:45], v[44:45], v[108:109], v[66:67]
	v_pk_fma_f32 v[42:43], v[42:43], v[106:107], v[90:91]
	v_pk_fma_f32 v[66:67], v[40:41], v[104:105], v[68:69]
	v_pk_fma_f32 v[40:41], v[38:39], v[102:103], v[92:93]
	v_cvt_pk_bf16_f32 v38, v42, v43
	v_cvt_pk_bf16_f32 v39, v44, v45
	global_load_dwordx4 v[42:45], v[54:55], off offset:256
	v_cvt_pk_bf16_f32 v40, v40, v41
	v_cvt_pk_bf16_f32 v41, v66, v67
	global_store_dwordx4 v[56:57], v[38:41], off sc1
	s_waitcnt vmcnt(1)
	v_lshlrev_b32_e32 v56, 16, v42
	v_and_b32_e32 v57, 0xffff0000, v42
	v_lshlrev_b32_e32 v42, 16, v43
	v_and_b32_e32 v43, 0xffff0000, v43
	v_lshlrev_b32_e32 v66, 16, v44
	v_and_b32_e32 v67, 0xffff0000, v44
	v_lshlrev_b32_e32 v44, 16, v45
	v_and_b32_e32 v45, 0xffff0000, v45
	v_pk_fma_f32 v[8:9], v[8:9], v[80:81], v[42:43]
	v_pk_fma_f32 v[6:7], v[6:7], v[78:79], v[56:57]
	v_pk_fma_f32 v[42:43], v[4:5], v[76:77], v[44:45]
	v_pk_fma_f32 v[4:5], v[2:3], v[74:75], v[66:67]
	v_cvt_pk_bf16_f32 v2, v6, v7
	v_cvt_pk_bf16_f32 v3, v8, v9
	v_cvt_pk_bf16_f32 v4, v4, v5
	v_cvt_pk_bf16_f32 v5, v42, v43
	global_store_dwordx4 v[54:55], v[2:5], off offset:256 sc1
	s_waitcnt vmcnt(0)
	s_barrier
	s_and_saveexec_b64 s[42:43], vcc
	s_cbranch_execz .LBB0_1942
	v_mul_u32_u24_e32 v6, 0x108, v185
	s_mov_b64 s[44:45], 0
	v_mov_b32_e32 v7, v184

; __device__ __forceinline__ u32x4 pack8(const f32x4 a, const f32x4 b) { u32x4 w; w.x = cvt_pk_bf16(a[0], a[1]); w.y = cvt_pk_bf16(a[2], a[3]); w.z = cvt_pk_bf16(b[0], b[1]); w.w = cvt_pk_bf16(b[2], b[3]); return w; }
;     __device__ __forceinline__ void fused(f32x4 (&acc)[2][2][4][2], const pg8::Unit& u_, int wr_, int wc_, int fr_, int fq_, LAS unsigned char* lds, int tid_) const {
;     ...
; #pragma unroll
;         for (int bj = 0; bj < 2; ++bj) { f32x4 G[2], SH[2];
; #pragma unroll
;             for (int n = 0; n < 2; ++n) { const int c = col0 + bj * HALF + 4 * n; const f32x4 gg = *(const f32x4*)(g2 + c), sc = *(const f32x4*)(mrow + 4 * D + c);
;                 G[n] = gg * (sc + 1.f); SH[n] = *(const f32x4*)(mrow + 3 * D + c); }
; #pragma unroll
;             for (int ai = 0; ai < 2; ++ai)
; #pragma unroll
;                 for (int m = 0; m < 4; ++m) { const int rl = ai * HALF + wr * 64 + m * 16 + fr; const float r = bad ? __builtin_nanf("") : Sr[rl];
;                     *(u32x4*)(HB + (size_t)(u.pm * BM + rl) * D + col0 + bj * HALF) = pack8(acc[ai][bj][m][0] * r * G[0] + SH[0], acc[ai][bj][m][1] * r * G[1] + SH[1]); }
;             asm volatile("" ::: "memory"); }
.LBB0_1986:
	s_waitcnt vmcnt(3)
	v_pk_add_f32 v[24:25], v[24:25], 1.0 op_sel_hi:[1,0]
	v_pk_add_f32 v[22:23], v[22:23], 1.0 op_sel_hi:[1,0]
	s_waitcnt vmcnt(1)
	v_pk_add_f32 v[18:19], v[18:19], 1.0 op_sel_hi:[1,0]
	v_pk_add_f32 v[20:21], v[20:21], 1.0 op_sel_hi:[1,0]
	v_pk_mul_f32 v[16:17], v[16:17], v[24:25]
	v_pk_mul_f32 v[14:15], v[14:15], v[22:23]
	v_pk_mul_f32 v[12:13], v[12:13], v[20:21]
	v_pk_mul_f32 v[10:11], v[10:11], v[18:19]
	s_waitcnt lgkmcnt(0)
	v_pk_mul_f32 v[18:19], v[186:187], v[98:99] op_sel_hi:[0,1]
	v_pk_mul_f32 v[20:21], v[186:187], v[96:97] op_sel_hi:[0,1]
	v_pk_fma_f32 v[22:23], v[16:17], v[18:19], v[8:9]
	v_pk_fma_f32 v[18:19], v[14:15], v[20:21], v[6:7]
	v_pk_mul_f32 v[20:21], v[186:187], v[94:95] op_sel_hi:[0,1]
	v_pk_mul_f32 v[24:25], v[186:187], v[92:93] op_sel_hi:[0,1]
	v_lshl_add_u64 v[168:169], v[168:169], 1, s[82:83]
	s_waitcnt vmcnt(0)
	v_pk_fma_f32 v[92:93], v[12:13], v[20:21], v[4:5]
	v_pk_fma_f32 v[20:21], v[10:11], v[24:25], v[2:3]
	v_cvt_pk_bf16_f32 v18, v18, v19
	v_cvt_pk_bf16_f32 v19, v22, v23
	v_cvt_pk_bf16_f32 v20, v20, v21
	v_cvt_pk_bf16_f32 v21, v92, v93
	v_lshl_add_u64 v[92:93], v[168:169], 0, v[170:171]
	s_and_b64 vcc, exec, s[6:7]
	v_add_u32_e32 v170, 16, v209
	global_store_dwordx4 v[92:93], v[18:21], off sc1
	s_cbranch_vccnz .LBB0_1988
	s_nop 0
	v_lshl_add_u32 v18, v170, 2, 0
	v_add_u32_e32 v18, 0x18300, v18
	ds_read_b32 v158, v18
.LBB0_1988:
	s_waitcnt lgkmcnt(0)
	v_pk_mul_f32 v[18:19], v[158:159], v[106:107] op_sel_hi:[0,1]
	v_pk_mul_f32 v[20:21], v[158:159], v[104:105] op_sel_hi:[0,1]
	v_pk_fma_f32 v[22:23], v[16:17], v[18:19], v[8:9]
	v_pk_fma_f32 v[18:19], v[14:15], v[20:21], v[6:7]
	v_pk_mul_f32 v[20:21], v[158:159], v[102:103] op_sel_hi:[0,1]
	v_cvt_pk_bf16_f32 v18, v18, v19
	v_cvt_pk_bf16_f32 v19, v22, v23
	v_add_u32_e32 v22, s27, v170
	v_pk_mul_f32 v[24:25], v[158:159], v[100:101] op_sel_hi:[0,1]
	v_ashrrev_i32_e32 v23, 31, v22
	v_pk_fma_f32 v[94:95], v[12:13], v[20:21], v[4:5]
	v_pk_fma_f32 v[20:21], v[10:11], v[24:25], v[2:3]
	v_lshlrev_b64 v[22:23], 11, v[22:23]
	v_cvt_pk_bf16_f32 v20, v20, v21
	v_cvt_pk_bf16_f32 v21, v94, v95
	v_lshl_add_u64 v[94:95], v[168:169], 0, v[22:23]
	global_store_dwordx4 v[94:95], v[18:21], off sc1
	v_add_u32_e32 v158, 32, v209
	s_and_b64 vcc, exec, s[6:7]
	v_mov_b32_e32 v18, 0x7fc00000
	v_mov_b32_e32 v20, 0x7fc00000
	s_cbranch_vccnz .LBB0_1990
	v_lshl_add_u32 v19, v158, 2, 0
	v_add_u32_e32 v19, 0x18300, v19
	ds_read_b32 v20, v19
.LBB0_1990:
	s_waitcnt lgkmcnt(0)
	v_pk_mul_f32 v[24:25], v[20:21], v[112:113] op_sel_hi:[0,1]
	v_pk_mul_f32 v[22:23], v[20:21], v[114:115] op_sel_hi:[0,1]
	v_pk_fma_f32 v[24:25], v[14:15], v[24:25], v[6:7]
	v_pk_mul_f32 v[96:97], v[20:21], v[110:111] op_sel_hi:[0,1]
	v_pk_mul_f32 v[20:21], v[20:21], v[108:109] op_sel_hi:[0,1]
	v_pk_fma_f32 v[98:99], v[10:11], v[20:21], v[2:3]
	v_cvt_pk_bf16_f32 v20, v24, v25
	v_add_u32_e32 v24, s27, v158
	v_ashrrev_i32_e32 v25, 31, v24
	v_pk_fma_f32 v[22:23], v[16:17], v[22:23], v[8:9]
	v_pk_fma_f32 v[96:97], v[12:13], v[96:97], v[4:5]
	v_lshlrev_b64 v[24:25], 11, v[24:25]
	v_cvt_pk_bf16_f32 v21, v22, v23
	v_cvt_pk_bf16_f32 v22, v98, v99
	v_cvt_pk_bf16_f32 v23, v96, v97
	v_lshl_add_u64 v[96:97], v[168:169], 0, v[24:25]
	s_and_b64 vcc, exec, s[6:7]
	v_add_u32_e32 v108, 48, v209
	global_store_dwordx4 v[96:97], v[20:23], off sc1
	s_cbranch_vccnz .LBB0_1992
	v_lshl_add_u32 v18, v108, 2, 0
	v_add_u32_e32 v18, 0x18300, v18
	ds_read_b32 v18, v18
.LBB0_1992:
	s_waitcnt lgkmcnt(0)
	v_pk_mul_f32 v[22:23], v[18:19], v[122:123] op_sel_hi:[0,1]
	v_pk_mul_f32 v[20:21], v[18:19], v[124:125] op_sel_hi:[0,1]
	v_pk_fma_f32 v[22:23], v[14:15], v[22:23], v[6:7]
	v_pk_mul_f32 v[24:25], v[18:19], v[120:121] op_sel_hi:[0,1]
	v_pk_mul_f32 v[18:19], v[18:19], v[118:119] op_sel_hi:[0,1]
	v_pk_fma_f32 v[98:99], v[10:11], v[18:19], v[2:3]
	v_cvt_pk_bf16_f32 v18, v22, v23
	v_add_u32_e32 v22, s27, v108
	v_ashrrev_i32_e32 v23, 31, v22
	v_pk_fma_f32 v[20:21], v[16:17], v[20:21], v[8:9]
	v_pk_fma_f32 v[24:25], v[12:13], v[24:25], v[4:5]
	v_lshlrev_b64 v[22:23], 11, v[22:23]
	v_cvt_pk_bf16_f32 v19, v20, v21
	v_cvt_pk_bf16_f32 v20, v98, v99
	v_cvt_pk_bf16_f32 v21, v24, v25
	v_lshl_add_u64 v[98:99], v[168:169], 0, v[22:23]
	global_store_dwordx4 v[98:99], v[18:21], off sc1
	v_add_u32_e32 v109, 0x80, v209
	s_and_b64 vcc, exec, s[6:7]
	v_mov_b32_e32 v18, 0x7fc00000
	v_mov_b32_e32 v20, 0x7fc00000
	s_cbranch_vccnz .LBB0_1994
	v_lshl_add_u32 v19, v109, 2, 0
	v_add_u32_e32 v19, 0x18300, v19
	ds_read_b32 v20, v19
.LBB0_1994:
	s_waitcnt lgkmcnt(0)
	v_pk_mul_f32 v[24:25], v[20:21], v[130:131] op_sel_hi:[0,1]
	v_pk_mul_f32 v[22:23], v[20:21], v[132:133] op_sel_hi:[0,1]
	v_pk_fma_f32 v[24:25], v[14:15], v[24:25], v[6:7]
	v_pk_mul_f32 v[100:101], v[20:21], v[128:129] op_sel_hi:[0,1]
	v_pk_mul_f32 v[20:21], v[20:21], v[126:127] op_sel_hi:[0,1]
	v_pk_fma_f32 v[102:103], v[10:11], v[20:21], v[2:3]
	v_cvt_pk_bf16_f32 v20, v24, v25
	v_add_u32_e32 v24, s27, v109
	v_ashrrev_i32_e32 v25, 31, v24
	v_pk_fma_f32 v[22:23], v[16:17], v[22:23], v[8:9]
	v_pk_fma_f32 v[100:101], v[12:13], v[100:101], v[4:5]
	v_lshlrev_b64 v[24:25], 11, v[24:25]
	v_cvt_pk_bf16_f32 v21, v22, v23
	v_cvt_pk_bf16_f32 v22, v102, v103
	v_cvt_pk_bf16_f32 v23, v100, v101
	v_lshl_add_u64 v[100:101], v[168:169], 0, v[24:25]
	s_and_b64 vcc, exec, s[6:7]
	v_add_u32_e32 v110, 0x90, v209
	global_store_dwordx4 v[100:101], v[20:23], off sc1
	s_cbranch_vccnz .LBB0_1996
	v_lshl_add_u32 v18, v110, 2, 0
	v_add_u32_e32 v18, 0x18300, v18
	ds_read_b32 v18, v18
; __device__ __forceinline__ u32x4 pack8(const f32x4 a, const f32x4 b) { u32x4 w; w.x = cvt_pk_bf16(a[0], a[1]); w.y = cvt_pk_bf16(a[2], a[3]); w.z = cvt_pk_bf16(b[0], b[1]); w.w = cvt_pk_bf16(b[2], b[3]); return w; }
;     __device__ __forceinline__ void fused(f32x4 (&acc)[2][2][4][2], const pg8::Unit& u_, int wr_, int wc_, int fr_, int fq_, LAS unsigned char* lds, int tid_) const {
;     ...
; #pragma unroll
;         for (int bj = 0; bj < 2; ++bj) { f32x4 G[2], SH[2];
; #pragma unroll
;             for (int n = 0; n < 2; ++n) { const int c = col0 + bj * HALF + 4 * n; const f32x4 gg = *(const f32x4*)(g2 + c), sc = *(const f32x4*)(mrow + 4 * D + c);
;                 G[n] = gg * (sc + 1.f); SH[n] = *(const f32x4*)(mrow + 3 * D + c); }
; #pragma unroll
;             for (int ai = 0; ai < 2; ++ai)
; #pragma unroll
;                 for (int m = 0; m < 4; ++m) { const int rl = ai * HALF + wr * 64 + m * 16 + fr; const float r = bad ? __builtin_nanf("") : Sr[rl];
;                     *(u32x4*)(HB + (size_t)(u.pm * BM + rl) * D + col0 + bj * HALF) = pack8(acc[ai][bj][m][0] * r * G[0] + SH[0], acc[ai][bj][m][1] * r * G[1] + SH[1]); }
;             asm volatile("" ::: "memory"); }
.LBB0_1996:
	s_waitcnt lgkmcnt(0)
	v_pk_mul_f32 v[22:23], v[18:19], v[138:139] op_sel_hi:[0,1]
	v_pk_mul_f32 v[20:21], v[18:19], v[140:141] op_sel_hi:[0,1]
	v_pk_fma_f32 v[22:23], v[14:15], v[22:23], v[6:7]
	v_pk_mul_f32 v[24:25], v[18:19], v[136:137] op_sel_hi:[0,1]
	v_pk_mul_f32 v[18:19], v[18:19], v[134:135] op_sel_hi:[0,1]
	v_pk_fma_f32 v[102:103], v[10:11], v[18:19], v[2:3]
	v_cvt_pk_bf16_f32 v18, v22, v23
	v_add_u32_e32 v22, s27, v110
	v_ashrrev_i32_e32 v23, 31, v22
	v_pk_fma_f32 v[20:21], v[16:17], v[20:21], v[8:9]
	v_pk_fma_f32 v[24:25], v[12:13], v[24:25], v[4:5]
	v_lshlrev_b64 v[22:23], 11, v[22:23]
	v_cvt_pk_bf16_f32 v19, v20, v21
	v_cvt_pk_bf16_f32 v20, v102, v103
	v_cvt_pk_bf16_f32 v21, v24, v25
	v_lshl_add_u64 v[102:103], v[168:169], 0, v[22:23]
	global_store_dwordx4 v[102:103], v[18:21], off sc1
	v_add_u32_e32 v111, 0xa0, v209
	s_and_b64 vcc, exec, s[6:7]
	v_mov_b32_e32 v18, 0x7fc00000
	v_mov_b32_e32 v20, 0x7fc00000
	s_cbranch_vccnz .LBB0_1998
	v_lshl_add_u32 v19, v111, 2, 0
	v_add_u32_e32 v19, 0x18300, v19
	ds_read_b32 v20, v19
.LBB0_1998:
	s_waitcnt lgkmcnt(0)
	v_pk_mul_f32 v[24:25], v[20:21], v[172:173] op_sel_hi:[0,1]
	v_pk_mul_f32 v[22:23], v[20:21], v[174:175] op_sel_hi:[0,1]
	v_pk_fma_f32 v[24:25], v[14:15], v[24:25], v[6:7]
	v_pk_mul_f32 v[104:105], v[20:21], v[144:145] op_sel_hi:[0,1]
	v_pk_mul_f32 v[20:21], v[20:21], v[142:143] op_sel_hi:[0,1]
	v_pk_fma_f32 v[106:107], v[10:11], v[20:21], v[2:3]
	v_cvt_pk_bf16_f32 v20, v24, v25
	v_add_u32_e32 v24, s27, v111
	v_ashrrev_i32_e32 v25, 31, v24
	v_pk_fma_f32 v[22:23], v[16:17], v[22:23], v[8:9]
	v_pk_fma_f32 v[104:105], v[12:13], v[104:105], v[4:5]
	v_lshlrev_b64 v[24:25], 11, v[24:25]
	v_cvt_pk_bf16_f32 v21, v22, v23
	v_cvt_pk_bf16_f32 v22, v106, v107
	v_cvt_pk_bf16_f32 v23, v104, v105
	v_lshl_add_u64 v[104:105], v[168:169], 0, v[24:25]
	s_and_b64 vcc, exec, s[6:7]
	v_add_u32_e32 v112, 0xb0, v209
	global_store_dwordx4 v[104:105], v[20:23], off sc1
	s_cbranch_vccnz .LBB0_2000
	v_lshl_add_u32 v18, v112, 2, 0
	v_add_u32_e32 v18, 0x18300, v18
	ds_read_b32 v18, v18
.LBB0_2000:
	s_waitcnt lgkmcnt(0)
	v_pk_mul_f32 v[20:21], v[18:19], v[182:183] op_sel_hi:[0,1]
	v_pk_mul_f32 v[22:23], v[18:19], v[180:181] op_sel_hi:[0,1]
	v_pk_fma_f32 v[8:9], v[16:17], v[20:21], v[8:9]
	v_pk_fma_f32 v[6:7], v[14:15], v[22:23], v[6:7]
	v_pk_mul_f32 v[14:15], v[18:19], v[178:179] op_sel_hi:[0,1]
	v_pk_mul_f32 v[16:17], v[18:19], v[176:177] op_sel_hi:[0,1]
	v_pk_fma_f32 v[12:13], v[12:13], v[14:15], v[4:5]
	v_pk_fma_f32 v[4:5], v[10:11], v[16:17], v[2:3]
	v_cvt_pk_bf16_f32 v2, v6, v7
	v_add_u32_e32 v6, s27, v112
	v_ashrrev_i32_e32 v7, 31, v6
	v_lshlrev_b64 v[6:7], 11, v[6:7]
	v_cvt_pk_bf16_f32 v3, v8, v9
	v_cvt_pk_bf16_f32 v4, v4, v5
	v_cvt_pk_bf16_f32 v5, v12, v13
	v_lshl_add_u64 v[106:107], v[168:169], 0, v[6:7]
	global_store_dwordx4 v[106:107], v[2:5], off sc1
	global_load_dwordx4 v[10:13], v[42:43], off offset:528
	global_load_dwordx4 v[18:21], v[42:43], off offset:512
	global_load_dwordx4 v[14:17], v[44:45], off offset:528
	global_load_dwordx4 v[22:25], v[44:45], off offset:512
	global_load_dwordx4 v[2:5], v[184:185], off offset:528
	global_load_dwordx4 v[6:9], v[184:185], off offset:512
	v_mov_b32_e32 v42, 0x7fc00000
	s_and_b64 vcc, exec, s[6:7]
	v_mov_b32_e32 v44, 0x7fc00000
	s_cbranch_vccnz .LBB0_2002
	v_lshl_add_u32 v43, v209, 2, 0
	v_add_u32_e32 v43, 0x18300, v43
	ds_read_b32 v44, v43
.LBB0_2002:
	s_waitcnt vmcnt(2)
	v_pk_add_f32 v[24:25], v[24:25], 1.0 op_sel_hi:[1,0]
	v_pk_add_f32 v[22:23], v[22:23], 1.0 op_sel_hi:[1,0]
	v_pk_add_f32 v[14:15], v[14:15], 1.0 op_sel_hi:[1,0]
	v_pk_add_f32 v[16:17], v[16:17], 1.0 op_sel_hi:[1,0]
	v_pk_mul_f32 v[20:21], v[20:21], v[24:25]
	v_pk_mul_f32 v[18:19], v[18:19], v[22:23]
	v_pk_mul_f32 v[12:13], v[12:13], v[16:17]
	v_pk_mul_f32 v[10:11], v[10:11], v[14:15]
	s_waitcnt lgkmcnt(0)
	v_pk_mul_f32 v[14:15], v[44:45], v[68:69] op_sel_hi:[0,1]
	v_pk_mul_f32 v[16:17], v[44:45], v[66:67] op_sel_hi:[0,1]
	s_waitcnt vmcnt(0)
	v_pk_fma_f32 v[22:23], v[20:21], v[14:15], v[8:9]
	v_pk_fma_f32 v[14:15], v[18:19], v[16:17], v[6:7]
	v_pk_mul_f32 v[16:17], v[44:45], v[56:57] op_sel_hi:[0,1]
	v_pk_mul_f32 v[24:25], v[44:45], v[54:55] op_sel_hi:[0,1]
	v_pk_fma_f32 v[44:45], v[12:13], v[16:17], v[4:5]
	v_pk_fma_f32 v[16:17], v[10:11], v[24:25], v[2:3]
	v_cvt_pk_bf16_f32 v14, v14, v15
	v_cvt_pk_bf16_f32 v15, v22, v23
	v_cvt_pk_bf16_f32 v16, v16, v17
	v_cvt_pk_bf16_f32 v17, v44, v45
	s_and_b64 vcc, exec, s[6:7]
	global_store_dwordx4 v[92:93], v[14:17], off offset:256 sc1
	s_cbranch_vccnz .LBB0_2004
	s_nop 0
	v_lshl_add_u32 v14, v170, 2, 0
	v_add_u32_e32 v14, 0x18300, v14
	ds_read_b32 v42, v14
.LBB0_2004:
	s_waitcnt lgkmcnt(0)
	v_pk_mul_f32 v[14:15], v[42:43], v[76:77] op_sel_hi:[0,1]
	v_pk_mul_f32 v[16:17], v[42:43], v[74:75] op_sel_hi:[0,1]
	v_pk_fma_f32 v[22:23], v[20:21], v[14:15], v[8:9]
	v_pk_fma_f32 v[14:15], v[18:19], v[16:17], v[6:7]
	v_pk_mul_f32 v[16:17], v[42:43], v[32:33] op_sel_hi:[0,1]
	v_pk_mul_f32 v[24:25], v[42:43], v[30:31] op_sel_hi:[0,1]
	v_pk_fma_f32 v[30:31], v[12:13], v[16:17], v[4:5]
	v_pk_fma_f32 v[16:17], v[10:11], v[24:25], v[2:3]
	v_cvt_pk_bf16_f32 v14, v14, v15
	v_cvt_pk_bf16_f32 v15, v22, v23
	v_cvt_pk_bf16_f32 v16, v16, v17
	v_cvt_pk_bf16_f32 v17, v30, v31
	global_store_dwordx4 v[94:95], v[14:17], off offset:256 sc1
	s_and_b64 vcc, exec, s[6:7]
	s_nop 0
	v_mov_b32_e32 v14, 0x7fc00000
	v_mov_b32_e32 v16, 0x7fc00000
	s_cbranch_vccnz .LBB0_2006
	v_lshl_add_u32 v15, v158, 2, 0
	v_add_u32_e32 v15, 0x18300, v15
	ds_read_b32 v16, v15
; __device__ __forceinline__ u32x4 pack8(const f32x4 a, const f32x4 b) { u32x4 w; w.x = cvt_pk_bf16(a[0], a[1]); w.y = cvt_pk_bf16(a[2], a[3]); w.z = cvt_pk_bf16(b[0], b[1]); w.w = cvt_pk_bf16(b[2], b[3]); return w; }
;     __device__ __forceinline__ void fused(f32x4 (&acc)[2][2][4][2], const pg8::Unit& u_, int wr_, int wc_, int fr_, int fq_, LAS unsigned char* lds, int tid_) const {
;     ...
; #pragma unroll
;         for (int bj = 0; bj < 2; ++bj) { f32x4 G[2], SH[2];
; #pragma unroll
;             for (int n = 0; n < 2; ++n) { const int c = col0 + bj * HALF + 4 * n; const f32x4 gg = *(const f32x4*)(g2 + c), sc = *(const f32x4*)(mrow + 4 * D + c);
;                 G[n] = gg * (sc + 1.f); SH[n] = *(const f32x4*)(mrow + 3 * D + c); }
; #pragma unroll
;             for (int ai = 0; ai < 2; ++ai)
; #pragma unroll
;                 for (int m = 0; m < 4; ++m) { const int rl = ai * HALF + wr * 64 + m * 16 + fr; const float r = bad ? __builtin_nanf("") : Sr[rl];
;                     *(u32x4*)(HB + (size_t)(u.pm * BM + rl) * D + col0 + bj * HALF) = pack8(acc[ai][bj][m][0] * r * G[0] + SH[0], acc[ai][bj][m][1] * r * G[1] + SH[1]); }
;             asm volatile("" ::: "memory"); }
.LBB0_2006:
	s_waitcnt lgkmcnt(0)
	v_pk_mul_f32 v[22:23], v[16:17], v[80:81] op_sel_hi:[0,1]
	v_pk_mul_f32 v[24:25], v[16:17], v[78:79] op_sel_hi:[0,1]
	v_pk_fma_f32 v[30:31], v[20:21], v[22:23], v[8:9]
	v_pk_fma_f32 v[22:23], v[18:19], v[24:25], v[6:7]
	v_pk_mul_f32 v[24:25], v[16:17], v[28:29] op_sel_hi:[0,1]
	v_pk_mul_f32 v[16:17], v[16:17], v[26:27] op_sel_hi:[0,1]
	v_pk_fma_f32 v[26:27], v[12:13], v[24:25], v[4:5]
	v_pk_fma_f32 v[16:17], v[10:11], v[16:17], v[2:3]
	v_cvt_pk_bf16_f32 v22, v22, v23
	v_cvt_pk_bf16_f32 v23, v30, v31
	v_cvt_pk_bf16_f32 v24, v16, v17
	v_cvt_pk_bf16_f32 v25, v26, v27
	s_and_b64 vcc, exec, s[6:7]
	global_store_dwordx4 v[96:97], v[22:25], off offset:256 sc1
	s_cbranch_vccnz .LBB0_2008
	v_lshl_add_u32 v14, v108, 2, 0
	v_add_u32_e32 v14, 0x18300, v14
	ds_read_b32 v14, v14
.LBB0_2008:
	s_waitcnt lgkmcnt(0)
	v_pk_mul_f32 v[16:17], v[14:15], v[46:47] op_sel_hi:[0,1]
	v_pk_mul_f32 v[22:23], v[14:15], v[90:91] op_sel_hi:[0,1]
	v_pk_mul_f32 v[24:25], v[14:15], v[36:37] op_sel_hi:[0,1]
	v_pk_mul_f32 v[14:15], v[14:15], v[34:35] op_sel_hi:[0,1]
	v_pk_fma_f32 v[16:17], v[20:21], v[16:17], v[8:9]
	v_pk_fma_f32 v[22:23], v[18:19], v[22:23], v[6:7]
	v_pk_fma_f32 v[24:25], v[12:13], v[24:25], v[4:5]
	v_pk_fma_f32 v[26:27], v[10:11], v[14:15], v[2:3]
	v_cvt_pk_bf16_f32 v14, v22, v23
	v_cvt_pk_bf16_f32 v15, v16, v17
	v_cvt_pk_bf16_f32 v16, v26, v27
	v_cvt_pk_bf16_f32 v17, v24, v25
	global_store_dwordx4 v[98:99], v[14:17], off offset:256 sc1
	s_and_b64 vcc, exec, s[6:7]
	s_nop 0
	v_mov_b32_e32 v14, 0x7fc00000
	v_mov_b32_e32 v16, 0x7fc00000
	s_cbranch_vccnz .LBB0_2010
	v_lshl_add_u32 v15, v109, 2, 0
	v_add_u32_e32 v15, 0x18300, v15
	ds_read_b32 v16, v15
.LBB0_2010:
	s_waitcnt lgkmcnt(0)
	v_pk_mul_f32 v[22:23], v[16:17], v[70:71] op_sel_hi:[0,1]
	v_pk_mul_f32 v[24:25], v[16:17], v[60:61] op_sel_hi:[0,1]
	v_pk_fma_f32 v[26:27], v[20:21], v[22:23], v[8:9]
	v_pk_fma_f32 v[22:23], v[18:19], v[24:25], v[6:7]
	v_pk_mul_f32 v[24:25], v[16:17], v[58:59] op_sel_hi:[0,1]
	v_pk_mul_f32 v[16:17], v[16:17], v[48:49] op_sel_hi:[0,1]
	v_pk_fma_f32 v[28:29], v[12:13], v[24:25], v[4:5]
	v_pk_fma_f32 v[16:17], v[10:11], v[16:17], v[2:3]
	v_cvt_pk_bf16_f32 v22, v22, v23
	v_cvt_pk_bf16_f32 v23, v26, v27
	v_cvt_pk_bf16_f32 v24, v16, v17
	v_cvt_pk_bf16_f32 v25, v28, v29
	s_and_b64 vcc, exec, s[6:7]
	global_store_dwordx4 v[100:101], v[22:25], off offset:256 sc1
	s_cbranch_vccnz .LBB0_2012
	v_lshl_add_u32 v14, v110, 2, 0
	v_add_u32_e32 v14, 0x18300, v14
	ds_read_b32 v14, v14
.LBB0_2012:
	s_waitcnt lgkmcnt(0)
	v_pk_mul_f32 v[16:17], v[14:15], v[86:87] op_sel_hi:[0,1]
	v_pk_mul_f32 v[22:23], v[14:15], v[84:85] op_sel_hi:[0,1]
	v_pk_mul_f32 v[24:25], v[14:15], v[82:83] op_sel_hi:[0,1]
	v_pk_mul_f32 v[14:15], v[14:15], v[72:73] op_sel_hi:[0,1]
	v_pk_fma_f32 v[16:17], v[20:21], v[16:17], v[8:9]
	v_pk_fma_f32 v[22:23], v[18:19], v[22:23], v[6:7]
	v_pk_fma_f32 v[24:25], v[12:13], v[24:25], v[4:5]
	v_pk_fma_f32 v[26:27], v[10:11], v[14:15], v[2:3]
	v_cvt_pk_bf16_f32 v14, v22, v23
	v_cvt_pk_bf16_f32 v15, v16, v17
	v_cvt_pk_bf16_f32 v16, v26, v27
	v_cvt_pk_bf16_f32 v17, v24, v25
	global_store_dwordx4 v[102:103], v[14:17], off offset:256 sc1
	s_and_b64 vcc, exec, s[6:7]
	s_nop 0
	v_mov_b32_e32 v14, 0x7fc00000
	v_mov_b32_e32 v16, 0x7fc00000
	s_cbranch_vccnz .LBB0_2014
	v_lshl_add_u32 v15, v111, 2, 0
	v_add_u32_e32 v15, 0x18300, v15
	ds_read_b32 v16, v15
.LBB0_2014:
	s_waitcnt lgkmcnt(0)
	v_pk_mul_f32 v[22:23], v[16:17], v[64:65] op_sel_hi:[0,1]
	v_pk_mul_f32 v[24:25], v[16:17], v[62:63] op_sel_hi:[0,1]
	v_pk_fma_f32 v[26:27], v[20:21], v[22:23], v[8:9]
	v_pk_fma_f32 v[22:23], v[18:19], v[24:25], v[6:7]
	v_pk_mul_f32 v[24:25], v[16:17], v[52:53] op_sel_hi:[0,1]
	v_pk_mul_f32 v[16:17], v[16:17], v[50:51] op_sel_hi:[0,1]
	v_pk_fma_f32 v[28:29], v[12:13], v[24:25], v[4:5]
	v_pk_fma_f32 v[16:17], v[10:11], v[16:17], v[2:3]
	v_cvt_pk_bf16_f32 v22, v22, v23
	v_cvt_pk_bf16_f32 v23, v26, v27
	v_cvt_pk_bf16_f32 v24, v16, v17
	v_cvt_pk_bf16_f32 v25, v28, v29
	s_and_b64 vcc, exec, s[6:7]
	global_store_dwordx4 v[104:105], v[22:25], off offset:256 sc1
	s_cbranch_vccnz .LBB0_2016
	v_lshl_add_u32 v14, v112, 2, 0
	v_add_u32_e32 v14, 0x18300, v14
	ds_read_b32 v14, v14
.LBB0_2016:
	s_waitcnt lgkmcnt(0)
	v_pk_mul_f32 v[16:17], v[14:15], v[116:117] op_sel_hi:[0,1]
	v_pk_mul_f32 v[22:23], v[14:15], v[88:89] op_sel_hi:[0,1]
	v_pk_fma_f32 v[8:9], v[20:21], v[16:17], v[8:9]
	v_pk_mul_f32 v[16:17], v[14:15], v[40:41] op_sel_hi:[0,1]
	v_pk_mul_f32 v[14:15], v[14:15], v[38:39] op_sel_hi:[0,1]
	v_pk_fma_f32 v[6:7], v[18:19], v[22:23], v[6:7]
	v_pk_fma_f32 v[12:13], v[12:13], v[16:17], v[4:5]
	v_pk_fma_f32 v[4:5], v[10:11], v[14:15], v[2:3]
	v_cvt_pk_bf16_f32 v2, v6, v7
	v_cvt_pk_bf16_f32 v3, v8, v9
	v_cvt_pk_bf16_f32 v4, v4, v5
	v_cvt_pk_bf16_f32 v5, v12, v13
	global_store_dwordx4 v[106:107], v[2:5], off offset:256 sc1
	s_andn2_b64 vcc, exec, s[2:3]
	s_mov_b64 s[0:1], -1
	s_cbranch_vccnz .LBB0_1926
	s_andn2_b64 vcc, exec, s[10:11]
	s_cbranch_vccnz .LBB0_1925
	s_barrier
	s_branch .LBB0_1925

; template <int VPT>
; __device__ __forceinline__ void topk_list(const Params& p, LAS unsigned char* lds, const float* a, int N, int cap, int rowbase, int mbase, int e) {
;     ...
;     if (active) {
; #pragma unroll
;         for (int j = 0; j < VPT; ++j) {
;             const int i = tid * VPT + j, row = rowbase + i; int slot = -1;
;             if (k[j] > T) slot = gtb++;
;             else if (k[j] == T) { if (eqb < need) slot = G + eqb; ++eqb; }
;             if (slot >= 0) { const int m = mbase + slot; WSP(int, OFF_RIDX)[e * MEXP + m] = row; WSP(float, OFF_GATE)[e * MEXP + m] = __uint_as_float(k[j] >> 2); WSP(int, OFF_SLOT)[row * 16 + e] = m; }
;             else WSP(int, OFF_SLOT)[row * 16 + e] = -1;
;         }
.LBB0_2261:
	s_or_b64 exec, exec, s[0:1]
	v_mov_b32_e32 v231, v3
	s_mul_i32 s98, s92, 0x4200
	v_subrev_u32_e32 v4, 15, v4
	v_add_u32_e32 v4, s98, v4
	v_ashrrev_i32_e32 v5, 31, v4
	v_lshl_add_u64 v[4:5], v[4:5], 2, s[4:5]
	global_store_dwordx4 v[4:5], v[216:219], off sc1
	global_store_dwordx4 v[4:5], v[220:223], off offset:16 sc1
	global_store_dwordx4 v[4:5], v[224:227], off offset:32 sc1
	global_store_dwordx4 v[4:5], v[228:231], off offset:48 sc1

; __device__ __forceinline__ float silu_fast(float v) { return v * __builtin_amdgcn_rcpf(1.f + __builtin_amdgcn_exp2f(-1.4426950408889634f * v)); }
; __device__ __forceinline__ u32x4 pack8(const f32x4 a, const f32x4 b) { u32x4 w; w.x = cvt_pk_bf16(a[0], a[1]); w.y = cvt_pk_bf16(a[2], a[3]); w.z = cvt_pk_bf16(b[0], b[1]); w.w = cvt_pk_bf16(b[2], b[3]); return w; }
;     __device__ __forceinline__ void operator()(const f32x4 (&acc)[2][2][4][2], const Unit& u, int wr, int wc, int fr, int fq) const {
;     ...
;             for (int m = 0; m < 4; ++m) { f32x4 h[2];
; #pragma unroll
;                 for (int n = 0; n < 2; ++n)
; #pragma unroll
;                     for (int j = 0; j < 4; ++j) h[n][j] = silu_fast(acc[ai][0][m][n][j]) * acc[ai][1][m][n][j];
;                 const int row = row0 + ai * HALF + m * 16;
;                 *(u32x4*)(base + ((size_t)(row >> 7) * (FF / 64) + (col0 >> 6)) * 8192 + (row & 127) * 64 + (col0 & 63)) = pack8(h[0], h[1]); }
.LBB0_2342:
	v_mul_f32_e32 v136, 0xbfb8aa3b, v126
	v_exp_f32_e32 v136, v136
	v_mul_f32_e32 v141, 0xbfb8aa3b, v127
	v_exp_f32_e32 v141, v141
	s_lshl_b32 s13, s52, 8
	v_add_f32_e32 v136, 1.0, v136
	v_rcp_f32_e32 v152, v136
	v_add_f32_e32 v136, 1.0, v141
	v_rcp_f32_e32 v153, v136
	v_mul_f32_e32 v136, 0xbfb8aa3b, v128
	v_mul_f32_e32 v141, 0xbfb8aa3b, v129
	v_exp_f32_e32 v136, v136
	v_exp_f32_e32 v141, v141
	v_pk_mul_f32 v[126:127], v[126:127], v[152:153]
	s_add_i32 s13, s13, s39
	v_pk_mul_f32 v[118:119], v[126:127], v[118:119]
	v_add_f32_e32 v126, 1.0, v136
	v_add_f32_e32 v127, 1.0, v141
	v_mul_f32_e32 v136, 0xbfb8aa3b, v122
	v_rcp_f32_e32 v126, v126
	v_rcp_f32_e32 v127, v127
	v_exp_f32_e32 v136, v136
	v_mul_f32_e32 v141, 0xbfb8aa3b, v123
	v_exp_f32_e32 v141, v141
	v_pk_mul_f32 v[126:127], v[128:129], v[126:127]
	v_add_f32_e32 v128, 1.0, v136
	v_mul_f32_e32 v136, 0xbfb8aa3b, v124
	v_add_f32_e32 v129, 1.0, v141
	v_exp_f32_e32 v136, v136
	v_mul_f32_e32 v141, 0xbfb8aa3b, v125
	v_exp_f32_e32 v141, v141
	v_rcp_f32_e32 v128, v128
	v_add_f32_e32 v136, 1.0, v136
	v_rcp_f32_e32 v129, v129
	v_rcp_f32_e32 v152, v136
	v_add_f32_e32 v136, 1.0, v141
	v_rcp_f32_e32 v153, v136
	s_lshl_b32 s2, s16, 7
	v_pk_mul_f32 v[122:123], v[122:123], v[128:129]
	s_or_b32 s2, s2, s40
	s_ashr_i32 s16, s13, 7
	v_pk_mul_f32 v[122:123], v[122:123], v[114:115]
	v_pk_mul_f32 v[114:115], v[124:125], v[152:153]
	s_ashr_i32 s3, s2, 6
	v_mad_i64_i32 v[148:149], s[18:19], s51, v163, v[138:139]
	s_mul_i32 s16, s16, 44
	v_pk_mul_f32 v[124:125], v[114:115], v[116:117]
	v_mul_f32_e32 v117, 0xbfb8aa3b, v110
	s_ashr_i32 s2, s3, 31
	s_ashr_i32 s19, s16, 31
	v_cvt_pk_bf16_f32 v114, v118, v119
	v_exp_f32_e32 v118, v117
	v_mul_f32_e32 v117, 0xbfb8aa3b, v111
	s_add_u32 s18, s16, s3
	v_exp_f32_e32 v119, v117
	s_addc_u32 s19, s19, s2
	s_lshl_b64 s[18:19], s[18:19], 14
	v_lshl_add_u64 v[150:151], v[148:149], 0, s[18:19]
	v_pk_mul_f32 v[120:121], v[126:127], v[120:121]
	v_mov_b32_e32 v141, v137
	v_cvt_pk_bf16_f32 v115, v120, v121
	v_cvt_pk_bf16_f32 v116, v122, v123
	v_cvt_pk_bf16_f32 v117, v124, v125
	v_add_f32_e32 v118, 1.0, v118
	v_add_f32_e32 v119, 1.0, v119
	v_lshl_add_u64 v[120:121], v[150:151], 0, v[140:141]
	v_rcp_f32_e32 v118, v118
	v_rcp_f32_e32 v119, v119
	global_store_dwordx4 v[120:121], v[114:117], off sc1
	v_mov_b32_e32 v143, v137
	v_mov_b32_e32 v145, v137
	v_mul_f32_e32 v114, 0xbfb8aa3b, v112
	v_mul_f32_e32 v115, 0xbfb8aa3b, v113
	v_exp_f32_e32 v114, v114
	v_exp_f32_e32 v115, v115
	v_pk_mul_f32 v[110:111], v[110:111], v[118:119]
	s_addk_i32 s13, 0x80
	v_pk_mul_f32 v[102:103], v[110:111], v[102:103]
	v_add_f32_e32 v110, 1.0, v114
	v_add_f32_e32 v111, 1.0, v115
	v_mul_f32_e32 v114, 0xbfb8aa3b, v106
	v_mul_f32_e32 v115, 0xbfb8aa3b, v107
	v_rcp_f32_e32 v110, v110
	v_rcp_f32_e32 v111, v111
	v_exp_f32_e32 v114, v114
	v_exp_f32_e32 v115, v115
	s_ashr_i32 s13, s13, 7
	v_pk_mul_f32 v[110:111], v[112:113], v[110:111]
	v_add_f32_e32 v112, 1.0, v114
	v_add_f32_e32 v113, 1.0, v115
	v_mul_f32_e32 v114, 0xbfb8aa3b, v108
	v_mul_f32_e32 v115, 0xbfb8aa3b, v109
	v_exp_f32_e32 v114, v114
	v_exp_f32_e32 v115, v115
	v_rcp_f32_e32 v112, v112
	v_rcp_f32_e32 v113, v113
	v_add_f32_e32 v114, 1.0, v114
	v_add_f32_e32 v115, 1.0, v115
	v_rcp_f32_e32 v114, v114
	v_rcp_f32_e32 v115, v115
	v_pk_mul_f32 v[106:107], v[106:107], v[112:113]
	v_pk_mul_f32 v[104:105], v[110:111], v[104:105]
	v_pk_mul_f32 v[106:107], v[106:107], v[98:99]
	v_pk_mul_f32 v[98:99], v[108:109], v[114:115]
	s_mul_i32 s13, s13, 44
	v_pk_mul_f32 v[108:109], v[98:99], v[100:101]
	v_mul_f32_e32 v99, 0xbfb8aa3b, v94
	v_exp_f32_e32 v100, v99
	v_mul_f32_e32 v99, 0xbfb8aa3b, v95
	v_exp_f32_e32 v101, v99
	v_cvt_pk_bf16_f32 v98, v102, v103
	v_add_f32_e32 v100, 1.0, v100
	v_rcp_f32_e32 v102, v100
	v_add_f32_e32 v100, 1.0, v101
	v_cvt_pk_bf16_f32 v99, v104, v105
	v_rcp_f32_e32 v103, v100
	v_cvt_pk_bf16_f32 v100, v106, v107
	v_cvt_pk_bf16_f32 v101, v108, v109
	global_store_dwordx4 v[120:121], v[98:101], off offset:2048 sc1
	v_pk_mul_f32 v[94:95], v[94:95], v[102:103]
	s_ashr_i32 s16, s13, 31
	v_mul_f32_e32 v98, 0xbfb8aa3b, v96
	v_mul_f32_e32 v99, 0xbfb8aa3b, v97
	v_exp_f32_e32 v98, v98
	v_exp_f32_e32 v99, v99
	v_pk_mul_f32 v[86:87], v[94:95], v[86:87]
	s_add_u32 s18, s13, s3
	v_add_f32_e32 v94, 1.0, v98
	v_add_f32_e32 v95, 1.0, v99
	v_mul_f32_e32 v98, 0xbfb8aa3b, v90
	v_mul_f32_e32 v99, 0xbfb8aa3b, v91
	v_rcp_f32_e32 v94, v94
	v_rcp_f32_e32 v95, v95
	v_exp_f32_e32 v98, v98
	v_exp_f32_e32 v99, v99
	s_addc_u32 s19, s16, s2
	v_pk_mul_f32 v[94:95], v[96:97], v[94:95]
	v_add_f32_e32 v96, 1.0, v98
	v_add_f32_e32 v97, 1.0, v99
	v_mul_f32_e32 v98, 0xbfb8aa3b, v92
	v_mul_f32_e32 v99, 0xbfb8aa3b, v93
	v_exp_f32_e32 v98, v98
	v_exp_f32_e32 v99, v99
	v_rcp_f32_e32 v96, v96
	v_rcp_f32_e32 v97, v97
	v_add_f32_e32 v98, 1.0, v98
	v_add_f32_e32 v99, 1.0, v99
	v_rcp_f32_e32 v98, v98
	v_rcp_f32_e32 v99, v99
	v_pk_mul_f32 v[90:91], v[90:91], v[96:97]
	v_pk_mul_f32 v[88:89], v[94:95], v[88:89]
	v_pk_mul_f32 v[90:91], v[90:91], v[82:83]
	v_pk_mul_f32 v[82:83], v[92:93], v[98:99]
	s_lshl_b64 s[2:3], s[18:19], 14
	v_pk_mul_f32 v[92:93], v[82:83], v[84:85]
	v_mul_f32_e32 v85, 0xbfb8aa3b, v78
	v_cvt_pk_bf16_f32 v82, v86, v87
	v_exp_f32_e32 v86, v85
	v_mul_f32_e32 v85, 0xbfb8aa3b, v79
	v_exp_f32_e32 v87, v85
	v_cvt_pk_bf16_f32 v83, v88, v89
	v_cvt_pk_bf16_f32 v84, v90, v91
	v_cvt_pk_bf16_f32 v85, v92, v93
	v_add_f32_e32 v86, 1.0, v86
	v_add_f32_e32 v87, 1.0, v87
	v_lshl_add_u64 v[88:89], v[150:151], 0, v[142:143]
	v_rcp_f32_e32 v86, v86
	v_rcp_f32_e32 v87, v87
	global_store_dwordx4 v[88:89], v[82:85], off sc1
	s_and_b64 vcc, exec, s[0:1]
	s_mov_b64 s[0:1], -1
	v_mul_f32_e32 v82, 0xbfb8aa3b, v80
; __device__ __forceinline__ float silu_fast(float v) { return v * __builtin_amdgcn_rcpf(1.f + __builtin_amdgcn_exp2f(-1.4426950408889634f * v)); }
; __device__ __forceinline__ u32x4 pack8(const f32x4 a, const f32x4 b) { u32x4 w; w.x = cvt_pk_bf16(a[0], a[1]); w.y = cvt_pk_bf16(a[2], a[3]); w.z = cvt_pk_bf16(b[0], b[1]); w.w = cvt_pk_bf16(b[2], b[3]); return w; }
;     __device__ __forceinline__ void operator()(const f32x4 (&acc)[2][2][4][2], const Unit& u, int wr, int wc, int fr, int fq) const {
;     ...
;             for (int m = 0; m < 4; ++m) { f32x4 h[2];
; #pragma unroll
;                 for (int n = 0; n < 2; ++n)
; #pragma unroll
;                     for (int j = 0; j < 4; ++j) h[n][j] = silu_fast(acc[ai][0][m][n][j]) * acc[ai][1][m][n][j];
;                 const int row = row0 + ai * HALF + m * 16;
;                 *(u32x4*)(base + ((size_t)(row >> 7) * (FF / 64) + (col0 >> 6)) * 8192 + (row & 127) * 64 + (col0 & 63)) = pack8(h[0], h[1]); }
	v_mul_f32_e32 v83, 0xbfb8aa3b, v81
	v_exp_f32_e32 v82, v82
	v_exp_f32_e32 v83, v83
	v_pk_mul_f32 v[78:79], v[78:79], v[86:87]
	s_nop 0
	v_pk_mul_f32 v[70:71], v[78:79], v[70:71]
	v_add_f32_e32 v78, 1.0, v82
	v_add_f32_e32 v79, 1.0, v83
	v_mul_f32_e32 v82, 0xbfb8aa3b, v74
	v_mul_f32_e32 v83, 0xbfb8aa3b, v75
	v_rcp_f32_e32 v78, v78
	v_rcp_f32_e32 v79, v79
	v_exp_f32_e32 v82, v82
	v_exp_f32_e32 v83, v83
	v_pk_mul_f32 v[78:79], v[80:81], v[78:79]
	v_add_f32_e32 v80, 1.0, v82
	v_add_f32_e32 v81, 1.0, v83
	v_mul_f32_e32 v82, 0xbfb8aa3b, v76
	v_mul_f32_e32 v83, 0xbfb8aa3b, v77
	v_exp_f32_e32 v82, v82
	v_exp_f32_e32 v83, v83
	v_rcp_f32_e32 v80, v80
	v_rcp_f32_e32 v81, v81
	v_add_f32_e32 v82, 1.0, v82
	v_add_f32_e32 v83, 1.0, v83
	v_rcp_f32_e32 v82, v82
	v_rcp_f32_e32 v83, v83
	v_pk_mul_f32 v[74:75], v[74:75], v[80:81]
	v_pk_mul_f32 v[72:73], v[78:79], v[72:73]
	v_pk_mul_f32 v[74:75], v[74:75], v[66:67]
	v_pk_mul_f32 v[66:67], v[76:77], v[82:83]
	s_nop 0
	v_pk_mul_f32 v[76:77], v[66:67], v[68:69]
	v_cvt_pk_bf16_f32 v66, v70, v71
	v_cvt_pk_bf16_f32 v67, v72, v73
	v_cvt_pk_bf16_f32 v68, v74, v75
	v_cvt_pk_bf16_f32 v69, v76, v77
	v_lshl_add_u64 v[70:71], v[150:151], 0, v[144:145]
	global_store_dwordx4 v[70:71], v[66:69], off sc1
	s_nop 1
	v_mul_f32_e32 v66, 0xbfb8aa3b, v62
	v_exp_f32_e32 v66, v66
	v_mul_f32_e32 v67, 0xbfb8aa3b, v63
	v_exp_f32_e32 v67, v67
	v_add_f32_e32 v66, 1.0, v66
	v_rcp_f32_e32 v68, v66
	v_add_f32_e32 v66, 1.0, v67
	v_rcp_f32_e32 v69, v66
	v_lshl_add_u64 v[66:67], v[148:149], 0, s[2:3]
	v_pk_mul_f32 v[62:63], v[62:63], v[68:69]
	v_mul_f32_e32 v68, 0xbfb8aa3b, v64
	v_mul_f32_e32 v69, 0xbfb8aa3b, v65
	v_exp_f32_e32 v68, v68
	v_exp_f32_e32 v69, v69
	v_pk_mul_f32 v[54:55], v[62:63], v[54:55]
	v_add_f32_e32 v62, 1.0, v68
	v_add_f32_e32 v63, 1.0, v69
	v_mul_f32_e32 v68, 0xbfb8aa3b, v58
	v_mul_f32_e32 v69, 0xbfb8aa3b, v59
	v_rcp_f32_e32 v62, v62
	v_rcp_f32_e32 v63, v63
	v_exp_f32_e32 v68, v68
	v_exp_f32_e32 v69, v69
	v_pk_mul_f32 v[62:63], v[64:65], v[62:63]
	v_add_f32_e32 v64, 1.0, v68
	v_add_f32_e32 v65, 1.0, v69
	v_mul_f32_e32 v68, 0xbfb8aa3b, v60
	v_mul_f32_e32 v69, 0xbfb8aa3b, v61
	v_exp_f32_e32 v68, v68
	v_exp_f32_e32 v69, v69
	v_rcp_f32_e32 v64, v64
	v_rcp_f32_e32 v65, v65
	v_add_f32_e32 v68, 1.0, v68
	v_add_f32_e32 v69, 1.0, v69
	v_rcp_f32_e32 v68, v68
	v_rcp_f32_e32 v69, v69
	v_pk_mul_f32 v[58:59], v[58:59], v[64:65]
	v_pk_mul_f32 v[56:57], v[62:63], v[56:57]
	v_pk_mul_f32 v[58:59], v[58:59], v[50:51]
	v_pk_mul_f32 v[50:51], v[60:61], v[68:69]
	s_nop 0
	v_pk_mul_f32 v[60:61], v[50:51], v[52:53]
	v_mul_f32_e32 v52, 0xbfb8aa3b, v46
	v_exp_f32_e32 v53, v52
	v_mul_f32_e32 v52, 0xbfb8aa3b, v47
	v_cvt_pk_bf16_f32 v50, v54, v55
	v_exp_f32_e32 v55, v52
	v_add_f32_e32 v53, 1.0, v53
	v_rcp_f32_e32 v54, v53
	v_cvt_pk_bf16_f32 v51, v56, v57
	v_add_f32_e32 v53, 1.0, v55
	v_cvt_pk_bf16_f32 v52, v58, v59
	v_rcp_f32_e32 v55, v53
	v_cvt_pk_bf16_f32 v53, v60, v61
	v_lshl_add_u64 v[56:57], v[66:67], 0, v[140:141]
	global_store_dwordx4 v[56:57], v[50:53], off sc1
	v_pk_mul_f32 v[46:47], v[46:47], v[54:55]
	s_nop 0
	v_mul_f32_e32 v50, 0xbfb8aa3b, v48
	v_mul_f32_e32 v51, 0xbfb8aa3b, v49
	v_exp_f32_e32 v50, v50
	v_exp_f32_e32 v51, v51
	v_pk_mul_f32 v[38:39], v[46:47], v[38:39]
	v_add_f32_e32 v46, 1.0, v50
	v_add_f32_e32 v47, 1.0, v51
	v_mul_f32_e32 v50, 0xbfb8aa3b, v42
	v_mul_f32_e32 v51, 0xbfb8aa3b, v43
	v_rcp_f32_e32 v46, v46
	v_rcp_f32_e32 v47, v47
	v_exp_f32_e32 v50, v50
	v_exp_f32_e32 v51, v51
	v_pk_mul_f32 v[46:47], v[48:49], v[46:47]
	v_add_f32_e32 v48, 1.0, v50
	v_add_f32_e32 v49, 1.0, v51
	v_mul_f32_e32 v50, 0xbfb8aa3b, v44
	v_mul_f32_e32 v51, 0xbfb8aa3b, v45
	v_exp_f32_e32 v50, v50
	v_exp_f32_e32 v51, v51
; __device__ __forceinline__ float silu_fast(float v) { return v * __builtin_amdgcn_rcpf(1.f + __builtin_amdgcn_exp2f(-1.4426950408889634f * v)); }
; __device__ __forceinline__ u32x4 pack8(const f32x4 a, const f32x4 b) { u32x4 w; w.x = cvt_pk_bf16(a[0], a[1]); w.y = cvt_pk_bf16(a[2], a[3]); w.z = cvt_pk_bf16(b[0], b[1]); w.w = cvt_pk_bf16(b[2], b[3]); return w; }
;     __device__ __forceinline__ void operator()(const f32x4 (&acc)[2][2][4][2], const Unit& u, int wr, int wc, int fr, int fq) const {
;     ...
;             for (int m = 0; m < 4; ++m) { f32x4 h[2];
; #pragma unroll
;                 for (int n = 0; n < 2; ++n)
; #pragma unroll
;                     for (int j = 0; j < 4; ++j) h[n][j] = silu_fast(acc[ai][0][m][n][j]) * acc[ai][1][m][n][j];
;                 const int row = row0 + ai * HALF + m * 16;
;                 *(u32x4*)(base + ((size_t)(row >> 7) * (FF / 64) + (col0 >> 6)) * 8192 + (row & 127) * 64 + (col0 & 63)) = pack8(h[0], h[1]); }
	v_rcp_f32_e32 v48, v48
	v_rcp_f32_e32 v49, v49
	v_add_f32_e32 v50, 1.0, v50
	v_add_f32_e32 v51, 1.0, v51
	v_rcp_f32_e32 v50, v50
	v_rcp_f32_e32 v51, v51
	v_pk_mul_f32 v[42:43], v[42:43], v[48:49]
	v_pk_mul_f32 v[40:41], v[46:47], v[40:41]
	v_pk_mul_f32 v[42:43], v[42:43], v[34:35]
	v_pk_mul_f32 v[34:35], v[44:45], v[50:51]
	s_nop 0
	v_pk_mul_f32 v[44:45], v[34:35], v[36:37]
	v_mul_f32_e32 v35, 0xbfb8aa3b, v30
	v_exp_f32_e32 v36, v35
	v_mul_f32_e32 v35, 0xbfb8aa3b, v31
	v_exp_f32_e32 v37, v35
	v_cvt_pk_bf16_f32 v34, v38, v39
	v_add_f32_e32 v36, 1.0, v36
	v_rcp_f32_e32 v38, v36
	v_add_f32_e32 v36, 1.0, v37
	v_cvt_pk_bf16_f32 v35, v40, v41
	v_rcp_f32_e32 v39, v36
	v_cvt_pk_bf16_f32 v36, v42, v43
	v_cvt_pk_bf16_f32 v37, v44, v45
	global_store_dwordx4 v[56:57], v[34:37], off offset:2048 sc1
	v_pk_mul_f32 v[30:31], v[30:31], v[38:39]
	s_nop 0
	v_mul_f32_e32 v34, 0xbfb8aa3b, v32
	v_mul_f32_e32 v35, 0xbfb8aa3b, v33
	v_exp_f32_e32 v34, v34
	v_exp_f32_e32 v35, v35
	v_pk_mul_f32 v[22:23], v[30:31], v[22:23]
	v_add_f32_e32 v30, 1.0, v34
	v_add_f32_e32 v31, 1.0, v35
	v_mul_f32_e32 v34, 0xbfb8aa3b, v26
	v_mul_f32_e32 v35, 0xbfb8aa3b, v27
	v_rcp_f32_e32 v30, v30
	v_rcp_f32_e32 v31, v31
	v_exp_f32_e32 v34, v34
	v_exp_f32_e32 v35, v35
	v_pk_mul_f32 v[30:31], v[32:33], v[30:31]
	v_add_f32_e32 v32, 1.0, v34
	v_add_f32_e32 v33, 1.0, v35
	v_mul_f32_e32 v34, 0xbfb8aa3b, v28
	v_mul_f32_e32 v35, 0xbfb8aa3b, v29
	v_exp_f32_e32 v34, v34
	v_exp_f32_e32 v35, v35
	v_rcp_f32_e32 v32, v32
	v_rcp_f32_e32 v33, v33
	v_add_f32_e32 v34, 1.0, v34
	v_add_f32_e32 v35, 1.0, v35
	v_rcp_f32_e32 v34, v34
	v_rcp_f32_e32 v35, v35
	v_pk_mul_f32 v[26:27], v[26:27], v[32:33]
	v_pk_mul_f32 v[24:25], v[30:31], v[24:25]
	v_pk_mul_f32 v[26:27], v[26:27], v[18:19]
	v_pk_mul_f32 v[18:19], v[28:29], v[34:35]
	s_nop 0
	v_pk_mul_f32 v[28:29], v[18:19], v[20:21]
	v_mul_f32_e32 v20, 0xbfb8aa3b, v14
	v_exp_f32_e32 v21, v20
	v_mul_f32_e32 v20, 0xbfb8aa3b, v15
	v_cvt_pk_bf16_f32 v18, v22, v23
	v_exp_f32_e32 v23, v20
	v_add_f32_e32 v21, 1.0, v21
	v_rcp_f32_e32 v22, v21
	v_cvt_pk_bf16_f32 v19, v24, v25
	v_add_f32_e32 v21, 1.0, v23
	v_cvt_pk_bf16_f32 v20, v26, v27
	v_rcp_f32_e32 v23, v21
	v_cvt_pk_bf16_f32 v21, v28, v29
	v_lshl_add_u64 v[24:25], v[66:67], 0, v[142:143]
	global_store_dwordx4 v[24:25], v[18:21], off sc1
	v_pk_mul_f32 v[14:15], v[14:15], v[22:23]
	s_nop 0
	v_mul_f32_e32 v18, 0xbfb8aa3b, v16
	v_mul_f32_e32 v19, 0xbfb8aa3b, v17
	v_exp_f32_e32 v18, v18
	v_exp_f32_e32 v19, v19
	v_pk_mul_f32 v[6:7], v[14:15], v[6:7]
	v_add_f32_e32 v14, 1.0, v18
	v_add_f32_e32 v15, 1.0, v19
	v_mul_f32_e32 v18, 0xbfb8aa3b, v10
	v_mul_f32_e32 v19, 0xbfb8aa3b, v11
	v_rcp_f32_e32 v14, v14
	v_rcp_f32_e32 v15, v15
	v_exp_f32_e32 v18, v18
	v_exp_f32_e32 v19, v19
	v_pk_mul_f32 v[14:15], v[16:17], v[14:15]
	v_add_f32_e32 v16, 1.0, v18
	v_add_f32_e32 v17, 1.0, v19
	v_mul_f32_e32 v18, 0xbfb8aa3b, v12
	v_mul_f32_e32 v19, 0xbfb8aa3b, v13
	v_exp_f32_e32 v18, v18
	v_exp_f32_e32 v19, v19
	v_rcp_f32_e32 v16, v16
	v_rcp_f32_e32 v17, v17
	v_add_f32_e32 v18, 1.0, v18
	v_add_f32_e32 v19, 1.0, v19
	v_rcp_f32_e32 v18, v18
	v_rcp_f32_e32 v19, v19
	v_pk_mul_f32 v[10:11], v[10:11], v[16:17]
	v_pk_mul_f32 v[8:9], v[14:15], v[8:9]
	v_pk_mul_f32 v[10:11], v[10:11], v[2:3]
	v_pk_mul_f32 v[2:3], v[12:13], v[18:19]
	s_nop 0
	v_pk_mul_f32 v[12:13], v[2:3], v[4:5]
	v_cvt_pk_bf16_f32 v2, v6, v7
	v_cvt_pk_bf16_f32 v3, v8, v9
	v_cvt_pk_bf16_f32 v4, v10, v11
	v_cvt_pk_bf16_f32 v5, v12, v13
	v_lshl_add_u64 v[6:7], v[66:67], 0, v[144:145]
	global_store_dwordx4 v[6:7], v[2:5], off sc1
	s_cbranch_vccnz .LBB0_2331
	s_andn2_b64 vcc, exec, s[4:5]
	s_cbranch_vccnz .LBB0_2330
	s_barrier
	s_branch .LBB0_2330

; __device__ __forceinline__ u32x4 pack8(const f32x4 a, const f32x4 b) { u32x4 w; w.x = cvt_pk_bf16(a[0], a[1]); w.y = cvt_pk_bf16(a[2], a[3]); w.z = cvt_pk_bf16(b[0], b[1]); w.w = cvt_pk_bf16(b[2], b[3]); return w; }
;     __device__ __forceinline__ void operator()(const f32x4 (&acc)[2][2][4][2], const Unit& u, int wr, int wc, int fr, int fq) const {
;     ...
; #pragma unroll
;         for (int ai = 0; ai < 2; ++ai)
; #pragma unroll
;             for (int m = 0; m < 4; ++m) { const int row = row0 + ai * HALF + m * 16; const float gsc = gvp[row];
; #pragma unroll
;                 for (int bj = 0; bj < 2; ++bj) *(u32x4*)(base + (size_t)row * D + col0 + bj * HALF) = pack8(acc[ai][bj][m][0] * gsc, acc[ai][bj][m][1] * gsc); }
.LBB0_2414:
	s_mul_i32 s18, s51, 0x480000
	s_mul_hi_i32 s19, s51, 0x480000
	s_add_u32 s18, s84, s18
	s_mul_i32 s20, s51, 0x900
	s_addc_u32 s19, s85, s19
	s_ashr_i32 s21, s20, 31
	s_lshl_b64 s[20:21], s[20:21], 2
	v_lshl_add_u32 v168, s53, 8, v1
	s_add_u32 s20, s96, s20
	s_addc_u32 s21, s97, s21
	v_ashrrev_i32_e32 v169, 31, v168
	v_lshl_add_u64 v[148:149], v[168:169], 2, s[20:21]
	global_load_dword v170, v[148:149], off
	v_lshl_or_b32 v146, s52, 8, v152
	v_ashrrev_i32_e32 v147, 31, v146
	v_lshlrev_b64 v[172:173], 11, v[168:169]
	v_lshl_add_u64 v[174:175], v[146:147], 1, s[18:19]
	v_lshl_add_u64 v[146:147], v[174:175], 0, v[172:173]
	s_waitcnt vmcnt(0)
	v_pk_mul_f32 v[128:129], v[128:129], v[170:171] op_sel_hi:[1,0]
	v_pk_mul_f32 v[126:127], v[126:127], v[170:171] op_sel_hi:[1,0]
	v_pk_mul_f32 v[124:125], v[124:125], v[170:171] op_sel_hi:[1,0]
	v_pk_mul_f32 v[122:123], v[122:123], v[170:171] op_sel_hi:[1,0]
	v_pk_mul_f32 v[120:121], v[120:121], v[170:171] op_sel_hi:[1,0]
	v_pk_mul_f32 v[118:119], v[118:119], v[170:171] op_sel_hi:[1,0]
	v_pk_mul_f32 v[172:173], v[112:113], v[170:171] op_sel_hi:[1,0]
	v_pk_mul_f32 v[170:171], v[110:111], v[170:171] op_sel_hi:[1,0]
	v_cvt_pk_bf16_f32 v110, v126, v127
	v_cvt_pk_bf16_f32 v111, v128, v129
	v_cvt_pk_bf16_f32 v112, v122, v123
	v_cvt_pk_bf16_f32 v113, v124, v125
	v_cvt_pk_bf16_f32 v118, v118, v119
	v_cvt_pk_bf16_f32 v119, v120, v121
	v_cvt_pk_bf16_f32 v120, v170, v171
	v_cvt_pk_bf16_f32 v121, v172, v173
	global_store_dwordx4 v[146:147], v[110:113], off sc1
	global_store_dwordx4 v[146:147], v[118:121], off offset:256 sc1
	global_load_dword v110, v[148:149], off offset:64
	v_or_b32_e32 v112, 16, v168
	v_ashrrev_i32_e32 v113, 31, v112
	v_lshlrev_b64 v[112:113], 11, v[112:113]
	v_lshl_add_u64 v[112:113], v[174:175], 0, v[112:113]
	s_waitcnt vmcnt(0)
	v_pk_mul_f32 v[116:117], v[116:117], v[110:111] op_sel_hi:[1,0]
	v_pk_mul_f32 v[114:115], v[114:115], v[110:111] op_sel_hi:[1,0]
	v_pk_mul_f32 v[108:109], v[108:109], v[110:111] op_sel_hi:[1,0]
	v_pk_mul_f32 v[106:107], v[106:107], v[110:111] op_sel_hi:[1,0]
	v_pk_mul_f32 v[104:105], v[104:105], v[110:111] op_sel_hi:[1,0]
	v_pk_mul_f32 v[102:103], v[102:103], v[110:111] op_sel_hi:[1,0]
	v_pk_mul_f32 v[118:119], v[96:97], v[110:111] op_sel_hi:[1,0]
	v_pk_mul_f32 v[110:111], v[94:95], v[110:111] op_sel_hi:[1,0]
	v_cvt_pk_bf16_f32 v94, v114, v115
	v_cvt_pk_bf16_f32 v95, v116, v117
	v_cvt_pk_bf16_f32 v96, v106, v107
	v_cvt_pk_bf16_f32 v97, v108, v109
	v_cvt_pk_bf16_f32 v102, v102, v103
	v_cvt_pk_bf16_f32 v103, v104, v105
	v_cvt_pk_bf16_f32 v104, v110, v111
	v_cvt_pk_bf16_f32 v105, v118, v119
	global_store_dwordx4 v[112:113], v[94:97], off sc1
	global_store_dwordx4 v[112:113], v[102:105], off offset:256 sc1
	global_load_dword v94, v[148:149], off offset:128
	v_or_b32_e32 v96, 32, v168
	v_ashrrev_i32_e32 v97, 31, v96
	v_lshlrev_b64 v[96:97], 11, v[96:97]
	v_lshl_add_u64 v[96:97], v[174:175], 0, v[96:97]
	s_waitcnt vmcnt(0)
	v_pk_mul_f32 v[100:101], v[100:101], v[94:95] op_sel_hi:[1,0]
	v_pk_mul_f32 v[98:99], v[98:99], v[94:95] op_sel_hi:[1,0]
	v_pk_mul_f32 v[92:93], v[92:93], v[94:95] op_sel_hi:[1,0]
	v_pk_mul_f32 v[90:91], v[90:91], v[94:95] op_sel_hi:[1,0]
	v_pk_mul_f32 v[88:89], v[88:89], v[94:95] op_sel_hi:[1,0]
	v_pk_mul_f32 v[86:87], v[86:87], v[94:95] op_sel_hi:[1,0]
	v_pk_mul_f32 v[102:103], v[80:81], v[94:95] op_sel_hi:[1,0]
	v_pk_mul_f32 v[94:95], v[78:79], v[94:95] op_sel_hi:[1,0]
	v_cvt_pk_bf16_f32 v78, v98, v99
	v_cvt_pk_bf16_f32 v79, v100, v101
	v_cvt_pk_bf16_f32 v80, v90, v91
	v_cvt_pk_bf16_f32 v81, v92, v93
	v_cvt_pk_bf16_f32 v86, v86, v87
	v_cvt_pk_bf16_f32 v87, v88, v89
	v_cvt_pk_bf16_f32 v88, v94, v95
	v_cvt_pk_bf16_f32 v89, v102, v103
	global_store_dwordx4 v[96:97], v[78:81], off sc1
	global_store_dwordx4 v[96:97], v[86:89], off offset:256 sc1
	global_load_dword v78, v[148:149], off offset:192
	v_or_b32_e32 v80, 48, v168
	v_ashrrev_i32_e32 v81, 31, v80
	v_lshlrev_b64 v[80:81], 11, v[80:81]
	v_lshl_add_u64 v[80:81], v[174:175], 0, v[80:81]
	s_waitcnt vmcnt(0)
	v_pk_mul_f32 v[84:85], v[84:85], v[78:79] op_sel_hi:[1,0]
	v_pk_mul_f32 v[82:83], v[82:83], v[78:79] op_sel_hi:[1,0]
	v_pk_mul_f32 v[76:77], v[76:77], v[78:79] op_sel_hi:[1,0]
	v_pk_mul_f32 v[74:75], v[74:75], v[78:79] op_sel_hi:[1,0]
	v_pk_mul_f32 v[72:73], v[72:73], v[78:79] op_sel_hi:[1,0]
	v_pk_mul_f32 v[70:71], v[70:71], v[78:79] op_sel_hi:[1,0]
	v_pk_mul_f32 v[86:87], v[68:69], v[78:79] op_sel_hi:[1,0]
	v_pk_mul_f32 v[78:79], v[66:67], v[78:79] op_sel_hi:[1,0]
	v_cvt_pk_bf16_f32 v66, v82, v83
	v_cvt_pk_bf16_f32 v67, v84, v85
	v_cvt_pk_bf16_f32 v68, v74, v75
	v_cvt_pk_bf16_f32 v69, v76, v77
	v_cvt_pk_bf16_f32 v70, v70, v71
	v_cvt_pk_bf16_f32 v71, v72, v73
	v_cvt_pk_bf16_f32 v72, v78, v79
	v_cvt_pk_bf16_f32 v73, v86, v87
	global_store_dwordx4 v[80:81], v[66:69], off sc1
	global_store_dwordx4 v[80:81], v[70:73], off offset:256 sc1
	global_load_dword v66, v[148:149], off offset:512
	v_lshl_add_u64 v[68:69], v[146:147], 0, s[6:7]
	v_add_co_u32_e32 v70, vcc, s44, v146
	s_waitcnt vmcnt(0)
; __device__ __forceinline__ u32x4 pack8(const f32x4 a, const f32x4 b) { u32x4 w; w.x = cvt_pk_bf16(a[0], a[1]); w.y = cvt_pk_bf16(a[2], a[3]); w.z = cvt_pk_bf16(b[0], b[1]); w.w = cvt_pk_bf16(b[2], b[3]); return w; }
;     __device__ __forceinline__ void operator()(const f32x4 (&acc)[2][2][4][2], const Unit& u, int wr, int wc, int fr, int fq) const {
;     ...
; #pragma unroll
;         for (int ai = 0; ai < 2; ++ai)
; #pragma unroll
;             for (int m = 0; m < 4; ++m) { const int row = row0 + ai * HALF + m * 16; const float gsc = gvp[row];
; #pragma unroll
;                 for (int bj = 0; bj < 2; ++bj) *(u32x4*)(base + (size_t)row * D + col0 + bj * HALF) = pack8(acc[ai][bj][m][0] * gsc, acc[ai][bj][m][1] * gsc); }
	v_pk_mul_f32 v[64:65], v[64:65], v[66:67] op_sel_hi:[1,0]
	v_pk_mul_f32 v[62:63], v[62:63], v[66:67] op_sel_hi:[1,0]
	v_pk_mul_f32 v[60:61], v[60:61], v[66:67] op_sel_hi:[1,0]
	v_pk_mul_f32 v[58:59], v[58:59], v[66:67] op_sel_hi:[1,0]
	v_addc_co_u32_e32 v71, vcc, 0, v147, vcc
	v_pk_mul_f32 v[56:57], v[56:57], v[66:67] op_sel_hi:[1,0]
	v_pk_mul_f32 v[54:55], v[54:55], v[66:67] op_sel_hi:[1,0]
	v_pk_mul_f32 v[72:73], v[52:53], v[66:67] op_sel_hi:[1,0]
	v_pk_mul_f32 v[66:67], v[50:51], v[66:67] op_sel_hi:[1,0]
	v_cvt_pk_bf16_f32 v50, v62, v63
	v_cvt_pk_bf16_f32 v51, v64, v65
	v_cvt_pk_bf16_f32 v52, v58, v59
	v_cvt_pk_bf16_f32 v53, v60, v61
	v_cvt_pk_bf16_f32 v54, v54, v55
	v_cvt_pk_bf16_f32 v55, v56, v57
	v_cvt_pk_bf16_f32 v56, v66, v67
	v_cvt_pk_bf16_f32 v57, v72, v73
	global_store_dwordx4 v[70:71], v[50:53], off sc1
	global_store_dwordx4 v[68:69], v[54:57], off offset:256 sc1
	global_load_dword v50, v[148:149], off offset:576
	v_lshl_add_u64 v[52:53], v[146:147], 0, s[8:9]
	v_add_co_u32_e32 v54, vcc, s45, v146
	s_waitcnt vmcnt(0)
	v_pk_mul_f32 v[48:49], v[48:49], v[50:51] op_sel_hi:[1,0]
	v_pk_mul_f32 v[46:47], v[46:47], v[50:51] op_sel_hi:[1,0]
	v_pk_mul_f32 v[44:45], v[44:45], v[50:51] op_sel_hi:[1,0]
	v_pk_mul_f32 v[42:43], v[42:43], v[50:51] op_sel_hi:[1,0]
	v_addc_co_u32_e32 v55, vcc, 0, v147, vcc
	v_pk_mul_f32 v[40:41], v[40:41], v[50:51] op_sel_hi:[1,0]
	v_pk_mul_f32 v[38:39], v[38:39], v[50:51] op_sel_hi:[1,0]
	v_pk_mul_f32 v[56:57], v[36:37], v[50:51] op_sel_hi:[1,0]
	v_pk_mul_f32 v[50:51], v[34:35], v[50:51] op_sel_hi:[1,0]
	v_cvt_pk_bf16_f32 v34, v46, v47
	v_cvt_pk_bf16_f32 v35, v48, v49
	v_cvt_pk_bf16_f32 v36, v42, v43
	v_cvt_pk_bf16_f32 v37, v44, v45
	v_cvt_pk_bf16_f32 v38, v38, v39
	v_cvt_pk_bf16_f32 v39, v40, v41
	v_cvt_pk_bf16_f32 v40, v50, v51
	v_cvt_pk_bf16_f32 v41, v56, v57
	global_store_dwordx4 v[54:55], v[34:37], off sc1
	global_store_dwordx4 v[52:53], v[38:41], off offset:256 sc1
	global_load_dword v34, v[148:149], off offset:640
	v_lshl_add_u64 v[36:37], v[146:147], 0, s[10:11]
	v_add_co_u32_e32 v38, vcc, s46, v146
	s_waitcnt vmcnt(0)
	v_pk_mul_f32 v[32:33], v[32:33], v[34:35] op_sel_hi:[1,0]
	v_pk_mul_f32 v[30:31], v[30:31], v[34:35] op_sel_hi:[1,0]
	v_pk_mul_f32 v[28:29], v[28:29], v[34:35] op_sel_hi:[1,0]
	v_pk_mul_f32 v[26:27], v[26:27], v[34:35] op_sel_hi:[1,0]
	v_addc_co_u32_e32 v39, vcc, 0, v147, vcc
	v_pk_mul_f32 v[24:25], v[24:25], v[34:35] op_sel_hi:[1,0]
	v_pk_mul_f32 v[22:23], v[22:23], v[34:35] op_sel_hi:[1,0]
	v_pk_mul_f32 v[40:41], v[20:21], v[34:35] op_sel_hi:[1,0]
	v_pk_mul_f32 v[34:35], v[18:19], v[34:35] op_sel_hi:[1,0]
	v_cvt_pk_bf16_f32 v18, v30, v31
	v_cvt_pk_bf16_f32 v19, v32, v33
	v_cvt_pk_bf16_f32 v20, v26, v27
	v_cvt_pk_bf16_f32 v21, v28, v29
	v_cvt_pk_bf16_f32 v22, v22, v23
	v_cvt_pk_bf16_f32 v23, v24, v25
	v_cvt_pk_bf16_f32 v24, v34, v35
	v_cvt_pk_bf16_f32 v25, v40, v41
	global_store_dwordx4 v[38:39], v[18:21], off sc1
	global_store_dwordx4 v[36:37], v[22:25], off offset:256 sc1
	global_load_dword v18, v[148:149], off offset:704
	v_lshl_add_u64 v[20:21], v[146:147], 0, s[12:13]
	v_add_co_u32_e32 v22, vcc, s47, v146
	s_waitcnt vmcnt(0)
	v_pk_mul_f32 v[16:17], v[16:17], v[18:19] op_sel_hi:[1,0]
	v_addc_co_u32_e32 v23, vcc, 0, v147, vcc
	v_pk_mul_f32 v[14:15], v[14:15], v[18:19] op_sel_hi:[1,0]
	v_pk_mul_f32 v[12:13], v[12:13], v[18:19] op_sel_hi:[1,0]
	v_pk_mul_f32 v[10:11], v[10:11], v[18:19] op_sel_hi:[1,0]
	s_and_b64 vcc, exec, s[0:1]
	v_pk_mul_f32 v[8:9], v[8:9], v[18:19] op_sel_hi:[1,0]
	v_pk_mul_f32 v[6:7], v[6:7], v[18:19] op_sel_hi:[1,0]
	v_pk_mul_f32 v[24:25], v[4:5], v[18:19] op_sel_hi:[1,0]
	v_pk_mul_f32 v[18:19], v[2:3], v[18:19] op_sel_hi:[1,0]
	v_cvt_pk_bf16_f32 v2, v14, v15
	v_cvt_pk_bf16_f32 v3, v16, v17
	v_cvt_pk_bf16_f32 v4, v10, v11
	v_cvt_pk_bf16_f32 v5, v12, v13
	s_mov_b64 s[0:1], -1
	v_cvt_pk_bf16_f32 v6, v6, v7
	v_cvt_pk_bf16_f32 v7, v8, v9
	v_cvt_pk_bf16_f32 v8, v18, v19
	v_cvt_pk_bf16_f32 v9, v24, v25
	global_store_dwordx4 v[22:23], v[2:5], off sc1
	global_store_dwordx4 v[20:21], v[6:9], off offset:256 sc1
	s_cbranch_vccnz .LBB0_2403
	s_andn2_b64 vcc, exec, s[2:3]
	s_cbranch_vccnz .LBB0_2402
	s_barrier
	s_branch .LBB0_2402
